# code placement: one s_nop pad before each misaligned MFMA run in the GEMM K-loops and peels so every 8-byte MFMA there is 8-byte aligned (39 pads)
# speedup vs baseline: 1.0038x; 1.0003x over previous
; #define PG8_STAGE(bufoff, gbase, voff) do { _Pragma("unroll") for (int _i = 0; _i < 2; ++_i) \
;         __builtin_amdgcn_global_load_lds((const unsigned*)((const char*)(gbase) + (voff)[_i]), (PG8_LAS unsigned*)(lds + (bufoff) + ldsw + _i * 8192), 16, 0, 0); } while (0)
; #define PG8_LDA(dst, b, h) do { _Pragma("unroll") for (int m = 0; m < 4; ++m) _Pragma("unroll") for (int k = 0; k < 2; ++k) dst[m][k] = *(const PG8_LAS bf16x8*)(lds + PG8_SA(b, h) + aoff + m * 2048 + k * 1024); } while (0)
; #define PG8_LDB(dst, b, h) do { _Pragma("unroll") for (int n = 0; n < 2; ++n) _Pragma("unroll") for (int k = 0; k < 2; ++k) dst[n][k] = *(const PG8_LAS bf16x8*)(lds + PG8_SB(b, h) + boff + n * 2048 + k * 1024); } while (0)
; #define PG8_WAIT_V(n) asm volatile("s_waitcnt vmcnt(" #n ")" ::: "memory")
; #define PG8_WAIT_L(n) asm volatile("s_waitcnt lgkmcnt(" #n ")" ::: "memory")
; #define PG8_BAR __builtin_amdgcn_s_barrier()
; #define PG8_SCHED __builtin_amdgcn_sched_barrier(0)
; template <class Epi, class Sched, bool ALIGN_EPI = false, bool SP2 = false>
; __device__ __forceinline__ void gemm_phase(PG8_LAS unsigned char* lds, const Gemm g, const Sched& S, const Epi& E, const int wid) {
;     ...
;         const bool has_next = S.next(ui + 1, nxt);
;         const char* nA = has_next ? (const char*)g.A + (size_t)nxt.pm * tstepA : cA; const char* nB = has_next ? (const char*)g.Bt + (size_t)nxt.pn * tstepB : cB;
;         for (int t = 0; t < nt; t += 2) {
;             const bool last = (t == nt - 2);
;             const char* a1 = cA + (size_t)(t + 1) * kstep;
;             const char* a2 = last ? nA : cA + (size_t)(t + 2) * kstep; const char* b2 = last ? nB : cB + (size_t)(t + 2) * kstep;
;             const char* a3 = a2 + kstep; const char* b3 = b2 + kstep;
;             if (last && has_next) S.a_ready(nxt);
;             if constexpr (SP2) {
;             PG8_LDB(B0, 0, 0); PG8_LDB(B1, 0, 1); PG8_SCHED; PG8_LDA(At, 0, 0); PG8_STAGE(PG8_SA(1, 1), a1 + hstepA, voffA);
;             PG8_WAIT_V(8); PG8_WAIT_L(0); PG8_BAR; PG8_MMA(0, 0, At, B0); PG8_MMA(0, 1, At, B1); PG8_BAR; PG8_SCHED;
;             PG8_LDA(At, 0, 1); PG8_STAGE(PG8_SB(0, 0), b2, voffB); PG8_STAGE(PG8_SB(0, 1), b2 + hstepB, voffB); PG8_STAGE(PG8_SA(0, 0), a2, voffA);
;             PG8_WAIT_V(8); PG8_WAIT_L(0); PG8_BAR; PG8_MMA(1, 0, At, B0); PG8_MMA(1, 1, At, B1); PG8_BAR; PG8_SCHED;
.LBB0_348:
	s_ashr_i32 s27, s26, 31
	s_lshl_b64 s[28:29], s[26:27], 19
	s_add_u32 s28, s0, s28
	s_addc_u32 s29, s1, s29
	s_and_b64 s[30:31], s[4:5], exec
	s_cselect_b32 s7, s29, s9
	s_cselect_b32 s27, s28, s8
	s_ashr_i32 s25, s24, 31
	s_lshl_b64 s[30:31], s[24:25], 19
	s_add_u32 s30, s33, s30
	s_addc_u32 s31, s44, s31
	s_and_b64 s[40:41], s[4:5], exec
	s_cselect_b32 s25, s31, s37
	s_cselect_b32 s35, s30, s36
	s_add_u32 s8, s8, 0x40080
	s_addc_u32 s9, s9, 0
	s_add_u32 s73, s36, 0x100
	s_addc_u32 s74, s37, 0
	s_mov_b32 s75, -2
	s_waitcnt lgkmcnt(0)
	v_add_u32_e32 v252, 0x18000, v178
	v_add_u32_e32 v253, 0x1c000, v178
	ds_read_b128 v[128:131], v183
	ds_read_b128 v[150:153], v183 offset:1024
	ds_read_b128 v[154:157], v183 offset:2048
	ds_read_b128 v[158:161], v183 offset:3072
	ds_read_b128 v[162:165], v184
	ds_read_b128 v[166:169], v184 offset:1024
	ds_read_b128 v[170:173], v184 offset:2048
	ds_read_b128 v[188:191], v184 offset:3072
	s_add_u32 s36, s8, 0xfffc0080
	s_addc_u32 s37, s9, -1
	s_cmp_eq_u32 s75, 12
	s_cselect_b32 s41, s7, s37
	s_cselect_b32 s40, s27, s36
	s_cselect_b32 s37, s25, s74
	s_cselect_b32 s36, s35, s73
	s_add_i32 m0, s46, 0xc000
	ds_read_b128 v[192:195], v185
	ds_read_b128 v[196:199], v185 offset:1024
	ds_read_b128 v[200:203], v185 offset:2048
	ds_read_b128 v[204:207], v185 offset:3072
	ds_read_b128 v[208:211], v185 offset:4096
	ds_read_b128 v[212:215], v185 offset:5120
	ds_read_b128 v[216:219], v185 offset:6144
	ds_read_b128 v[220:223], v185 offset:7168
	global_load_lds_dwordx4 v142, s[8:9]
	s_add_i32 m0, s46, 0xe000
	s_nop 0
	global_load_lds_dwordx4 v144, s[8:9]
	s_waitcnt vmcnt(8) lgkmcnt(0)
	s_barrier
	s_setprio 1
	v_mfma_f32_16x16x32_bf16 v[124:127], v[128:131], v[192:195], 0
	v_mfma_f32_16x16x32_bf16 v[120:123], v[154:157], v[192:195], 0
	v_mfma_f32_16x16x32_bf16 v[108:111], v[128:131], v[200:203], 0
	v_mfma_f32_16x16x32_bf16 v[104:107], v[154:157], v[200:203], 0
	v_mfma_f32_16x16x32_bf16 v[92:95], v[128:131], v[208:211], 0
	v_mfma_f32_16x16x32_bf16 v[88:91], v[154:157], v[208:211], 0
	v_mfma_f32_16x16x32_bf16 v[76:79], v[128:131], v[216:219], 0
	v_mfma_f32_16x16x32_bf16 v[72:75], v[154:157], v[216:219], 0
	v_mfma_f32_16x16x32_bf16 v[124:127], v[150:153], v[196:199], v[124:127]
	v_mfma_f32_16x16x32_bf16 v[120:123], v[158:161], v[196:199], v[120:123]
	v_mfma_f32_16x16x32_bf16 v[108:111], v[150:153], v[204:207], v[108:111]
	v_mfma_f32_16x16x32_bf16 v[104:107], v[158:161], v[204:207], v[104:107]
	v_mfma_f32_16x16x32_bf16 v[92:95], v[150:153], v[212:215], v[92:95]
	v_mfma_f32_16x16x32_bf16 v[88:91], v[158:161], v[212:215], v[88:91]
	v_mfma_f32_16x16x32_bf16 v[76:79], v[150:153], v[220:223], v[76:79]
	v_mfma_f32_16x16x32_bf16 v[72:75], v[158:161], v[220:223], v[72:75]
	s_setprio 0
	s_setprio 1
	v_mfma_f32_16x16x32_bf16 v[116:119], v[162:165], v[192:195], 0
	v_mfma_f32_16x16x32_bf16 v[112:115], v[170:173], v[192:195], 0
	v_mfma_f32_16x16x32_bf16 v[100:103], v[162:165], v[200:203], 0
	v_mfma_f32_16x16x32_bf16 v[96:99], v[170:173], v[200:203], 0
	v_mfma_f32_16x16x32_bf16 v[84:87], v[162:165], v[208:211], 0
	v_mfma_f32_16x16x32_bf16 v[80:83], v[170:173], v[208:211], 0
	v_mfma_f32_16x16x32_bf16 v[68:71], v[162:165], v[216:219], 0
	v_mfma_f32_16x16x32_bf16 v[64:67], v[170:173], v[216:219], 0
	v_mfma_f32_16x16x32_bf16 v[116:119], v[166:169], v[196:199], v[116:119]
	v_mfma_f32_16x16x32_bf16 v[112:115], v[188:191], v[196:199], v[112:115]
	v_mfma_f32_16x16x32_bf16 v[100:103], v[166:169], v[204:207], v[100:103]
	v_mfma_f32_16x16x32_bf16 v[96:99], v[188:191], v[204:207], v[96:99]
	v_mfma_f32_16x16x32_bf16 v[84:87], v[166:169], v[212:215], v[84:87]
	v_mfma_f32_16x16x32_bf16 v[80:83], v[188:191], v[212:215], v[80:83]
	v_mfma_f32_16x16x32_bf16 v[68:71], v[166:169], v[220:223], v[68:71]
	v_mfma_f32_16x16x32_bf16 v[64:67], v[188:191], v[220:223], v[64:67]
	s_setprio 0
	s_barrier
	s_add_i32 s76, s69, s45
	s_add_u32 s98, s36, 0x80
	s_addc_u32 s99, s37, 0
	s_mov_b32 m0, s76
	ds_read_b128 v[192:195], v185 offset:16384
	ds_read_b128 v[196:199], v185 offset:17408
	ds_read_b128 v[200:203], v185 offset:18432
	ds_read_b128 v[204:207], v185 offset:19456
	ds_read_b128 v[208:211], v185 offset:20480
	ds_read_b128 v[212:215], v185 offset:21504
	ds_read_b128 v[216:219], v185 offset:22528
	ds_read_b128 v[220:223], v185 offset:23552
	global_load_lds_dwordx4 v134, s[36:37]
	s_add_i32 m0, s76, 0x2000
	s_add_u32 s76, s36, 0x40000
	s_addc_u32 s77, s37, 0
	s_add_i32 s78, s70, s45
	global_load_lds_dwordx4 v138, s[36:37]
	s_mov_b32 m0, s78
	s_add_u32 s100, s40, 0x80
	s_addc_u32 s101, s41, 0
	global_load_lds_dwordx4 v134, s[76:77]
	s_add_i32 m0, s78, 0x2000
	s_nop 0
	global_load_lds_dwordx4 v138, s[76:77]
	s_mov_b32 m0, s46
	s_nop 0
	global_load_lds_dwordx4 v132, s[40:41]
	s_mov_b32 m0, s47
	s_nop 0
	global_load_lds_dwordx4 v136, s[40:41]
	s_waitcnt vmcnt(8) lgkmcnt(0)
	s_barrier
; #define PG8_STAGE(bufoff, gbase, voff) do { _Pragma("unroll") for (int _i = 0; _i < 2; ++_i) \
;         __builtin_amdgcn_global_load_lds((const unsigned*)((const char*)(gbase) + (voff)[_i]), (PG8_LAS unsigned*)(lds + (bufoff) + ldsw + _i * 8192), 16, 0, 0); } while (0)
; #define PG8_LDA(dst, b, h) do { _Pragma("unroll") for (int m = 0; m < 4; ++m) _Pragma("unroll") for (int k = 0; k < 2; ++k) dst[m][k] = *(const PG8_LAS bf16x8*)(lds + PG8_SA(b, h) + aoff + m * 2048 + k * 1024); } while (0)
; #define PG8_LDB(dst, b, h) do { _Pragma("unroll") for (int n = 0; n < 2; ++n) _Pragma("unroll") for (int k = 0; k < 2; ++k) dst[n][k] = *(const PG8_LAS bf16x8*)(lds + PG8_SB(b, h) + boff + n * 2048 + k * 1024); } while (0)
; #define PG8_MMA(ai, bj, At, Bt) do { __builtin_amdgcn_s_setprio(1); _Pragma("unroll") for (int m = 0; m < 4; ++m) _Pragma("unroll") for (int n = 0; n < 2; ++n) _Pragma("unroll") for (int k = 0; k < 2; ++k) \
;         acc[ai][bj][m][n] = __builtin_amdgcn_mfma_f32_16x16x32_bf16(Bt[n][k], At[m][k], acc[ai][bj][m][n], 0, 0, 0); __builtin_amdgcn_s_setprio(0); } while (0)
; #define PG8_WAIT_V(n) asm volatile("s_waitcnt vmcnt(" #n ")" ::: "memory")
; #define PG8_WAIT_L(n) asm volatile("s_waitcnt lgkmcnt(" #n ")" ::: "memory")
; #define PG8_BAR __builtin_amdgcn_s_barrier()
; #define PG8_SCHED __builtin_amdgcn_sched_barrier(0)
; template <class Epi, class Sched, bool ALIGN_EPI = false, bool SP2 = false>
; __device__ __forceinline__ void gemm_phase(PG8_LAS unsigned char* lds, const Gemm g, const Sched& S, const Epi& E, const int wid) {
;     ...
;             PG8_WAIT_V(8); PG8_WAIT_L(0); PG8_BAR; PG8_MMA(0, 0, At, B0); PG8_MMA(0, 1, At, B1); PG8_BAR; PG8_SCHED;
;             PG8_LDA(At, 0, 1); PG8_STAGE(PG8_SB(0, 0), b2, voffB); PG8_STAGE(PG8_SB(0, 1), b2 + hstepB, voffB); PG8_STAGE(PG8_SA(0, 0), a2, voffA);
;             PG8_WAIT_V(8); PG8_WAIT_L(0); PG8_BAR; PG8_MMA(1, 0, At, B0); PG8_MMA(1, 1, At, B1); PG8_BAR; PG8_SCHED;
;             PG8_LDB(B0, 1, 0); PG8_LDB(B1, 1, 1); PG8_SCHED; PG8_LDA(At, 1, 0); PG8_STAGE(PG8_SA(0, 1), a2 + hstepA, voffA);
;             PG8_WAIT_V(8); PG8_WAIT_L(0); PG8_BAR; PG8_MMA(0, 0, At, B0); PG8_MMA(0, 1, At, B1); PG8_BAR; PG8_SCHED;
	s_nop 0
	s_setprio 1
	v_mfma_f32_16x16x32_bf16 v[60:63], v[128:131], v[192:195], 0
	v_mfma_f32_16x16x32_bf16 v[56:59], v[154:157], v[192:195], 0
	v_mfma_f32_16x16x32_bf16 v[44:47], v[128:131], v[200:203], 0
	v_mfma_f32_16x16x32_bf16 v[40:43], v[154:157], v[200:203], 0
	v_mfma_f32_16x16x32_bf16 v[28:31], v[128:131], v[208:211], 0
	v_mfma_f32_16x16x32_bf16 v[24:27], v[154:157], v[208:211], 0
	v_mfma_f32_16x16x32_bf16 v[12:15], v[128:131], v[216:219], 0
	v_mfma_f32_16x16x32_bf16 v[8:11], v[154:157], v[216:219], 0
	v_mfma_f32_16x16x32_bf16 v[60:63], v[150:153], v[196:199], v[60:63]
	v_mfma_f32_16x16x32_bf16 v[56:59], v[158:161], v[196:199], v[56:59]
	v_mfma_f32_16x16x32_bf16 v[44:47], v[150:153], v[204:207], v[44:47]
	v_mfma_f32_16x16x32_bf16 v[40:43], v[158:161], v[204:207], v[40:43]
	v_mfma_f32_16x16x32_bf16 v[28:31], v[150:153], v[212:215], v[28:31]
	v_mfma_f32_16x16x32_bf16 v[24:27], v[158:161], v[212:215], v[24:27]
	v_mfma_f32_16x16x32_bf16 v[12:15], v[150:153], v[220:223], v[12:15]
	v_mfma_f32_16x16x32_bf16 v[8:11], v[158:161], v[220:223], v[8:11]
	s_setprio 0
	s_setprio 1
	v_mfma_f32_16x16x32_bf16 v[52:55], v[162:165], v[192:195], 0
	v_mfma_f32_16x16x32_bf16 v[48:51], v[170:173], v[192:195], 0
	v_mfma_f32_16x16x32_bf16 v[36:39], v[162:165], v[200:203], 0
	v_mfma_f32_16x16x32_bf16 v[32:35], v[170:173], v[200:203], 0
	v_mfma_f32_16x16x32_bf16 v[20:23], v[162:165], v[208:211], 0
	v_mfma_f32_16x16x32_bf16 v[16:19], v[170:173], v[208:211], 0
	v_mfma_f32_16x16x32_bf16 v[4:7], v[162:165], v[216:219], 0
	v_mfma_f32_16x16x32_bf16 v[0:3], v[170:173], v[216:219], 0
	v_mfma_f32_16x16x32_bf16 v[52:55], v[166:169], v[196:199], v[52:55]
	v_mfma_f32_16x16x32_bf16 v[48:51], v[188:191], v[196:199], v[48:51]
	v_mfma_f32_16x16x32_bf16 v[36:39], v[166:169], v[204:207], v[36:39]
	v_mfma_f32_16x16x32_bf16 v[32:35], v[188:191], v[204:207], v[32:35]
	v_mfma_f32_16x16x32_bf16 v[20:23], v[166:169], v[212:215], v[20:23]
	v_mfma_f32_16x16x32_bf16 v[16:19], v[188:191], v[212:215], v[16:19]
	v_mfma_f32_16x16x32_bf16 v[4:7], v[166:169], v[220:223], v[4:7]
	v_mfma_f32_16x16x32_bf16 v[0:3], v[188:191], v[220:223], v[0:3]
	s_setprio 0
	s_barrier
	s_add_i32 s76, 0, 0x18000
	s_add_i32 s77, 0, 0x1c000
	ds_read_b128 v[128:131], v252
	ds_read_b128 v[150:153], v252 offset:1024
	ds_read_b128 v[154:157], v252 offset:2048
	ds_read_b128 v[158:161], v252 offset:3072
	ds_read_b128 v[162:165], v253
	ds_read_b128 v[166:169], v253 offset:1024
	ds_read_b128 v[170:173], v253 offset:2048
	ds_read_b128 v[188:191], v253 offset:3072
	s_add_u32 s40, s40, 0x40000
	s_addc_u32 s41, s41, 0
	s_mov_b32 m0, s48
	ds_read_b128 v[192:195], v185 offset:32768
	ds_read_b128 v[196:199], v185 offset:33792
	ds_read_b128 v[200:203], v185 offset:34816
	ds_read_b128 v[204:207], v185 offset:35840
	ds_read_b128 v[208:211], v185 offset:36864
	ds_read_b128 v[212:215], v185 offset:37888
	ds_read_b128 v[216:219], v185 offset:38912
	ds_read_b128 v[220:223], v185 offset:39936
	global_load_lds_dwordx4 v132, s[40:41]
	s_mov_b32 m0, s49
	s_nop 0
	global_load_lds_dwordx4 v136, s[40:41]
	s_waitcnt vmcnt(8) lgkmcnt(0)
	s_barrier
	s_nop 0
	s_setprio 1
	v_mfma_f32_16x16x32_bf16 v[124:127], v[128:131], v[192:195], v[124:127]
	v_mfma_f32_16x16x32_bf16 v[120:123], v[154:157], v[192:195], v[120:123]
	v_mfma_f32_16x16x32_bf16 v[108:111], v[128:131], v[200:203], v[108:111]
	v_mfma_f32_16x16x32_bf16 v[104:107], v[154:157], v[200:203], v[104:107]
	v_mfma_f32_16x16x32_bf16 v[92:95], v[128:131], v[208:211], v[92:95]
	v_mfma_f32_16x16x32_bf16 v[88:91], v[154:157], v[208:211], v[88:91]
	v_mfma_f32_16x16x32_bf16 v[76:79], v[128:131], v[216:219], v[76:79]
	v_mfma_f32_16x16x32_bf16 v[72:75], v[154:157], v[216:219], v[72:75]
	v_mfma_f32_16x16x32_bf16 v[124:127], v[150:153], v[196:199], v[124:127]
	v_mfma_f32_16x16x32_bf16 v[120:123], v[158:161], v[196:199], v[120:123]
	v_mfma_f32_16x16x32_bf16 v[108:111], v[150:153], v[204:207], v[108:111]
	v_mfma_f32_16x16x32_bf16 v[104:107], v[158:161], v[204:207], v[104:107]
	v_mfma_f32_16x16x32_bf16 v[92:95], v[150:153], v[212:215], v[92:95]
	v_mfma_f32_16x16x32_bf16 v[88:91], v[158:161], v[212:215], v[88:91]
	v_mfma_f32_16x16x32_bf16 v[76:79], v[150:153], v[220:223], v[76:79]
	v_mfma_f32_16x16x32_bf16 v[72:75], v[158:161], v[220:223], v[72:75]
	s_setprio 0
	s_setprio 1
	v_mfma_f32_16x16x32_bf16 v[116:119], v[162:165], v[192:195], v[116:119]
	v_mfma_f32_16x16x32_bf16 v[112:115], v[170:173], v[192:195], v[112:115]
	v_mfma_f32_16x16x32_bf16 v[100:103], v[162:165], v[200:203], v[100:103]
	v_mfma_f32_16x16x32_bf16 v[96:99], v[170:173], v[200:203], v[96:99]
	v_mfma_f32_16x16x32_bf16 v[84:87], v[162:165], v[208:211], v[84:87]
	v_mfma_f32_16x16x32_bf16 v[80:83], v[170:173], v[208:211], v[80:83]
	v_mfma_f32_16x16x32_bf16 v[68:71], v[162:165], v[216:219], v[68:71]
	v_mfma_f32_16x16x32_bf16 v[64:67], v[170:173], v[216:219], v[64:67]
	v_mfma_f32_16x16x32_bf16 v[116:119], v[166:169], v[196:199], v[116:119]
	v_mfma_f32_16x16x32_bf16 v[112:115], v[188:191], v[196:199], v[112:115]
	v_mfma_f32_16x16x32_bf16 v[100:103], v[166:169], v[204:207], v[100:103]
	v_mfma_f32_16x16x32_bf16 v[96:99], v[188:191], v[204:207], v[96:99]
	v_mfma_f32_16x16x32_bf16 v[84:87], v[166:169], v[212:215], v[84:87]
	v_mfma_f32_16x16x32_bf16 v[80:83], v[188:191], v[212:215], v[80:83]
	v_mfma_f32_16x16x32_bf16 v[68:71], v[166:169], v[220:223], v[68:71]
	v_mfma_f32_16x16x32_bf16 v[64:67], v[188:191], v[220:223], v[64:67]
	s_setprio 0
	s_barrier
; #define PG8_STAGE(bufoff, gbase, voff) do { _Pragma("unroll") for (int _i = 0; _i < 2; ++_i) \
;         __builtin_amdgcn_global_load_lds((const unsigned*)((const char*)(gbase) + (voff)[_i]), (PG8_LAS unsigned*)(lds + (bufoff) + ldsw + _i * 8192), 16, 0, 0); } while (0)
; #define PG8_LDA(dst, b, h) do { _Pragma("unroll") for (int m = 0; m < 4; ++m) _Pragma("unroll") for (int k = 0; k < 2; ++k) dst[m][k] = *(const PG8_LAS bf16x8*)(lds + PG8_SA(b, h) + aoff + m * 2048 + k * 1024); } while (0)
; #define PG8_WAIT_V(n) asm volatile("s_waitcnt vmcnt(" #n ")" ::: "memory")
; #define PG8_WAIT_L(n) asm volatile("s_waitcnt lgkmcnt(" #n ")" ::: "memory")
; #define PG8_BAR __builtin_amdgcn_s_barrier()
; template <class Epi, class Sched, bool ALIGN_EPI = false, bool SP2 = false>
; __device__ __forceinline__ void gemm_phase(PG8_LAS unsigned char* lds, const Gemm g, const Sched& S, const Epi& E, const int wid) {
;     ...
;         for (int t = 0; t < nt; t += 2) {
;             const bool last = (t == nt - 2);
;             const char* a1 = cA + (size_t)(t + 1) * kstep;
;             const char* a2 = last ? nA : cA + (size_t)(t + 2) * kstep; const char* b2 = last ? nB : cB + (size_t)(t + 2) * kstep;
;             const char* a3 = a2 + kstep; const char* b3 = b2 + kstep;
;             if (last && has_next) S.a_ready(nxt);
;             if constexpr (SP2) {
;             PG8_LDB(B0, 0, 0); PG8_LDB(B1, 0, 1); PG8_SCHED; PG8_LDA(At, 0, 0); PG8_STAGE(PG8_SA(1, 1), a1 + hstepA, voffA);
;             PG8_WAIT_V(8); PG8_WAIT_L(0); PG8_BAR; PG8_MMA(0, 0, At, B0); PG8_MMA(0, 1, At, B1); PG8_BAR; PG8_SCHED;
;             PG8_LDA(At, 0, 1); PG8_STAGE(PG8_SB(0, 0), b2, voffB); PG8_STAGE(PG8_SB(0, 1), b2 + hstepB, voffB); PG8_STAGE(PG8_SA(0, 0), a2, voffA);
;             PG8_WAIT_V(8); PG8_WAIT_L(0); PG8_BAR; PG8_MMA(1, 0, At, B0); PG8_MMA(1, 1, At, B1); PG8_BAR; PG8_SCHED;
;             PG8_LDB(B0, 1, 0); PG8_LDB(B1, 1, 1); PG8_SCHED; PG8_LDA(At, 1, 0); PG8_STAGE(PG8_SA(0, 1), a2 + hstepA, voffA);
;             PG8_WAIT_V(8); PG8_WAIT_L(0); PG8_BAR; PG8_MMA(0, 0, At, B0); PG8_MMA(0, 1, At, B1); PG8_BAR; PG8_SCHED;
;             PG8_LDA(At, 1, 1); PG8_STAGE(PG8_SB(1, 0), b3, voffB); PG8_STAGE(PG8_SB(1, 1), b3 + hstepB, voffB); PG8_STAGE(PG8_SA(1, 0), a3, voffA);
;             PG8_WAIT_V(8); PG8_WAIT_L(0); PG8_BAR; PG8_MMA(1, 0, At, B0); PG8_MMA(1, 1, At, B1); PG8_BAR; PG8_SCHED;
	s_add_i32 s40, s76, s45
	s_mov_b32 m0, s40
	ds_read_b128 v[192:195], v185 offset:49152
	ds_read_b128 v[196:199], v185 offset:50176
	ds_read_b128 v[200:203], v185 offset:51200
	ds_read_b128 v[204:207], v185 offset:52224
	ds_read_b128 v[208:211], v185 offset:53248
	ds_read_b128 v[212:215], v185 offset:54272
	ds_read_b128 v[216:219], v185 offset:55296
	ds_read_b128 v[220:223], v185 offset:56320
	global_load_lds_dwordx4 v134, s[98:99]
	s_add_i32 m0, s40, 0x2000
	s_add_u32 s36, s36, 0x40080
	s_addc_u32 s37, s37, 0
	s_add_i32 s40, s77, s45
	global_load_lds_dwordx4 v138, s[98:99]
	s_mov_b32 m0, s40
	s_nop 0
	global_load_lds_dwordx4 v134, s[36:37]
	s_add_i32 m0, s40, 0x2000
	s_nop 0
	global_load_lds_dwordx4 v138, s[36:37]
	s_mov_b32 m0, s64
	s_nop 0
	global_load_lds_dwordx4 v132, s[100:101]
	s_mov_b32 m0, s65
	s_nop 0
	global_load_lds_dwordx4 v136, s[100:101]
	s_waitcnt vmcnt(8) lgkmcnt(0)
	s_barrier
	s_setprio 1
	v_mfma_f32_16x16x32_bf16 v[60:63], v[128:131], v[192:195], v[60:63]
	v_mfma_f32_16x16x32_bf16 v[56:59], v[154:157], v[192:195], v[56:59]
	v_mfma_f32_16x16x32_bf16 v[44:47], v[128:131], v[200:203], v[44:47]
	v_mfma_f32_16x16x32_bf16 v[40:43], v[154:157], v[200:203], v[40:43]
	v_mfma_f32_16x16x32_bf16 v[28:31], v[128:131], v[208:211], v[28:31]
	v_mfma_f32_16x16x32_bf16 v[24:27], v[154:157], v[208:211], v[24:27]
	v_mfma_f32_16x16x32_bf16 v[12:15], v[128:131], v[216:219], v[12:15]
	v_mfma_f32_16x16x32_bf16 v[8:11], v[154:157], v[216:219], v[8:11]
	v_mfma_f32_16x16x32_bf16 v[60:63], v[150:153], v[196:199], v[60:63]
	v_mfma_f32_16x16x32_bf16 v[56:59], v[158:161], v[196:199], v[56:59]
	v_mfma_f32_16x16x32_bf16 v[44:47], v[150:153], v[204:207], v[44:47]
	v_mfma_f32_16x16x32_bf16 v[40:43], v[158:161], v[204:207], v[40:43]
	v_mfma_f32_16x16x32_bf16 v[28:31], v[150:153], v[212:215], v[28:31]
	v_mfma_f32_16x16x32_bf16 v[24:27], v[158:161], v[212:215], v[24:27]
	v_mfma_f32_16x16x32_bf16 v[12:15], v[150:153], v[220:223], v[12:15]
	v_mfma_f32_16x16x32_bf16 v[8:11], v[158:161], v[220:223], v[8:11]
	s_setprio 0
	s_setprio 1
	v_mfma_f32_16x16x32_bf16 v[52:55], v[162:165], v[192:195], v[52:55]
	v_mfma_f32_16x16x32_bf16 v[48:51], v[170:173], v[192:195], v[48:51]
	v_mfma_f32_16x16x32_bf16 v[36:39], v[162:165], v[200:203], v[36:39]
	v_mfma_f32_16x16x32_bf16 v[32:35], v[170:173], v[200:203], v[32:35]
	v_mfma_f32_16x16x32_bf16 v[20:23], v[162:165], v[208:211], v[20:23]
	v_mfma_f32_16x16x32_bf16 v[16:19], v[170:173], v[208:211], v[16:19]
	v_mfma_f32_16x16x32_bf16 v[4:7], v[162:165], v[216:219], v[4:7]
	v_mfma_f32_16x16x32_bf16 v[0:3], v[170:173], v[216:219], v[0:3]
	v_mfma_f32_16x16x32_bf16 v[52:55], v[166:169], v[196:199], v[52:55]
	v_mfma_f32_16x16x32_bf16 v[48:51], v[188:191], v[196:199], v[48:51]
	v_mfma_f32_16x16x32_bf16 v[36:39], v[166:169], v[204:207], v[36:39]
	v_mfma_f32_16x16x32_bf16 v[32:35], v[188:191], v[204:207], v[32:35]
	v_mfma_f32_16x16x32_bf16 v[20:23], v[166:169], v[212:215], v[20:23]
	v_mfma_f32_16x16x32_bf16 v[16:19], v[188:191], v[212:215], v[16:19]
	v_mfma_f32_16x16x32_bf16 v[4:7], v[166:169], v[220:223], v[4:7]
	v_mfma_f32_16x16x32_bf16 v[0:3], v[188:191], v[220:223], v[0:3]
	s_setprio 0
	s_barrier
	s_add_i32 s75, s75, 2
	s_add_u32 s8, s8, 0x100
	s_addc_u32 s9, s9, 0
	s_add_u32 s73, s73, 0x100
	s_addc_u32 s74, s74, 0
	s_cmp_gt_u32 s75, 13
.LBB0_349:
	ds_read_b128 v[128:131], v183
	ds_read_b128 v[150:153], v183 offset:1024
	ds_read_b128 v[154:157], v183 offset:2048
	ds_read_b128 v[158:161], v183 offset:3072
	ds_read_b128 v[162:165], v184
	ds_read_b128 v[166:169], v184 offset:1024
	ds_read_b128 v[170:173], v184 offset:2048
	ds_read_b128 v[188:191], v184 offset:3072
	s_add_u32 s36, s8, 0xfffc0080
	s_addc_u32 s37, s9, -1
	s_cmp_eq_u32 s75, 12
	s_cselect_b32 s41, s7, s37
	s_cselect_b32 s40, s27, s36
	s_cselect_b32 s37, s25, s74
	s_cselect_b32 s36, s35, s73
	s_add_i32 m0, s46, 0xc000
	ds_read_b128 v[192:195], v185
	ds_read_b128 v[196:199], v185 offset:1024
	ds_read_b128 v[200:203], v185 offset:2048
	ds_read_b128 v[204:207], v185 offset:3072
	ds_read_b128 v[208:211], v185 offset:4096
	ds_read_b128 v[212:215], v185 offset:5120
	ds_read_b128 v[216:219], v185 offset:6144
	ds_read_b128 v[220:223], v185 offset:7168
	global_load_lds_dwordx4 v142, s[8:9]
	s_add_i32 m0, s46, 0xe000
	s_nop 0
	global_load_lds_dwordx4 v144, s[8:9]
	s_waitcnt vmcnt(8) lgkmcnt(0)
	s_barrier
	s_setprio 1
	v_mfma_f32_16x16x32_bf16 v[124:127], v[128:131], v[192:195], v[124:127]
	v_mfma_f32_16x16x32_bf16 v[120:123], v[154:157], v[192:195], v[120:123]
	v_mfma_f32_16x16x32_bf16 v[108:111], v[128:131], v[200:203], v[108:111]
	v_mfma_f32_16x16x32_bf16 v[104:107], v[154:157], v[200:203], v[104:107]
	v_mfma_f32_16x16x32_bf16 v[92:95], v[128:131], v[208:211], v[92:95]
	v_mfma_f32_16x16x32_bf16 v[88:91], v[154:157], v[208:211], v[88:91]
	v_mfma_f32_16x16x32_bf16 v[76:79], v[128:131], v[216:219], v[76:79]
	v_mfma_f32_16x16x32_bf16 v[72:75], v[154:157], v[216:219], v[72:75]
	v_mfma_f32_16x16x32_bf16 v[124:127], v[150:153], v[196:199], v[124:127]
	v_mfma_f32_16x16x32_bf16 v[120:123], v[158:161], v[196:199], v[120:123]
	v_mfma_f32_16x16x32_bf16 v[108:111], v[150:153], v[204:207], v[108:111]
	v_mfma_f32_16x16x32_bf16 v[104:107], v[158:161], v[204:207], v[104:107]
	v_mfma_f32_16x16x32_bf16 v[92:95], v[150:153], v[212:215], v[92:95]
	v_mfma_f32_16x16x32_bf16 v[88:91], v[158:161], v[212:215], v[88:91]
	v_mfma_f32_16x16x32_bf16 v[76:79], v[150:153], v[220:223], v[76:79]
	v_mfma_f32_16x16x32_bf16 v[72:75], v[158:161], v[220:223], v[72:75]
	s_setprio 0
	s_setprio 1
	v_mfma_f32_16x16x32_bf16 v[116:119], v[162:165], v[192:195], v[116:119]
	v_mfma_f32_16x16x32_bf16 v[112:115], v[170:173], v[192:195], v[112:115]
	v_mfma_f32_16x16x32_bf16 v[100:103], v[162:165], v[200:203], v[100:103]
	v_mfma_f32_16x16x32_bf16 v[96:99], v[170:173], v[200:203], v[96:99]
	v_mfma_f32_16x16x32_bf16 v[84:87], v[162:165], v[208:211], v[84:87]
	v_mfma_f32_16x16x32_bf16 v[80:83], v[170:173], v[208:211], v[80:83]
	v_mfma_f32_16x16x32_bf16 v[68:71], v[162:165], v[216:219], v[68:71]
	v_mfma_f32_16x16x32_bf16 v[64:67], v[170:173], v[216:219], v[64:67]
	v_mfma_f32_16x16x32_bf16 v[116:119], v[166:169], v[196:199], v[116:119]
	v_mfma_f32_16x16x32_bf16 v[112:115], v[188:191], v[196:199], v[112:115]
	v_mfma_f32_16x16x32_bf16 v[100:103], v[166:169], v[204:207], v[100:103]
	v_mfma_f32_16x16x32_bf16 v[96:99], v[188:191], v[204:207], v[96:99]
	v_mfma_f32_16x16x32_bf16 v[84:87], v[166:169], v[212:215], v[84:87]
	v_mfma_f32_16x16x32_bf16 v[80:83], v[188:191], v[212:215], v[80:83]
	v_mfma_f32_16x16x32_bf16 v[68:71], v[166:169], v[220:223], v[68:71]
	v_mfma_f32_16x16x32_bf16 v[64:67], v[188:191], v[220:223], v[64:67]
	s_setprio 0
	s_barrier
; #define PG8_STAGE(bufoff, gbase, voff) do { _Pragma("unroll") for (int _i = 0; _i < 2; ++_i) \
;         __builtin_amdgcn_global_load_lds((const unsigned*)((const char*)(gbase) + (voff)[_i]), (PG8_LAS unsigned*)(lds + (bufoff) + ldsw + _i * 8192), 16, 0, 0); } while (0)
; #define PG8_LDA(dst, b, h) do { _Pragma("unroll") for (int m = 0; m < 4; ++m) _Pragma("unroll") for (int k = 0; k < 2; ++k) dst[m][k] = *(const PG8_LAS bf16x8*)(lds + PG8_SA(b, h) + aoff + m * 2048 + k * 1024); } while (0)
; #define PG8_LDB(dst, b, h) do { _Pragma("unroll") for (int n = 0; n < 2; ++n) _Pragma("unroll") for (int k = 0; k < 2; ++k) dst[n][k] = *(const PG8_LAS bf16x8*)(lds + PG8_SB(b, h) + boff + n * 2048 + k * 1024); } while (0)
; #define PG8_MMA(ai, bj, At, Bt) do { __builtin_amdgcn_s_setprio(1); _Pragma("unroll") for (int m = 0; m < 4; ++m) _Pragma("unroll") for (int n = 0; n < 2; ++n) _Pragma("unroll") for (int k = 0; k < 2; ++k) \
;         acc[ai][bj][m][n] = __builtin_amdgcn_mfma_f32_16x16x32_bf16(Bt[n][k], At[m][k], acc[ai][bj][m][n], 0, 0, 0); __builtin_amdgcn_s_setprio(0); } while (0)
; #define PG8_WAIT_V(n) asm volatile("s_waitcnt vmcnt(" #n ")" ::: "memory")
; #define PG8_WAIT_L(n) asm volatile("s_waitcnt lgkmcnt(" #n ")" ::: "memory")
; #define PG8_BAR __builtin_amdgcn_s_barrier()
; #define PG8_SCHED __builtin_amdgcn_sched_barrier(0)
; template <class Epi, class Sched, bool ALIGN_EPI = false, bool SP2 = false>
; __device__ __forceinline__ void gemm_phase(PG8_LAS unsigned char* lds, const Gemm g, const Sched& S, const Epi& E, const int wid) {
;     ...
;             PG8_WAIT_V(8); PG8_WAIT_L(0); PG8_BAR; PG8_MMA(0, 0, At, B0); PG8_MMA(0, 1, At, B1); PG8_BAR; PG8_SCHED;
;             PG8_LDA(At, 0, 1); PG8_STAGE(PG8_SB(0, 0), b2, voffB); PG8_STAGE(PG8_SB(0, 1), b2 + hstepB, voffB); PG8_STAGE(PG8_SA(0, 0), a2, voffA);
;             PG8_WAIT_V(8); PG8_WAIT_L(0); PG8_BAR; PG8_MMA(1, 0, At, B0); PG8_MMA(1, 1, At, B1); PG8_BAR; PG8_SCHED;
;             PG8_LDB(B0, 1, 0); PG8_LDB(B1, 1, 1); PG8_SCHED; PG8_LDA(At, 1, 0); PG8_STAGE(PG8_SA(0, 1), a2 + hstepA, voffA);
	s_add_i32 s76, s69, s45
	s_add_u32 s98, s36, 0x80
	s_addc_u32 s99, s37, 0
	s_mov_b32 m0, s76
	ds_read_b128 v[192:195], v185 offset:16384
	ds_read_b128 v[196:199], v185 offset:17408
	ds_read_b128 v[200:203], v185 offset:18432
	ds_read_b128 v[204:207], v185 offset:19456
	ds_read_b128 v[208:211], v185 offset:20480
	ds_read_b128 v[212:215], v185 offset:21504
	ds_read_b128 v[216:219], v185 offset:22528
	ds_read_b128 v[220:223], v185 offset:23552
	global_load_lds_dwordx4 v134, s[36:37]
	s_add_i32 m0, s76, 0x2000
	s_add_u32 s76, s36, 0x40000
	s_addc_u32 s77, s37, 0
	s_add_i32 s78, s70, s45
	global_load_lds_dwordx4 v138, s[36:37]
	s_mov_b32 m0, s78
	s_add_u32 s100, s40, 0x80
	s_addc_u32 s101, s41, 0
	global_load_lds_dwordx4 v134, s[76:77]
	s_add_i32 m0, s78, 0x2000
	s_nop 0
	global_load_lds_dwordx4 v138, s[76:77]
	s_mov_b32 m0, s46
	s_nop 0
	global_load_lds_dwordx4 v132, s[40:41]
	s_mov_b32 m0, s47
	s_nop 0
	global_load_lds_dwordx4 v136, s[40:41]
	s_waitcnt vmcnt(8) lgkmcnt(0)
	s_barrier
	s_nop 0
	s_setprio 1
	v_mfma_f32_16x16x32_bf16 v[60:63], v[128:131], v[192:195], v[60:63]
	v_mfma_f32_16x16x32_bf16 v[56:59], v[154:157], v[192:195], v[56:59]
	v_mfma_f32_16x16x32_bf16 v[44:47], v[128:131], v[200:203], v[44:47]
	v_mfma_f32_16x16x32_bf16 v[40:43], v[154:157], v[200:203], v[40:43]
	v_mfma_f32_16x16x32_bf16 v[28:31], v[128:131], v[208:211], v[28:31]
	v_mfma_f32_16x16x32_bf16 v[24:27], v[154:157], v[208:211], v[24:27]
	v_mfma_f32_16x16x32_bf16 v[12:15], v[128:131], v[216:219], v[12:15]
	v_mfma_f32_16x16x32_bf16 v[8:11], v[154:157], v[216:219], v[8:11]
	v_mfma_f32_16x16x32_bf16 v[60:63], v[150:153], v[196:199], v[60:63]
	v_mfma_f32_16x16x32_bf16 v[56:59], v[158:161], v[196:199], v[56:59]
	v_mfma_f32_16x16x32_bf16 v[44:47], v[150:153], v[204:207], v[44:47]
	v_mfma_f32_16x16x32_bf16 v[40:43], v[158:161], v[204:207], v[40:43]
	v_mfma_f32_16x16x32_bf16 v[28:31], v[150:153], v[212:215], v[28:31]
	v_mfma_f32_16x16x32_bf16 v[24:27], v[158:161], v[212:215], v[24:27]
	v_mfma_f32_16x16x32_bf16 v[12:15], v[150:153], v[220:223], v[12:15]
	v_mfma_f32_16x16x32_bf16 v[8:11], v[158:161], v[220:223], v[8:11]
	s_setprio 0
	s_setprio 1
	v_mfma_f32_16x16x32_bf16 v[52:55], v[162:165], v[192:195], v[52:55]
	v_mfma_f32_16x16x32_bf16 v[48:51], v[170:173], v[192:195], v[48:51]
	v_mfma_f32_16x16x32_bf16 v[36:39], v[162:165], v[200:203], v[36:39]
	v_mfma_f32_16x16x32_bf16 v[32:35], v[170:173], v[200:203], v[32:35]
	v_mfma_f32_16x16x32_bf16 v[20:23], v[162:165], v[208:211], v[20:23]
	v_mfma_f32_16x16x32_bf16 v[16:19], v[170:173], v[208:211], v[16:19]
	v_mfma_f32_16x16x32_bf16 v[4:7], v[162:165], v[216:219], v[4:7]
	v_mfma_f32_16x16x32_bf16 v[0:3], v[170:173], v[216:219], v[0:3]
	v_mfma_f32_16x16x32_bf16 v[52:55], v[166:169], v[196:199], v[52:55]
	v_mfma_f32_16x16x32_bf16 v[48:51], v[188:191], v[196:199], v[48:51]
	v_mfma_f32_16x16x32_bf16 v[36:39], v[166:169], v[204:207], v[36:39]
	v_mfma_f32_16x16x32_bf16 v[32:35], v[188:191], v[204:207], v[32:35]
	v_mfma_f32_16x16x32_bf16 v[20:23], v[166:169], v[212:215], v[20:23]
	v_mfma_f32_16x16x32_bf16 v[16:19], v[188:191], v[212:215], v[16:19]
	v_mfma_f32_16x16x32_bf16 v[4:7], v[166:169], v[220:223], v[4:7]
	v_mfma_f32_16x16x32_bf16 v[0:3], v[188:191], v[220:223], v[0:3]
	s_setprio 0
	s_barrier
	s_add_i32 s76, 0, 0x18000
	s_add_i32 s77, 0, 0x1c000
	ds_read_b128 v[128:131], v252
	ds_read_b128 v[150:153], v252 offset:1024
	ds_read_b128 v[154:157], v252 offset:2048
	ds_read_b128 v[158:161], v252 offset:3072
	ds_read_b128 v[162:165], v253
	ds_read_b128 v[166:169], v253 offset:1024
	ds_read_b128 v[170:173], v253 offset:2048
	ds_read_b128 v[188:191], v253 offset:3072
	s_add_u32 s40, s40, 0x40000
	s_addc_u32 s41, s41, 0
	s_mov_b32 m0, s48
	ds_read_b128 v[192:195], v185 offset:32768
	ds_read_b128 v[196:199], v185 offset:33792
	ds_read_b128 v[200:203], v185 offset:34816
	ds_read_b128 v[204:207], v185 offset:35840
	ds_read_b128 v[208:211], v185 offset:36864
	ds_read_b128 v[212:215], v185 offset:37888
	ds_read_b128 v[216:219], v185 offset:38912
	ds_read_b128 v[220:223], v185 offset:39936
	global_load_lds_dwordx4 v132, s[40:41]
	s_mov_b32 m0, s49
	s_nop 0
	global_load_lds_dwordx4 v136, s[40:41]
	s_waitcnt vmcnt(8) lgkmcnt(0)
	s_barrier
; #define PG8_WAIT_V(n) asm volatile("s_waitcnt vmcnt(" #n ")" ::: "memory")
; #define PG8_WAIT_L(n) asm volatile("s_waitcnt lgkmcnt(" #n ")" ::: "memory")
; template <class Epi, class Sched, bool ALIGN_EPI = false, bool SP2 = false>
; __device__ __forceinline__ void gemm_phase(PG8_LAS unsigned char* lds, const Gemm g, const Sched& S, const Epi& E, const int wid) {
;     ...
;             PG8_WAIT_V(8); PG8_WAIT_L(0); PG8_BAR; PG8_MMA(1, 0, At, B0); PG8_MMA(1, 1, At, B1); PG8_BAR; PG8_SCHED;
;             PG8_LDB(B0, 1, 0); PG8_LDB(B1, 1, 1); PG8_SCHED; PG8_LDA(At, 1, 0); PG8_STAGE(PG8_SA(0, 1), a2 + hstepA, voffA);
;             PG8_WAIT_V(8); PG8_WAIT_L(0); PG8_BAR; PG8_MMA(0, 0, At, B0); PG8_MMA(0, 1, At, B1); PG8_BAR; PG8_SCHED;
;             PG8_LDA(At, 1, 1); PG8_STAGE(PG8_SB(1, 0), b3, voffB); PG8_STAGE(PG8_SB(1, 1), b3 + hstepB, voffB); PG8_STAGE(PG8_SA(1, 0), a3, voffA);
;             PG8_WAIT_V(8); PG8_WAIT_L(0); PG8_BAR; PG8_MMA(1, 0, At, B0); PG8_MMA(1, 1, At, B1); PG8_BAR; PG8_SCHED;
;             } else {
;             PG8_LDB(B0, 0, 0); PG8_SCHED; PG8_LDA(At, 0, 0); PG8_STAGE(PG8_SA(1, 1), a1 + hstepA, voffA);
;             PG8_WAIT_L(8); PG8_BAR; PG8_WAIT_L(0); PG8_MMA(0, 0, At, B0); PG8_BAR; PG8_SCHED;
;             PG8_LDB(B1, 0, 1); PG8_STAGE(PG8_SB(0, 0), b2, voffB);
;             PG8_BAR; PG8_WAIT_L(0); PG8_MMA(0, 1, At, B1); PG8_BAR;
;             PG8_LDA(At, 0, 1); PG8_STAGE(PG8_SA(0, 0), a2, voffA);
;             PG8_BAR; PG8_WAIT_L(0); PG8_MMA(1, 0, At, B0); PG8_BAR; PG8_SCHED;
;             PG8_STAGE(PG8_SB(0, 1), b2 + hstepB, voffB);
;             PG8_WAIT_V(6); PG8_BAR; PG8_MMA(1, 1, At, B1); PG8_BAR;
;             PG8_LDB(B0, 1, 0); PG8_SCHED; PG8_LDA(At, 1, 0); PG8_STAGE(PG8_SA(0, 1), a2 + hstepA, voffA);
;             PG8_WAIT_L(8); PG8_BAR; PG8_WAIT_L(0); PG8_MMA(0, 0, At, B0); PG8_BAR; PG8_SCHED;
;             PG8_LDB(B1, 1, 1); PG8_STAGE(PG8_SB(1, 0), b3, voffB);
;             PG8_BAR; PG8_WAIT_L(0); PG8_MMA(0, 1, At, B1); PG8_BAR;
;             PG8_LDA(At, 1, 1); PG8_STAGE(PG8_SA(1, 0), a3, voffA);
;             PG8_BAR; PG8_WAIT_L(0); PG8_MMA(1, 0, At, B0); PG8_BAR; PG8_SCHED;
;             PG8_STAGE(PG8_SB(1, 1), b3 + hstepB, voffB);
;             PG8_WAIT_V(6); PG8_BAR; PG8_MMA(1, 1, At, B1); PG8_BAR;
;             }
;         }
;         if constexpr (ALIGN_EPI) { if (wr == 0) PG8_BAR; }
	s_nop 0
	s_setprio 1
	v_mfma_f32_16x16x32_bf16 v[124:127], v[128:131], v[192:195], v[124:127]
	v_mfma_f32_16x16x32_bf16 v[120:123], v[154:157], v[192:195], v[120:123]
	v_mfma_f32_16x16x32_bf16 v[108:111], v[128:131], v[200:203], v[108:111]
	v_mfma_f32_16x16x32_bf16 v[104:107], v[154:157], v[200:203], v[104:107]
	v_mfma_f32_16x16x32_bf16 v[92:95], v[128:131], v[208:211], v[92:95]
	v_mfma_f32_16x16x32_bf16 v[88:91], v[154:157], v[208:211], v[88:91]
	v_mfma_f32_16x16x32_bf16 v[76:79], v[128:131], v[216:219], v[76:79]
	v_mfma_f32_16x16x32_bf16 v[72:75], v[154:157], v[216:219], v[72:75]
	v_mfma_f32_16x16x32_bf16 v[124:127], v[150:153], v[196:199], v[124:127]
	v_mfma_f32_16x16x32_bf16 v[120:123], v[158:161], v[196:199], v[120:123]
	v_mfma_f32_16x16x32_bf16 v[108:111], v[150:153], v[204:207], v[108:111]
	v_mfma_f32_16x16x32_bf16 v[104:107], v[158:161], v[204:207], v[104:107]
	v_mfma_f32_16x16x32_bf16 v[92:95], v[150:153], v[212:215], v[92:95]
	v_mfma_f32_16x16x32_bf16 v[88:91], v[158:161], v[212:215], v[88:91]
	v_mfma_f32_16x16x32_bf16 v[76:79], v[150:153], v[220:223], v[76:79]
	v_mfma_f32_16x16x32_bf16 v[72:75], v[158:161], v[220:223], v[72:75]
	s_setprio 0
	s_setprio 1
	v_mfma_f32_16x16x32_bf16 v[116:119], v[162:165], v[192:195], v[116:119]
	v_mfma_f32_16x16x32_bf16 v[112:115], v[170:173], v[192:195], v[112:115]
	v_mfma_f32_16x16x32_bf16 v[100:103], v[162:165], v[200:203], v[100:103]
	v_mfma_f32_16x16x32_bf16 v[96:99], v[170:173], v[200:203], v[96:99]
	v_mfma_f32_16x16x32_bf16 v[84:87], v[162:165], v[208:211], v[84:87]
	v_mfma_f32_16x16x32_bf16 v[80:83], v[170:173], v[208:211], v[80:83]
	v_mfma_f32_16x16x32_bf16 v[68:71], v[162:165], v[216:219], v[68:71]
	v_mfma_f32_16x16x32_bf16 v[64:67], v[170:173], v[216:219], v[64:67]
	v_mfma_f32_16x16x32_bf16 v[116:119], v[166:169], v[196:199], v[116:119]
	v_mfma_f32_16x16x32_bf16 v[112:115], v[188:191], v[196:199], v[112:115]
	v_mfma_f32_16x16x32_bf16 v[100:103], v[166:169], v[204:207], v[100:103]
	v_mfma_f32_16x16x32_bf16 v[96:99], v[188:191], v[204:207], v[96:99]
	v_mfma_f32_16x16x32_bf16 v[84:87], v[166:169], v[212:215], v[84:87]
	v_mfma_f32_16x16x32_bf16 v[80:83], v[188:191], v[212:215], v[80:83]
	v_mfma_f32_16x16x32_bf16 v[68:71], v[166:169], v[220:223], v[68:71]
	v_mfma_f32_16x16x32_bf16 v[64:67], v[188:191], v[220:223], v[64:67]
	s_setprio 0
	s_barrier
	s_add_i32 s40, s76, s45
	s_mov_b32 m0, s40
	ds_read_b128 v[192:195], v185 offset:49152
	ds_read_b128 v[196:199], v185 offset:50176
	ds_read_b128 v[200:203], v185 offset:51200
	ds_read_b128 v[204:207], v185 offset:52224
	ds_read_b128 v[208:211], v185 offset:53248
	ds_read_b128 v[212:215], v185 offset:54272
	ds_read_b128 v[216:219], v185 offset:55296
	ds_read_b128 v[220:223], v185 offset:56320
	global_load_lds_dwordx4 v134, s[98:99]
	s_add_i32 m0, s40, 0x2000
	s_add_u32 s36, s36, 0x40080
	s_addc_u32 s37, s37, 0
	s_add_i32 s40, s77, s45
	global_load_lds_dwordx4 v138, s[98:99]
	s_mov_b32 m0, s40
	s_nop 0
	global_load_lds_dwordx4 v134, s[36:37]
	s_add_i32 m0, s40, 0x2000
	s_nop 0
	global_load_lds_dwordx4 v138, s[36:37]
	s_mov_b32 m0, s64
	s_nop 0
	global_load_lds_dwordx4 v132, s[100:101]
	s_mov_b32 m0, s65
	s_nop 0
	global_load_lds_dwordx4 v136, s[100:101]
	s_waitcnt vmcnt(8) lgkmcnt(0)
	s_barrier
	s_setprio 1
	v_mfma_f32_16x16x32_bf16 v[60:63], v[128:131], v[192:195], v[60:63]
	v_mfma_f32_16x16x32_bf16 v[56:59], v[154:157], v[192:195], v[56:59]
	v_mfma_f32_16x16x32_bf16 v[44:47], v[128:131], v[200:203], v[44:47]
	v_mfma_f32_16x16x32_bf16 v[40:43], v[154:157], v[200:203], v[40:43]
	v_mfma_f32_16x16x32_bf16 v[28:31], v[128:131], v[208:211], v[28:31]
	v_mfma_f32_16x16x32_bf16 v[24:27], v[154:157], v[208:211], v[24:27]
	v_mfma_f32_16x16x32_bf16 v[12:15], v[128:131], v[216:219], v[12:15]
	v_mfma_f32_16x16x32_bf16 v[8:11], v[154:157], v[216:219], v[8:11]
	v_mfma_f32_16x16x32_bf16 v[60:63], v[150:153], v[196:199], v[60:63]
	v_mfma_f32_16x16x32_bf16 v[56:59], v[158:161], v[196:199], v[56:59]
	v_mfma_f32_16x16x32_bf16 v[44:47], v[150:153], v[204:207], v[44:47]
	v_mfma_f32_16x16x32_bf16 v[40:43], v[158:161], v[204:207], v[40:43]
	v_mfma_f32_16x16x32_bf16 v[28:31], v[150:153], v[212:215], v[28:31]
	v_mfma_f32_16x16x32_bf16 v[24:27], v[158:161], v[212:215], v[24:27]
	v_mfma_f32_16x16x32_bf16 v[12:15], v[150:153], v[220:223], v[12:15]
	v_mfma_f32_16x16x32_bf16 v[8:11], v[158:161], v[220:223], v[8:11]
	s_setprio 0
	s_setprio 1
	v_mfma_f32_16x16x32_bf16 v[52:55], v[162:165], v[192:195], v[52:55]
	v_mfma_f32_16x16x32_bf16 v[48:51], v[170:173], v[192:195], v[48:51]
	v_mfma_f32_16x16x32_bf16 v[36:39], v[162:165], v[200:203], v[36:39]
	v_mfma_f32_16x16x32_bf16 v[32:35], v[170:173], v[200:203], v[32:35]
	v_mfma_f32_16x16x32_bf16 v[20:23], v[162:165], v[208:211], v[20:23]
	v_mfma_f32_16x16x32_bf16 v[16:19], v[170:173], v[208:211], v[16:19]
	v_mfma_f32_16x16x32_bf16 v[4:7], v[162:165], v[216:219], v[4:7]
	v_mfma_f32_16x16x32_bf16 v[0:3], v[170:173], v[216:219], v[0:3]
	v_mfma_f32_16x16x32_bf16 v[52:55], v[166:169], v[196:199], v[52:55]
	v_mfma_f32_16x16x32_bf16 v[48:51], v[188:191], v[196:199], v[48:51]
	v_mfma_f32_16x16x32_bf16 v[36:39], v[166:169], v[204:207], v[36:39]
	v_mfma_f32_16x16x32_bf16 v[32:35], v[188:191], v[204:207], v[32:35]
	v_mfma_f32_16x16x32_bf16 v[20:23], v[166:169], v[212:215], v[20:23]
	v_mfma_f32_16x16x32_bf16 v[16:19], v[188:191], v[212:215], v[16:19]
	v_mfma_f32_16x16x32_bf16 v[4:7], v[166:169], v[220:223], v[4:7]
	v_mfma_f32_16x16x32_bf16 v[0:3], v[188:191], v[220:223], v[0:3]
	s_setprio 0
	s_barrier
	s_add_i32 s75, s75, 2
	s_add_u32 s8, s8, 0x100
	s_addc_u32 s9, s9, 0
	s_add_u32 s73, s73, 0x100
	s_addc_u32 s74, s74, 0
	s_cmp_gt_u32 s75, 13
	s_cbranch_scc0 .LBB0_349
	s_and_b64 vcc, exec, s[20:21]
	s_cbranch_vccz .LBB0_352
	s_barrier

; #define PG8_STAGE(bufoff, gbase, voff) do { _Pragma("unroll") for (int _i = 0; _i < 2; ++_i) \
;         __builtin_amdgcn_global_load_lds((const unsigned*)((const char*)(gbase) + (voff)[_i]), (PG8_LAS unsigned*)(lds + (bufoff) + ldsw + _i * 8192), 16, 0, 0); } while (0)
; #define PG8_LDA(dst, b, h) do { _Pragma("unroll") for (int m = 0; m < 4; ++m) _Pragma("unroll") for (int k = 0; k < 2; ++k) dst[m][k] = *(const PG8_LAS bf16x8*)(lds + PG8_SA(b, h) + aoff + m * 2048 + k * 1024); } while (0)
; #define PG8_LDB(dst, b, h) do { _Pragma("unroll") for (int n = 0; n < 2; ++n) _Pragma("unroll") for (int k = 0; k < 2; ++k) dst[n][k] = *(const PG8_LAS bf16x8*)(lds + PG8_SB(b, h) + boff + n * 2048 + k * 1024); } while (0)
; #define PG8_WAIT_V(n) asm volatile("s_waitcnt vmcnt(" #n ")" ::: "memory")
; #define PG8_WAIT_L(n) asm volatile("s_waitcnt lgkmcnt(" #n ")" ::: "memory")
; #define PG8_BAR __builtin_amdgcn_s_barrier()
; #define PG8_SCHED __builtin_amdgcn_sched_barrier(0)
; template <class Epi, class Sched, bool ALIGN_EPI = false, bool SP2 = false>
; __device__ __forceinline__ void gemm_phase(PG8_LAS unsigned char* lds, const Gemm g, const Sched& S, const Epi& E, const int wid) {
;     ...
;         const bool has_next = S.next(ui + 1, nxt);
;         const char* nA = has_next ? (const char*)g.A + (size_t)nxt.pm * tstepA : cA; const char* nB = has_next ? (const char*)g.Bt + (size_t)nxt.pn * tstepB : cB;
;         for (int t = 0; t < nt; t += 2) {
;             const bool last = (t == nt - 2);
;             const char* a1 = cA + (size_t)(t + 1) * kstep;
;             const char* a2 = last ? nA : cA + (size_t)(t + 2) * kstep; const char* b2 = last ? nB : cB + (size_t)(t + 2) * kstep;
;             const char* a3 = a2 + kstep; const char* b3 = b2 + kstep;
;             if (last && has_next) S.a_ready(nxt);
;             if constexpr (SP2) {
;             PG8_LDB(B0, 0, 0); PG8_LDB(B1, 0, 1); PG8_SCHED; PG8_LDA(At, 0, 0); PG8_STAGE(PG8_SA(1, 1), a1 + hstepA, voffA);
;             PG8_WAIT_V(8); PG8_WAIT_L(0); PG8_BAR; PG8_MMA(0, 0, At, B0); PG8_MMA(0, 1, At, B1); PG8_BAR; PG8_SCHED;
;             PG8_LDA(At, 0, 1); PG8_STAGE(PG8_SB(0, 0), b2, voffB); PG8_STAGE(PG8_SB(0, 1), b2 + hstepB, voffB); PG8_STAGE(PG8_SA(0, 0), a2, voffA);
;             PG8_WAIT_V(8); PG8_WAIT_L(0); PG8_BAR; PG8_MMA(1, 0, At, B0); PG8_MMA(1, 1, At, B1); PG8_BAR; PG8_SCHED;
.LBB0_1779:
	s_ashr_i32 s21, s20, 31
	s_lshl_b64 s[22:23], s[20:21], 19
	s_add_u32 s22, s0, s22
	s_addc_u32 s23, s1, s23
	s_and_b64 s[24:25], s[4:5], exec
	s_cselect_b32 s21, s23, s31
	s_cselect_b32 s27, s22, s30
	s_ashr_i32 s19, s18, 31
	s_lshl_b64 s[24:25], s[18:19], 19
	s_add_u32 s24, s33, s24
	s_addc_u32 s25, s38, s25
	s_and_b64 s[36:37], s[4:5], exec
	s_cselect_b32 s19, s25, s35
	s_cselect_b32 s29, s24, s34
	s_add_u32 s30, s30, 0x40080
	s_addc_u32 s31, s31, 0
	s_add_u32 s68, s34, 0x100
	s_addc_u32 s69, s35, 0
	s_mov_b32 s70, -2
	s_waitcnt lgkmcnt(0)
	v_add_u32_e32 v252, 0x18000, v189
	v_add_u32_e32 v253, 0x1c000, v189
	ds_read_b128 v[128:131], v190
	ds_read_b128 v[132:135], v190 offset:1024
	ds_read_b128 v[136:139], v190 offset:2048
	ds_read_b128 v[140:143], v190 offset:3072
	ds_read_b128 v[144:147], v191
	ds_read_b128 v[148:151], v191 offset:1024
	ds_read_b128 v[172:175], v191 offset:2048
	ds_read_b128 v[176:179], v191 offset:3072
	s_add_u32 s34, s30, 0xfffc0080
	s_addc_u32 s35, s31, -1
	s_cmp_eq_u32 s70, 12
	s_cselect_b32 s37, s21, s35
	s_cselect_b32 s36, s27, s34
	s_cselect_b32 s35, s19, s69
	s_cselect_b32 s34, s29, s68
	s_add_i32 m0, s40, 0xc000
	ds_read_b128 v[180:183], v192
	ds_read_b128 v[184:187], v192 offset:1024
	ds_read_b128 v[194:197], v192 offset:2048
	ds_read_b128 v[198:201], v192 offset:3072
	ds_read_b128 v[202:205], v192 offset:4096
	ds_read_b128 v[206:209], v192 offset:5120
	ds_read_b128 v[210:213], v192 offset:6144
	ds_read_b128 v[214:217], v192 offset:7168
	global_load_lds_dwordx4 v164, s[30:31]
	s_add_i32 m0, s40, 0xe000
	s_nop 0
	global_load_lds_dwordx4 v166, s[30:31]
	s_waitcnt vmcnt(8) lgkmcnt(0)
	s_barrier
	s_setprio 1
	v_mfma_f32_16x16x32_bf16 v[124:127], v[128:131], v[180:183], 0
	v_mfma_f32_16x16x32_bf16 v[120:123], v[136:139], v[180:183], 0
	v_mfma_f32_16x16x32_bf16 v[108:111], v[128:131], v[194:197], 0
	v_mfma_f32_16x16x32_bf16 v[104:107], v[136:139], v[194:197], 0
	v_mfma_f32_16x16x32_bf16 v[92:95], v[128:131], v[202:205], 0
	v_mfma_f32_16x16x32_bf16 v[88:91], v[136:139], v[202:205], 0
	v_mfma_f32_16x16x32_bf16 v[76:79], v[128:131], v[210:213], 0
	v_mfma_f32_16x16x32_bf16 v[72:75], v[136:139], v[210:213], 0
	v_mfma_f32_16x16x32_bf16 v[124:127], v[132:135], v[184:187], v[124:127]
	v_mfma_f32_16x16x32_bf16 v[120:123], v[140:143], v[184:187], v[120:123]
	v_mfma_f32_16x16x32_bf16 v[108:111], v[132:135], v[198:201], v[108:111]
	v_mfma_f32_16x16x32_bf16 v[104:107], v[140:143], v[198:201], v[104:107]
	v_mfma_f32_16x16x32_bf16 v[92:95], v[132:135], v[206:209], v[92:95]
	v_mfma_f32_16x16x32_bf16 v[88:91], v[140:143], v[206:209], v[88:91]
	v_mfma_f32_16x16x32_bf16 v[76:79], v[132:135], v[214:217], v[76:79]
	v_mfma_f32_16x16x32_bf16 v[72:75], v[140:143], v[214:217], v[72:75]
	s_setprio 0
	s_setprio 1
	v_mfma_f32_16x16x32_bf16 v[116:119], v[144:147], v[180:183], 0
	v_mfma_f32_16x16x32_bf16 v[112:115], v[172:175], v[180:183], 0
	v_mfma_f32_16x16x32_bf16 v[100:103], v[144:147], v[194:197], 0
	v_mfma_f32_16x16x32_bf16 v[96:99], v[172:175], v[194:197], 0
	v_mfma_f32_16x16x32_bf16 v[84:87], v[144:147], v[202:205], 0
	v_mfma_f32_16x16x32_bf16 v[80:83], v[172:175], v[202:205], 0
	v_mfma_f32_16x16x32_bf16 v[68:71], v[144:147], v[210:213], 0
	v_mfma_f32_16x16x32_bf16 v[64:67], v[172:175], v[210:213], 0
	v_mfma_f32_16x16x32_bf16 v[116:119], v[148:151], v[184:187], v[116:119]
	v_mfma_f32_16x16x32_bf16 v[112:115], v[176:179], v[184:187], v[112:115]
	v_mfma_f32_16x16x32_bf16 v[100:103], v[148:151], v[198:201], v[100:103]
	v_mfma_f32_16x16x32_bf16 v[96:99], v[176:179], v[198:201], v[96:99]
	v_mfma_f32_16x16x32_bf16 v[84:87], v[148:151], v[206:209], v[84:87]
	v_mfma_f32_16x16x32_bf16 v[80:83], v[176:179], v[206:209], v[80:83]
	v_mfma_f32_16x16x32_bf16 v[68:71], v[148:151], v[214:217], v[68:71]
	v_mfma_f32_16x16x32_bf16 v[64:67], v[176:179], v[214:217], v[64:67]
	s_setprio 0
	s_barrier
	s_add_i32 s71, s65, s39
	s_add_u32 s98, s34, 0x80
	s_addc_u32 s99, s35, 0
	s_mov_b32 m0, s71
	ds_read_b128 v[180:183], v192 offset:16384
	ds_read_b128 v[184:187], v192 offset:17408
	ds_read_b128 v[194:197], v192 offset:18432
	ds_read_b128 v[198:201], v192 offset:19456
	ds_read_b128 v[202:205], v192 offset:20480
	ds_read_b128 v[206:209], v192 offset:21504
	ds_read_b128 v[210:213], v192 offset:22528
	ds_read_b128 v[214:217], v192 offset:23552
	global_load_lds_dwordx4 v154, s[34:35]
	s_add_i32 m0, s71, 0x2000
	s_add_u32 s72, s34, 0x40000
	s_addc_u32 s73, s35, 0
	s_add_i32 s71, s66, s39
	global_load_lds_dwordx4 v158, s[34:35]
	s_mov_b32 m0, s71
	s_add_u32 s100, s36, 0x80
	s_addc_u32 s101, s37, 0
	global_load_lds_dwordx4 v154, s[72:73]
	s_add_i32 m0, s71, 0x2000
	s_nop 0
	global_load_lds_dwordx4 v158, s[72:73]
	s_mov_b32 m0, s40
	s_nop 0
	global_load_lds_dwordx4 v152, s[36:37]
	s_mov_b32 m0, s41
	s_nop 0
	global_load_lds_dwordx4 v156, s[36:37]
	s_waitcnt vmcnt(8) lgkmcnt(0)
	s_barrier
; #define PG8_STAGE(bufoff, gbase, voff) do { _Pragma("unroll") for (int _i = 0; _i < 2; ++_i) \
;         __builtin_amdgcn_global_load_lds((const unsigned*)((const char*)(gbase) + (voff)[_i]), (PG8_LAS unsigned*)(lds + (bufoff) + ldsw + _i * 8192), 16, 0, 0); } while (0)
; #define PG8_LDA(dst, b, h) do { _Pragma("unroll") for (int m = 0; m < 4; ++m) _Pragma("unroll") for (int k = 0; k < 2; ++k) dst[m][k] = *(const PG8_LAS bf16x8*)(lds + PG8_SA(b, h) + aoff + m * 2048 + k * 1024); } while (0)
; #define PG8_LDB(dst, b, h) do { _Pragma("unroll") for (int n = 0; n < 2; ++n) _Pragma("unroll") for (int k = 0; k < 2; ++k) dst[n][k] = *(const PG8_LAS bf16x8*)(lds + PG8_SB(b, h) + boff + n * 2048 + k * 1024); } while (0)
; #define PG8_MMA(ai, bj, At, Bt) do { __builtin_amdgcn_s_setprio(1); _Pragma("unroll") for (int m = 0; m < 4; ++m) _Pragma("unroll") for (int n = 0; n < 2; ++n) _Pragma("unroll") for (int k = 0; k < 2; ++k) \
;         acc[ai][bj][m][n] = __builtin_amdgcn_mfma_f32_16x16x32_bf16(Bt[n][k], At[m][k], acc[ai][bj][m][n], 0, 0, 0); __builtin_amdgcn_s_setprio(0); } while (0)
; #define PG8_WAIT_V(n) asm volatile("s_waitcnt vmcnt(" #n ")" ::: "memory")
; #define PG8_WAIT_L(n) asm volatile("s_waitcnt lgkmcnt(" #n ")" ::: "memory")
; #define PG8_BAR __builtin_amdgcn_s_barrier()
; #define PG8_SCHED __builtin_amdgcn_sched_barrier(0)
; template <class Epi, class Sched, bool ALIGN_EPI = false, bool SP2 = false>
; __device__ __forceinline__ void gemm_phase(PG8_LAS unsigned char* lds, const Gemm g, const Sched& S, const Epi& E, const int wid) {
;     ...
;             PG8_WAIT_V(8); PG8_WAIT_L(0); PG8_BAR; PG8_MMA(0, 0, At, B0); PG8_MMA(0, 1, At, B1); PG8_BAR; PG8_SCHED;
;             PG8_LDA(At, 0, 1); PG8_STAGE(PG8_SB(0, 0), b2, voffB); PG8_STAGE(PG8_SB(0, 1), b2 + hstepB, voffB); PG8_STAGE(PG8_SA(0, 0), a2, voffA);
;             PG8_WAIT_V(8); PG8_WAIT_L(0); PG8_BAR; PG8_MMA(1, 0, At, B0); PG8_MMA(1, 1, At, B1); PG8_BAR; PG8_SCHED;
;             PG8_LDB(B0, 1, 0); PG8_LDB(B1, 1, 1); PG8_SCHED; PG8_LDA(At, 1, 0); PG8_STAGE(PG8_SA(0, 1), a2 + hstepA, voffA);
;             PG8_WAIT_V(8); PG8_WAIT_L(0); PG8_BAR; PG8_MMA(0, 0, At, B0); PG8_MMA(0, 1, At, B1); PG8_BAR; PG8_SCHED;
	s_nop 0
	s_setprio 1
	v_mfma_f32_16x16x32_bf16 v[60:63], v[128:131], v[180:183], 0
	v_mfma_f32_16x16x32_bf16 v[56:59], v[136:139], v[180:183], 0
	v_mfma_f32_16x16x32_bf16 v[44:47], v[128:131], v[194:197], 0
	v_mfma_f32_16x16x32_bf16 v[40:43], v[136:139], v[194:197], 0
	v_mfma_f32_16x16x32_bf16 v[28:31], v[128:131], v[202:205], 0
	v_mfma_f32_16x16x32_bf16 v[24:27], v[136:139], v[202:205], 0
	v_mfma_f32_16x16x32_bf16 v[12:15], v[128:131], v[210:213], 0
	v_mfma_f32_16x16x32_bf16 v[8:11], v[136:139], v[210:213], 0
	v_mfma_f32_16x16x32_bf16 v[60:63], v[132:135], v[184:187], v[60:63]
	v_mfma_f32_16x16x32_bf16 v[56:59], v[140:143], v[184:187], v[56:59]
	v_mfma_f32_16x16x32_bf16 v[44:47], v[132:135], v[198:201], v[44:47]
	v_mfma_f32_16x16x32_bf16 v[40:43], v[140:143], v[198:201], v[40:43]
	v_mfma_f32_16x16x32_bf16 v[28:31], v[132:135], v[206:209], v[28:31]
	v_mfma_f32_16x16x32_bf16 v[24:27], v[140:143], v[206:209], v[24:27]
	v_mfma_f32_16x16x32_bf16 v[12:15], v[132:135], v[214:217], v[12:15]
	v_mfma_f32_16x16x32_bf16 v[8:11], v[140:143], v[214:217], v[8:11]
	s_setprio 0
	s_setprio 1
	v_mfma_f32_16x16x32_bf16 v[52:55], v[144:147], v[180:183], 0
	v_mfma_f32_16x16x32_bf16 v[48:51], v[172:175], v[180:183], 0
	v_mfma_f32_16x16x32_bf16 v[36:39], v[144:147], v[194:197], 0
	v_mfma_f32_16x16x32_bf16 v[32:35], v[172:175], v[194:197], 0
	v_mfma_f32_16x16x32_bf16 v[20:23], v[144:147], v[202:205], 0
	v_mfma_f32_16x16x32_bf16 v[16:19], v[172:175], v[202:205], 0
	v_mfma_f32_16x16x32_bf16 v[4:7], v[144:147], v[210:213], 0
	v_mfma_f32_16x16x32_bf16 v[0:3], v[172:175], v[210:213], 0
	v_mfma_f32_16x16x32_bf16 v[52:55], v[148:151], v[184:187], v[52:55]
	v_mfma_f32_16x16x32_bf16 v[48:51], v[176:179], v[184:187], v[48:51]
	v_mfma_f32_16x16x32_bf16 v[36:39], v[148:151], v[198:201], v[36:39]
	v_mfma_f32_16x16x32_bf16 v[32:35], v[176:179], v[198:201], v[32:35]
	v_mfma_f32_16x16x32_bf16 v[20:23], v[148:151], v[206:209], v[20:23]
	v_mfma_f32_16x16x32_bf16 v[16:19], v[176:179], v[206:209], v[16:19]
	v_mfma_f32_16x16x32_bf16 v[4:7], v[148:151], v[214:217], v[4:7]
	v_mfma_f32_16x16x32_bf16 v[0:3], v[176:179], v[214:217], v[0:3]
	s_setprio 0
	s_barrier
	s_add_i32 s71, 0, 0x18000
	s_add_i32 s72, 0, 0x1c000
	ds_read_b128 v[128:131], v252
	ds_read_b128 v[132:135], v252 offset:1024
	ds_read_b128 v[136:139], v252 offset:2048
	ds_read_b128 v[140:143], v252 offset:3072
	ds_read_b128 v[144:147], v253
	ds_read_b128 v[148:151], v253 offset:1024
	ds_read_b128 v[172:175], v253 offset:2048
	ds_read_b128 v[176:179], v253 offset:3072
	s_add_u32 s36, s36, 0x40000
	s_addc_u32 s37, s37, 0
	s_mov_b32 m0, s44
	ds_read_b128 v[180:183], v192 offset:32768
	ds_read_b128 v[184:187], v192 offset:33792
	ds_read_b128 v[194:197], v192 offset:34816
	ds_read_b128 v[198:201], v192 offset:35840
	ds_read_b128 v[202:205], v192 offset:36864
	ds_read_b128 v[206:209], v192 offset:37888
	ds_read_b128 v[210:213], v192 offset:38912
	ds_read_b128 v[214:217], v192 offset:39936
	global_load_lds_dwordx4 v152, s[36:37]
	s_mov_b32 m0, s45
	s_nop 0
	global_load_lds_dwordx4 v156, s[36:37]
	s_waitcnt vmcnt(8) lgkmcnt(0)
	s_barrier
	s_nop 0
	s_setprio 1
	v_mfma_f32_16x16x32_bf16 v[124:127], v[128:131], v[180:183], v[124:127]
	v_mfma_f32_16x16x32_bf16 v[120:123], v[136:139], v[180:183], v[120:123]
	v_mfma_f32_16x16x32_bf16 v[108:111], v[128:131], v[194:197], v[108:111]
	v_mfma_f32_16x16x32_bf16 v[104:107], v[136:139], v[194:197], v[104:107]
	v_mfma_f32_16x16x32_bf16 v[92:95], v[128:131], v[202:205], v[92:95]
	v_mfma_f32_16x16x32_bf16 v[88:91], v[136:139], v[202:205], v[88:91]
	v_mfma_f32_16x16x32_bf16 v[76:79], v[128:131], v[210:213], v[76:79]
	v_mfma_f32_16x16x32_bf16 v[72:75], v[136:139], v[210:213], v[72:75]
	v_mfma_f32_16x16x32_bf16 v[124:127], v[132:135], v[184:187], v[124:127]
	v_mfma_f32_16x16x32_bf16 v[120:123], v[140:143], v[184:187], v[120:123]
	v_mfma_f32_16x16x32_bf16 v[108:111], v[132:135], v[198:201], v[108:111]
	v_mfma_f32_16x16x32_bf16 v[104:107], v[140:143], v[198:201], v[104:107]
	v_mfma_f32_16x16x32_bf16 v[92:95], v[132:135], v[206:209], v[92:95]
	v_mfma_f32_16x16x32_bf16 v[88:91], v[140:143], v[206:209], v[88:91]
	v_mfma_f32_16x16x32_bf16 v[76:79], v[132:135], v[214:217], v[76:79]
	v_mfma_f32_16x16x32_bf16 v[72:75], v[140:143], v[214:217], v[72:75]
	s_setprio 0
	s_setprio 1
	v_mfma_f32_16x16x32_bf16 v[116:119], v[144:147], v[180:183], v[116:119]
	v_mfma_f32_16x16x32_bf16 v[112:115], v[172:175], v[180:183], v[112:115]
	v_mfma_f32_16x16x32_bf16 v[100:103], v[144:147], v[194:197], v[100:103]
	v_mfma_f32_16x16x32_bf16 v[96:99], v[172:175], v[194:197], v[96:99]
	v_mfma_f32_16x16x32_bf16 v[84:87], v[144:147], v[202:205], v[84:87]
	v_mfma_f32_16x16x32_bf16 v[80:83], v[172:175], v[202:205], v[80:83]
	v_mfma_f32_16x16x32_bf16 v[68:71], v[144:147], v[210:213], v[68:71]
	v_mfma_f32_16x16x32_bf16 v[64:67], v[172:175], v[210:213], v[64:67]
	v_mfma_f32_16x16x32_bf16 v[116:119], v[148:151], v[184:187], v[116:119]
	v_mfma_f32_16x16x32_bf16 v[112:115], v[176:179], v[184:187], v[112:115]
	v_mfma_f32_16x16x32_bf16 v[100:103], v[148:151], v[198:201], v[100:103]
	v_mfma_f32_16x16x32_bf16 v[96:99], v[176:179], v[198:201], v[96:99]
	v_mfma_f32_16x16x32_bf16 v[84:87], v[148:151], v[206:209], v[84:87]
	v_mfma_f32_16x16x32_bf16 v[80:83], v[176:179], v[206:209], v[80:83]
	v_mfma_f32_16x16x32_bf16 v[68:71], v[148:151], v[214:217], v[68:71]
	v_mfma_f32_16x16x32_bf16 v[64:67], v[176:179], v[214:217], v[64:67]
	s_setprio 0
	s_barrier
; #define PG8_STAGE(bufoff, gbase, voff) do { _Pragma("unroll") for (int _i = 0; _i < 2; ++_i) \
;         __builtin_amdgcn_global_load_lds((const unsigned*)((const char*)(gbase) + (voff)[_i]), (PG8_LAS unsigned*)(lds + (bufoff) + ldsw + _i * 8192), 16, 0, 0); } while (0)
; #define PG8_LDA(dst, b, h) do { _Pragma("unroll") for (int m = 0; m < 4; ++m) _Pragma("unroll") for (int k = 0; k < 2; ++k) dst[m][k] = *(const PG8_LAS bf16x8*)(lds + PG8_SA(b, h) + aoff + m * 2048 + k * 1024); } while (0)
; #define PG8_WAIT_V(n) asm volatile("s_waitcnt vmcnt(" #n ")" ::: "memory")
; #define PG8_WAIT_L(n) asm volatile("s_waitcnt lgkmcnt(" #n ")" ::: "memory")
; #define PG8_BAR __builtin_amdgcn_s_barrier()
; template <class Epi, class Sched, bool ALIGN_EPI = false, bool SP2 = false>
; __device__ __forceinline__ void gemm_phase(PG8_LAS unsigned char* lds, const Gemm g, const Sched& S, const Epi& E, const int wid) {
;     ...
;         for (int t = 0; t < nt; t += 2) {
;             const bool last = (t == nt - 2);
;             const char* a1 = cA + (size_t)(t + 1) * kstep;
;             const char* a2 = last ? nA : cA + (size_t)(t + 2) * kstep; const char* b2 = last ? nB : cB + (size_t)(t + 2) * kstep;
;             const char* a3 = a2 + kstep; const char* b3 = b2 + kstep;
;             if (last && has_next) S.a_ready(nxt);
;             if constexpr (SP2) {
;             PG8_LDB(B0, 0, 0); PG8_LDB(B1, 0, 1); PG8_SCHED; PG8_LDA(At, 0, 0); PG8_STAGE(PG8_SA(1, 1), a1 + hstepA, voffA);
;             PG8_WAIT_V(8); PG8_WAIT_L(0); PG8_BAR; PG8_MMA(0, 0, At, B0); PG8_MMA(0, 1, At, B1); PG8_BAR; PG8_SCHED;
;             PG8_LDA(At, 0, 1); PG8_STAGE(PG8_SB(0, 0), b2, voffB); PG8_STAGE(PG8_SB(0, 1), b2 + hstepB, voffB); PG8_STAGE(PG8_SA(0, 0), a2, voffA);
;             PG8_WAIT_V(8); PG8_WAIT_L(0); PG8_BAR; PG8_MMA(1, 0, At, B0); PG8_MMA(1, 1, At, B1); PG8_BAR; PG8_SCHED;
;             PG8_LDB(B0, 1, 0); PG8_LDB(B1, 1, 1); PG8_SCHED; PG8_LDA(At, 1, 0); PG8_STAGE(PG8_SA(0, 1), a2 + hstepA, voffA);
;             PG8_WAIT_V(8); PG8_WAIT_L(0); PG8_BAR; PG8_MMA(0, 0, At, B0); PG8_MMA(0, 1, At, B1); PG8_BAR; PG8_SCHED;
;             PG8_LDA(At, 1, 1); PG8_STAGE(PG8_SB(1, 0), b3, voffB); PG8_STAGE(PG8_SB(1, 1), b3 + hstepB, voffB); PG8_STAGE(PG8_SA(1, 0), a3, voffA);
;             PG8_WAIT_V(8); PG8_WAIT_L(0); PG8_BAR; PG8_MMA(1, 0, At, B0); PG8_MMA(1, 1, At, B1); PG8_BAR; PG8_SCHED;
	s_add_i32 s36, s71, s39
	s_mov_b32 m0, s36
	ds_read_b128 v[180:183], v192 offset:49152
	ds_read_b128 v[184:187], v192 offset:50176
	ds_read_b128 v[194:197], v192 offset:51200
	ds_read_b128 v[198:201], v192 offset:52224
	ds_read_b128 v[202:205], v192 offset:53248
	ds_read_b128 v[206:209], v192 offset:54272
	ds_read_b128 v[210:213], v192 offset:55296
	ds_read_b128 v[214:217], v192 offset:56320
	global_load_lds_dwordx4 v154, s[98:99]
	s_add_i32 m0, s36, 0x2000
	s_add_u32 s34, s34, 0x40080
	s_addc_u32 s35, s35, 0
	s_add_i32 s36, s72, s39
	global_load_lds_dwordx4 v158, s[98:99]
	s_mov_b32 m0, s36
	s_nop 0
	global_load_lds_dwordx4 v154, s[34:35]
	s_add_i32 m0, s36, 0x2000
	s_nop 0
	global_load_lds_dwordx4 v158, s[34:35]
	s_mov_b32 m0, s47
	s_nop 0
	global_load_lds_dwordx4 v152, s[100:101]
	s_mov_b32 m0, s48
	s_nop 0
	global_load_lds_dwordx4 v156, s[100:101]
	s_waitcnt vmcnt(8) lgkmcnt(0)
	s_barrier
	s_setprio 1
	v_mfma_f32_16x16x32_bf16 v[60:63], v[128:131], v[180:183], v[60:63]
	v_mfma_f32_16x16x32_bf16 v[56:59], v[136:139], v[180:183], v[56:59]
	v_mfma_f32_16x16x32_bf16 v[44:47], v[128:131], v[194:197], v[44:47]
	v_mfma_f32_16x16x32_bf16 v[40:43], v[136:139], v[194:197], v[40:43]
	v_mfma_f32_16x16x32_bf16 v[28:31], v[128:131], v[202:205], v[28:31]
	v_mfma_f32_16x16x32_bf16 v[24:27], v[136:139], v[202:205], v[24:27]
	v_mfma_f32_16x16x32_bf16 v[12:15], v[128:131], v[210:213], v[12:15]
	v_mfma_f32_16x16x32_bf16 v[8:11], v[136:139], v[210:213], v[8:11]
	v_mfma_f32_16x16x32_bf16 v[60:63], v[132:135], v[184:187], v[60:63]
	v_mfma_f32_16x16x32_bf16 v[56:59], v[140:143], v[184:187], v[56:59]
	v_mfma_f32_16x16x32_bf16 v[44:47], v[132:135], v[198:201], v[44:47]
	v_mfma_f32_16x16x32_bf16 v[40:43], v[140:143], v[198:201], v[40:43]
	v_mfma_f32_16x16x32_bf16 v[28:31], v[132:135], v[206:209], v[28:31]
	v_mfma_f32_16x16x32_bf16 v[24:27], v[140:143], v[206:209], v[24:27]
	v_mfma_f32_16x16x32_bf16 v[12:15], v[132:135], v[214:217], v[12:15]
	v_mfma_f32_16x16x32_bf16 v[8:11], v[140:143], v[214:217], v[8:11]
	s_setprio 0
	s_setprio 1
	v_mfma_f32_16x16x32_bf16 v[52:55], v[144:147], v[180:183], v[52:55]
	v_mfma_f32_16x16x32_bf16 v[48:51], v[172:175], v[180:183], v[48:51]
	v_mfma_f32_16x16x32_bf16 v[36:39], v[144:147], v[194:197], v[36:39]
	v_mfma_f32_16x16x32_bf16 v[32:35], v[172:175], v[194:197], v[32:35]
	v_mfma_f32_16x16x32_bf16 v[20:23], v[144:147], v[202:205], v[20:23]
	v_mfma_f32_16x16x32_bf16 v[16:19], v[172:175], v[202:205], v[16:19]
	v_mfma_f32_16x16x32_bf16 v[4:7], v[144:147], v[210:213], v[4:7]
	v_mfma_f32_16x16x32_bf16 v[0:3], v[172:175], v[210:213], v[0:3]
	v_mfma_f32_16x16x32_bf16 v[52:55], v[148:151], v[184:187], v[52:55]
	v_mfma_f32_16x16x32_bf16 v[48:51], v[176:179], v[184:187], v[48:51]
	v_mfma_f32_16x16x32_bf16 v[36:39], v[148:151], v[198:201], v[36:39]
	v_mfma_f32_16x16x32_bf16 v[32:35], v[176:179], v[198:201], v[32:35]
	v_mfma_f32_16x16x32_bf16 v[20:23], v[148:151], v[206:209], v[20:23]
	v_mfma_f32_16x16x32_bf16 v[16:19], v[176:179], v[206:209], v[16:19]
	v_mfma_f32_16x16x32_bf16 v[4:7], v[148:151], v[214:217], v[4:7]
	v_mfma_f32_16x16x32_bf16 v[0:3], v[176:179], v[214:217], v[0:3]
	s_setprio 0
	s_barrier
	s_add_i32 s70, s70, 2
	s_add_u32 s30, s30, 0x100
	s_addc_u32 s31, s31, 0
	s_add_u32 s68, s68, 0x100
	s_addc_u32 s69, s69, 0
	s_cmp_gt_u32 s70, 13
.LBB0_1780:
	ds_read_b128 v[128:131], v190
	ds_read_b128 v[132:135], v190 offset:1024
	ds_read_b128 v[136:139], v190 offset:2048
	ds_read_b128 v[140:143], v190 offset:3072
	ds_read_b128 v[144:147], v191
	ds_read_b128 v[148:151], v191 offset:1024
	ds_read_b128 v[172:175], v191 offset:2048
	ds_read_b128 v[176:179], v191 offset:3072
	s_add_u32 s34, s30, 0xfffc0080
	s_addc_u32 s35, s31, -1
	s_cmp_eq_u32 s70, 12
	s_cselect_b32 s37, s21, s35
	s_cselect_b32 s36, s27, s34
	s_cselect_b32 s35, s19, s69
	s_cselect_b32 s34, s29, s68
	s_add_i32 m0, s40, 0xc000
	ds_read_b128 v[180:183], v192
	ds_read_b128 v[184:187], v192 offset:1024
	ds_read_b128 v[194:197], v192 offset:2048
	ds_read_b128 v[198:201], v192 offset:3072
	ds_read_b128 v[202:205], v192 offset:4096
	ds_read_b128 v[206:209], v192 offset:5120
	ds_read_b128 v[210:213], v192 offset:6144
	ds_read_b128 v[214:217], v192 offset:7168
	global_load_lds_dwordx4 v164, s[30:31]
	s_add_i32 m0, s40, 0xe000
	s_nop 0
	global_load_lds_dwordx4 v166, s[30:31]
	s_waitcnt vmcnt(8) lgkmcnt(0)
	s_barrier
	s_setprio 1
	v_mfma_f32_16x16x32_bf16 v[124:127], v[128:131], v[180:183], v[124:127]
	v_mfma_f32_16x16x32_bf16 v[120:123], v[136:139], v[180:183], v[120:123]
	v_mfma_f32_16x16x32_bf16 v[108:111], v[128:131], v[194:197], v[108:111]
	v_mfma_f32_16x16x32_bf16 v[104:107], v[136:139], v[194:197], v[104:107]
	v_mfma_f32_16x16x32_bf16 v[92:95], v[128:131], v[202:205], v[92:95]
	v_mfma_f32_16x16x32_bf16 v[88:91], v[136:139], v[202:205], v[88:91]
	v_mfma_f32_16x16x32_bf16 v[76:79], v[128:131], v[210:213], v[76:79]
	v_mfma_f32_16x16x32_bf16 v[72:75], v[136:139], v[210:213], v[72:75]
	v_mfma_f32_16x16x32_bf16 v[124:127], v[132:135], v[184:187], v[124:127]
	v_mfma_f32_16x16x32_bf16 v[120:123], v[140:143], v[184:187], v[120:123]
	v_mfma_f32_16x16x32_bf16 v[108:111], v[132:135], v[198:201], v[108:111]
	v_mfma_f32_16x16x32_bf16 v[104:107], v[140:143], v[198:201], v[104:107]
	v_mfma_f32_16x16x32_bf16 v[92:95], v[132:135], v[206:209], v[92:95]
	v_mfma_f32_16x16x32_bf16 v[88:91], v[140:143], v[206:209], v[88:91]
	v_mfma_f32_16x16x32_bf16 v[76:79], v[132:135], v[214:217], v[76:79]
	v_mfma_f32_16x16x32_bf16 v[72:75], v[140:143], v[214:217], v[72:75]
	s_setprio 0
	s_setprio 1
	v_mfma_f32_16x16x32_bf16 v[116:119], v[144:147], v[180:183], v[116:119]
	v_mfma_f32_16x16x32_bf16 v[112:115], v[172:175], v[180:183], v[112:115]
	v_mfma_f32_16x16x32_bf16 v[100:103], v[144:147], v[194:197], v[100:103]
	v_mfma_f32_16x16x32_bf16 v[96:99], v[172:175], v[194:197], v[96:99]
	v_mfma_f32_16x16x32_bf16 v[84:87], v[144:147], v[202:205], v[84:87]
	v_mfma_f32_16x16x32_bf16 v[80:83], v[172:175], v[202:205], v[80:83]
	v_mfma_f32_16x16x32_bf16 v[68:71], v[144:147], v[210:213], v[68:71]
	v_mfma_f32_16x16x32_bf16 v[64:67], v[172:175], v[210:213], v[64:67]
	v_mfma_f32_16x16x32_bf16 v[116:119], v[148:151], v[184:187], v[116:119]
	v_mfma_f32_16x16x32_bf16 v[112:115], v[176:179], v[184:187], v[112:115]
	v_mfma_f32_16x16x32_bf16 v[100:103], v[148:151], v[198:201], v[100:103]
	v_mfma_f32_16x16x32_bf16 v[96:99], v[176:179], v[198:201], v[96:99]
	v_mfma_f32_16x16x32_bf16 v[84:87], v[148:151], v[206:209], v[84:87]
	v_mfma_f32_16x16x32_bf16 v[80:83], v[176:179], v[206:209], v[80:83]
	v_mfma_f32_16x16x32_bf16 v[68:71], v[148:151], v[214:217], v[68:71]
	v_mfma_f32_16x16x32_bf16 v[64:67], v[176:179], v[214:217], v[64:67]
	s_setprio 0
	s_barrier
; #define PG8_STAGE(bufoff, gbase, voff) do { _Pragma("unroll") for (int _i = 0; _i < 2; ++_i) \
;         __builtin_amdgcn_global_load_lds((const unsigned*)((const char*)(gbase) + (voff)[_i]), (PG8_LAS unsigned*)(lds + (bufoff) + ldsw + _i * 8192), 16, 0, 0); } while (0)
; #define PG8_LDA(dst, b, h) do { _Pragma("unroll") for (int m = 0; m < 4; ++m) _Pragma("unroll") for (int k = 0; k < 2; ++k) dst[m][k] = *(const PG8_LAS bf16x8*)(lds + PG8_SA(b, h) + aoff + m * 2048 + k * 1024); } while (0)
; #define PG8_LDB(dst, b, h) do { _Pragma("unroll") for (int n = 0; n < 2; ++n) _Pragma("unroll") for (int k = 0; k < 2; ++k) dst[n][k] = *(const PG8_LAS bf16x8*)(lds + PG8_SB(b, h) + boff + n * 2048 + k * 1024); } while (0)
; #define PG8_MMA(ai, bj, At, Bt) do { __builtin_amdgcn_s_setprio(1); _Pragma("unroll") for (int m = 0; m < 4; ++m) _Pragma("unroll") for (int n = 0; n < 2; ++n) _Pragma("unroll") for (int k = 0; k < 2; ++k) \
;         acc[ai][bj][m][n] = __builtin_amdgcn_mfma_f32_16x16x32_bf16(Bt[n][k], At[m][k], acc[ai][bj][m][n], 0, 0, 0); __builtin_amdgcn_s_setprio(0); } while (0)
; #define PG8_WAIT_V(n) asm volatile("s_waitcnt vmcnt(" #n ")" ::: "memory")
; #define PG8_WAIT_L(n) asm volatile("s_waitcnt lgkmcnt(" #n ")" ::: "memory")
; #define PG8_BAR __builtin_amdgcn_s_barrier()
; #define PG8_SCHED __builtin_amdgcn_sched_barrier(0)
; template <class Epi, class Sched, bool ALIGN_EPI = false, bool SP2 = false>
; __device__ __forceinline__ void gemm_phase(PG8_LAS unsigned char* lds, const Gemm g, const Sched& S, const Epi& E, const int wid) {
;     ...
;             PG8_WAIT_V(8); PG8_WAIT_L(0); PG8_BAR; PG8_MMA(0, 0, At, B0); PG8_MMA(0, 1, At, B1); PG8_BAR; PG8_SCHED;
;             PG8_LDA(At, 0, 1); PG8_STAGE(PG8_SB(0, 0), b2, voffB); PG8_STAGE(PG8_SB(0, 1), b2 + hstepB, voffB); PG8_STAGE(PG8_SA(0, 0), a2, voffA);
;             PG8_WAIT_V(8); PG8_WAIT_L(0); PG8_BAR; PG8_MMA(1, 0, At, B0); PG8_MMA(1, 1, At, B1); PG8_BAR; PG8_SCHED;
;             PG8_LDB(B0, 1, 0); PG8_LDB(B1, 1, 1); PG8_SCHED; PG8_LDA(At, 1, 0); PG8_STAGE(PG8_SA(0, 1), a2 + hstepA, voffA);
	s_add_i32 s71, s65, s39
	s_add_u32 s98, s34, 0x80
	s_addc_u32 s99, s35, 0
	s_mov_b32 m0, s71
	ds_read_b128 v[180:183], v192 offset:16384
	ds_read_b128 v[184:187], v192 offset:17408
	ds_read_b128 v[194:197], v192 offset:18432
	ds_read_b128 v[198:201], v192 offset:19456
	ds_read_b128 v[202:205], v192 offset:20480
	ds_read_b128 v[206:209], v192 offset:21504
	ds_read_b128 v[210:213], v192 offset:22528
	ds_read_b128 v[214:217], v192 offset:23552
	global_load_lds_dwordx4 v154, s[34:35]
	s_add_i32 m0, s71, 0x2000
	s_add_u32 s72, s34, 0x40000
	s_addc_u32 s73, s35, 0
	s_add_i32 s71, s66, s39
	global_load_lds_dwordx4 v158, s[34:35]
	s_mov_b32 m0, s71
	s_add_u32 s100, s36, 0x80
	s_addc_u32 s101, s37, 0
	global_load_lds_dwordx4 v154, s[72:73]
	s_add_i32 m0, s71, 0x2000
	s_nop 0
	global_load_lds_dwordx4 v158, s[72:73]
	s_mov_b32 m0, s40
	s_nop 0
	global_load_lds_dwordx4 v152, s[36:37]
	s_mov_b32 m0, s41
	s_nop 0
	global_load_lds_dwordx4 v156, s[36:37]
	s_waitcnt vmcnt(8) lgkmcnt(0)
	s_barrier
	s_nop 0
	s_setprio 1
	v_mfma_f32_16x16x32_bf16 v[60:63], v[128:131], v[180:183], v[60:63]
	v_mfma_f32_16x16x32_bf16 v[56:59], v[136:139], v[180:183], v[56:59]
	v_mfma_f32_16x16x32_bf16 v[44:47], v[128:131], v[194:197], v[44:47]
	v_mfma_f32_16x16x32_bf16 v[40:43], v[136:139], v[194:197], v[40:43]
	v_mfma_f32_16x16x32_bf16 v[28:31], v[128:131], v[202:205], v[28:31]
	v_mfma_f32_16x16x32_bf16 v[24:27], v[136:139], v[202:205], v[24:27]
	v_mfma_f32_16x16x32_bf16 v[12:15], v[128:131], v[210:213], v[12:15]
	v_mfma_f32_16x16x32_bf16 v[8:11], v[136:139], v[210:213], v[8:11]
	v_mfma_f32_16x16x32_bf16 v[60:63], v[132:135], v[184:187], v[60:63]
	v_mfma_f32_16x16x32_bf16 v[56:59], v[140:143], v[184:187], v[56:59]
	v_mfma_f32_16x16x32_bf16 v[44:47], v[132:135], v[198:201], v[44:47]
	v_mfma_f32_16x16x32_bf16 v[40:43], v[140:143], v[198:201], v[40:43]
	v_mfma_f32_16x16x32_bf16 v[28:31], v[132:135], v[206:209], v[28:31]
	v_mfma_f32_16x16x32_bf16 v[24:27], v[140:143], v[206:209], v[24:27]
	v_mfma_f32_16x16x32_bf16 v[12:15], v[132:135], v[214:217], v[12:15]
	v_mfma_f32_16x16x32_bf16 v[8:11], v[140:143], v[214:217], v[8:11]
	s_setprio 0
	s_setprio 1
	v_mfma_f32_16x16x32_bf16 v[52:55], v[144:147], v[180:183], v[52:55]
	v_mfma_f32_16x16x32_bf16 v[48:51], v[172:175], v[180:183], v[48:51]
	v_mfma_f32_16x16x32_bf16 v[36:39], v[144:147], v[194:197], v[36:39]
	v_mfma_f32_16x16x32_bf16 v[32:35], v[172:175], v[194:197], v[32:35]
	v_mfma_f32_16x16x32_bf16 v[20:23], v[144:147], v[202:205], v[20:23]
	v_mfma_f32_16x16x32_bf16 v[16:19], v[172:175], v[202:205], v[16:19]
	v_mfma_f32_16x16x32_bf16 v[4:7], v[144:147], v[210:213], v[4:7]
	v_mfma_f32_16x16x32_bf16 v[0:3], v[172:175], v[210:213], v[0:3]
	v_mfma_f32_16x16x32_bf16 v[52:55], v[148:151], v[184:187], v[52:55]
	v_mfma_f32_16x16x32_bf16 v[48:51], v[176:179], v[184:187], v[48:51]
	v_mfma_f32_16x16x32_bf16 v[36:39], v[148:151], v[198:201], v[36:39]
	v_mfma_f32_16x16x32_bf16 v[32:35], v[176:179], v[198:201], v[32:35]
	v_mfma_f32_16x16x32_bf16 v[20:23], v[148:151], v[206:209], v[20:23]
	v_mfma_f32_16x16x32_bf16 v[16:19], v[176:179], v[206:209], v[16:19]
	v_mfma_f32_16x16x32_bf16 v[4:7], v[148:151], v[214:217], v[4:7]
	v_mfma_f32_16x16x32_bf16 v[0:3], v[176:179], v[214:217], v[0:3]
	s_setprio 0
	s_barrier
	s_add_i32 s71, 0, 0x18000
	s_add_i32 s72, 0, 0x1c000
	ds_read_b128 v[128:131], v252
	ds_read_b128 v[132:135], v252 offset:1024
	ds_read_b128 v[136:139], v252 offset:2048
	ds_read_b128 v[140:143], v252 offset:3072
	ds_read_b128 v[144:147], v253
	ds_read_b128 v[148:151], v253 offset:1024
	ds_read_b128 v[172:175], v253 offset:2048
	ds_read_b128 v[176:179], v253 offset:3072
	s_add_u32 s36, s36, 0x40000
	s_addc_u32 s37, s37, 0
	s_mov_b32 m0, s44
	ds_read_b128 v[180:183], v192 offset:32768
	ds_read_b128 v[184:187], v192 offset:33792
	ds_read_b128 v[194:197], v192 offset:34816
	ds_read_b128 v[198:201], v192 offset:35840
	ds_read_b128 v[202:205], v192 offset:36864
	ds_read_b128 v[206:209], v192 offset:37888
	ds_read_b128 v[210:213], v192 offset:38912
	ds_read_b128 v[214:217], v192 offset:39936
	global_load_lds_dwordx4 v152, s[36:37]
	s_mov_b32 m0, s45
	s_nop 0
	global_load_lds_dwordx4 v156, s[36:37]
	s_waitcnt vmcnt(8) lgkmcnt(0)
	s_barrier
; #define PG8_WAIT_V(n) asm volatile("s_waitcnt vmcnt(" #n ")" ::: "memory")
; #define PG8_WAIT_L(n) asm volatile("s_waitcnt lgkmcnt(" #n ")" ::: "memory")
; template <class Epi, class Sched, bool ALIGN_EPI = false, bool SP2 = false>
; __device__ __forceinline__ void gemm_phase(PG8_LAS unsigned char* lds, const Gemm g, const Sched& S, const Epi& E, const int wid) {
;     ...
;             PG8_WAIT_V(8); PG8_WAIT_L(0); PG8_BAR; PG8_MMA(1, 0, At, B0); PG8_MMA(1, 1, At, B1); PG8_BAR; PG8_SCHED;
;             PG8_LDB(B0, 1, 0); PG8_LDB(B1, 1, 1); PG8_SCHED; PG8_LDA(At, 1, 0); PG8_STAGE(PG8_SA(0, 1), a2 + hstepA, voffA);
;             PG8_WAIT_V(8); PG8_WAIT_L(0); PG8_BAR; PG8_MMA(0, 0, At, B0); PG8_MMA(0, 1, At, B1); PG8_BAR; PG8_SCHED;
;             PG8_LDA(At, 1, 1); PG8_STAGE(PG8_SB(1, 0), b3, voffB); PG8_STAGE(PG8_SB(1, 1), b3 + hstepB, voffB); PG8_STAGE(PG8_SA(1, 0), a3, voffA);
;             PG8_WAIT_V(8); PG8_WAIT_L(0); PG8_BAR; PG8_MMA(1, 0, At, B0); PG8_MMA(1, 1, At, B1); PG8_BAR; PG8_SCHED;
;             } else {
;             PG8_LDB(B0, 0, 0); PG8_SCHED; PG8_LDA(At, 0, 0); PG8_STAGE(PG8_SA(1, 1), a1 + hstepA, voffA);
;             PG8_WAIT_L(8); PG8_BAR; PG8_WAIT_L(0); PG8_MMA(0, 0, At, B0); PG8_BAR; PG8_SCHED;
;             PG8_LDB(B1, 0, 1); PG8_STAGE(PG8_SB(0, 0), b2, voffB);
;             PG8_BAR; PG8_WAIT_L(0); PG8_MMA(0, 1, At, B1); PG8_BAR;
;             PG8_LDA(At, 0, 1); PG8_STAGE(PG8_SA(0, 0), a2, voffA);
;             PG8_BAR; PG8_WAIT_L(0); PG8_MMA(1, 0, At, B0); PG8_BAR; PG8_SCHED;
;             PG8_STAGE(PG8_SB(0, 1), b2 + hstepB, voffB);
;             PG8_WAIT_V(6); PG8_BAR; PG8_MMA(1, 1, At, B1); PG8_BAR;
;             PG8_LDB(B0, 1, 0); PG8_SCHED; PG8_LDA(At, 1, 0); PG8_STAGE(PG8_SA(0, 1), a2 + hstepA, voffA);
;             PG8_WAIT_L(8); PG8_BAR; PG8_WAIT_L(0); PG8_MMA(0, 0, At, B0); PG8_BAR; PG8_SCHED;
;             PG8_LDB(B1, 1, 1); PG8_STAGE(PG8_SB(1, 0), b3, voffB);
;             PG8_BAR; PG8_WAIT_L(0); PG8_MMA(0, 1, At, B1); PG8_BAR;
;             PG8_LDA(At, 1, 1); PG8_STAGE(PG8_SA(1, 0), a3, voffA);
;             PG8_BAR; PG8_WAIT_L(0); PG8_MMA(1, 0, At, B0); PG8_BAR; PG8_SCHED;
;             PG8_STAGE(PG8_SB(1, 1), b3 + hstepB, voffB);
;             PG8_WAIT_V(6); PG8_BAR; PG8_MMA(1, 1, At, B1); PG8_BAR;
;             }
;         }
;         if constexpr (ALIGN_EPI) { if (wr == 0) PG8_BAR; }
	s_nop 0
	s_setprio 1
	v_mfma_f32_16x16x32_bf16 v[124:127], v[128:131], v[180:183], v[124:127]
	v_mfma_f32_16x16x32_bf16 v[120:123], v[136:139], v[180:183], v[120:123]
	v_mfma_f32_16x16x32_bf16 v[108:111], v[128:131], v[194:197], v[108:111]
	v_mfma_f32_16x16x32_bf16 v[104:107], v[136:139], v[194:197], v[104:107]
	v_mfma_f32_16x16x32_bf16 v[92:95], v[128:131], v[202:205], v[92:95]
	v_mfma_f32_16x16x32_bf16 v[88:91], v[136:139], v[202:205], v[88:91]
	v_mfma_f32_16x16x32_bf16 v[76:79], v[128:131], v[210:213], v[76:79]
	v_mfma_f32_16x16x32_bf16 v[72:75], v[136:139], v[210:213], v[72:75]
	v_mfma_f32_16x16x32_bf16 v[124:127], v[132:135], v[184:187], v[124:127]
	v_mfma_f32_16x16x32_bf16 v[120:123], v[140:143], v[184:187], v[120:123]
	v_mfma_f32_16x16x32_bf16 v[108:111], v[132:135], v[198:201], v[108:111]
	v_mfma_f32_16x16x32_bf16 v[104:107], v[140:143], v[198:201], v[104:107]
	v_mfma_f32_16x16x32_bf16 v[92:95], v[132:135], v[206:209], v[92:95]
	v_mfma_f32_16x16x32_bf16 v[88:91], v[140:143], v[206:209], v[88:91]
	v_mfma_f32_16x16x32_bf16 v[76:79], v[132:135], v[214:217], v[76:79]
	v_mfma_f32_16x16x32_bf16 v[72:75], v[140:143], v[214:217], v[72:75]
	s_setprio 0
	s_setprio 1
	v_mfma_f32_16x16x32_bf16 v[116:119], v[144:147], v[180:183], v[116:119]
	v_mfma_f32_16x16x32_bf16 v[112:115], v[172:175], v[180:183], v[112:115]
	v_mfma_f32_16x16x32_bf16 v[100:103], v[144:147], v[194:197], v[100:103]
	v_mfma_f32_16x16x32_bf16 v[96:99], v[172:175], v[194:197], v[96:99]
	v_mfma_f32_16x16x32_bf16 v[84:87], v[144:147], v[202:205], v[84:87]
	v_mfma_f32_16x16x32_bf16 v[80:83], v[172:175], v[202:205], v[80:83]
	v_mfma_f32_16x16x32_bf16 v[68:71], v[144:147], v[210:213], v[68:71]
	v_mfma_f32_16x16x32_bf16 v[64:67], v[172:175], v[210:213], v[64:67]
	v_mfma_f32_16x16x32_bf16 v[116:119], v[148:151], v[184:187], v[116:119]
	v_mfma_f32_16x16x32_bf16 v[112:115], v[176:179], v[184:187], v[112:115]
	v_mfma_f32_16x16x32_bf16 v[100:103], v[148:151], v[198:201], v[100:103]
	v_mfma_f32_16x16x32_bf16 v[96:99], v[176:179], v[198:201], v[96:99]
	v_mfma_f32_16x16x32_bf16 v[84:87], v[148:151], v[206:209], v[84:87]
	v_mfma_f32_16x16x32_bf16 v[80:83], v[176:179], v[206:209], v[80:83]
	v_mfma_f32_16x16x32_bf16 v[68:71], v[148:151], v[214:217], v[68:71]
	v_mfma_f32_16x16x32_bf16 v[64:67], v[176:179], v[214:217], v[64:67]
	s_setprio 0
	s_barrier
	s_add_i32 s36, s71, s39
	s_mov_b32 m0, s36
	ds_read_b128 v[180:183], v192 offset:49152
	ds_read_b128 v[184:187], v192 offset:50176
	ds_read_b128 v[194:197], v192 offset:51200
	ds_read_b128 v[198:201], v192 offset:52224
	ds_read_b128 v[202:205], v192 offset:53248
	ds_read_b128 v[206:209], v192 offset:54272
	ds_read_b128 v[210:213], v192 offset:55296
	ds_read_b128 v[214:217], v192 offset:56320
	global_load_lds_dwordx4 v154, s[98:99]
	s_add_i32 m0, s36, 0x2000
	s_add_u32 s34, s34, 0x40080
	s_addc_u32 s35, s35, 0
	s_add_i32 s36, s72, s39
	global_load_lds_dwordx4 v158, s[98:99]
	s_mov_b32 m0, s36
	s_nop 0
	global_load_lds_dwordx4 v154, s[34:35]
	s_add_i32 m0, s36, 0x2000
	s_nop 0
	global_load_lds_dwordx4 v158, s[34:35]
	s_mov_b32 m0, s47
	s_nop 0
	global_load_lds_dwordx4 v152, s[100:101]
	s_mov_b32 m0, s48
	s_nop 0
	global_load_lds_dwordx4 v156, s[100:101]
	s_waitcnt vmcnt(8) lgkmcnt(0)
	s_barrier
	s_setprio 1
	v_mfma_f32_16x16x32_bf16 v[60:63], v[128:131], v[180:183], v[60:63]
	v_mfma_f32_16x16x32_bf16 v[56:59], v[136:139], v[180:183], v[56:59]
	v_mfma_f32_16x16x32_bf16 v[44:47], v[128:131], v[194:197], v[44:47]
	v_mfma_f32_16x16x32_bf16 v[40:43], v[136:139], v[194:197], v[40:43]
	v_mfma_f32_16x16x32_bf16 v[28:31], v[128:131], v[202:205], v[28:31]
	v_mfma_f32_16x16x32_bf16 v[24:27], v[136:139], v[202:205], v[24:27]
	v_mfma_f32_16x16x32_bf16 v[12:15], v[128:131], v[210:213], v[12:15]
	v_mfma_f32_16x16x32_bf16 v[8:11], v[136:139], v[210:213], v[8:11]
	v_mfma_f32_16x16x32_bf16 v[60:63], v[132:135], v[184:187], v[60:63]
	v_mfma_f32_16x16x32_bf16 v[56:59], v[140:143], v[184:187], v[56:59]
	v_mfma_f32_16x16x32_bf16 v[44:47], v[132:135], v[198:201], v[44:47]
	v_mfma_f32_16x16x32_bf16 v[40:43], v[140:143], v[198:201], v[40:43]
	v_mfma_f32_16x16x32_bf16 v[28:31], v[132:135], v[206:209], v[28:31]
	v_mfma_f32_16x16x32_bf16 v[24:27], v[140:143], v[206:209], v[24:27]
	v_mfma_f32_16x16x32_bf16 v[12:15], v[132:135], v[214:217], v[12:15]
	v_mfma_f32_16x16x32_bf16 v[8:11], v[140:143], v[214:217], v[8:11]
	s_setprio 0
	s_setprio 1
	v_mfma_f32_16x16x32_bf16 v[52:55], v[144:147], v[180:183], v[52:55]
	v_mfma_f32_16x16x32_bf16 v[48:51], v[172:175], v[180:183], v[48:51]
	v_mfma_f32_16x16x32_bf16 v[36:39], v[144:147], v[194:197], v[36:39]
	v_mfma_f32_16x16x32_bf16 v[32:35], v[172:175], v[194:197], v[32:35]
	v_mfma_f32_16x16x32_bf16 v[20:23], v[144:147], v[202:205], v[20:23]
	v_mfma_f32_16x16x32_bf16 v[16:19], v[172:175], v[202:205], v[16:19]
	v_mfma_f32_16x16x32_bf16 v[4:7], v[144:147], v[210:213], v[4:7]
	v_mfma_f32_16x16x32_bf16 v[0:3], v[172:175], v[210:213], v[0:3]
	v_mfma_f32_16x16x32_bf16 v[52:55], v[148:151], v[184:187], v[52:55]
	v_mfma_f32_16x16x32_bf16 v[48:51], v[176:179], v[184:187], v[48:51]
	v_mfma_f32_16x16x32_bf16 v[36:39], v[148:151], v[198:201], v[36:39]
	v_mfma_f32_16x16x32_bf16 v[32:35], v[176:179], v[198:201], v[32:35]
	v_mfma_f32_16x16x32_bf16 v[20:23], v[148:151], v[206:209], v[20:23]
	v_mfma_f32_16x16x32_bf16 v[16:19], v[176:179], v[206:209], v[16:19]
	v_mfma_f32_16x16x32_bf16 v[4:7], v[148:151], v[214:217], v[4:7]
	v_mfma_f32_16x16x32_bf16 v[0:3], v[176:179], v[214:217], v[0:3]
	s_setprio 0
	s_barrier
	s_add_i32 s70, s70, 2
	s_add_u32 s30, s30, 0x100
	s_addc_u32 s31, s31, 0
	s_add_u32 s68, s68, 0x100
	s_addc_u32 s69, s69, 0
	s_cmp_gt_u32 s70, 13
	s_cbranch_scc0 .LBB0_1780
	s_and_b64 vcc, exec, s[16:17]
	s_cbranch_vccz .LBB0_1783
	s_barrier

; #define PG8_STAGE(bufoff, gbase, voff) do { _Pragma("unroll") for (int _i = 0; _i < 2; ++_i) \
;         __builtin_amdgcn_global_load_lds((const unsigned*)((const char*)(gbase) + (voff)[_i]), (PG8_LAS unsigned*)(lds + (bufoff) + ldsw + _i * 8192), 16, 0, 0); } while (0)
; #define PG8_LDA(dst, b, h) do { _Pragma("unroll") for (int m = 0; m < 4; ++m) _Pragma("unroll") for (int k = 0; k < 2; ++k) dst[m][k] = *(const PG8_LAS bf16x8*)(lds + PG8_SA(b, h) + aoff + m * 2048 + k * 1024); } while (0)
; #define PG8_LDB(dst, b, h) do { _Pragma("unroll") for (int n = 0; n < 2; ++n) _Pragma("unroll") for (int k = 0; k < 2; ++k) dst[n][k] = *(const PG8_LAS bf16x8*)(lds + PG8_SB(b, h) + boff + n * 2048 + k * 1024); } while (0)
; #define PG8_WAIT_V(n) asm volatile("s_waitcnt vmcnt(" #n ")" ::: "memory")
; #define PG8_WAIT_L(n) asm volatile("s_waitcnt lgkmcnt(" #n ")" ::: "memory")
; #define PG8_BAR __builtin_amdgcn_s_barrier()
; #define PG8_SCHED __builtin_amdgcn_sched_barrier(0)
; template <class Epi, class Sched, bool ALIGN_EPI = false, bool SP2 = false>
; __device__ __forceinline__ void gemm_phase(PG8_LAS unsigned char* lds, const Gemm g, const Sched& S, const Epi& E, const int wid) {
;     ...
;         const bool has_next = S.next(ui + 1, nxt);
;         const char* nA = has_next ? (const char*)g.A + (size_t)nxt.pm * tstepA : cA; const char* nB = has_next ? (const char*)g.Bt + (size_t)nxt.pn * tstepB : cB;
;         for (int t = 0; t < nt; t += 2) {
;             const bool last = (t == nt - 2);
;             const char* a1 = cA + (size_t)(t + 1) * kstep;
;             const char* a2 = last ? nA : cA + (size_t)(t + 2) * kstep; const char* b2 = last ? nB : cB + (size_t)(t + 2) * kstep;
;             const char* a3 = a2 + kstep; const char* b3 = b2 + kstep;
;             if (last && has_next) S.a_ready(nxt);
;             if constexpr (SP2) {
;             PG8_LDB(B0, 0, 0); PG8_LDB(B1, 0, 1); PG8_SCHED; PG8_LDA(At, 0, 0); PG8_STAGE(PG8_SA(1, 1), a1 + hstepA, voffA);
;             PG8_WAIT_V(8); PG8_WAIT_L(0); PG8_BAR; PG8_MMA(0, 0, At, B0); PG8_MMA(0, 1, At, B1); PG8_BAR; PG8_SCHED;
;             PG8_LDA(At, 0, 1); PG8_STAGE(PG8_SB(0, 0), b2, voffB); PG8_STAGE(PG8_SB(0, 1), b2 + hstepB, voffB); PG8_STAGE(PG8_SA(0, 0), a2, voffA);
;             PG8_WAIT_V(8); PG8_WAIT_L(0); PG8_BAR; PG8_MMA(1, 0, At, B0); PG8_MMA(1, 1, At, B1); PG8_BAR; PG8_SCHED;
.LBB0_1866:
	s_ashr_i32 s17, s16, 31
	s_lshl_b64 s[18:19], s[16:17], 19
	s_add_u32 s18, s0, s18
	s_addc_u32 s19, s1, s19
	s_and_b64 s[20:21], s[2:3], exec
	s_cselect_b32 s17, s19, s25
	s_cselect_b32 s49, s18, s24
	s_ashr_i32 s15, s14, 31
	s_lshl_b64 s[20:21], s[14:15], 19
	s_add_u32 s20, s30, s20
	s_addc_u32 s21, s31, s21
	s_and_b64 s[28:29], s[2:3], exec
	s_cselect_b32 s15, s21, s27
	s_cselect_b32 s64, s20, s26
	s_add_u32 s24, s24, 0x40080
	s_addc_u32 s25, s25, 0
	s_add_u32 s65, s26, 0x100
	s_addc_u32 s66, s27, 0
	s_mov_b32 s67, -2
	v_add_u32_e32 v252, 0x18000, v165
	v_add_u32_e32 v253, 0x1c000, v165
	ds_read_b128 v[148:151], v166
	ds_read_b128 v[152:155], v166 offset:1024
	ds_read_b128 v[156:159], v166 offset:2048
	ds_read_b128 v[160:163], v166 offset:3072
	ds_read_b128 v[172:175], v167
	ds_read_b128 v[176:179], v167 offset:1024
	ds_read_b128 v[180:183], v167 offset:2048
	ds_read_b128 v[184:187], v167 offset:3072
	s_add_u32 s26, s24, 0xfffc0080
	s_addc_u32 s27, s25, -1
	s_cmp_eq_u32 s67, 12
	s_cselect_b32 s29, s17, s27
	s_cselect_b32 s28, s49, s26
	s_cselect_b32 s27, s15, s66
	s_cselect_b32 s26, s64, s65
	s_add_i32 m0, s36, 0xc000
	ds_read_b128 v[188:191], v168
	ds_read_b128 v[192:195], v168 offset:1024
	ds_read_b128 v[196:199], v168 offset:2048
	ds_read_b128 v[200:203], v168 offset:3072
	ds_read_b128 v[204:207], v168 offset:4096
	ds_read_b128 v[208:211], v168 offset:5120
	ds_read_b128 v[212:215], v168 offset:6144
	ds_read_b128 v[216:219], v168 offset:7168
	global_load_lds_dwordx4 v140, s[24:25]
	s_add_i32 m0, s36, 0xe000
	s_nop 0
	global_load_lds_dwordx4 v142, s[24:25]
	s_waitcnt vmcnt(8) lgkmcnt(0)
	v_lshl_add_u32 v220, s22, 8, v164
	v_add_u32_e32 v236, 0x80, v220
	v_ashrrev_i32_e32 v221, 31, v220
	v_ashrrev_i32_e32 v237, 31, v236
	v_lshlrev_b64 v[220:221], 6, v[220:221]
	v_lshlrev_b64 v[236:237], 6, v[236:237]
	v_lshl_add_u64 v[220:221], v[138:139], 0, v[220:221]
	v_lshl_add_u64 v[236:237], v[138:139], 0, v[236:237]
	global_load_dwordx4 v[224:227], v[220:221], off offset:1024
	global_load_dwordx4 v[228:231], v[220:221], off offset:2048
	global_load_dwordx4 v[232:235], v[220:221], off offset:3072
	global_load_dwordx4 v[240:243], v[236:237], off offset:1024
	global_load_dwordx4 v[244:247], v[236:237], off offset:2048
	global_load_dwordx4 v[248:251], v[236:237], off offset:3072
	s_nop 0
	global_load_dwordx4 v[220:223], v[220:221], off
	s_nop 0
	global_load_dwordx4 v[236:239], v[236:237], off
	s_barrier
	s_nop 0
	s_setprio 1
	v_mfma_f32_16x16x32_bf16 v[124:127], v[148:151], v[188:191], 0
	v_mfma_f32_16x16x32_bf16 v[116:119], v[156:159], v[188:191], 0
	v_mfma_f32_16x16x32_bf16 v[108:111], v[148:151], v[196:199], 0
	v_mfma_f32_16x16x32_bf16 v[100:103], v[156:159], v[196:199], 0
	v_mfma_f32_16x16x32_bf16 v[92:95], v[148:151], v[204:207], 0
	v_mfma_f32_16x16x32_bf16 v[84:87], v[156:159], v[204:207], 0
	v_mfma_f32_16x16x32_bf16 v[76:79], v[148:151], v[212:215], 0
	v_mfma_f32_16x16x32_bf16 v[68:71], v[156:159], v[212:215], 0
	v_mfma_f32_16x16x32_bf16 v[124:127], v[152:155], v[192:195], v[124:127]
	v_mfma_f32_16x16x32_bf16 v[116:119], v[160:163], v[192:195], v[116:119]
	v_mfma_f32_16x16x32_bf16 v[108:111], v[152:155], v[200:203], v[108:111]
	v_mfma_f32_16x16x32_bf16 v[100:103], v[160:163], v[200:203], v[100:103]
	v_mfma_f32_16x16x32_bf16 v[92:95], v[152:155], v[208:211], v[92:95]
	v_mfma_f32_16x16x32_bf16 v[84:87], v[160:163], v[208:211], v[84:87]
	v_mfma_f32_16x16x32_bf16 v[76:79], v[152:155], v[216:219], v[76:79]
	v_mfma_f32_16x16x32_bf16 v[68:71], v[160:163], v[216:219], v[68:71]
	s_setprio 0
	s_setprio 1
	v_mfma_f32_16x16x32_bf16 v[120:123], v[172:175], v[188:191], 0
	v_mfma_f32_16x16x32_bf16 v[112:115], v[180:183], v[188:191], 0
	v_mfma_f32_16x16x32_bf16 v[104:107], v[172:175], v[196:199], 0
	v_mfma_f32_16x16x32_bf16 v[96:99], v[180:183], v[196:199], 0
	v_mfma_f32_16x16x32_bf16 v[88:91], v[172:175], v[204:207], 0
	v_mfma_f32_16x16x32_bf16 v[80:83], v[180:183], v[204:207], 0
	v_mfma_f32_16x16x32_bf16 v[72:75], v[172:175], v[212:215], 0
	v_mfma_f32_16x16x32_bf16 v[64:67], v[180:183], v[212:215], 0
	v_mfma_f32_16x16x32_bf16 v[120:123], v[176:179], v[192:195], v[120:123]
	v_mfma_f32_16x16x32_bf16 v[112:115], v[184:187], v[192:195], v[112:115]
	v_mfma_f32_16x16x32_bf16 v[104:107], v[176:179], v[200:203], v[104:107]
	v_mfma_f32_16x16x32_bf16 v[96:99], v[184:187], v[200:203], v[96:99]
	v_mfma_f32_16x16x32_bf16 v[88:91], v[176:179], v[208:211], v[88:91]
	v_mfma_f32_16x16x32_bf16 v[80:83], v[184:187], v[208:211], v[80:83]
	v_mfma_f32_16x16x32_bf16 v[72:75], v[176:179], v[216:219], v[72:75]
	v_mfma_f32_16x16x32_bf16 v[64:67], v[184:187], v[216:219], v[64:67]
	s_setprio 0
	s_barrier
	s_add_i32 s68, s45, s33
	s_add_u32 s98, s26, 0x80
	s_addc_u32 s99, s27, 0
	s_mov_b32 m0, s68
	ds_read_b128 v[188:191], v168 offset:16384
	ds_read_b128 v[192:195], v168 offset:17408
	ds_read_b128 v[196:199], v168 offset:18432
	ds_read_b128 v[200:203], v168 offset:19456
	ds_read_b128 v[204:207], v168 offset:20480
	ds_read_b128 v[208:211], v168 offset:21504
	ds_read_b128 v[212:215], v168 offset:22528
	ds_read_b128 v[216:219], v168 offset:23552
	global_load_lds_dwordx4 v132, s[26:27]
	s_add_i32 m0, s68, 0x2000
	s_add_u32 s68, s26, 0x40000
	s_addc_u32 s69, s27, 0
	s_add_i32 s70, s46, s33
	global_load_lds_dwordx4 v128, s[26:27]
	s_mov_b32 m0, s70
	s_add_u32 s100, s28, 0x80
	s_addc_u32 s101, s29, 0
	global_load_lds_dwordx4 v132, s[68:69]
	s_add_i32 m0, s70, 0x2000
	s_nop 0
	global_load_lds_dwordx4 v128, s[68:69]
	s_mov_b32 m0, s36
	s_nop 0
	global_load_lds_dwordx4 v134, s[28:29]
	s_mov_b32 m0, s37
	s_nop 0
	global_load_lds_dwordx4 v130, s[28:29]
	s_waitcnt vmcnt(8) lgkmcnt(0)
	s_barrier
; #define PG8_STAGE(bufoff, gbase, voff) do { _Pragma("unroll") for (int _i = 0; _i < 2; ++_i) \
;         __builtin_amdgcn_global_load_lds((const unsigned*)((const char*)(gbase) + (voff)[_i]), (PG8_LAS unsigned*)(lds + (bufoff) + ldsw + _i * 8192), 16, 0, 0); } while (0)
; #define PG8_LDA(dst, b, h) do { _Pragma("unroll") for (int m = 0; m < 4; ++m) _Pragma("unroll") for (int k = 0; k < 2; ++k) dst[m][k] = *(const PG8_LAS bf16x8*)(lds + PG8_SA(b, h) + aoff + m * 2048 + k * 1024); } while (0)
; #define PG8_LDB(dst, b, h) do { _Pragma("unroll") for (int n = 0; n < 2; ++n) _Pragma("unroll") for (int k = 0; k < 2; ++k) dst[n][k] = *(const PG8_LAS bf16x8*)(lds + PG8_SB(b, h) + boff + n * 2048 + k * 1024); } while (0)
; #define PG8_MMA(ai, bj, At, Bt) do { __builtin_amdgcn_s_setprio(1); _Pragma("unroll") for (int m = 0; m < 4; ++m) _Pragma("unroll") for (int n = 0; n < 2; ++n) _Pragma("unroll") for (int k = 0; k < 2; ++k) \
;         acc[ai][bj][m][n] = __builtin_amdgcn_mfma_f32_16x16x32_bf16(Bt[n][k], At[m][k], acc[ai][bj][m][n], 0, 0, 0); __builtin_amdgcn_s_setprio(0); } while (0)
; #define PG8_WAIT_V(n) asm volatile("s_waitcnt vmcnt(" #n ")" ::: "memory")
; #define PG8_WAIT_L(n) asm volatile("s_waitcnt lgkmcnt(" #n ")" ::: "memory")
; #define PG8_BAR __builtin_amdgcn_s_barrier()
; #define PG8_SCHED __builtin_amdgcn_sched_barrier(0)
; template <class Epi, class Sched, bool ALIGN_EPI = false, bool SP2 = false>
; __device__ __forceinline__ void gemm_phase(PG8_LAS unsigned char* lds, const Gemm g, const Sched& S, const Epi& E, const int wid) {
;     ...
;             PG8_WAIT_V(8); PG8_WAIT_L(0); PG8_BAR; PG8_MMA(0, 0, At, B0); PG8_MMA(0, 1, At, B1); PG8_BAR; PG8_SCHED;
;             PG8_LDA(At, 0, 1); PG8_STAGE(PG8_SB(0, 0), b2, voffB); PG8_STAGE(PG8_SB(0, 1), b2 + hstepB, voffB); PG8_STAGE(PG8_SA(0, 0), a2, voffA);
;             PG8_WAIT_V(8); PG8_WAIT_L(0); PG8_BAR; PG8_MMA(1, 0, At, B0); PG8_MMA(1, 1, At, B1); PG8_BAR; PG8_SCHED;
;             PG8_LDB(B0, 1, 0); PG8_LDB(B1, 1, 1); PG8_SCHED; PG8_LDA(At, 1, 0); PG8_STAGE(PG8_SA(0, 1), a2 + hstepA, voffA);
;             PG8_WAIT_V(8); PG8_WAIT_L(0); PG8_BAR; PG8_MMA(0, 0, At, B0); PG8_MMA(0, 1, At, B1); PG8_BAR; PG8_SCHED;
	s_nop 0
	s_setprio 1
	v_mfma_f32_16x16x32_bf16 v[60:63], v[148:151], v[188:191], 0
	v_mfma_f32_16x16x32_bf16 v[52:55], v[156:159], v[188:191], 0
	v_mfma_f32_16x16x32_bf16 v[44:47], v[148:151], v[196:199], 0
	v_mfma_f32_16x16x32_bf16 v[36:39], v[156:159], v[196:199], 0
	v_mfma_f32_16x16x32_bf16 v[28:31], v[148:151], v[204:207], 0
	v_mfma_f32_16x16x32_bf16 v[20:23], v[156:159], v[204:207], 0
	v_mfma_f32_16x16x32_bf16 v[12:15], v[148:151], v[212:215], 0
	v_mfma_f32_16x16x32_bf16 v[4:7], v[156:159], v[212:215], 0
	v_mfma_f32_16x16x32_bf16 v[60:63], v[152:155], v[192:195], v[60:63]
	v_mfma_f32_16x16x32_bf16 v[52:55], v[160:163], v[192:195], v[52:55]
	v_mfma_f32_16x16x32_bf16 v[44:47], v[152:155], v[200:203], v[44:47]
	v_mfma_f32_16x16x32_bf16 v[36:39], v[160:163], v[200:203], v[36:39]
	v_mfma_f32_16x16x32_bf16 v[28:31], v[152:155], v[208:211], v[28:31]
	v_mfma_f32_16x16x32_bf16 v[20:23], v[160:163], v[208:211], v[20:23]
	v_mfma_f32_16x16x32_bf16 v[12:15], v[152:155], v[216:219], v[12:15]
	v_mfma_f32_16x16x32_bf16 v[4:7], v[160:163], v[216:219], v[4:7]
	s_setprio 0
	s_setprio 1
	v_mfma_f32_16x16x32_bf16 v[56:59], v[172:175], v[188:191], 0
	v_mfma_f32_16x16x32_bf16 v[48:51], v[180:183], v[188:191], 0
	v_mfma_f32_16x16x32_bf16 v[40:43], v[172:175], v[196:199], 0
	v_mfma_f32_16x16x32_bf16 v[32:35], v[180:183], v[196:199], 0
	v_mfma_f32_16x16x32_bf16 v[24:27], v[172:175], v[204:207], 0
	v_mfma_f32_16x16x32_bf16 v[16:19], v[180:183], v[204:207], 0
	v_mfma_f32_16x16x32_bf16 v[8:11], v[172:175], v[212:215], 0
	v_mfma_f32_16x16x32_bf16 v[0:3], v[180:183], v[212:215], 0
	v_mfma_f32_16x16x32_bf16 v[56:59], v[176:179], v[192:195], v[56:59]
	v_mfma_f32_16x16x32_bf16 v[48:51], v[184:187], v[192:195], v[48:51]
	v_mfma_f32_16x16x32_bf16 v[40:43], v[176:179], v[200:203], v[40:43]
	v_mfma_f32_16x16x32_bf16 v[32:35], v[184:187], v[200:203], v[32:35]
	v_mfma_f32_16x16x32_bf16 v[24:27], v[176:179], v[208:211], v[24:27]
	v_mfma_f32_16x16x32_bf16 v[16:19], v[184:187], v[208:211], v[16:19]
	v_mfma_f32_16x16x32_bf16 v[8:11], v[176:179], v[216:219], v[8:11]
	v_mfma_f32_16x16x32_bf16 v[0:3], v[184:187], v[216:219], v[0:3]
	s_setprio 0
	s_barrier
	s_add_i32 s68, 0, 0x18000
	s_add_i32 s69, 0, 0x1c000
	ds_read_b128 v[148:151], v252
	ds_read_b128 v[152:155], v252 offset:1024
	ds_read_b128 v[156:159], v252 offset:2048
	ds_read_b128 v[160:163], v252 offset:3072
	ds_read_b128 v[172:175], v253
	ds_read_b128 v[176:179], v253 offset:1024
	ds_read_b128 v[180:183], v253 offset:2048
	ds_read_b128 v[184:187], v253 offset:3072
	s_add_u32 s28, s28, 0x40000
	s_addc_u32 s29, s29, 0
	s_mov_b32 m0, s38
	ds_read_b128 v[188:191], v168 offset:32768
	ds_read_b128 v[192:195], v168 offset:33792
	ds_read_b128 v[196:199], v168 offset:34816
	ds_read_b128 v[200:203], v168 offset:35840
	ds_read_b128 v[204:207], v168 offset:36864
	ds_read_b128 v[208:211], v168 offset:37888
	ds_read_b128 v[212:215], v168 offset:38912
	ds_read_b128 v[216:219], v168 offset:39936
	global_load_lds_dwordx4 v134, s[28:29]
	s_mov_b32 m0, s39
	s_nop 0
	global_load_lds_dwordx4 v130, s[28:29]
	s_waitcnt vmcnt(8) lgkmcnt(0)
	s_barrier
	s_nop 0
	s_setprio 1
	v_mfma_f32_16x16x32_bf16 v[124:127], v[148:151], v[188:191], v[124:127]
	v_mfma_f32_16x16x32_bf16 v[116:119], v[156:159], v[188:191], v[116:119]
	v_mfma_f32_16x16x32_bf16 v[108:111], v[148:151], v[196:199], v[108:111]
	v_mfma_f32_16x16x32_bf16 v[100:103], v[156:159], v[196:199], v[100:103]
	v_mfma_f32_16x16x32_bf16 v[92:95], v[148:151], v[204:207], v[92:95]
	v_mfma_f32_16x16x32_bf16 v[84:87], v[156:159], v[204:207], v[84:87]
	v_mfma_f32_16x16x32_bf16 v[76:79], v[148:151], v[212:215], v[76:79]
	v_mfma_f32_16x16x32_bf16 v[68:71], v[156:159], v[212:215], v[68:71]
	v_mfma_f32_16x16x32_bf16 v[124:127], v[152:155], v[192:195], v[124:127]
	v_mfma_f32_16x16x32_bf16 v[116:119], v[160:163], v[192:195], v[116:119]
	v_mfma_f32_16x16x32_bf16 v[108:111], v[152:155], v[200:203], v[108:111]
	v_mfma_f32_16x16x32_bf16 v[100:103], v[160:163], v[200:203], v[100:103]
	v_mfma_f32_16x16x32_bf16 v[92:95], v[152:155], v[208:211], v[92:95]
	v_mfma_f32_16x16x32_bf16 v[84:87], v[160:163], v[208:211], v[84:87]
	v_mfma_f32_16x16x32_bf16 v[76:79], v[152:155], v[216:219], v[76:79]
	v_mfma_f32_16x16x32_bf16 v[68:71], v[160:163], v[216:219], v[68:71]
	s_setprio 0
	s_setprio 1
	v_mfma_f32_16x16x32_bf16 v[120:123], v[172:175], v[188:191], v[120:123]
	v_mfma_f32_16x16x32_bf16 v[112:115], v[180:183], v[188:191], v[112:115]
	v_mfma_f32_16x16x32_bf16 v[104:107], v[172:175], v[196:199], v[104:107]
	v_mfma_f32_16x16x32_bf16 v[96:99], v[180:183], v[196:199], v[96:99]
	v_mfma_f32_16x16x32_bf16 v[88:91], v[172:175], v[204:207], v[88:91]
	v_mfma_f32_16x16x32_bf16 v[80:83], v[180:183], v[204:207], v[80:83]
	v_mfma_f32_16x16x32_bf16 v[72:75], v[172:175], v[212:215], v[72:75]
	v_mfma_f32_16x16x32_bf16 v[64:67], v[180:183], v[212:215], v[64:67]
	v_mfma_f32_16x16x32_bf16 v[120:123], v[176:179], v[192:195], v[120:123]
	v_mfma_f32_16x16x32_bf16 v[112:115], v[184:187], v[192:195], v[112:115]
	v_mfma_f32_16x16x32_bf16 v[104:107], v[176:179], v[200:203], v[104:107]
	v_mfma_f32_16x16x32_bf16 v[96:99], v[184:187], v[200:203], v[96:99]
	v_mfma_f32_16x16x32_bf16 v[88:91], v[176:179], v[208:211], v[88:91]
	v_mfma_f32_16x16x32_bf16 v[80:83], v[184:187], v[208:211], v[80:83]
	v_mfma_f32_16x16x32_bf16 v[72:75], v[176:179], v[216:219], v[72:75]
	v_mfma_f32_16x16x32_bf16 v[64:67], v[184:187], v[216:219], v[64:67]
	s_setprio 0
	s_barrier
; #define PG8_STAGE(bufoff, gbase, voff) do { _Pragma("unroll") for (int _i = 0; _i < 2; ++_i) \
;         __builtin_amdgcn_global_load_lds((const unsigned*)((const char*)(gbase) + (voff)[_i]), (PG8_LAS unsigned*)(lds + (bufoff) + ldsw + _i * 8192), 16, 0, 0); } while (0)
; #define PG8_LDA(dst, b, h) do { _Pragma("unroll") for (int m = 0; m < 4; ++m) _Pragma("unroll") for (int k = 0; k < 2; ++k) dst[m][k] = *(const PG8_LAS bf16x8*)(lds + PG8_SA(b, h) + aoff + m * 2048 + k * 1024); } while (0)
; #define PG8_WAIT_V(n) asm volatile("s_waitcnt vmcnt(" #n ")" ::: "memory")
; #define PG8_WAIT_L(n) asm volatile("s_waitcnt lgkmcnt(" #n ")" ::: "memory")
; #define PG8_BAR __builtin_amdgcn_s_barrier()
; template <class Epi, class Sched, bool ALIGN_EPI = false, bool SP2 = false>
; __device__ __forceinline__ void gemm_phase(PG8_LAS unsigned char* lds, const Gemm g, const Sched& S, const Epi& E, const int wid) {
;     ...
;         for (int t = 0; t < nt; t += 2) {
;             const bool last = (t == nt - 2);
;             const char* a1 = cA + (size_t)(t + 1) * kstep;
;             const char* a2 = last ? nA : cA + (size_t)(t + 2) * kstep; const char* b2 = last ? nB : cB + (size_t)(t + 2) * kstep;
;             const char* a3 = a2 + kstep; const char* b3 = b2 + kstep;
;             if (last && has_next) S.a_ready(nxt);
;             if constexpr (SP2) {
;             PG8_LDB(B0, 0, 0); PG8_LDB(B1, 0, 1); PG8_SCHED; PG8_LDA(At, 0, 0); PG8_STAGE(PG8_SA(1, 1), a1 + hstepA, voffA);
;             PG8_WAIT_V(8); PG8_WAIT_L(0); PG8_BAR; PG8_MMA(0, 0, At, B0); PG8_MMA(0, 1, At, B1); PG8_BAR; PG8_SCHED;
;             PG8_LDA(At, 0, 1); PG8_STAGE(PG8_SB(0, 0), b2, voffB); PG8_STAGE(PG8_SB(0, 1), b2 + hstepB, voffB); PG8_STAGE(PG8_SA(0, 0), a2, voffA);
;             PG8_WAIT_V(8); PG8_WAIT_L(0); PG8_BAR; PG8_MMA(1, 0, At, B0); PG8_MMA(1, 1, At, B1); PG8_BAR; PG8_SCHED;
;             PG8_LDB(B0, 1, 0); PG8_LDB(B1, 1, 1); PG8_SCHED; PG8_LDA(At, 1, 0); PG8_STAGE(PG8_SA(0, 1), a2 + hstepA, voffA);
;             PG8_WAIT_V(8); PG8_WAIT_L(0); PG8_BAR; PG8_MMA(0, 0, At, B0); PG8_MMA(0, 1, At, B1); PG8_BAR; PG8_SCHED;
;             PG8_LDA(At, 1, 1); PG8_STAGE(PG8_SB(1, 0), b3, voffB); PG8_STAGE(PG8_SB(1, 1), b3 + hstepB, voffB); PG8_STAGE(PG8_SA(1, 0), a3, voffA);
;             PG8_WAIT_V(8); PG8_WAIT_L(0); PG8_BAR; PG8_MMA(1, 0, At, B0); PG8_MMA(1, 1, At, B1); PG8_BAR; PG8_SCHED;
	s_add_i32 s28, s68, s33
	s_mov_b32 m0, s28
	ds_read_b128 v[188:191], v168 offset:49152
	ds_read_b128 v[192:195], v168 offset:50176
	ds_read_b128 v[196:199], v168 offset:51200
	ds_read_b128 v[200:203], v168 offset:52224
	ds_read_b128 v[204:207], v168 offset:53248
	ds_read_b128 v[208:211], v168 offset:54272
	ds_read_b128 v[212:215], v168 offset:55296
	ds_read_b128 v[216:219], v168 offset:56320
	global_load_lds_dwordx4 v132, s[98:99]
	s_add_i32 m0, s28, 0x2000
	s_add_u32 s26, s26, 0x40080
	s_addc_u32 s27, s27, 0
	s_add_i32 s28, s69, s33
	global_load_lds_dwordx4 v128, s[98:99]
	s_mov_b32 m0, s28
	s_nop 0
	global_load_lds_dwordx4 v132, s[26:27]
	s_add_i32 m0, s28, 0x2000
	s_nop 0
	global_load_lds_dwordx4 v128, s[26:27]
	s_mov_b32 m0, s40
	s_nop 0
	global_load_lds_dwordx4 v134, s[100:101]
	s_mov_b32 m0, s41
	s_nop 0
	global_load_lds_dwordx4 v130, s[100:101]
	s_waitcnt vmcnt(8) lgkmcnt(0)
	s_barrier
	s_setprio 1
	v_mfma_f32_16x16x32_bf16 v[60:63], v[148:151], v[188:191], v[60:63]
	v_mfma_f32_16x16x32_bf16 v[52:55], v[156:159], v[188:191], v[52:55]
	v_mfma_f32_16x16x32_bf16 v[44:47], v[148:151], v[196:199], v[44:47]
	v_mfma_f32_16x16x32_bf16 v[36:39], v[156:159], v[196:199], v[36:39]
	v_mfma_f32_16x16x32_bf16 v[28:31], v[148:151], v[204:207], v[28:31]
	v_mfma_f32_16x16x32_bf16 v[20:23], v[156:159], v[204:207], v[20:23]
	v_mfma_f32_16x16x32_bf16 v[12:15], v[148:151], v[212:215], v[12:15]
	v_mfma_f32_16x16x32_bf16 v[4:7], v[156:159], v[212:215], v[4:7]
	v_mfma_f32_16x16x32_bf16 v[60:63], v[152:155], v[192:195], v[60:63]
	v_mfma_f32_16x16x32_bf16 v[52:55], v[160:163], v[192:195], v[52:55]
	v_mfma_f32_16x16x32_bf16 v[44:47], v[152:155], v[200:203], v[44:47]
	v_mfma_f32_16x16x32_bf16 v[36:39], v[160:163], v[200:203], v[36:39]
	v_mfma_f32_16x16x32_bf16 v[28:31], v[152:155], v[208:211], v[28:31]
	v_mfma_f32_16x16x32_bf16 v[20:23], v[160:163], v[208:211], v[20:23]
	v_mfma_f32_16x16x32_bf16 v[12:15], v[152:155], v[216:219], v[12:15]
	v_mfma_f32_16x16x32_bf16 v[4:7], v[160:163], v[216:219], v[4:7]
	s_setprio 0
	s_setprio 1
	v_mfma_f32_16x16x32_bf16 v[56:59], v[172:175], v[188:191], v[56:59]
	v_mfma_f32_16x16x32_bf16 v[48:51], v[180:183], v[188:191], v[48:51]
	v_mfma_f32_16x16x32_bf16 v[40:43], v[172:175], v[196:199], v[40:43]
	v_mfma_f32_16x16x32_bf16 v[32:35], v[180:183], v[196:199], v[32:35]
	v_mfma_f32_16x16x32_bf16 v[24:27], v[172:175], v[204:207], v[24:27]
	v_mfma_f32_16x16x32_bf16 v[16:19], v[180:183], v[204:207], v[16:19]
	v_mfma_f32_16x16x32_bf16 v[8:11], v[172:175], v[212:215], v[8:11]
	v_mfma_f32_16x16x32_bf16 v[0:3], v[180:183], v[212:215], v[0:3]
	v_mfma_f32_16x16x32_bf16 v[56:59], v[176:179], v[192:195], v[56:59]
	v_mfma_f32_16x16x32_bf16 v[48:51], v[184:187], v[192:195], v[48:51]
	v_mfma_f32_16x16x32_bf16 v[40:43], v[176:179], v[200:203], v[40:43]
	v_mfma_f32_16x16x32_bf16 v[32:35], v[184:187], v[200:203], v[32:35]
	v_mfma_f32_16x16x32_bf16 v[24:27], v[176:179], v[208:211], v[24:27]
	v_mfma_f32_16x16x32_bf16 v[16:19], v[184:187], v[208:211], v[16:19]
	v_mfma_f32_16x16x32_bf16 v[8:11], v[176:179], v[216:219], v[8:11]
	v_mfma_f32_16x16x32_bf16 v[0:3], v[184:187], v[216:219], v[0:3]
	s_setprio 0
	s_barrier
	s_add_i32 s67, s67, 2
	s_add_u32 s24, s24, 0x100
	s_addc_u32 s25, s25, 0
	s_add_u32 s65, s65, 0x100
	s_addc_u32 s66, s66, 0
	s_cmp_gt_u32 s67, 13
.LBB0_1867:
	ds_read_b128 v[148:151], v166
	ds_read_b128 v[152:155], v166 offset:1024
	ds_read_b128 v[156:159], v166 offset:2048
	ds_read_b128 v[160:163], v166 offset:3072
	ds_read_b128 v[172:175], v167
	ds_read_b128 v[176:179], v167 offset:1024
	ds_read_b128 v[180:183], v167 offset:2048
	ds_read_b128 v[184:187], v167 offset:3072
	s_add_u32 s26, s24, 0xfffc0080
	s_addc_u32 s27, s25, -1
	s_cmp_eq_u32 s67, 12
	s_cselect_b32 s29, s17, s27
	s_cselect_b32 s28, s49, s26
	s_cselect_b32 s27, s15, s66
	s_cselect_b32 s26, s64, s65
	s_add_i32 m0, s36, 0xc000
	ds_read_b128 v[188:191], v168
	ds_read_b128 v[192:195], v168 offset:1024
	ds_read_b128 v[196:199], v168 offset:2048
	ds_read_b128 v[200:203], v168 offset:3072
	ds_read_b128 v[204:207], v168 offset:4096
	ds_read_b128 v[208:211], v168 offset:5120
	ds_read_b128 v[212:215], v168 offset:6144
	ds_read_b128 v[216:219], v168 offset:7168
	global_load_lds_dwordx4 v140, s[24:25]
	s_add_i32 m0, s36, 0xe000
	s_nop 0
	global_load_lds_dwordx4 v142, s[24:25]
	s_waitcnt vmcnt(8) lgkmcnt(0)
	s_barrier
	s_setprio 1
	v_mfma_f32_16x16x32_bf16 v[124:127], v[148:151], v[188:191], v[124:127]
	v_mfma_f32_16x16x32_bf16 v[116:119], v[156:159], v[188:191], v[116:119]
	v_mfma_f32_16x16x32_bf16 v[108:111], v[148:151], v[196:199], v[108:111]
	v_mfma_f32_16x16x32_bf16 v[100:103], v[156:159], v[196:199], v[100:103]
	v_mfma_f32_16x16x32_bf16 v[92:95], v[148:151], v[204:207], v[92:95]
	v_mfma_f32_16x16x32_bf16 v[84:87], v[156:159], v[204:207], v[84:87]
	v_mfma_f32_16x16x32_bf16 v[76:79], v[148:151], v[212:215], v[76:79]
	v_mfma_f32_16x16x32_bf16 v[68:71], v[156:159], v[212:215], v[68:71]
	v_mfma_f32_16x16x32_bf16 v[124:127], v[152:155], v[192:195], v[124:127]
	v_mfma_f32_16x16x32_bf16 v[116:119], v[160:163], v[192:195], v[116:119]
	v_mfma_f32_16x16x32_bf16 v[108:111], v[152:155], v[200:203], v[108:111]
	v_mfma_f32_16x16x32_bf16 v[100:103], v[160:163], v[200:203], v[100:103]
	v_mfma_f32_16x16x32_bf16 v[92:95], v[152:155], v[208:211], v[92:95]
	v_mfma_f32_16x16x32_bf16 v[84:87], v[160:163], v[208:211], v[84:87]
	v_mfma_f32_16x16x32_bf16 v[76:79], v[152:155], v[216:219], v[76:79]
	v_mfma_f32_16x16x32_bf16 v[68:71], v[160:163], v[216:219], v[68:71]
	s_setprio 0
	s_setprio 1
	v_mfma_f32_16x16x32_bf16 v[120:123], v[172:175], v[188:191], v[120:123]
	v_mfma_f32_16x16x32_bf16 v[112:115], v[180:183], v[188:191], v[112:115]
	v_mfma_f32_16x16x32_bf16 v[104:107], v[172:175], v[196:199], v[104:107]
	v_mfma_f32_16x16x32_bf16 v[96:99], v[180:183], v[196:199], v[96:99]
	v_mfma_f32_16x16x32_bf16 v[88:91], v[172:175], v[204:207], v[88:91]
	v_mfma_f32_16x16x32_bf16 v[80:83], v[180:183], v[204:207], v[80:83]
	v_mfma_f32_16x16x32_bf16 v[72:75], v[172:175], v[212:215], v[72:75]
	v_mfma_f32_16x16x32_bf16 v[64:67], v[180:183], v[212:215], v[64:67]
	v_mfma_f32_16x16x32_bf16 v[120:123], v[176:179], v[192:195], v[120:123]
	v_mfma_f32_16x16x32_bf16 v[112:115], v[184:187], v[192:195], v[112:115]
	v_mfma_f32_16x16x32_bf16 v[104:107], v[176:179], v[200:203], v[104:107]
	v_mfma_f32_16x16x32_bf16 v[96:99], v[184:187], v[200:203], v[96:99]
	v_mfma_f32_16x16x32_bf16 v[88:91], v[176:179], v[208:211], v[88:91]
	v_mfma_f32_16x16x32_bf16 v[80:83], v[184:187], v[208:211], v[80:83]
	v_mfma_f32_16x16x32_bf16 v[72:75], v[176:179], v[216:219], v[72:75]
	v_mfma_f32_16x16x32_bf16 v[64:67], v[184:187], v[216:219], v[64:67]
	s_setprio 0
	s_barrier
; #define PG8_STAGE(bufoff, gbase, voff) do { _Pragma("unroll") for (int _i = 0; _i < 2; ++_i) \
;         __builtin_amdgcn_global_load_lds((const unsigned*)((const char*)(gbase) + (voff)[_i]), (PG8_LAS unsigned*)(lds + (bufoff) + ldsw + _i * 8192), 16, 0, 0); } while (0)
; #define PG8_LDA(dst, b, h) do { _Pragma("unroll") for (int m = 0; m < 4; ++m) _Pragma("unroll") for (int k = 0; k < 2; ++k) dst[m][k] = *(const PG8_LAS bf16x8*)(lds + PG8_SA(b, h) + aoff + m * 2048 + k * 1024); } while (0)
; #define PG8_LDB(dst, b, h) do { _Pragma("unroll") for (int n = 0; n < 2; ++n) _Pragma("unroll") for (int k = 0; k < 2; ++k) dst[n][k] = *(const PG8_LAS bf16x8*)(lds + PG8_SB(b, h) + boff + n * 2048 + k * 1024); } while (0)
; #define PG8_MMA(ai, bj, At, Bt) do { __builtin_amdgcn_s_setprio(1); _Pragma("unroll") for (int m = 0; m < 4; ++m) _Pragma("unroll") for (int n = 0; n < 2; ++n) _Pragma("unroll") for (int k = 0; k < 2; ++k) \
;         acc[ai][bj][m][n] = __builtin_amdgcn_mfma_f32_16x16x32_bf16(Bt[n][k], At[m][k], acc[ai][bj][m][n], 0, 0, 0); __builtin_amdgcn_s_setprio(0); } while (0)
; #define PG8_WAIT_V(n) asm volatile("s_waitcnt vmcnt(" #n ")" ::: "memory")
; #define PG8_WAIT_L(n) asm volatile("s_waitcnt lgkmcnt(" #n ")" ::: "memory")
; #define PG8_BAR __builtin_amdgcn_s_barrier()
; #define PG8_SCHED __builtin_amdgcn_sched_barrier(0)
; template <class Epi, class Sched, bool ALIGN_EPI = false, bool SP2 = false>
; __device__ __forceinline__ void gemm_phase(PG8_LAS unsigned char* lds, const Gemm g, const Sched& S, const Epi& E, const int wid) {
;     ...
;             PG8_WAIT_V(8); PG8_WAIT_L(0); PG8_BAR; PG8_MMA(0, 0, At, B0); PG8_MMA(0, 1, At, B1); PG8_BAR; PG8_SCHED;
;             PG8_LDA(At, 0, 1); PG8_STAGE(PG8_SB(0, 0), b2, voffB); PG8_STAGE(PG8_SB(0, 1), b2 + hstepB, voffB); PG8_STAGE(PG8_SA(0, 0), a2, voffA);
;             PG8_WAIT_V(8); PG8_WAIT_L(0); PG8_BAR; PG8_MMA(1, 0, At, B0); PG8_MMA(1, 1, At, B1); PG8_BAR; PG8_SCHED;
;             PG8_LDB(B0, 1, 0); PG8_LDB(B1, 1, 1); PG8_SCHED; PG8_LDA(At, 1, 0); PG8_STAGE(PG8_SA(0, 1), a2 + hstepA, voffA);
	s_add_i32 s68, s45, s33
	s_add_u32 s98, s26, 0x80
	s_addc_u32 s99, s27, 0
	s_mov_b32 m0, s68
	ds_read_b128 v[188:191], v168 offset:16384
	ds_read_b128 v[192:195], v168 offset:17408
	ds_read_b128 v[196:199], v168 offset:18432
	ds_read_b128 v[200:203], v168 offset:19456
	ds_read_b128 v[204:207], v168 offset:20480
	ds_read_b128 v[208:211], v168 offset:21504
	ds_read_b128 v[212:215], v168 offset:22528
	ds_read_b128 v[216:219], v168 offset:23552
	global_load_lds_dwordx4 v132, s[26:27]
	s_add_i32 m0, s68, 0x2000
	s_add_u32 s68, s26, 0x40000
	s_addc_u32 s69, s27, 0
	s_add_i32 s70, s46, s33
	global_load_lds_dwordx4 v128, s[26:27]
	s_mov_b32 m0, s70
	s_add_u32 s100, s28, 0x80
	s_addc_u32 s101, s29, 0
	global_load_lds_dwordx4 v132, s[68:69]
	s_add_i32 m0, s70, 0x2000
	s_nop 0
	global_load_lds_dwordx4 v128, s[68:69]
	s_mov_b32 m0, s36
	s_nop 0
	global_load_lds_dwordx4 v134, s[28:29]
	s_mov_b32 m0, s37
	s_nop 0
	global_load_lds_dwordx4 v130, s[28:29]
	s_waitcnt vmcnt(8) lgkmcnt(0)
	s_barrier
	s_nop 0
	s_setprio 1
	v_mfma_f32_16x16x32_bf16 v[60:63], v[148:151], v[188:191], v[60:63]
	v_mfma_f32_16x16x32_bf16 v[52:55], v[156:159], v[188:191], v[52:55]
	v_mfma_f32_16x16x32_bf16 v[44:47], v[148:151], v[196:199], v[44:47]
	v_mfma_f32_16x16x32_bf16 v[36:39], v[156:159], v[196:199], v[36:39]
	v_mfma_f32_16x16x32_bf16 v[28:31], v[148:151], v[204:207], v[28:31]
	v_mfma_f32_16x16x32_bf16 v[20:23], v[156:159], v[204:207], v[20:23]
	v_mfma_f32_16x16x32_bf16 v[12:15], v[148:151], v[212:215], v[12:15]
	v_mfma_f32_16x16x32_bf16 v[4:7], v[156:159], v[212:215], v[4:7]
	v_mfma_f32_16x16x32_bf16 v[60:63], v[152:155], v[192:195], v[60:63]
	v_mfma_f32_16x16x32_bf16 v[52:55], v[160:163], v[192:195], v[52:55]
	v_mfma_f32_16x16x32_bf16 v[44:47], v[152:155], v[200:203], v[44:47]
	v_mfma_f32_16x16x32_bf16 v[36:39], v[160:163], v[200:203], v[36:39]
	v_mfma_f32_16x16x32_bf16 v[28:31], v[152:155], v[208:211], v[28:31]
	v_mfma_f32_16x16x32_bf16 v[20:23], v[160:163], v[208:211], v[20:23]
	v_mfma_f32_16x16x32_bf16 v[12:15], v[152:155], v[216:219], v[12:15]
	v_mfma_f32_16x16x32_bf16 v[4:7], v[160:163], v[216:219], v[4:7]
	s_setprio 0
	s_setprio 1
	v_mfma_f32_16x16x32_bf16 v[56:59], v[172:175], v[188:191], v[56:59]
	v_mfma_f32_16x16x32_bf16 v[48:51], v[180:183], v[188:191], v[48:51]
	v_mfma_f32_16x16x32_bf16 v[40:43], v[172:175], v[196:199], v[40:43]
	v_mfma_f32_16x16x32_bf16 v[32:35], v[180:183], v[196:199], v[32:35]
	v_mfma_f32_16x16x32_bf16 v[24:27], v[172:175], v[204:207], v[24:27]
	v_mfma_f32_16x16x32_bf16 v[16:19], v[180:183], v[204:207], v[16:19]
	v_mfma_f32_16x16x32_bf16 v[8:11], v[172:175], v[212:215], v[8:11]
	v_mfma_f32_16x16x32_bf16 v[0:3], v[180:183], v[212:215], v[0:3]
	v_mfma_f32_16x16x32_bf16 v[56:59], v[176:179], v[192:195], v[56:59]
	v_mfma_f32_16x16x32_bf16 v[48:51], v[184:187], v[192:195], v[48:51]
	v_mfma_f32_16x16x32_bf16 v[40:43], v[176:179], v[200:203], v[40:43]
	v_mfma_f32_16x16x32_bf16 v[32:35], v[184:187], v[200:203], v[32:35]
	v_mfma_f32_16x16x32_bf16 v[24:27], v[176:179], v[208:211], v[24:27]
	v_mfma_f32_16x16x32_bf16 v[16:19], v[184:187], v[208:211], v[16:19]
	v_mfma_f32_16x16x32_bf16 v[8:11], v[176:179], v[216:219], v[8:11]
	v_mfma_f32_16x16x32_bf16 v[0:3], v[184:187], v[216:219], v[0:3]
	s_setprio 0
	s_barrier
	s_add_i32 s68, 0, 0x18000
	s_add_i32 s69, 0, 0x1c000
	ds_read_b128 v[148:151], v252
	ds_read_b128 v[152:155], v252 offset:1024
	ds_read_b128 v[156:159], v252 offset:2048
	ds_read_b128 v[160:163], v252 offset:3072
	ds_read_b128 v[172:175], v253
	ds_read_b128 v[176:179], v253 offset:1024
	ds_read_b128 v[180:183], v253 offset:2048
	ds_read_b128 v[184:187], v253 offset:3072
	s_add_u32 s28, s28, 0x40000
	s_addc_u32 s29, s29, 0
	s_mov_b32 m0, s38
	ds_read_b128 v[188:191], v168 offset:32768
	ds_read_b128 v[192:195], v168 offset:33792
	ds_read_b128 v[196:199], v168 offset:34816
	ds_read_b128 v[200:203], v168 offset:35840
	ds_read_b128 v[204:207], v168 offset:36864
	ds_read_b128 v[208:211], v168 offset:37888
	ds_read_b128 v[212:215], v168 offset:38912
	ds_read_b128 v[216:219], v168 offset:39936
	global_load_lds_dwordx4 v134, s[28:29]
	s_mov_b32 m0, s39
	s_nop 0
	global_load_lds_dwordx4 v130, s[28:29]
	s_waitcnt vmcnt(8) lgkmcnt(0)
	s_barrier
; #define PG8_WAIT_V(n) asm volatile("s_waitcnt vmcnt(" #n ")" ::: "memory")
; #define PG8_WAIT_L(n) asm volatile("s_waitcnt lgkmcnt(" #n ")" ::: "memory")
; template <class Epi, class Sched, bool ALIGN_EPI = false, bool SP2 = false>
; __device__ __forceinline__ void gemm_phase(PG8_LAS unsigned char* lds, const Gemm g, const Sched& S, const Epi& E, const int wid) {
;     ...
;             PG8_WAIT_V(8); PG8_WAIT_L(0); PG8_BAR; PG8_MMA(1, 0, At, B0); PG8_MMA(1, 1, At, B1); PG8_BAR; PG8_SCHED;
;             PG8_LDB(B0, 1, 0); PG8_LDB(B1, 1, 1); PG8_SCHED; PG8_LDA(At, 1, 0); PG8_STAGE(PG8_SA(0, 1), a2 + hstepA, voffA);
;             PG8_WAIT_V(8); PG8_WAIT_L(0); PG8_BAR; PG8_MMA(0, 0, At, B0); PG8_MMA(0, 1, At, B1); PG8_BAR; PG8_SCHED;
;             PG8_LDA(At, 1, 1); PG8_STAGE(PG8_SB(1, 0), b3, voffB); PG8_STAGE(PG8_SB(1, 1), b3 + hstepB, voffB); PG8_STAGE(PG8_SA(1, 0), a3, voffA);
;             PG8_WAIT_V(8); PG8_WAIT_L(0); PG8_BAR; PG8_MMA(1, 0, At, B0); PG8_MMA(1, 1, At, B1); PG8_BAR; PG8_SCHED;
;             } else {
;             PG8_LDB(B0, 0, 0); PG8_SCHED; PG8_LDA(At, 0, 0); PG8_STAGE(PG8_SA(1, 1), a1 + hstepA, voffA);
;             PG8_WAIT_L(8); PG8_BAR; PG8_WAIT_L(0); PG8_MMA(0, 0, At, B0); PG8_BAR; PG8_SCHED;
;             PG8_LDB(B1, 0, 1); PG8_STAGE(PG8_SB(0, 0), b2, voffB);
;             PG8_BAR; PG8_WAIT_L(0); PG8_MMA(0, 1, At, B1); PG8_BAR;
;             PG8_LDA(At, 0, 1); PG8_STAGE(PG8_SA(0, 0), a2, voffA);
;             PG8_BAR; PG8_WAIT_L(0); PG8_MMA(1, 0, At, B0); PG8_BAR; PG8_SCHED;
;             PG8_STAGE(PG8_SB(0, 1), b2 + hstepB, voffB);
;             PG8_WAIT_V(6); PG8_BAR; PG8_MMA(1, 1, At, B1); PG8_BAR;
;             PG8_LDB(B0, 1, 0); PG8_SCHED; PG8_LDA(At, 1, 0); PG8_STAGE(PG8_SA(0, 1), a2 + hstepA, voffA);
;             PG8_WAIT_L(8); PG8_BAR; PG8_WAIT_L(0); PG8_MMA(0, 0, At, B0); PG8_BAR; PG8_SCHED;
;             PG8_LDB(B1, 1, 1); PG8_STAGE(PG8_SB(1, 0), b3, voffB);
;             PG8_BAR; PG8_WAIT_L(0); PG8_MMA(0, 1, At, B1); PG8_BAR;
;             PG8_LDA(At, 1, 1); PG8_STAGE(PG8_SA(1, 0), a3, voffA);
;             PG8_BAR; PG8_WAIT_L(0); PG8_MMA(1, 0, At, B0); PG8_BAR; PG8_SCHED;
;             PG8_STAGE(PG8_SB(1, 1), b3 + hstepB, voffB);
;             PG8_WAIT_V(6); PG8_BAR; PG8_MMA(1, 1, At, B1); PG8_BAR;
;             }
;         }
;         if constexpr (ALIGN_EPI) { if (wr == 0) PG8_BAR; }
	s_nop 0
	s_setprio 1
	v_mfma_f32_16x16x32_bf16 v[124:127], v[148:151], v[188:191], v[124:127]
	v_mfma_f32_16x16x32_bf16 v[116:119], v[156:159], v[188:191], v[116:119]
	v_mfma_f32_16x16x32_bf16 v[108:111], v[148:151], v[196:199], v[108:111]
	v_mfma_f32_16x16x32_bf16 v[100:103], v[156:159], v[196:199], v[100:103]
	v_mfma_f32_16x16x32_bf16 v[92:95], v[148:151], v[204:207], v[92:95]
	v_mfma_f32_16x16x32_bf16 v[84:87], v[156:159], v[204:207], v[84:87]
	v_mfma_f32_16x16x32_bf16 v[76:79], v[148:151], v[212:215], v[76:79]
	v_mfma_f32_16x16x32_bf16 v[68:71], v[156:159], v[212:215], v[68:71]
	v_mfma_f32_16x16x32_bf16 v[124:127], v[152:155], v[192:195], v[124:127]
	v_mfma_f32_16x16x32_bf16 v[116:119], v[160:163], v[192:195], v[116:119]
	v_mfma_f32_16x16x32_bf16 v[108:111], v[152:155], v[200:203], v[108:111]
	v_mfma_f32_16x16x32_bf16 v[100:103], v[160:163], v[200:203], v[100:103]
	v_mfma_f32_16x16x32_bf16 v[92:95], v[152:155], v[208:211], v[92:95]
	v_mfma_f32_16x16x32_bf16 v[84:87], v[160:163], v[208:211], v[84:87]
	v_mfma_f32_16x16x32_bf16 v[76:79], v[152:155], v[216:219], v[76:79]
	v_mfma_f32_16x16x32_bf16 v[68:71], v[160:163], v[216:219], v[68:71]
	s_setprio 0
	s_setprio 1
	v_mfma_f32_16x16x32_bf16 v[120:123], v[172:175], v[188:191], v[120:123]
	v_mfma_f32_16x16x32_bf16 v[112:115], v[180:183], v[188:191], v[112:115]
	v_mfma_f32_16x16x32_bf16 v[104:107], v[172:175], v[196:199], v[104:107]
	v_mfma_f32_16x16x32_bf16 v[96:99], v[180:183], v[196:199], v[96:99]
	v_mfma_f32_16x16x32_bf16 v[88:91], v[172:175], v[204:207], v[88:91]
	v_mfma_f32_16x16x32_bf16 v[80:83], v[180:183], v[204:207], v[80:83]
	v_mfma_f32_16x16x32_bf16 v[72:75], v[172:175], v[212:215], v[72:75]
	v_mfma_f32_16x16x32_bf16 v[64:67], v[180:183], v[212:215], v[64:67]
	v_mfma_f32_16x16x32_bf16 v[120:123], v[176:179], v[192:195], v[120:123]
	v_mfma_f32_16x16x32_bf16 v[112:115], v[184:187], v[192:195], v[112:115]
	v_mfma_f32_16x16x32_bf16 v[104:107], v[176:179], v[200:203], v[104:107]
	v_mfma_f32_16x16x32_bf16 v[96:99], v[184:187], v[200:203], v[96:99]
	v_mfma_f32_16x16x32_bf16 v[88:91], v[176:179], v[208:211], v[88:91]
	v_mfma_f32_16x16x32_bf16 v[80:83], v[184:187], v[208:211], v[80:83]
	v_mfma_f32_16x16x32_bf16 v[72:75], v[176:179], v[216:219], v[72:75]
	v_mfma_f32_16x16x32_bf16 v[64:67], v[184:187], v[216:219], v[64:67]
	s_setprio 0
	s_barrier
	s_add_i32 s28, s68, s33
	s_mov_b32 m0, s28
	ds_read_b128 v[188:191], v168 offset:49152
	ds_read_b128 v[192:195], v168 offset:50176
	ds_read_b128 v[196:199], v168 offset:51200
	ds_read_b128 v[200:203], v168 offset:52224
	ds_read_b128 v[204:207], v168 offset:53248
	ds_read_b128 v[208:211], v168 offset:54272
	ds_read_b128 v[212:215], v168 offset:55296
	ds_read_b128 v[216:219], v168 offset:56320
	global_load_lds_dwordx4 v132, s[98:99]
	s_add_i32 m0, s28, 0x2000
	s_add_u32 s26, s26, 0x40080
	s_addc_u32 s27, s27, 0
	s_add_i32 s28, s69, s33
	global_load_lds_dwordx4 v128, s[98:99]
	s_mov_b32 m0, s28
	s_nop 0
	global_load_lds_dwordx4 v132, s[26:27]
	s_add_i32 m0, s28, 0x2000
	s_nop 0
	global_load_lds_dwordx4 v128, s[26:27]
	s_mov_b32 m0, s40
	s_nop 0
	global_load_lds_dwordx4 v134, s[100:101]
	s_mov_b32 m0, s41
	s_nop 0
	global_load_lds_dwordx4 v130, s[100:101]
	s_waitcnt vmcnt(8) lgkmcnt(0)
	s_barrier
	s_setprio 1
	v_mfma_f32_16x16x32_bf16 v[60:63], v[148:151], v[188:191], v[60:63]
	v_mfma_f32_16x16x32_bf16 v[52:55], v[156:159], v[188:191], v[52:55]
	v_mfma_f32_16x16x32_bf16 v[44:47], v[148:151], v[196:199], v[44:47]
	v_mfma_f32_16x16x32_bf16 v[36:39], v[156:159], v[196:199], v[36:39]
	v_mfma_f32_16x16x32_bf16 v[28:31], v[148:151], v[204:207], v[28:31]
	v_mfma_f32_16x16x32_bf16 v[20:23], v[156:159], v[204:207], v[20:23]
	v_mfma_f32_16x16x32_bf16 v[12:15], v[148:151], v[212:215], v[12:15]
	v_mfma_f32_16x16x32_bf16 v[4:7], v[156:159], v[212:215], v[4:7]
	v_mfma_f32_16x16x32_bf16 v[60:63], v[152:155], v[192:195], v[60:63]
	v_mfma_f32_16x16x32_bf16 v[52:55], v[160:163], v[192:195], v[52:55]
	v_mfma_f32_16x16x32_bf16 v[44:47], v[152:155], v[200:203], v[44:47]
	v_mfma_f32_16x16x32_bf16 v[36:39], v[160:163], v[200:203], v[36:39]
	v_mfma_f32_16x16x32_bf16 v[28:31], v[152:155], v[208:211], v[28:31]
	v_mfma_f32_16x16x32_bf16 v[20:23], v[160:163], v[208:211], v[20:23]
	v_mfma_f32_16x16x32_bf16 v[12:15], v[152:155], v[216:219], v[12:15]
	v_mfma_f32_16x16x32_bf16 v[4:7], v[160:163], v[216:219], v[4:7]
	s_setprio 0
	s_setprio 1
	v_mfma_f32_16x16x32_bf16 v[56:59], v[172:175], v[188:191], v[56:59]
	v_mfma_f32_16x16x32_bf16 v[48:51], v[180:183], v[188:191], v[48:51]
	v_mfma_f32_16x16x32_bf16 v[40:43], v[172:175], v[196:199], v[40:43]
	v_mfma_f32_16x16x32_bf16 v[32:35], v[180:183], v[196:199], v[32:35]
	v_mfma_f32_16x16x32_bf16 v[24:27], v[172:175], v[204:207], v[24:27]
	v_mfma_f32_16x16x32_bf16 v[16:19], v[180:183], v[204:207], v[16:19]
	v_mfma_f32_16x16x32_bf16 v[8:11], v[172:175], v[212:215], v[8:11]
	v_mfma_f32_16x16x32_bf16 v[0:3], v[180:183], v[212:215], v[0:3]
	v_mfma_f32_16x16x32_bf16 v[56:59], v[176:179], v[192:195], v[56:59]
	v_mfma_f32_16x16x32_bf16 v[48:51], v[184:187], v[192:195], v[48:51]
	v_mfma_f32_16x16x32_bf16 v[40:43], v[176:179], v[200:203], v[40:43]
	v_mfma_f32_16x16x32_bf16 v[32:35], v[184:187], v[200:203], v[32:35]
	v_mfma_f32_16x16x32_bf16 v[24:27], v[176:179], v[208:211], v[24:27]
	v_mfma_f32_16x16x32_bf16 v[16:19], v[184:187], v[208:211], v[16:19]
	v_mfma_f32_16x16x32_bf16 v[8:11], v[176:179], v[216:219], v[8:11]
	v_mfma_f32_16x16x32_bf16 v[0:3], v[184:187], v[216:219], v[0:3]
	s_setprio 0
	s_barrier
	s_add_i32 s67, s67, 2
	s_add_u32 s24, s24, 0x100
	s_addc_u32 s25, s25, 0
	s_add_u32 s65, s65, 0x100
	s_addc_u32 s66, s66, 0
	s_cmp_gt_u32 s67, 13
	s_cbranch_scc0 .LBB0_1867
	s_and_b64 vcc, exec, s[12:13]
	s_cbranch_vccz .LBB0_1870
	s_barrier

; #define PG8_STAGE(bufoff, gbase, voff) do { _Pragma("unroll") for (int _i = 0; _i < 2; ++_i) \
;         __builtin_amdgcn_global_load_lds((const unsigned*)((const char*)(gbase) + (voff)[_i]), (PG8_LAS unsigned*)(lds + (bufoff) + ldsw + _i * 8192), 16, 0, 0); } while (0)
; #define PG8_LDA(dst, b, h) do { _Pragma("unroll") for (int m = 0; m < 4; ++m) _Pragma("unroll") for (int k = 0; k < 2; ++k) dst[m][k] = *(const PG8_LAS bf16x8*)(lds + PG8_SA(b, h) + aoff + m * 2048 + k * 1024); } while (0)
; #define PG8_LDB(dst, b, h) do { _Pragma("unroll") for (int n = 0; n < 2; ++n) _Pragma("unroll") for (int k = 0; k < 2; ++k) dst[n][k] = *(const PG8_LAS bf16x8*)(lds + PG8_SB(b, h) + boff + n * 2048 + k * 1024); } while (0)
; template <class Epi, class Sched, bool ALIGN_EPI = false, bool SP2 = false>
; __device__ __forceinline__ void gemm_phase(PG8_LAS unsigned char* lds, const Gemm g, const Sched& S, const Epi& E, const int wid) {
;     ...
;         const bool has_next = S.next(ui + 1, nxt);
;         const char* nA = has_next ? (const char*)g.A + (size_t)nxt.pm * tstepA : cA; const char* nB = has_next ? (const char*)g.Bt + (size_t)nxt.pn * tstepB : cB;
;         for (int t = 0; t < nt; t += 2) {
;             const bool last = (t == nt - 2);
;             const char* a1 = cA + (size_t)(t + 1) * kstep;
;             const char* a2 = last ? nA : cA + (size_t)(t + 2) * kstep; const char* b2 = last ? nB : cB + (size_t)(t + 2) * kstep;
;             const char* a3 = a2 + kstep; const char* b3 = b2 + kstep;
;             if (last && has_next) S.a_ready(nxt);
;             if constexpr (SP2) {
;             PG8_LDB(B0, 0, 0); PG8_LDB(B1, 0, 1); PG8_SCHED; PG8_LDA(At, 0, 0); PG8_STAGE(PG8_SA(1, 1), a1 + hstepA, voffA);
;             PG8_WAIT_V(8); PG8_WAIT_L(0); PG8_BAR; PG8_MMA(0, 0, At, B0); PG8_MMA(0, 1, At, B1); PG8_BAR; PG8_SCHED;
;             PG8_LDA(At, 0, 1); PG8_STAGE(PG8_SB(0, 0), b2, voffB); PG8_STAGE(PG8_SB(0, 1), b2 + hstepB, voffB); PG8_STAGE(PG8_SA(0, 0), a2, voffA);
;             PG8_WAIT_V(8); PG8_WAIT_L(0); PG8_BAR; PG8_MMA(1, 0, At, B0); PG8_MMA(1, 1, At, B1); PG8_BAR; PG8_SCHED;
;             PG8_LDB(B0, 1, 0); PG8_LDB(B1, 1, 1); PG8_SCHED; PG8_LDA(At, 1, 0); PG8_STAGE(PG8_SA(0, 1), a2 + hstepA, voffA);
;             PG8_WAIT_V(8); PG8_WAIT_L(0); PG8_BAR; PG8_MMA(0, 0, At, B0); PG8_MMA(0, 1, At, B1); PG8_BAR; PG8_SCHED;
.LBB0_1951:
	s_add_u32 s66, s24, 0x100
	s_addc_u32 s67, s25, 0
	s_mov_b32 s68, -2
	s_waitcnt lgkmcnt(0)
	v_add_u32_e32 v252, 0x18000, v189
	v_add_u32_e32 v253, 0x1c000, v189
	ds_read_b128 v[128:131], v190
	ds_read_b128 v[132:135], v190 offset:1024
	ds_read_b128 v[136:139], v190 offset:2048
	ds_read_b128 v[140:143], v190 offset:3072
	ds_read_b128 v[144:147], v191
	ds_read_b128 v[148:151], v191 offset:1024
	ds_read_b128 v[172:175], v191 offset:2048
	ds_read_b128 v[176:179], v191 offset:3072
	s_add_u32 s24, s22, 0x100
	s_addc_u32 s25, s23, 0
	s_cmp_eq_u32 s68, 40
	s_cselect_b32 s29, s7, s25
	s_cselect_b32 s28, s6, s24
	s_cselect_b32 s27, s21, s67
	s_cselect_b32 s26, s20, s66
	s_add_i32 m0, s34, 0xc000
	ds_read_b128 v[180:183], v192
	ds_read_b128 v[184:187], v192 offset:1024
	ds_read_b128 v[194:197], v192 offset:2048
	ds_read_b128 v[198:201], v192 offset:3072
	ds_read_b128 v[202:205], v192 offset:4096
	ds_read_b128 v[206:209], v192 offset:5120
	ds_read_b128 v[210:213], v192 offset:6144
	ds_read_b128 v[214:217], v192 offset:7168
	global_load_lds_dwordx4 v164, s[22:23]
	s_add_i32 m0, s34, 0xe000
	s_nop 0
	global_load_lds_dwordx4 v166, s[22:23]
	s_waitcnt vmcnt(8) lgkmcnt(0)
	s_barrier
	s_setprio 1
	v_mfma_f32_16x16x32_bf16 v[124:127], v[128:131], v[180:183], 0
	v_mfma_f32_16x16x32_bf16 v[120:123], v[136:139], v[180:183], 0
	v_mfma_f32_16x16x32_bf16 v[108:111], v[128:131], v[194:197], 0
	v_mfma_f32_16x16x32_bf16 v[104:107], v[136:139], v[194:197], 0
	v_mfma_f32_16x16x32_bf16 v[92:95], v[128:131], v[202:205], 0
	v_mfma_f32_16x16x32_bf16 v[88:91], v[136:139], v[202:205], 0
	v_mfma_f32_16x16x32_bf16 v[76:79], v[128:131], v[210:213], 0
	v_mfma_f32_16x16x32_bf16 v[72:75], v[136:139], v[210:213], 0
	v_mfma_f32_16x16x32_bf16 v[124:127], v[132:135], v[184:187], v[124:127]
	v_mfma_f32_16x16x32_bf16 v[120:123], v[140:143], v[184:187], v[120:123]
	v_mfma_f32_16x16x32_bf16 v[108:111], v[132:135], v[198:201], v[108:111]
	v_mfma_f32_16x16x32_bf16 v[104:107], v[140:143], v[198:201], v[104:107]
	v_mfma_f32_16x16x32_bf16 v[92:95], v[132:135], v[206:209], v[92:95]
	v_mfma_f32_16x16x32_bf16 v[88:91], v[140:143], v[206:209], v[88:91]
	v_mfma_f32_16x16x32_bf16 v[76:79], v[132:135], v[214:217], v[76:79]
	v_mfma_f32_16x16x32_bf16 v[72:75], v[140:143], v[214:217], v[72:75]
	s_setprio 0
	s_setprio 1
	v_mfma_f32_16x16x32_bf16 v[116:119], v[144:147], v[180:183], 0
	v_mfma_f32_16x16x32_bf16 v[112:115], v[172:175], v[180:183], 0
	v_mfma_f32_16x16x32_bf16 v[100:103], v[144:147], v[194:197], 0
	v_mfma_f32_16x16x32_bf16 v[96:99], v[172:175], v[194:197], 0
	v_mfma_f32_16x16x32_bf16 v[84:87], v[144:147], v[202:205], 0
	v_mfma_f32_16x16x32_bf16 v[80:83], v[172:175], v[202:205], 0
	v_mfma_f32_16x16x32_bf16 v[68:71], v[144:147], v[210:213], 0
	v_mfma_f32_16x16x32_bf16 v[64:67], v[172:175], v[210:213], 0
	v_mfma_f32_16x16x32_bf16 v[116:119], v[148:151], v[184:187], v[116:119]
	v_mfma_f32_16x16x32_bf16 v[112:115], v[176:179], v[184:187], v[112:115]
	v_mfma_f32_16x16x32_bf16 v[100:103], v[148:151], v[198:201], v[100:103]
	v_mfma_f32_16x16x32_bf16 v[96:99], v[176:179], v[198:201], v[96:99]
	v_mfma_f32_16x16x32_bf16 v[84:87], v[148:151], v[206:209], v[84:87]
	v_mfma_f32_16x16x32_bf16 v[80:83], v[176:179], v[206:209], v[80:83]
	v_mfma_f32_16x16x32_bf16 v[68:71], v[148:151], v[214:217], v[68:71]
	v_mfma_f32_16x16x32_bf16 v[64:67], v[176:179], v[214:217], v[64:67]
	s_setprio 0
	s_barrier
	s_add_i32 s22, s45, s33
	s_add_u32 s98, s26, 0x80
	s_addc_u32 s99, s27, 0
	s_mov_b32 m0, s22
	ds_read_b128 v[180:183], v192 offset:16384
	ds_read_b128 v[184:187], v192 offset:17408
	ds_read_b128 v[194:197], v192 offset:18432
	ds_read_b128 v[198:201], v192 offset:19456
	ds_read_b128 v[202:205], v192 offset:20480
	ds_read_b128 v[206:209], v192 offset:21504
	ds_read_b128 v[210:213], v192 offset:22528
	ds_read_b128 v[214:217], v192 offset:23552
	global_load_lds_dwordx4 v154, s[26:27]
	s_add_i32 m0, s22, 0x2000
	s_add_u32 s22, s26, 0xb0000
	s_addc_u32 s23, s27, 0
	s_add_i32 s69, s46, s33
	global_load_lds_dwordx4 v158, s[26:27]
	s_mov_b32 m0, s69
	s_add_u32 s100, s28, 0x80
	s_addc_u32 s101, s29, 0
	global_load_lds_dwordx4 v154, s[22:23]
	s_add_i32 m0, s69, 0x2000
	s_nop 0
	global_load_lds_dwordx4 v158, s[22:23]
	s_mov_b32 m0, s34
	s_nop 0
	global_load_lds_dwordx4 v152, s[28:29]
	s_mov_b32 m0, s35
	s_nop 0
	global_load_lds_dwordx4 v156, s[28:29]
	s_waitcnt vmcnt(8) lgkmcnt(0)
	s_barrier
	s_nop 0
	s_setprio 1
	v_mfma_f32_16x16x32_bf16 v[60:63], v[128:131], v[180:183], 0
	v_mfma_f32_16x16x32_bf16 v[56:59], v[136:139], v[180:183], 0
	v_mfma_f32_16x16x32_bf16 v[44:47], v[128:131], v[194:197], 0
	v_mfma_f32_16x16x32_bf16 v[40:43], v[136:139], v[194:197], 0
	v_mfma_f32_16x16x32_bf16 v[28:31], v[128:131], v[202:205], 0
	v_mfma_f32_16x16x32_bf16 v[24:27], v[136:139], v[202:205], 0
	v_mfma_f32_16x16x32_bf16 v[12:15], v[128:131], v[210:213], 0
	v_mfma_f32_16x16x32_bf16 v[8:11], v[136:139], v[210:213], 0
	v_mfma_f32_16x16x32_bf16 v[60:63], v[132:135], v[184:187], v[60:63]
	v_mfma_f32_16x16x32_bf16 v[56:59], v[140:143], v[184:187], v[56:59]
	v_mfma_f32_16x16x32_bf16 v[44:47], v[132:135], v[198:201], v[44:47]
	v_mfma_f32_16x16x32_bf16 v[40:43], v[140:143], v[198:201], v[40:43]
	v_mfma_f32_16x16x32_bf16 v[28:31], v[132:135], v[206:209], v[28:31]
	v_mfma_f32_16x16x32_bf16 v[24:27], v[140:143], v[206:209], v[24:27]
	v_mfma_f32_16x16x32_bf16 v[12:15], v[132:135], v[214:217], v[12:15]
	v_mfma_f32_16x16x32_bf16 v[8:11], v[140:143], v[214:217], v[8:11]
	s_setprio 0
	s_setprio 1
	v_mfma_f32_16x16x32_bf16 v[52:55], v[144:147], v[180:183], 0
	v_mfma_f32_16x16x32_bf16 v[48:51], v[172:175], v[180:183], 0
	v_mfma_f32_16x16x32_bf16 v[36:39], v[144:147], v[194:197], 0
	v_mfma_f32_16x16x32_bf16 v[32:35], v[172:175], v[194:197], 0
	v_mfma_f32_16x16x32_bf16 v[20:23], v[144:147], v[202:205], 0
	v_mfma_f32_16x16x32_bf16 v[16:19], v[172:175], v[202:205], 0
	v_mfma_f32_16x16x32_bf16 v[4:7], v[144:147], v[210:213], 0
	v_mfma_f32_16x16x32_bf16 v[0:3], v[172:175], v[210:213], 0
	v_mfma_f32_16x16x32_bf16 v[52:55], v[148:151], v[184:187], v[52:55]
	v_mfma_f32_16x16x32_bf16 v[48:51], v[176:179], v[184:187], v[48:51]
	v_mfma_f32_16x16x32_bf16 v[36:39], v[148:151], v[198:201], v[36:39]
	v_mfma_f32_16x16x32_bf16 v[32:35], v[176:179], v[198:201], v[32:35]
	v_mfma_f32_16x16x32_bf16 v[20:23], v[148:151], v[206:209], v[20:23]
	v_mfma_f32_16x16x32_bf16 v[16:19], v[176:179], v[206:209], v[16:19]
	v_mfma_f32_16x16x32_bf16 v[4:7], v[148:151], v[214:217], v[4:7]
	v_mfma_f32_16x16x32_bf16 v[0:3], v[176:179], v[214:217], v[0:3]
	s_setprio 0
	s_barrier
; #define PG8_STAGE(bufoff, gbase, voff) do { _Pragma("unroll") for (int _i = 0; _i < 2; ++_i) \
;         __builtin_amdgcn_global_load_lds((const unsigned*)((const char*)(gbase) + (voff)[_i]), (PG8_LAS unsigned*)(lds + (bufoff) + ldsw + _i * 8192), 16, 0, 0); } while (0)
; #define PG8_LDA(dst, b, h) do { _Pragma("unroll") for (int m = 0; m < 4; ++m) _Pragma("unroll") for (int k = 0; k < 2; ++k) dst[m][k] = *(const PG8_LAS bf16x8*)(lds + PG8_SA(b, h) + aoff + m * 2048 + k * 1024); } while (0)
; #define PG8_LDB(dst, b, h) do { _Pragma("unroll") for (int n = 0; n < 2; ++n) _Pragma("unroll") for (int k = 0; k < 2; ++k) dst[n][k] = *(const PG8_LAS bf16x8*)(lds + PG8_SB(b, h) + boff + n * 2048 + k * 1024); } while (0)
; #define PG8_MMA(ai, bj, At, Bt) do { __builtin_amdgcn_s_setprio(1); _Pragma("unroll") for (int m = 0; m < 4; ++m) _Pragma("unroll") for (int n = 0; n < 2; ++n) _Pragma("unroll") for (int k = 0; k < 2; ++k) \
;         acc[ai][bj][m][n] = __builtin_amdgcn_mfma_f32_16x16x32_bf16(Bt[n][k], At[m][k], acc[ai][bj][m][n], 0, 0, 0); __builtin_amdgcn_s_setprio(0); } while (0)
; #define PG8_WAIT_V(n) asm volatile("s_waitcnt vmcnt(" #n ")" ::: "memory")
; #define PG8_WAIT_L(n) asm volatile("s_waitcnt lgkmcnt(" #n ")" ::: "memory")
; #define PG8_BAR __builtin_amdgcn_s_barrier()
; #define PG8_SCHED __builtin_amdgcn_sched_barrier(0)
; template <class Epi, class Sched, bool ALIGN_EPI = false, bool SP2 = false>
; __device__ __forceinline__ void gemm_phase(PG8_LAS unsigned char* lds, const Gemm g, const Sched& S, const Epi& E, const int wid) {
;     ...
;             PG8_LDB(B0, 1, 0); PG8_LDB(B1, 1, 1); PG8_SCHED; PG8_LDA(At, 1, 0); PG8_STAGE(PG8_SA(0, 1), a2 + hstepA, voffA);
;             PG8_WAIT_V(8); PG8_WAIT_L(0); PG8_BAR; PG8_MMA(0, 0, At, B0); PG8_MMA(0, 1, At, B1); PG8_BAR; PG8_SCHED;
;             PG8_LDA(At, 1, 1); PG8_STAGE(PG8_SB(1, 0), b3, voffB); PG8_STAGE(PG8_SB(1, 1), b3 + hstepB, voffB); PG8_STAGE(PG8_SA(1, 0), a3, voffA);
;             PG8_WAIT_V(8); PG8_WAIT_L(0); PG8_BAR; PG8_MMA(1, 0, At, B0); PG8_MMA(1, 1, At, B1); PG8_BAR; PG8_SCHED;
	s_add_i32 s69, 0, 0x18000
	s_add_i32 s70, 0, 0x1c000
	ds_read_b128 v[128:131], v252
	ds_read_b128 v[132:135], v252 offset:1024
	ds_read_b128 v[136:139], v252 offset:2048
	ds_read_b128 v[140:143], v252 offset:3072
	ds_read_b128 v[144:147], v253
	ds_read_b128 v[148:151], v253 offset:1024
	ds_read_b128 v[172:175], v253 offset:2048
	ds_read_b128 v[176:179], v253 offset:3072
	s_add_u32 s22, s28, 0xb0000
	s_addc_u32 s23, s29, 0
	s_mov_b32 m0, s36
	ds_read_b128 v[180:183], v192 offset:32768
	ds_read_b128 v[184:187], v192 offset:33792
	ds_read_b128 v[194:197], v192 offset:34816
	ds_read_b128 v[198:201], v192 offset:35840
	ds_read_b128 v[202:205], v192 offset:36864
	ds_read_b128 v[206:209], v192 offset:37888
	ds_read_b128 v[210:213], v192 offset:38912
	ds_read_b128 v[214:217], v192 offset:39936
	global_load_lds_dwordx4 v152, s[22:23]
	s_mov_b32 m0, s37
	s_nop 0
	global_load_lds_dwordx4 v156, s[22:23]
	s_waitcnt vmcnt(8) lgkmcnt(0)
	s_barrier
	s_nop 0
	s_setprio 1
	v_mfma_f32_16x16x32_bf16 v[124:127], v[128:131], v[180:183], v[124:127]
	v_mfma_f32_16x16x32_bf16 v[120:123], v[136:139], v[180:183], v[120:123]
	v_mfma_f32_16x16x32_bf16 v[108:111], v[128:131], v[194:197], v[108:111]
	v_mfma_f32_16x16x32_bf16 v[104:107], v[136:139], v[194:197], v[104:107]
	v_mfma_f32_16x16x32_bf16 v[92:95], v[128:131], v[202:205], v[92:95]
	v_mfma_f32_16x16x32_bf16 v[88:91], v[136:139], v[202:205], v[88:91]
	v_mfma_f32_16x16x32_bf16 v[76:79], v[128:131], v[210:213], v[76:79]
	v_mfma_f32_16x16x32_bf16 v[72:75], v[136:139], v[210:213], v[72:75]
	v_mfma_f32_16x16x32_bf16 v[124:127], v[132:135], v[184:187], v[124:127]
	v_mfma_f32_16x16x32_bf16 v[120:123], v[140:143], v[184:187], v[120:123]
	v_mfma_f32_16x16x32_bf16 v[108:111], v[132:135], v[198:201], v[108:111]
	v_mfma_f32_16x16x32_bf16 v[104:107], v[140:143], v[198:201], v[104:107]
	v_mfma_f32_16x16x32_bf16 v[92:95], v[132:135], v[206:209], v[92:95]
	v_mfma_f32_16x16x32_bf16 v[88:91], v[140:143], v[206:209], v[88:91]
	v_mfma_f32_16x16x32_bf16 v[76:79], v[132:135], v[214:217], v[76:79]
	v_mfma_f32_16x16x32_bf16 v[72:75], v[140:143], v[214:217], v[72:75]
	s_setprio 0
	s_setprio 1
	v_mfma_f32_16x16x32_bf16 v[116:119], v[144:147], v[180:183], v[116:119]
	v_mfma_f32_16x16x32_bf16 v[112:115], v[172:175], v[180:183], v[112:115]
	v_mfma_f32_16x16x32_bf16 v[100:103], v[144:147], v[194:197], v[100:103]
	v_mfma_f32_16x16x32_bf16 v[96:99], v[172:175], v[194:197], v[96:99]
	v_mfma_f32_16x16x32_bf16 v[84:87], v[144:147], v[202:205], v[84:87]
	v_mfma_f32_16x16x32_bf16 v[80:83], v[172:175], v[202:205], v[80:83]
	v_mfma_f32_16x16x32_bf16 v[68:71], v[144:147], v[210:213], v[68:71]
	v_mfma_f32_16x16x32_bf16 v[64:67], v[172:175], v[210:213], v[64:67]
	v_mfma_f32_16x16x32_bf16 v[116:119], v[148:151], v[184:187], v[116:119]
	v_mfma_f32_16x16x32_bf16 v[112:115], v[176:179], v[184:187], v[112:115]
	v_mfma_f32_16x16x32_bf16 v[100:103], v[148:151], v[198:201], v[100:103]
	v_mfma_f32_16x16x32_bf16 v[96:99], v[176:179], v[198:201], v[96:99]
	v_mfma_f32_16x16x32_bf16 v[84:87], v[148:151], v[206:209], v[84:87]
	v_mfma_f32_16x16x32_bf16 v[80:83], v[176:179], v[206:209], v[80:83]
	v_mfma_f32_16x16x32_bf16 v[68:71], v[148:151], v[214:217], v[68:71]
	v_mfma_f32_16x16x32_bf16 v[64:67], v[176:179], v[214:217], v[64:67]
	s_setprio 0
	s_barrier
	s_add_i32 s22, s69, s33
	s_mov_b32 m0, s22
	ds_read_b128 v[180:183], v192 offset:49152
	ds_read_b128 v[184:187], v192 offset:50176
	ds_read_b128 v[194:197], v192 offset:51200
	ds_read_b128 v[198:201], v192 offset:52224
	ds_read_b128 v[202:205], v192 offset:53248
	ds_read_b128 v[206:209], v192 offset:54272
	ds_read_b128 v[210:213], v192 offset:55296
	ds_read_b128 v[214:217], v192 offset:56320
	global_load_lds_dwordx4 v154, s[98:99]
	s_add_i32 m0, s22, 0x2000
	s_add_u32 s22, s26, 0xb0080
	s_addc_u32 s23, s27, 0
	s_add_i32 s26, s70, s33
	global_load_lds_dwordx4 v158, s[98:99]
	s_mov_b32 m0, s26
	s_nop 0
	global_load_lds_dwordx4 v154, s[22:23]
	s_add_i32 m0, s26, 0x2000
	s_nop 0
	global_load_lds_dwordx4 v158, s[22:23]
	s_mov_b32 m0, s39
	s_nop 0
	global_load_lds_dwordx4 v152, s[100:101]
	s_mov_b32 m0, s40
	s_nop 0
	global_load_lds_dwordx4 v156, s[100:101]
	s_waitcnt vmcnt(8) lgkmcnt(0)
	s_barrier
	s_setprio 1
	v_mfma_f32_16x16x32_bf16 v[60:63], v[128:131], v[180:183], v[60:63]
	v_mfma_f32_16x16x32_bf16 v[56:59], v[136:139], v[180:183], v[56:59]
	v_mfma_f32_16x16x32_bf16 v[44:47], v[128:131], v[194:197], v[44:47]
	v_mfma_f32_16x16x32_bf16 v[40:43], v[136:139], v[194:197], v[40:43]
	v_mfma_f32_16x16x32_bf16 v[28:31], v[128:131], v[202:205], v[28:31]
	v_mfma_f32_16x16x32_bf16 v[24:27], v[136:139], v[202:205], v[24:27]
	v_mfma_f32_16x16x32_bf16 v[12:15], v[128:131], v[210:213], v[12:15]
	v_mfma_f32_16x16x32_bf16 v[8:11], v[136:139], v[210:213], v[8:11]
	v_mfma_f32_16x16x32_bf16 v[60:63], v[132:135], v[184:187], v[60:63]
	v_mfma_f32_16x16x32_bf16 v[56:59], v[140:143], v[184:187], v[56:59]
	v_mfma_f32_16x16x32_bf16 v[44:47], v[132:135], v[198:201], v[44:47]
	v_mfma_f32_16x16x32_bf16 v[40:43], v[140:143], v[198:201], v[40:43]
	v_mfma_f32_16x16x32_bf16 v[28:31], v[132:135], v[206:209], v[28:31]
	v_mfma_f32_16x16x32_bf16 v[24:27], v[140:143], v[206:209], v[24:27]
	v_mfma_f32_16x16x32_bf16 v[12:15], v[132:135], v[214:217], v[12:15]
	v_mfma_f32_16x16x32_bf16 v[8:11], v[140:143], v[214:217], v[8:11]
	s_setprio 0
	s_setprio 1
	v_mfma_f32_16x16x32_bf16 v[52:55], v[144:147], v[180:183], v[52:55]
	v_mfma_f32_16x16x32_bf16 v[48:51], v[172:175], v[180:183], v[48:51]
	v_mfma_f32_16x16x32_bf16 v[36:39], v[144:147], v[194:197], v[36:39]
	v_mfma_f32_16x16x32_bf16 v[32:35], v[172:175], v[194:197], v[32:35]
	v_mfma_f32_16x16x32_bf16 v[20:23], v[144:147], v[202:205], v[20:23]
	v_mfma_f32_16x16x32_bf16 v[16:19], v[172:175], v[202:205], v[16:19]
	v_mfma_f32_16x16x32_bf16 v[4:7], v[144:147], v[210:213], v[4:7]
	v_mfma_f32_16x16x32_bf16 v[0:3], v[172:175], v[210:213], v[0:3]
	v_mfma_f32_16x16x32_bf16 v[52:55], v[148:151], v[184:187], v[52:55]
	v_mfma_f32_16x16x32_bf16 v[48:51], v[176:179], v[184:187], v[48:51]
	v_mfma_f32_16x16x32_bf16 v[36:39], v[148:151], v[198:201], v[36:39]
	v_mfma_f32_16x16x32_bf16 v[32:35], v[176:179], v[198:201], v[32:35]
	v_mfma_f32_16x16x32_bf16 v[20:23], v[148:151], v[206:209], v[20:23]
	v_mfma_f32_16x16x32_bf16 v[16:19], v[176:179], v[206:209], v[16:19]
	v_mfma_f32_16x16x32_bf16 v[4:7], v[148:151], v[214:217], v[4:7]
	v_mfma_f32_16x16x32_bf16 v[0:3], v[176:179], v[214:217], v[0:3]
	s_setprio 0
	s_barrier
	s_add_i32 s68, s68, 2
	s_add_u32 s66, s66, 0x100
	s_addc_u32 s67, s67, 0
	s_cmp_gt_u32 s68, 41
	s_mov_b64 s[22:23], s[24:25]
; #define PG8_STAGE(bufoff, gbase, voff) do { _Pragma("unroll") for (int _i = 0; _i < 2; ++_i) \
;         __builtin_amdgcn_global_load_lds((const unsigned*)((const char*)(gbase) + (voff)[_i]), (PG8_LAS unsigned*)(lds + (bufoff) + ldsw + _i * 8192), 16, 0, 0); } while (0)
; #define PG8_LDA(dst, b, h) do { _Pragma("unroll") for (int m = 0; m < 4; ++m) _Pragma("unroll") for (int k = 0; k < 2; ++k) dst[m][k] = *(const PG8_LAS bf16x8*)(lds + PG8_SA(b, h) + aoff + m * 2048 + k * 1024); } while (0)
; #define PG8_LDB(dst, b, h) do { _Pragma("unroll") for (int n = 0; n < 2; ++n) _Pragma("unroll") for (int k = 0; k < 2; ++k) dst[n][k] = *(const PG8_LAS bf16x8*)(lds + PG8_SB(b, h) + boff + n * 2048 + k * 1024); } while (0)
; #define PG8_MMA(ai, bj, At, Bt) do { __builtin_amdgcn_s_setprio(1); _Pragma("unroll") for (int m = 0; m < 4; ++m) _Pragma("unroll") for (int n = 0; n < 2; ++n) _Pragma("unroll") for (int k = 0; k < 2; ++k) \
;         acc[ai][bj][m][n] = __builtin_amdgcn_mfma_f32_16x16x32_bf16(Bt[n][k], At[m][k], acc[ai][bj][m][n], 0, 0, 0); __builtin_amdgcn_s_setprio(0); } while (0)
; #define PG8_WAIT_V(n) asm volatile("s_waitcnt vmcnt(" #n ")" ::: "memory")
; #define PG8_BAR __builtin_amdgcn_s_barrier()
; template <class Epi, class Sched, bool ALIGN_EPI = false, bool SP2 = false>
; __device__ __forceinline__ void gemm_phase(PG8_LAS unsigned char* lds, const Gemm g, const Sched& S, const Epi& E, const int wid) {
;     ...
;         for (int t = 0; t < nt; t += 2) {
;             const bool last = (t == nt - 2);
;             const char* a1 = cA + (size_t)(t + 1) * kstep;
;             const char* a2 = last ? nA : cA + (size_t)(t + 2) * kstep; const char* b2 = last ? nB : cB + (size_t)(t + 2) * kstep;
;             const char* a3 = a2 + kstep; const char* b3 = b2 + kstep;
;             if (last && has_next) S.a_ready(nxt);
;             if constexpr (SP2) {
;             PG8_LDB(B0, 0, 0); PG8_LDB(B1, 0, 1); PG8_SCHED; PG8_LDA(At, 0, 0); PG8_STAGE(PG8_SA(1, 1), a1 + hstepA, voffA);
;             PG8_WAIT_V(8); PG8_WAIT_L(0); PG8_BAR; PG8_MMA(0, 0, At, B0); PG8_MMA(0, 1, At, B1); PG8_BAR; PG8_SCHED;
;             PG8_LDA(At, 0, 1); PG8_STAGE(PG8_SB(0, 0), b2, voffB); PG8_STAGE(PG8_SB(0, 1), b2 + hstepB, voffB); PG8_STAGE(PG8_SA(0, 0), a2, voffA);
;             PG8_WAIT_V(8); PG8_WAIT_L(0); PG8_BAR; PG8_MMA(1, 0, At, B0); PG8_MMA(1, 1, At, B1); PG8_BAR; PG8_SCHED;
.LBB0_1952:
	ds_read_b128 v[128:131], v190
	ds_read_b128 v[132:135], v190 offset:1024
	ds_read_b128 v[136:139], v190 offset:2048
	ds_read_b128 v[140:143], v190 offset:3072
	ds_read_b128 v[144:147], v191
	ds_read_b128 v[148:151], v191 offset:1024
	ds_read_b128 v[172:175], v191 offset:2048
	ds_read_b128 v[176:179], v191 offset:3072
	s_add_u32 s24, s22, 0x100
	s_addc_u32 s25, s23, 0
	s_cmp_eq_u32 s68, 40
	s_cselect_b32 s29, s7, s25
	s_cselect_b32 s28, s6, s24
	s_cselect_b32 s27, s21, s67
	s_cselect_b32 s26, s20, s66
	s_add_i32 m0, s34, 0xc000
	ds_read_b128 v[180:183], v192
	ds_read_b128 v[184:187], v192 offset:1024
	ds_read_b128 v[194:197], v192 offset:2048
	ds_read_b128 v[198:201], v192 offset:3072
	ds_read_b128 v[202:205], v192 offset:4096
	ds_read_b128 v[206:209], v192 offset:5120
	ds_read_b128 v[210:213], v192 offset:6144
	ds_read_b128 v[214:217], v192 offset:7168
	global_load_lds_dwordx4 v164, s[22:23]
	s_add_i32 m0, s34, 0xe000
	s_nop 0
	global_load_lds_dwordx4 v166, s[22:23]
	s_waitcnt vmcnt(8) lgkmcnt(0)
	s_barrier
	s_setprio 1
	v_mfma_f32_16x16x32_bf16 v[124:127], v[128:131], v[180:183], v[124:127]
	v_mfma_f32_16x16x32_bf16 v[120:123], v[136:139], v[180:183], v[120:123]
	v_mfma_f32_16x16x32_bf16 v[108:111], v[128:131], v[194:197], v[108:111]
	v_mfma_f32_16x16x32_bf16 v[104:107], v[136:139], v[194:197], v[104:107]
	v_mfma_f32_16x16x32_bf16 v[92:95], v[128:131], v[202:205], v[92:95]
	v_mfma_f32_16x16x32_bf16 v[88:91], v[136:139], v[202:205], v[88:91]
	v_mfma_f32_16x16x32_bf16 v[76:79], v[128:131], v[210:213], v[76:79]
	v_mfma_f32_16x16x32_bf16 v[72:75], v[136:139], v[210:213], v[72:75]
	v_mfma_f32_16x16x32_bf16 v[124:127], v[132:135], v[184:187], v[124:127]
	v_mfma_f32_16x16x32_bf16 v[120:123], v[140:143], v[184:187], v[120:123]
	v_mfma_f32_16x16x32_bf16 v[108:111], v[132:135], v[198:201], v[108:111]
	v_mfma_f32_16x16x32_bf16 v[104:107], v[140:143], v[198:201], v[104:107]
	v_mfma_f32_16x16x32_bf16 v[92:95], v[132:135], v[206:209], v[92:95]
	v_mfma_f32_16x16x32_bf16 v[88:91], v[140:143], v[206:209], v[88:91]
	v_mfma_f32_16x16x32_bf16 v[76:79], v[132:135], v[214:217], v[76:79]
	v_mfma_f32_16x16x32_bf16 v[72:75], v[140:143], v[214:217], v[72:75]
	s_setprio 0
	s_setprio 1
	v_mfma_f32_16x16x32_bf16 v[116:119], v[144:147], v[180:183], v[116:119]
	v_mfma_f32_16x16x32_bf16 v[112:115], v[172:175], v[180:183], v[112:115]
	v_mfma_f32_16x16x32_bf16 v[100:103], v[144:147], v[194:197], v[100:103]
	v_mfma_f32_16x16x32_bf16 v[96:99], v[172:175], v[194:197], v[96:99]
	v_mfma_f32_16x16x32_bf16 v[84:87], v[144:147], v[202:205], v[84:87]
	v_mfma_f32_16x16x32_bf16 v[80:83], v[172:175], v[202:205], v[80:83]
	v_mfma_f32_16x16x32_bf16 v[68:71], v[144:147], v[210:213], v[68:71]
	v_mfma_f32_16x16x32_bf16 v[64:67], v[172:175], v[210:213], v[64:67]
	v_mfma_f32_16x16x32_bf16 v[116:119], v[148:151], v[184:187], v[116:119]
	v_mfma_f32_16x16x32_bf16 v[112:115], v[176:179], v[184:187], v[112:115]
	v_mfma_f32_16x16x32_bf16 v[100:103], v[148:151], v[198:201], v[100:103]
	v_mfma_f32_16x16x32_bf16 v[96:99], v[176:179], v[198:201], v[96:99]
	v_mfma_f32_16x16x32_bf16 v[84:87], v[148:151], v[206:209], v[84:87]
	v_mfma_f32_16x16x32_bf16 v[80:83], v[176:179], v[206:209], v[80:83]
	v_mfma_f32_16x16x32_bf16 v[68:71], v[148:151], v[214:217], v[68:71]
	v_mfma_f32_16x16x32_bf16 v[64:67], v[176:179], v[214:217], v[64:67]
	s_setprio 0
	s_barrier
	s_add_i32 s22, s45, s33
	s_add_u32 s98, s26, 0x80
	s_addc_u32 s99, s27, 0
	s_mov_b32 m0, s22
	ds_read_b128 v[180:183], v192 offset:16384
	ds_read_b128 v[184:187], v192 offset:17408
	ds_read_b128 v[194:197], v192 offset:18432
	ds_read_b128 v[198:201], v192 offset:19456
	ds_read_b128 v[202:205], v192 offset:20480
	ds_read_b128 v[206:209], v192 offset:21504
	ds_read_b128 v[210:213], v192 offset:22528
	ds_read_b128 v[214:217], v192 offset:23552
	global_load_lds_dwordx4 v154, s[26:27]
	s_add_i32 m0, s22, 0x2000
	s_add_u32 s22, s26, 0xb0000
	s_addc_u32 s23, s27, 0
	s_add_i32 s69, s46, s33
	global_load_lds_dwordx4 v158, s[26:27]
	s_mov_b32 m0, s69
	s_add_u32 s100, s28, 0x80
	s_addc_u32 s101, s29, 0
	global_load_lds_dwordx4 v154, s[22:23]
	s_add_i32 m0, s69, 0x2000
	s_nop 0
	global_load_lds_dwordx4 v158, s[22:23]
	s_mov_b32 m0, s34
	s_nop 0
	global_load_lds_dwordx4 v152, s[28:29]
	s_mov_b32 m0, s35
	s_nop 0
	global_load_lds_dwordx4 v156, s[28:29]
	s_waitcnt vmcnt(8) lgkmcnt(0)
	s_barrier
	s_nop 0
	s_setprio 1
	v_mfma_f32_16x16x32_bf16 v[60:63], v[128:131], v[180:183], v[60:63]
	v_mfma_f32_16x16x32_bf16 v[56:59], v[136:139], v[180:183], v[56:59]
	v_mfma_f32_16x16x32_bf16 v[44:47], v[128:131], v[194:197], v[44:47]
	v_mfma_f32_16x16x32_bf16 v[40:43], v[136:139], v[194:197], v[40:43]
	v_mfma_f32_16x16x32_bf16 v[28:31], v[128:131], v[202:205], v[28:31]
	v_mfma_f32_16x16x32_bf16 v[24:27], v[136:139], v[202:205], v[24:27]
	v_mfma_f32_16x16x32_bf16 v[12:15], v[128:131], v[210:213], v[12:15]
	v_mfma_f32_16x16x32_bf16 v[8:11], v[136:139], v[210:213], v[8:11]
	v_mfma_f32_16x16x32_bf16 v[60:63], v[132:135], v[184:187], v[60:63]
	v_mfma_f32_16x16x32_bf16 v[56:59], v[140:143], v[184:187], v[56:59]
	v_mfma_f32_16x16x32_bf16 v[44:47], v[132:135], v[198:201], v[44:47]
	v_mfma_f32_16x16x32_bf16 v[40:43], v[140:143], v[198:201], v[40:43]
	v_mfma_f32_16x16x32_bf16 v[28:31], v[132:135], v[206:209], v[28:31]
	v_mfma_f32_16x16x32_bf16 v[24:27], v[140:143], v[206:209], v[24:27]
	v_mfma_f32_16x16x32_bf16 v[12:15], v[132:135], v[214:217], v[12:15]
	v_mfma_f32_16x16x32_bf16 v[8:11], v[140:143], v[214:217], v[8:11]
	s_setprio 0
	s_setprio 1
	v_mfma_f32_16x16x32_bf16 v[52:55], v[144:147], v[180:183], v[52:55]
	v_mfma_f32_16x16x32_bf16 v[48:51], v[172:175], v[180:183], v[48:51]
	v_mfma_f32_16x16x32_bf16 v[36:39], v[144:147], v[194:197], v[36:39]
	v_mfma_f32_16x16x32_bf16 v[32:35], v[172:175], v[194:197], v[32:35]
	v_mfma_f32_16x16x32_bf16 v[20:23], v[144:147], v[202:205], v[20:23]
	v_mfma_f32_16x16x32_bf16 v[16:19], v[172:175], v[202:205], v[16:19]
	v_mfma_f32_16x16x32_bf16 v[4:7], v[144:147], v[210:213], v[4:7]
	v_mfma_f32_16x16x32_bf16 v[0:3], v[172:175], v[210:213], v[0:3]
	v_mfma_f32_16x16x32_bf16 v[52:55], v[148:151], v[184:187], v[52:55]
	v_mfma_f32_16x16x32_bf16 v[48:51], v[176:179], v[184:187], v[48:51]
	v_mfma_f32_16x16x32_bf16 v[36:39], v[148:151], v[198:201], v[36:39]
	v_mfma_f32_16x16x32_bf16 v[32:35], v[176:179], v[198:201], v[32:35]
	v_mfma_f32_16x16x32_bf16 v[20:23], v[148:151], v[206:209], v[20:23]
	v_mfma_f32_16x16x32_bf16 v[16:19], v[176:179], v[206:209], v[16:19]
	v_mfma_f32_16x16x32_bf16 v[4:7], v[148:151], v[214:217], v[4:7]
	v_mfma_f32_16x16x32_bf16 v[0:3], v[176:179], v[214:217], v[0:3]
	s_setprio 0
	s_barrier
; #define PG8_STAGE(bufoff, gbase, voff) do { _Pragma("unroll") for (int _i = 0; _i < 2; ++_i) \
;         __builtin_amdgcn_global_load_lds((const unsigned*)((const char*)(gbase) + (voff)[_i]), (PG8_LAS unsigned*)(lds + (bufoff) + ldsw + _i * 8192), 16, 0, 0); } while (0)
; #define PG8_LDA(dst, b, h) do { _Pragma("unroll") for (int m = 0; m < 4; ++m) _Pragma("unroll") for (int k = 0; k < 2; ++k) dst[m][k] = *(const PG8_LAS bf16x8*)(lds + PG8_SA(b, h) + aoff + m * 2048 + k * 1024); } while (0)
; #define PG8_LDB(dst, b, h) do { _Pragma("unroll") for (int n = 0; n < 2; ++n) _Pragma("unroll") for (int k = 0; k < 2; ++k) dst[n][k] = *(const PG8_LAS bf16x8*)(lds + PG8_SB(b, h) + boff + n * 2048 + k * 1024); } while (0)
; #define PG8_MMA(ai, bj, At, Bt) do { __builtin_amdgcn_s_setprio(1); _Pragma("unroll") for (int m = 0; m < 4; ++m) _Pragma("unroll") for (int n = 0; n < 2; ++n) _Pragma("unroll") for (int k = 0; k < 2; ++k) \
;         acc[ai][bj][m][n] = __builtin_amdgcn_mfma_f32_16x16x32_bf16(Bt[n][k], At[m][k], acc[ai][bj][m][n], 0, 0, 0); __builtin_amdgcn_s_setprio(0); } while (0)
; #define PG8_WAIT_V(n) asm volatile("s_waitcnt vmcnt(" #n ")" ::: "memory")
; #define PG8_WAIT_L(n) asm volatile("s_waitcnt lgkmcnt(" #n ")" ::: "memory")
; #define PG8_BAR __builtin_amdgcn_s_barrier()
; #define PG8_SCHED __builtin_amdgcn_sched_barrier(0)
; template <class Epi, class Sched, bool ALIGN_EPI = false, bool SP2 = false>
; __device__ __forceinline__ void gemm_phase(PG8_LAS unsigned char* lds, const Gemm g, const Sched& S, const Epi& E, const int wid) {
;     ...
;             PG8_LDB(B0, 1, 0); PG8_LDB(B1, 1, 1); PG8_SCHED; PG8_LDA(At, 1, 0); PG8_STAGE(PG8_SA(0, 1), a2 + hstepA, voffA);
;             PG8_WAIT_V(8); PG8_WAIT_L(0); PG8_BAR; PG8_MMA(0, 0, At, B0); PG8_MMA(0, 1, At, B1); PG8_BAR; PG8_SCHED;
;             PG8_LDA(At, 1, 1); PG8_STAGE(PG8_SB(1, 0), b3, voffB); PG8_STAGE(PG8_SB(1, 1), b3 + hstepB, voffB); PG8_STAGE(PG8_SA(1, 0), a3, voffA);
;             PG8_WAIT_V(8); PG8_WAIT_L(0); PG8_BAR; PG8_MMA(1, 0, At, B0); PG8_MMA(1, 1, At, B1); PG8_BAR; PG8_SCHED;
;     ...
;         if constexpr (ALIGN_EPI) { if (wr == 0) PG8_BAR; }
	s_add_i32 s69, 0, 0x18000
	s_add_i32 s70, 0, 0x1c000
	ds_read_b128 v[128:131], v252
	ds_read_b128 v[132:135], v252 offset:1024
	ds_read_b128 v[136:139], v252 offset:2048
	ds_read_b128 v[140:143], v252 offset:3072
	ds_read_b128 v[144:147], v253
	ds_read_b128 v[148:151], v253 offset:1024
	ds_read_b128 v[172:175], v253 offset:2048
	ds_read_b128 v[176:179], v253 offset:3072
	s_add_u32 s22, s28, 0xb0000
	s_addc_u32 s23, s29, 0
	s_mov_b32 m0, s36
	ds_read_b128 v[180:183], v192 offset:32768
	ds_read_b128 v[184:187], v192 offset:33792
	ds_read_b128 v[194:197], v192 offset:34816
	ds_read_b128 v[198:201], v192 offset:35840
	ds_read_b128 v[202:205], v192 offset:36864
	ds_read_b128 v[206:209], v192 offset:37888
	ds_read_b128 v[210:213], v192 offset:38912
	ds_read_b128 v[214:217], v192 offset:39936
	global_load_lds_dwordx4 v152, s[22:23]
	s_mov_b32 m0, s37
	s_nop 0
	global_load_lds_dwordx4 v156, s[22:23]
	s_waitcnt vmcnt(8) lgkmcnt(0)
	s_barrier
	s_nop 0
	s_setprio 1
	v_mfma_f32_16x16x32_bf16 v[124:127], v[128:131], v[180:183], v[124:127]
	v_mfma_f32_16x16x32_bf16 v[120:123], v[136:139], v[180:183], v[120:123]
	v_mfma_f32_16x16x32_bf16 v[108:111], v[128:131], v[194:197], v[108:111]
	v_mfma_f32_16x16x32_bf16 v[104:107], v[136:139], v[194:197], v[104:107]
	v_mfma_f32_16x16x32_bf16 v[92:95], v[128:131], v[202:205], v[92:95]
	v_mfma_f32_16x16x32_bf16 v[88:91], v[136:139], v[202:205], v[88:91]
	v_mfma_f32_16x16x32_bf16 v[76:79], v[128:131], v[210:213], v[76:79]
	v_mfma_f32_16x16x32_bf16 v[72:75], v[136:139], v[210:213], v[72:75]
	v_mfma_f32_16x16x32_bf16 v[124:127], v[132:135], v[184:187], v[124:127]
	v_mfma_f32_16x16x32_bf16 v[120:123], v[140:143], v[184:187], v[120:123]
	v_mfma_f32_16x16x32_bf16 v[108:111], v[132:135], v[198:201], v[108:111]
	v_mfma_f32_16x16x32_bf16 v[104:107], v[140:143], v[198:201], v[104:107]
	v_mfma_f32_16x16x32_bf16 v[92:95], v[132:135], v[206:209], v[92:95]
	v_mfma_f32_16x16x32_bf16 v[88:91], v[140:143], v[206:209], v[88:91]
	v_mfma_f32_16x16x32_bf16 v[76:79], v[132:135], v[214:217], v[76:79]
	v_mfma_f32_16x16x32_bf16 v[72:75], v[140:143], v[214:217], v[72:75]
	s_setprio 0
	s_setprio 1
	v_mfma_f32_16x16x32_bf16 v[116:119], v[144:147], v[180:183], v[116:119]
	v_mfma_f32_16x16x32_bf16 v[112:115], v[172:175], v[180:183], v[112:115]
	v_mfma_f32_16x16x32_bf16 v[100:103], v[144:147], v[194:197], v[100:103]
	v_mfma_f32_16x16x32_bf16 v[96:99], v[172:175], v[194:197], v[96:99]
	v_mfma_f32_16x16x32_bf16 v[84:87], v[144:147], v[202:205], v[84:87]
	v_mfma_f32_16x16x32_bf16 v[80:83], v[172:175], v[202:205], v[80:83]
	v_mfma_f32_16x16x32_bf16 v[68:71], v[144:147], v[210:213], v[68:71]
	v_mfma_f32_16x16x32_bf16 v[64:67], v[172:175], v[210:213], v[64:67]
	v_mfma_f32_16x16x32_bf16 v[116:119], v[148:151], v[184:187], v[116:119]
	v_mfma_f32_16x16x32_bf16 v[112:115], v[176:179], v[184:187], v[112:115]
	v_mfma_f32_16x16x32_bf16 v[100:103], v[148:151], v[198:201], v[100:103]
	v_mfma_f32_16x16x32_bf16 v[96:99], v[176:179], v[198:201], v[96:99]
	v_mfma_f32_16x16x32_bf16 v[84:87], v[148:151], v[206:209], v[84:87]
	v_mfma_f32_16x16x32_bf16 v[80:83], v[176:179], v[206:209], v[80:83]
	v_mfma_f32_16x16x32_bf16 v[68:71], v[148:151], v[214:217], v[68:71]
	v_mfma_f32_16x16x32_bf16 v[64:67], v[176:179], v[214:217], v[64:67]
	s_setprio 0
	s_barrier
	s_add_i32 s22, s69, s33
	s_mov_b32 m0, s22
	ds_read_b128 v[180:183], v192 offset:49152
	ds_read_b128 v[184:187], v192 offset:50176
	ds_read_b128 v[194:197], v192 offset:51200
	ds_read_b128 v[198:201], v192 offset:52224
	ds_read_b128 v[202:205], v192 offset:53248
	ds_read_b128 v[206:209], v192 offset:54272
	ds_read_b128 v[210:213], v192 offset:55296
	ds_read_b128 v[214:217], v192 offset:56320
	global_load_lds_dwordx4 v154, s[98:99]
	s_add_i32 m0, s22, 0x2000
	s_add_u32 s22, s26, 0xb0080
	s_addc_u32 s23, s27, 0
	s_add_i32 s26, s70, s33
	global_load_lds_dwordx4 v158, s[98:99]
	s_mov_b32 m0, s26
	s_nop 0
	global_load_lds_dwordx4 v154, s[22:23]
	s_add_i32 m0, s26, 0x2000
	s_nop 0
	global_load_lds_dwordx4 v158, s[22:23]
	s_mov_b32 m0, s39
	s_nop 0
	global_load_lds_dwordx4 v152, s[100:101]
	s_mov_b32 m0, s40
	s_nop 0
	global_load_lds_dwordx4 v156, s[100:101]
	s_waitcnt vmcnt(8) lgkmcnt(0)
	s_barrier
	s_setprio 1
	v_mfma_f32_16x16x32_bf16 v[60:63], v[128:131], v[180:183], v[60:63]
	v_mfma_f32_16x16x32_bf16 v[56:59], v[136:139], v[180:183], v[56:59]
	v_mfma_f32_16x16x32_bf16 v[44:47], v[128:131], v[194:197], v[44:47]
	v_mfma_f32_16x16x32_bf16 v[40:43], v[136:139], v[194:197], v[40:43]
	v_mfma_f32_16x16x32_bf16 v[28:31], v[128:131], v[202:205], v[28:31]
	v_mfma_f32_16x16x32_bf16 v[24:27], v[136:139], v[202:205], v[24:27]
	v_mfma_f32_16x16x32_bf16 v[12:15], v[128:131], v[210:213], v[12:15]
	v_mfma_f32_16x16x32_bf16 v[8:11], v[136:139], v[210:213], v[8:11]
	v_mfma_f32_16x16x32_bf16 v[60:63], v[132:135], v[184:187], v[60:63]
	v_mfma_f32_16x16x32_bf16 v[56:59], v[140:143], v[184:187], v[56:59]
	v_mfma_f32_16x16x32_bf16 v[44:47], v[132:135], v[198:201], v[44:47]
	v_mfma_f32_16x16x32_bf16 v[40:43], v[140:143], v[198:201], v[40:43]
	v_mfma_f32_16x16x32_bf16 v[28:31], v[132:135], v[206:209], v[28:31]
	v_mfma_f32_16x16x32_bf16 v[24:27], v[140:143], v[206:209], v[24:27]
	v_mfma_f32_16x16x32_bf16 v[12:15], v[132:135], v[214:217], v[12:15]
	v_mfma_f32_16x16x32_bf16 v[8:11], v[140:143], v[214:217], v[8:11]
	s_setprio 0
	s_setprio 1
	v_mfma_f32_16x16x32_bf16 v[52:55], v[144:147], v[180:183], v[52:55]
	v_mfma_f32_16x16x32_bf16 v[48:51], v[172:175], v[180:183], v[48:51]
	v_mfma_f32_16x16x32_bf16 v[36:39], v[144:147], v[194:197], v[36:39]
	v_mfma_f32_16x16x32_bf16 v[32:35], v[172:175], v[194:197], v[32:35]
	v_mfma_f32_16x16x32_bf16 v[20:23], v[144:147], v[202:205], v[20:23]
	v_mfma_f32_16x16x32_bf16 v[16:19], v[172:175], v[202:205], v[16:19]
	v_mfma_f32_16x16x32_bf16 v[4:7], v[144:147], v[210:213], v[4:7]
	v_mfma_f32_16x16x32_bf16 v[0:3], v[172:175], v[210:213], v[0:3]
	v_mfma_f32_16x16x32_bf16 v[52:55], v[148:151], v[184:187], v[52:55]
	v_mfma_f32_16x16x32_bf16 v[48:51], v[176:179], v[184:187], v[48:51]
	v_mfma_f32_16x16x32_bf16 v[36:39], v[148:151], v[198:201], v[36:39]
	v_mfma_f32_16x16x32_bf16 v[32:35], v[176:179], v[198:201], v[32:35]
	v_mfma_f32_16x16x32_bf16 v[20:23], v[148:151], v[206:209], v[20:23]
	v_mfma_f32_16x16x32_bf16 v[16:19], v[176:179], v[206:209], v[16:19]
	v_mfma_f32_16x16x32_bf16 v[4:7], v[148:151], v[214:217], v[4:7]
	v_mfma_f32_16x16x32_bf16 v[0:3], v[176:179], v[214:217], v[0:3]
	s_setprio 0
	s_barrier
	s_add_i32 s68, s68, 2
	s_add_u32 s66, s66, 0x100
	s_addc_u32 s67, s67, 0
	s_cmp_gt_u32 s68, 41
	s_mov_b64 s[22:23], s[24:25]
	s_cbranch_scc0 .LBB0_1952
	s_and_b64 vcc, exec, s[18:19]
	s_cbranch_vccz .LBB0_1955
	s_barrier

; #define PG8_STAGE(bufoff, gbase, voff) do { _Pragma("unroll") for (int _i = 0; _i < 2; ++_i) \
;         __builtin_amdgcn_global_load_lds((const unsigned*)((const char*)(gbase) + (voff)[_i]), (PG8_LAS unsigned*)(lds + (bufoff) + ldsw + _i * 8192), 16, 0, 0); } while (0)
; #define PG8_LDA(dst, b, h) do { _Pragma("unroll") for (int m = 0; m < 4; ++m) _Pragma("unroll") for (int k = 0; k < 2; ++k) dst[m][k] = *(const PG8_LAS bf16x8*)(lds + PG8_SA(b, h) + aoff + m * 2048 + k * 1024); } while (0)
; #define PG8_LDB(dst, b, h) do { _Pragma("unroll") for (int n = 0; n < 2; ++n) _Pragma("unroll") for (int k = 0; k < 2; ++k) dst[n][k] = *(const PG8_LAS bf16x8*)(lds + PG8_SB(b, h) + boff + n * 2048 + k * 1024); } while (0)
; #define PG8_WAIT_V(n) asm volatile("s_waitcnt vmcnt(" #n ")" ::: "memory")
; #define PG8_WAIT_L(n) asm volatile("s_waitcnt lgkmcnt(" #n ")" ::: "memory")
; #define PG8_BAR __builtin_amdgcn_s_barrier()
; #define PG8_SCHED __builtin_amdgcn_sched_barrier(0)
; template <class Epi, class Sched, bool ALIGN_EPI = false, bool SP2 = false>
; __device__ __forceinline__ void gemm_phase(PG8_LAS unsigned char* lds, const Gemm g, const Sched& S, const Epi& E, const int wid) {
;     ...
;         const bool has_next = S.next(ui + 1, nxt);
;         const char* nA = has_next ? (const char*)g.A + (size_t)nxt.pm * tstepA : cA; const char* nB = has_next ? (const char*)g.Bt + (size_t)nxt.pn * tstepB : cB;
;         for (int t = 0; t < nt; t += 2) {
;             const bool last = (t == nt - 2);
;             const char* a1 = cA + (size_t)(t + 1) * kstep;
;             const char* a2 = last ? nA : cA + (size_t)(t + 2) * kstep; const char* b2 = last ? nB : cB + (size_t)(t + 2) * kstep;
;             const char* a3 = a2 + kstep; const char* b3 = b2 + kstep;
;             if (last && has_next) S.a_ready(nxt);
;             if constexpr (SP2) {
;             PG8_LDB(B0, 0, 0); PG8_LDB(B1, 0, 1); PG8_SCHED; PG8_LDA(At, 0, 0); PG8_STAGE(PG8_SA(1, 1), a1 + hstepA, voffA);
;             PG8_WAIT_V(8); PG8_WAIT_L(0); PG8_BAR; PG8_MMA(0, 0, At, B0); PG8_MMA(0, 1, At, B1); PG8_BAR; PG8_SCHED;
;             PG8_LDA(At, 0, 1); PG8_STAGE(PG8_SB(0, 0), b2, voffB); PG8_STAGE(PG8_SB(0, 1), b2 + hstepB, voffB); PG8_STAGE(PG8_SA(0, 0), a2, voffA);
;             PG8_WAIT_V(8); PG8_WAIT_L(0); PG8_BAR; PG8_MMA(1, 0, At, B0); PG8_MMA(1, 1, At, B1); PG8_BAR; PG8_SCHED;
.LBB0_2048:
	s_ashr_i32 s31, s30, 31
	s_lshl_b64 s[34:35], s[30:31], 19
	s_add_u32 s34, s0, s34
	s_addc_u32 s35, s1, s35
	s_and_b64 s[36:37], s[4:5], exec
	s_cselect_b32 s7, s35, s9
	s_cselect_b32 s11, s34, s8
	s_ashr_i32 s29, s28, 31
	s_lshl_b64 s[36:37], s[28:29], 19
	s_add_u32 s36, s33, s36
	s_addc_u32 s37, s44, s37
	s_and_b64 s[38:39], s[4:5], exec
	s_cselect_b32 s29, s37, s13
	s_cselect_b32 s31, s36, s12
	s_add_u32 s8, s8, 0x40080
	s_addc_u32 s9, s9, 0
	s_add_u32 s40, s12, 0x100
	s_addc_u32 s41, s13, 0
	s_mov_b32 s71, -2
	s_waitcnt lgkmcnt(0)
	v_add_u32_e32 v252, 0x18000, v174
	v_add_u32_e32 v253, 0x1c000, v174
	ds_read_b128 v[146:149], v179
	ds_read_b128 v[150:153], v179 offset:1024
	ds_read_b128 v[154:157], v179 offset:2048
	ds_read_b128 v[158:161], v179 offset:3072
	ds_read_b128 v[162:165], v180
	ds_read_b128 v[166:169], v180 offset:1024
	ds_read_b128 v[184:187], v180 offset:2048
	ds_read_b128 v[188:191], v180 offset:3072
	s_add_u32 s12, s8, 0xfffc0080
	s_addc_u32 s13, s9, -1
	s_cmp_eq_u32 s71, 12
	s_cselect_b32 s39, s7, s13
	s_cselect_b32 s38, s11, s12
	s_cselect_b32 s13, s29, s41
	s_cselect_b32 s12, s31, s40
	s_add_i32 m0, s46, 0xc000
	ds_read_b128 v[192:195], v181
	ds_read_b128 v[196:199], v181 offset:1024
	ds_read_b128 v[200:203], v181 offset:2048
	ds_read_b128 v[204:207], v181 offset:3072
	ds_read_b128 v[208:211], v181 offset:4096
	ds_read_b128 v[212:215], v181 offset:5120
	ds_read_b128 v[216:219], v181 offset:6144
	ds_read_b128 v[220:223], v181 offset:7168
	global_load_lds_dwordx4 v138, s[8:9]
	s_add_i32 m0, s46, 0xe000
	s_nop 0
	global_load_lds_dwordx4 v140, s[8:9]
	s_waitcnt vmcnt(8) lgkmcnt(0)
	s_barrier
	s_nop 0
	s_setprio 1
	v_mfma_f32_16x16x32_bf16 v[124:127], v[146:149], v[192:195], 0
	v_mfma_f32_16x16x32_bf16 v[120:123], v[154:157], v[192:195], 0
	v_mfma_f32_16x16x32_bf16 v[108:111], v[146:149], v[200:203], 0
	v_mfma_f32_16x16x32_bf16 v[104:107], v[154:157], v[200:203], 0
	v_mfma_f32_16x16x32_bf16 v[92:95], v[146:149], v[208:211], 0
	v_mfma_f32_16x16x32_bf16 v[88:91], v[154:157], v[208:211], 0
	v_mfma_f32_16x16x32_bf16 v[76:79], v[146:149], v[216:219], 0
	v_mfma_f32_16x16x32_bf16 v[72:75], v[154:157], v[216:219], 0
	v_mfma_f32_16x16x32_bf16 v[124:127], v[150:153], v[196:199], v[124:127]
	v_mfma_f32_16x16x32_bf16 v[120:123], v[158:161], v[196:199], v[120:123]
	v_mfma_f32_16x16x32_bf16 v[108:111], v[150:153], v[204:207], v[108:111]
	v_mfma_f32_16x16x32_bf16 v[104:107], v[158:161], v[204:207], v[104:107]
	v_mfma_f32_16x16x32_bf16 v[92:95], v[150:153], v[212:215], v[92:95]
	v_mfma_f32_16x16x32_bf16 v[88:91], v[158:161], v[212:215], v[88:91]
	v_mfma_f32_16x16x32_bf16 v[76:79], v[150:153], v[220:223], v[76:79]
	v_mfma_f32_16x16x32_bf16 v[72:75], v[158:161], v[220:223], v[72:75]
	s_setprio 0
	s_setprio 1
	v_mfma_f32_16x16x32_bf16 v[116:119], v[162:165], v[192:195], 0
	v_mfma_f32_16x16x32_bf16 v[112:115], v[184:187], v[192:195], 0
	v_mfma_f32_16x16x32_bf16 v[100:103], v[162:165], v[200:203], 0
	v_mfma_f32_16x16x32_bf16 v[96:99], v[184:187], v[200:203], 0
	v_mfma_f32_16x16x32_bf16 v[84:87], v[162:165], v[208:211], 0
	v_mfma_f32_16x16x32_bf16 v[80:83], v[184:187], v[208:211], 0
	v_mfma_f32_16x16x32_bf16 v[68:71], v[162:165], v[216:219], 0
	v_mfma_f32_16x16x32_bf16 v[64:67], v[184:187], v[216:219], 0
	v_mfma_f32_16x16x32_bf16 v[116:119], v[166:169], v[196:199], v[116:119]
	v_mfma_f32_16x16x32_bf16 v[112:115], v[188:191], v[196:199], v[112:115]
	v_mfma_f32_16x16x32_bf16 v[100:103], v[166:169], v[204:207], v[100:103]
	v_mfma_f32_16x16x32_bf16 v[96:99], v[188:191], v[204:207], v[96:99]
	v_mfma_f32_16x16x32_bf16 v[84:87], v[166:169], v[212:215], v[84:87]
	v_mfma_f32_16x16x32_bf16 v[80:83], v[188:191], v[212:215], v[80:83]
	v_mfma_f32_16x16x32_bf16 v[68:71], v[166:169], v[220:223], v[68:71]
	v_mfma_f32_16x16x32_bf16 v[64:67], v[188:191], v[220:223], v[64:67]
	s_setprio 0
	s_barrier
	s_add_i32 s72, s69, s45
	s_add_u32 s98, s12, 0x80
	s_addc_u32 s99, s13, 0
	s_mov_b32 m0, s72
	ds_read_b128 v[192:195], v181 offset:16384
	ds_read_b128 v[196:199], v181 offset:17408
	ds_read_b128 v[200:203], v181 offset:18432
	ds_read_b128 v[204:207], v181 offset:19456
	ds_read_b128 v[208:211], v181 offset:20480
	ds_read_b128 v[212:215], v181 offset:21504
	ds_read_b128 v[216:219], v181 offset:22528
	ds_read_b128 v[220:223], v181 offset:23552
	global_load_lds_dwordx4 v130, s[12:13]
	s_add_i32 m0, s72, 0x2000
	s_add_u32 s72, s12, 0x40000
	s_addc_u32 s73, s13, 0
	s_add_i32 s74, s70, s45
	global_load_lds_dwordx4 v134, s[12:13]
	s_mov_b32 m0, s74
	s_add_u32 s100, s38, 0x80
	s_addc_u32 s101, s39, 0
	global_load_lds_dwordx4 v130, s[72:73]
	s_add_i32 m0, s74, 0x2000
	s_nop 0
	global_load_lds_dwordx4 v134, s[72:73]
	s_mov_b32 m0, s46
	s_nop 0
	global_load_lds_dwordx4 v128, s[38:39]
	s_mov_b32 m0, s47
	s_nop 0
	global_load_lds_dwordx4 v132, s[38:39]
	s_waitcnt vmcnt(8) lgkmcnt(0)
	s_barrier
; #define PG8_STAGE(bufoff, gbase, voff) do { _Pragma("unroll") for (int _i = 0; _i < 2; ++_i) \
;         __builtin_amdgcn_global_load_lds((const unsigned*)((const char*)(gbase) + (voff)[_i]), (PG8_LAS unsigned*)(lds + (bufoff) + ldsw + _i * 8192), 16, 0, 0); } while (0)
; #define PG8_LDA(dst, b, h) do { _Pragma("unroll") for (int m = 0; m < 4; ++m) _Pragma("unroll") for (int k = 0; k < 2; ++k) dst[m][k] = *(const PG8_LAS bf16x8*)(lds + PG8_SA(b, h) + aoff + m * 2048 + k * 1024); } while (0)
; #define PG8_LDB(dst, b, h) do { _Pragma("unroll") for (int n = 0; n < 2; ++n) _Pragma("unroll") for (int k = 0; k < 2; ++k) dst[n][k] = *(const PG8_LAS bf16x8*)(lds + PG8_SB(b, h) + boff + n * 2048 + k * 1024); } while (0)
; #define PG8_MMA(ai, bj, At, Bt) do { __builtin_amdgcn_s_setprio(1); _Pragma("unroll") for (int m = 0; m < 4; ++m) _Pragma("unroll") for (int n = 0; n < 2; ++n) _Pragma("unroll") for (int k = 0; k < 2; ++k) \
;         acc[ai][bj][m][n] = __builtin_amdgcn_mfma_f32_16x16x32_bf16(Bt[n][k], At[m][k], acc[ai][bj][m][n], 0, 0, 0); __builtin_amdgcn_s_setprio(0); } while (0)
; #define PG8_WAIT_V(n) asm volatile("s_waitcnt vmcnt(" #n ")" ::: "memory")
; #define PG8_WAIT_L(n) asm volatile("s_waitcnt lgkmcnt(" #n ")" ::: "memory")
; #define PG8_BAR __builtin_amdgcn_s_barrier()
; #define PG8_SCHED __builtin_amdgcn_sched_barrier(0)
; template <class Epi, class Sched, bool ALIGN_EPI = false, bool SP2 = false>
; __device__ __forceinline__ void gemm_phase(PG8_LAS unsigned char* lds, const Gemm g, const Sched& S, const Epi& E, const int wid) {
;     ...
;             PG8_WAIT_V(8); PG8_WAIT_L(0); PG8_BAR; PG8_MMA(0, 0, At, B0); PG8_MMA(0, 1, At, B1); PG8_BAR; PG8_SCHED;
;             PG8_LDA(At, 0, 1); PG8_STAGE(PG8_SB(0, 0), b2, voffB); PG8_STAGE(PG8_SB(0, 1), b2 + hstepB, voffB); PG8_STAGE(PG8_SA(0, 0), a2, voffA);
;             PG8_WAIT_V(8); PG8_WAIT_L(0); PG8_BAR; PG8_MMA(1, 0, At, B0); PG8_MMA(1, 1, At, B1); PG8_BAR; PG8_SCHED;
;             PG8_LDB(B0, 1, 0); PG8_LDB(B1, 1, 1); PG8_SCHED; PG8_LDA(At, 1, 0); PG8_STAGE(PG8_SA(0, 1), a2 + hstepA, voffA);
;             PG8_WAIT_V(8); PG8_WAIT_L(0); PG8_BAR; PG8_MMA(0, 0, At, B0); PG8_MMA(0, 1, At, B1); PG8_BAR; PG8_SCHED;
	s_nop 0
	s_setprio 1
	v_mfma_f32_16x16x32_bf16 v[60:63], v[146:149], v[192:195], 0
	v_mfma_f32_16x16x32_bf16 v[56:59], v[154:157], v[192:195], 0
	v_mfma_f32_16x16x32_bf16 v[44:47], v[146:149], v[200:203], 0
	v_mfma_f32_16x16x32_bf16 v[40:43], v[154:157], v[200:203], 0
	v_mfma_f32_16x16x32_bf16 v[28:31], v[146:149], v[208:211], 0
	v_mfma_f32_16x16x32_bf16 v[24:27], v[154:157], v[208:211], 0
	v_mfma_f32_16x16x32_bf16 v[12:15], v[146:149], v[216:219], 0
	v_mfma_f32_16x16x32_bf16 v[8:11], v[154:157], v[216:219], 0
	v_mfma_f32_16x16x32_bf16 v[60:63], v[150:153], v[196:199], v[60:63]
	v_mfma_f32_16x16x32_bf16 v[56:59], v[158:161], v[196:199], v[56:59]
	v_mfma_f32_16x16x32_bf16 v[44:47], v[150:153], v[204:207], v[44:47]
	v_mfma_f32_16x16x32_bf16 v[40:43], v[158:161], v[204:207], v[40:43]
	v_mfma_f32_16x16x32_bf16 v[28:31], v[150:153], v[212:215], v[28:31]
	v_mfma_f32_16x16x32_bf16 v[24:27], v[158:161], v[212:215], v[24:27]
	v_mfma_f32_16x16x32_bf16 v[12:15], v[150:153], v[220:223], v[12:15]
	v_mfma_f32_16x16x32_bf16 v[8:11], v[158:161], v[220:223], v[8:11]
	s_setprio 0
	s_setprio 1
	v_mfma_f32_16x16x32_bf16 v[52:55], v[162:165], v[192:195], 0
	v_mfma_f32_16x16x32_bf16 v[48:51], v[184:187], v[192:195], 0
	v_mfma_f32_16x16x32_bf16 v[36:39], v[162:165], v[200:203], 0
	v_mfma_f32_16x16x32_bf16 v[32:35], v[184:187], v[200:203], 0
	v_mfma_f32_16x16x32_bf16 v[20:23], v[162:165], v[208:211], 0
	v_mfma_f32_16x16x32_bf16 v[16:19], v[184:187], v[208:211], 0
	v_mfma_f32_16x16x32_bf16 v[4:7], v[162:165], v[216:219], 0
	v_mfma_f32_16x16x32_bf16 v[0:3], v[184:187], v[216:219], 0
	v_mfma_f32_16x16x32_bf16 v[52:55], v[166:169], v[196:199], v[52:55]
	v_mfma_f32_16x16x32_bf16 v[48:51], v[188:191], v[196:199], v[48:51]
	v_mfma_f32_16x16x32_bf16 v[36:39], v[166:169], v[204:207], v[36:39]
	v_mfma_f32_16x16x32_bf16 v[32:35], v[188:191], v[204:207], v[32:35]
	v_mfma_f32_16x16x32_bf16 v[20:23], v[166:169], v[212:215], v[20:23]
	v_mfma_f32_16x16x32_bf16 v[16:19], v[188:191], v[212:215], v[16:19]
	v_mfma_f32_16x16x32_bf16 v[4:7], v[166:169], v[220:223], v[4:7]
	v_mfma_f32_16x16x32_bf16 v[0:3], v[188:191], v[220:223], v[0:3]
	s_setprio 0
	s_barrier
	s_add_i32 s72, 0, 0x18000
	s_add_i32 s73, 0, 0x1c000
	ds_read_b128 v[146:149], v252
	ds_read_b128 v[150:153], v252 offset:1024
	ds_read_b128 v[154:157], v252 offset:2048
	ds_read_b128 v[158:161], v252 offset:3072
	ds_read_b128 v[162:165], v253
	ds_read_b128 v[166:169], v253 offset:1024
	ds_read_b128 v[184:187], v253 offset:2048
	ds_read_b128 v[188:191], v253 offset:3072
	s_add_u32 s38, s38, 0x40000
	s_addc_u32 s39, s39, 0
	s_mov_b32 m0, s48
	ds_read_b128 v[192:195], v181 offset:32768
	ds_read_b128 v[196:199], v181 offset:33792
	ds_read_b128 v[200:203], v181 offset:34816
	ds_read_b128 v[204:207], v181 offset:35840
	ds_read_b128 v[208:211], v181 offset:36864
	ds_read_b128 v[212:215], v181 offset:37888
	ds_read_b128 v[216:219], v181 offset:38912
	ds_read_b128 v[220:223], v181 offset:39936
	global_load_lds_dwordx4 v128, s[38:39]
	s_mov_b32 m0, s49
	s_nop 0
	global_load_lds_dwordx4 v132, s[38:39]
	s_waitcnt vmcnt(8) lgkmcnt(0)
	s_barrier
	s_nop 0
	s_setprio 1
	v_mfma_f32_16x16x32_bf16 v[124:127], v[146:149], v[192:195], v[124:127]
	v_mfma_f32_16x16x32_bf16 v[120:123], v[154:157], v[192:195], v[120:123]
	v_mfma_f32_16x16x32_bf16 v[108:111], v[146:149], v[200:203], v[108:111]
	v_mfma_f32_16x16x32_bf16 v[104:107], v[154:157], v[200:203], v[104:107]
	v_mfma_f32_16x16x32_bf16 v[92:95], v[146:149], v[208:211], v[92:95]
	v_mfma_f32_16x16x32_bf16 v[88:91], v[154:157], v[208:211], v[88:91]
	v_mfma_f32_16x16x32_bf16 v[76:79], v[146:149], v[216:219], v[76:79]
	v_mfma_f32_16x16x32_bf16 v[72:75], v[154:157], v[216:219], v[72:75]
	v_mfma_f32_16x16x32_bf16 v[124:127], v[150:153], v[196:199], v[124:127]
	v_mfma_f32_16x16x32_bf16 v[120:123], v[158:161], v[196:199], v[120:123]
	v_mfma_f32_16x16x32_bf16 v[108:111], v[150:153], v[204:207], v[108:111]
	v_mfma_f32_16x16x32_bf16 v[104:107], v[158:161], v[204:207], v[104:107]
	v_mfma_f32_16x16x32_bf16 v[92:95], v[150:153], v[212:215], v[92:95]
	v_mfma_f32_16x16x32_bf16 v[88:91], v[158:161], v[212:215], v[88:91]
	v_mfma_f32_16x16x32_bf16 v[76:79], v[150:153], v[220:223], v[76:79]
	v_mfma_f32_16x16x32_bf16 v[72:75], v[158:161], v[220:223], v[72:75]
	s_setprio 0
	s_setprio 1
	v_mfma_f32_16x16x32_bf16 v[116:119], v[162:165], v[192:195], v[116:119]
	v_mfma_f32_16x16x32_bf16 v[112:115], v[184:187], v[192:195], v[112:115]
	v_mfma_f32_16x16x32_bf16 v[100:103], v[162:165], v[200:203], v[100:103]
	v_mfma_f32_16x16x32_bf16 v[96:99], v[184:187], v[200:203], v[96:99]
	v_mfma_f32_16x16x32_bf16 v[84:87], v[162:165], v[208:211], v[84:87]
	v_mfma_f32_16x16x32_bf16 v[80:83], v[184:187], v[208:211], v[80:83]
	v_mfma_f32_16x16x32_bf16 v[68:71], v[162:165], v[216:219], v[68:71]
	v_mfma_f32_16x16x32_bf16 v[64:67], v[184:187], v[216:219], v[64:67]
	v_mfma_f32_16x16x32_bf16 v[116:119], v[166:169], v[196:199], v[116:119]
	v_mfma_f32_16x16x32_bf16 v[112:115], v[188:191], v[196:199], v[112:115]
	v_mfma_f32_16x16x32_bf16 v[100:103], v[166:169], v[204:207], v[100:103]
	v_mfma_f32_16x16x32_bf16 v[96:99], v[188:191], v[204:207], v[96:99]
	v_mfma_f32_16x16x32_bf16 v[84:87], v[166:169], v[212:215], v[84:87]
	v_mfma_f32_16x16x32_bf16 v[80:83], v[188:191], v[212:215], v[80:83]
	v_mfma_f32_16x16x32_bf16 v[68:71], v[166:169], v[220:223], v[68:71]
	v_mfma_f32_16x16x32_bf16 v[64:67], v[188:191], v[220:223], v[64:67]
	s_setprio 0
	s_barrier
; #define PG8_STAGE(bufoff, gbase, voff) do { _Pragma("unroll") for (int _i = 0; _i < 2; ++_i) \
;         __builtin_amdgcn_global_load_lds((const unsigned*)((const char*)(gbase) + (voff)[_i]), (PG8_LAS unsigned*)(lds + (bufoff) + ldsw + _i * 8192), 16, 0, 0); } while (0)
; #define PG8_LDA(dst, b, h) do { _Pragma("unroll") for (int m = 0; m < 4; ++m) _Pragma("unroll") for (int k = 0; k < 2; ++k) dst[m][k] = *(const PG8_LAS bf16x8*)(lds + PG8_SA(b, h) + aoff + m * 2048 + k * 1024); } while (0)
; #define PG8_LDB(dst, b, h) do { _Pragma("unroll") for (int n = 0; n < 2; ++n) _Pragma("unroll") for (int k = 0; k < 2; ++k) dst[n][k] = *(const PG8_LAS bf16x8*)(lds + PG8_SB(b, h) + boff + n * 2048 + k * 1024); } while (0)
; #define PG8_MMA(ai, bj, At, Bt) do { __builtin_amdgcn_s_setprio(1); _Pragma("unroll") for (int m = 0; m < 4; ++m) _Pragma("unroll") for (int n = 0; n < 2; ++n) _Pragma("unroll") for (int k = 0; k < 2; ++k) \
;         acc[ai][bj][m][n] = __builtin_amdgcn_mfma_f32_16x16x32_bf16(Bt[n][k], At[m][k], acc[ai][bj][m][n], 0, 0, 0); __builtin_amdgcn_s_setprio(0); } while (0)
; #define PG8_WAIT_V(n) asm volatile("s_waitcnt vmcnt(" #n ")" ::: "memory")
; #define PG8_WAIT_L(n) asm volatile("s_waitcnt lgkmcnt(" #n ")" ::: "memory")
; #define PG8_BAR __builtin_amdgcn_s_barrier()
; #define PG8_SCHED __builtin_amdgcn_sched_barrier(0)
; template <class Epi, class Sched, bool ALIGN_EPI = false, bool SP2 = false>
; __device__ __forceinline__ void gemm_phase(PG8_LAS unsigned char* lds, const Gemm g, const Sched& S, const Epi& E, const int wid) {
;     ...
;             if constexpr (SP2) {
;             PG8_LDB(B0, 0, 0); PG8_LDB(B1, 0, 1); PG8_SCHED; PG8_LDA(At, 0, 0); PG8_STAGE(PG8_SA(1, 1), a1 + hstepA, voffA);
;             PG8_WAIT_V(8); PG8_WAIT_L(0); PG8_BAR; PG8_MMA(0, 0, At, B0); PG8_MMA(0, 1, At, B1); PG8_BAR; PG8_SCHED;
;     ...
;             PG8_LDA(At, 1, 1); PG8_STAGE(PG8_SB(1, 0), b3, voffB); PG8_STAGE(PG8_SB(1, 1), b3 + hstepB, voffB); PG8_STAGE(PG8_SA(1, 0), a3, voffA);
;             PG8_WAIT_V(8); PG8_WAIT_L(0); PG8_BAR; PG8_MMA(1, 0, At, B0); PG8_MMA(1, 1, At, B1); PG8_BAR; PG8_SCHED;
	s_add_i32 s38, s72, s45
	s_mov_b32 m0, s38
	ds_read_b128 v[192:195], v181 offset:49152
	ds_read_b128 v[196:199], v181 offset:50176
	ds_read_b128 v[200:203], v181 offset:51200
	ds_read_b128 v[204:207], v181 offset:52224
	ds_read_b128 v[208:211], v181 offset:53248
	ds_read_b128 v[212:215], v181 offset:54272
	ds_read_b128 v[216:219], v181 offset:55296
	ds_read_b128 v[220:223], v181 offset:56320
	global_load_lds_dwordx4 v130, s[98:99]
	s_add_i32 m0, s38, 0x2000
	s_add_u32 s12, s12, 0x40080
	s_addc_u32 s13, s13, 0
	s_add_i32 s38, s73, s45
	global_load_lds_dwordx4 v134, s[98:99]
	s_mov_b32 m0, s38
	s_nop 0
	global_load_lds_dwordx4 v130, s[12:13]
	s_add_i32 m0, s38, 0x2000
	s_nop 0
	global_load_lds_dwordx4 v134, s[12:13]
	s_mov_b32 m0, s65
	s_nop 0
	global_load_lds_dwordx4 v128, s[100:101]
	s_mov_b32 m0, s66
	s_nop 0
	global_load_lds_dwordx4 v132, s[100:101]
	s_waitcnt vmcnt(8) lgkmcnt(0)
	s_barrier
	s_setprio 1
	v_mfma_f32_16x16x32_bf16 v[60:63], v[146:149], v[192:195], v[60:63]
	v_mfma_f32_16x16x32_bf16 v[56:59], v[154:157], v[192:195], v[56:59]
	v_mfma_f32_16x16x32_bf16 v[44:47], v[146:149], v[200:203], v[44:47]
	v_mfma_f32_16x16x32_bf16 v[40:43], v[154:157], v[200:203], v[40:43]
	v_mfma_f32_16x16x32_bf16 v[28:31], v[146:149], v[208:211], v[28:31]
	v_mfma_f32_16x16x32_bf16 v[24:27], v[154:157], v[208:211], v[24:27]
	v_mfma_f32_16x16x32_bf16 v[12:15], v[146:149], v[216:219], v[12:15]
	v_mfma_f32_16x16x32_bf16 v[8:11], v[154:157], v[216:219], v[8:11]
	v_mfma_f32_16x16x32_bf16 v[60:63], v[150:153], v[196:199], v[60:63]
	v_mfma_f32_16x16x32_bf16 v[56:59], v[158:161], v[196:199], v[56:59]
	v_mfma_f32_16x16x32_bf16 v[44:47], v[150:153], v[204:207], v[44:47]
	v_mfma_f32_16x16x32_bf16 v[40:43], v[158:161], v[204:207], v[40:43]
	v_mfma_f32_16x16x32_bf16 v[28:31], v[150:153], v[212:215], v[28:31]
	v_mfma_f32_16x16x32_bf16 v[24:27], v[158:161], v[212:215], v[24:27]
	v_mfma_f32_16x16x32_bf16 v[12:15], v[150:153], v[220:223], v[12:15]
	v_mfma_f32_16x16x32_bf16 v[8:11], v[158:161], v[220:223], v[8:11]
	s_setprio 0
	s_setprio 1
	v_mfma_f32_16x16x32_bf16 v[52:55], v[162:165], v[192:195], v[52:55]
	v_mfma_f32_16x16x32_bf16 v[48:51], v[184:187], v[192:195], v[48:51]
	v_mfma_f32_16x16x32_bf16 v[36:39], v[162:165], v[200:203], v[36:39]
	v_mfma_f32_16x16x32_bf16 v[32:35], v[184:187], v[200:203], v[32:35]
	v_mfma_f32_16x16x32_bf16 v[20:23], v[162:165], v[208:211], v[20:23]
	v_mfma_f32_16x16x32_bf16 v[16:19], v[184:187], v[208:211], v[16:19]
	v_mfma_f32_16x16x32_bf16 v[4:7], v[162:165], v[216:219], v[4:7]
	v_mfma_f32_16x16x32_bf16 v[0:3], v[184:187], v[216:219], v[0:3]
	v_mfma_f32_16x16x32_bf16 v[52:55], v[166:169], v[196:199], v[52:55]
	v_mfma_f32_16x16x32_bf16 v[48:51], v[188:191], v[196:199], v[48:51]
	v_mfma_f32_16x16x32_bf16 v[36:39], v[166:169], v[204:207], v[36:39]
	v_mfma_f32_16x16x32_bf16 v[32:35], v[188:191], v[204:207], v[32:35]
	v_mfma_f32_16x16x32_bf16 v[20:23], v[166:169], v[212:215], v[20:23]
	v_mfma_f32_16x16x32_bf16 v[16:19], v[188:191], v[212:215], v[16:19]
	v_mfma_f32_16x16x32_bf16 v[4:7], v[166:169], v[220:223], v[4:7]
	v_mfma_f32_16x16x32_bf16 v[0:3], v[188:191], v[220:223], v[0:3]
	s_setprio 0
	s_barrier
	s_add_i32 s71, s71, 2
	s_add_u32 s8, s8, 0x100
	s_addc_u32 s9, s9, 0
	s_add_u32 s40, s40, 0x100
	s_addc_u32 s41, s41, 0
	s_cmp_gt_u32 s71, 13
.LBB0_2049:
	ds_read_b128 v[146:149], v179
	ds_read_b128 v[150:153], v179 offset:1024
	ds_read_b128 v[154:157], v179 offset:2048
	ds_read_b128 v[158:161], v179 offset:3072
	ds_read_b128 v[162:165], v180
	ds_read_b128 v[166:169], v180 offset:1024
	ds_read_b128 v[184:187], v180 offset:2048
	ds_read_b128 v[188:191], v180 offset:3072
	s_add_u32 s12, s8, 0xfffc0080
	s_addc_u32 s13, s9, -1
	s_cmp_eq_u32 s71, 12
	s_cselect_b32 s39, s7, s13
	s_cselect_b32 s38, s11, s12
	s_cselect_b32 s13, s29, s41
	s_cselect_b32 s12, s31, s40
	s_add_i32 m0, s46, 0xc000
	ds_read_b128 v[192:195], v181
	ds_read_b128 v[196:199], v181 offset:1024
	ds_read_b128 v[200:203], v181 offset:2048
	ds_read_b128 v[204:207], v181 offset:3072
	ds_read_b128 v[208:211], v181 offset:4096
	ds_read_b128 v[212:215], v181 offset:5120
	ds_read_b128 v[216:219], v181 offset:6144
	ds_read_b128 v[220:223], v181 offset:7168
	global_load_lds_dwordx4 v138, s[8:9]
	s_add_i32 m0, s46, 0xe000
	s_nop 0
	global_load_lds_dwordx4 v140, s[8:9]
	s_waitcnt vmcnt(8) lgkmcnt(0)
	s_barrier
	s_setprio 1
	v_mfma_f32_16x16x32_bf16 v[124:127], v[146:149], v[192:195], v[124:127]
	v_mfma_f32_16x16x32_bf16 v[120:123], v[154:157], v[192:195], v[120:123]
	v_mfma_f32_16x16x32_bf16 v[108:111], v[146:149], v[200:203], v[108:111]
	v_mfma_f32_16x16x32_bf16 v[104:107], v[154:157], v[200:203], v[104:107]
	v_mfma_f32_16x16x32_bf16 v[92:95], v[146:149], v[208:211], v[92:95]
	v_mfma_f32_16x16x32_bf16 v[88:91], v[154:157], v[208:211], v[88:91]
	v_mfma_f32_16x16x32_bf16 v[76:79], v[146:149], v[216:219], v[76:79]
	v_mfma_f32_16x16x32_bf16 v[72:75], v[154:157], v[216:219], v[72:75]
	v_mfma_f32_16x16x32_bf16 v[124:127], v[150:153], v[196:199], v[124:127]
	v_mfma_f32_16x16x32_bf16 v[120:123], v[158:161], v[196:199], v[120:123]
	v_mfma_f32_16x16x32_bf16 v[108:111], v[150:153], v[204:207], v[108:111]
	v_mfma_f32_16x16x32_bf16 v[104:107], v[158:161], v[204:207], v[104:107]
	v_mfma_f32_16x16x32_bf16 v[92:95], v[150:153], v[212:215], v[92:95]
	v_mfma_f32_16x16x32_bf16 v[88:91], v[158:161], v[212:215], v[88:91]
	v_mfma_f32_16x16x32_bf16 v[76:79], v[150:153], v[220:223], v[76:79]
	v_mfma_f32_16x16x32_bf16 v[72:75], v[158:161], v[220:223], v[72:75]
	s_setprio 0
	s_setprio 1
	v_mfma_f32_16x16x32_bf16 v[116:119], v[162:165], v[192:195], v[116:119]
	v_mfma_f32_16x16x32_bf16 v[112:115], v[184:187], v[192:195], v[112:115]
	v_mfma_f32_16x16x32_bf16 v[100:103], v[162:165], v[200:203], v[100:103]
	v_mfma_f32_16x16x32_bf16 v[96:99], v[184:187], v[200:203], v[96:99]
	v_mfma_f32_16x16x32_bf16 v[84:87], v[162:165], v[208:211], v[84:87]
	v_mfma_f32_16x16x32_bf16 v[80:83], v[184:187], v[208:211], v[80:83]
	v_mfma_f32_16x16x32_bf16 v[68:71], v[162:165], v[216:219], v[68:71]
	v_mfma_f32_16x16x32_bf16 v[64:67], v[184:187], v[216:219], v[64:67]
	v_mfma_f32_16x16x32_bf16 v[116:119], v[166:169], v[196:199], v[116:119]
	v_mfma_f32_16x16x32_bf16 v[112:115], v[188:191], v[196:199], v[112:115]
	v_mfma_f32_16x16x32_bf16 v[100:103], v[166:169], v[204:207], v[100:103]
	v_mfma_f32_16x16x32_bf16 v[96:99], v[188:191], v[204:207], v[96:99]
	v_mfma_f32_16x16x32_bf16 v[84:87], v[166:169], v[212:215], v[84:87]
	v_mfma_f32_16x16x32_bf16 v[80:83], v[188:191], v[212:215], v[80:83]
	v_mfma_f32_16x16x32_bf16 v[68:71], v[166:169], v[220:223], v[68:71]
	v_mfma_f32_16x16x32_bf16 v[64:67], v[188:191], v[220:223], v[64:67]
	s_setprio 0
	s_barrier
; #define PG8_STAGE(bufoff, gbase, voff) do { _Pragma("unroll") for (int _i = 0; _i < 2; ++_i) \
;         __builtin_amdgcn_global_load_lds((const unsigned*)((const char*)(gbase) + (voff)[_i]), (PG8_LAS unsigned*)(lds + (bufoff) + ldsw + _i * 8192), 16, 0, 0); } while (0)
; #define PG8_LDA(dst, b, h) do { _Pragma("unroll") for (int m = 0; m < 4; ++m) _Pragma("unroll") for (int k = 0; k < 2; ++k) dst[m][k] = *(const PG8_LAS bf16x8*)(lds + PG8_SA(b, h) + aoff + m * 2048 + k * 1024); } while (0)
; #define PG8_LDB(dst, b, h) do { _Pragma("unroll") for (int n = 0; n < 2; ++n) _Pragma("unroll") for (int k = 0; k < 2; ++k) dst[n][k] = *(const PG8_LAS bf16x8*)(lds + PG8_SB(b, h) + boff + n * 2048 + k * 1024); } while (0)
; #define PG8_MMA(ai, bj, At, Bt) do { __builtin_amdgcn_s_setprio(1); _Pragma("unroll") for (int m = 0; m < 4; ++m) _Pragma("unroll") for (int n = 0; n < 2; ++n) _Pragma("unroll") for (int k = 0; k < 2; ++k) \
;         acc[ai][bj][m][n] = __builtin_amdgcn_mfma_f32_16x16x32_bf16(Bt[n][k], At[m][k], acc[ai][bj][m][n], 0, 0, 0); __builtin_amdgcn_s_setprio(0); } while (0)
; #define PG8_WAIT_V(n) asm volatile("s_waitcnt vmcnt(" #n ")" ::: "memory")
; #define PG8_WAIT_L(n) asm volatile("s_waitcnt lgkmcnt(" #n ")" ::: "memory")
; #define PG8_BAR __builtin_amdgcn_s_barrier()
; #define PG8_SCHED __builtin_amdgcn_sched_barrier(0)
; template <class Epi, class Sched, bool ALIGN_EPI = false, bool SP2 = false>
; __device__ __forceinline__ void gemm_phase(PG8_LAS unsigned char* lds, const Gemm g, const Sched& S, const Epi& E, const int wid) {
;     ...
;             PG8_LDA(At, 0, 1); PG8_STAGE(PG8_SB(0, 0), b2, voffB); PG8_STAGE(PG8_SB(0, 1), b2 + hstepB, voffB); PG8_STAGE(PG8_SA(0, 0), a2, voffA);
;             PG8_WAIT_V(8); PG8_WAIT_L(0); PG8_BAR; PG8_MMA(1, 0, At, B0); PG8_MMA(1, 1, At, B1); PG8_BAR; PG8_SCHED;
;             PG8_LDB(B0, 1, 0); PG8_LDB(B1, 1, 1); PG8_SCHED; PG8_LDA(At, 1, 0); PG8_STAGE(PG8_SA(0, 1), a2 + hstepA, voffA);
	s_add_i32 s72, s69, s45
	s_add_u32 s98, s12, 0x80
	s_addc_u32 s99, s13, 0
	s_mov_b32 m0, s72
	ds_read_b128 v[192:195], v181 offset:16384
	ds_read_b128 v[196:199], v181 offset:17408
	ds_read_b128 v[200:203], v181 offset:18432
	ds_read_b128 v[204:207], v181 offset:19456
	ds_read_b128 v[208:211], v181 offset:20480
	ds_read_b128 v[212:215], v181 offset:21504
	ds_read_b128 v[216:219], v181 offset:22528
	ds_read_b128 v[220:223], v181 offset:23552
	global_load_lds_dwordx4 v130, s[12:13]
	s_add_i32 m0, s72, 0x2000
	s_add_u32 s72, s12, 0x40000
	s_addc_u32 s73, s13, 0
	s_add_i32 s74, s70, s45
	global_load_lds_dwordx4 v134, s[12:13]
	s_mov_b32 m0, s74
	s_add_u32 s100, s38, 0x80
	s_addc_u32 s101, s39, 0
	global_load_lds_dwordx4 v130, s[72:73]
	s_add_i32 m0, s74, 0x2000
	s_nop 0
	global_load_lds_dwordx4 v134, s[72:73]
	s_mov_b32 m0, s46
	s_nop 0
	global_load_lds_dwordx4 v128, s[38:39]
	s_mov_b32 m0, s47
	s_nop 0
	global_load_lds_dwordx4 v132, s[38:39]
	s_waitcnt vmcnt(8) lgkmcnt(0)
	s_barrier
	s_nop 0
	s_setprio 1
	v_mfma_f32_16x16x32_bf16 v[60:63], v[146:149], v[192:195], v[60:63]
	v_mfma_f32_16x16x32_bf16 v[56:59], v[154:157], v[192:195], v[56:59]
	v_mfma_f32_16x16x32_bf16 v[44:47], v[146:149], v[200:203], v[44:47]
	v_mfma_f32_16x16x32_bf16 v[40:43], v[154:157], v[200:203], v[40:43]
	v_mfma_f32_16x16x32_bf16 v[28:31], v[146:149], v[208:211], v[28:31]
	v_mfma_f32_16x16x32_bf16 v[24:27], v[154:157], v[208:211], v[24:27]
	v_mfma_f32_16x16x32_bf16 v[12:15], v[146:149], v[216:219], v[12:15]
	v_mfma_f32_16x16x32_bf16 v[8:11], v[154:157], v[216:219], v[8:11]
	v_mfma_f32_16x16x32_bf16 v[60:63], v[150:153], v[196:199], v[60:63]
	v_mfma_f32_16x16x32_bf16 v[56:59], v[158:161], v[196:199], v[56:59]
	v_mfma_f32_16x16x32_bf16 v[44:47], v[150:153], v[204:207], v[44:47]
	v_mfma_f32_16x16x32_bf16 v[40:43], v[158:161], v[204:207], v[40:43]
	v_mfma_f32_16x16x32_bf16 v[28:31], v[150:153], v[212:215], v[28:31]
	v_mfma_f32_16x16x32_bf16 v[24:27], v[158:161], v[212:215], v[24:27]
	v_mfma_f32_16x16x32_bf16 v[12:15], v[150:153], v[220:223], v[12:15]
	v_mfma_f32_16x16x32_bf16 v[8:11], v[158:161], v[220:223], v[8:11]
	s_setprio 0
	s_setprio 1
	v_mfma_f32_16x16x32_bf16 v[52:55], v[162:165], v[192:195], v[52:55]
	v_mfma_f32_16x16x32_bf16 v[48:51], v[184:187], v[192:195], v[48:51]
	v_mfma_f32_16x16x32_bf16 v[36:39], v[162:165], v[200:203], v[36:39]
	v_mfma_f32_16x16x32_bf16 v[32:35], v[184:187], v[200:203], v[32:35]
	v_mfma_f32_16x16x32_bf16 v[20:23], v[162:165], v[208:211], v[20:23]
	v_mfma_f32_16x16x32_bf16 v[16:19], v[184:187], v[208:211], v[16:19]
	v_mfma_f32_16x16x32_bf16 v[4:7], v[162:165], v[216:219], v[4:7]
	v_mfma_f32_16x16x32_bf16 v[0:3], v[184:187], v[216:219], v[0:3]
	v_mfma_f32_16x16x32_bf16 v[52:55], v[166:169], v[196:199], v[52:55]
	v_mfma_f32_16x16x32_bf16 v[48:51], v[188:191], v[196:199], v[48:51]
	v_mfma_f32_16x16x32_bf16 v[36:39], v[166:169], v[204:207], v[36:39]
	v_mfma_f32_16x16x32_bf16 v[32:35], v[188:191], v[204:207], v[32:35]
	v_mfma_f32_16x16x32_bf16 v[20:23], v[166:169], v[212:215], v[20:23]
	v_mfma_f32_16x16x32_bf16 v[16:19], v[188:191], v[212:215], v[16:19]
	v_mfma_f32_16x16x32_bf16 v[4:7], v[166:169], v[220:223], v[4:7]
	v_mfma_f32_16x16x32_bf16 v[0:3], v[188:191], v[220:223], v[0:3]
	s_setprio 0
	s_barrier
	s_add_i32 s72, 0, 0x18000
	s_add_i32 s73, 0, 0x1c000
	ds_read_b128 v[146:149], v252
	ds_read_b128 v[150:153], v252 offset:1024
	ds_read_b128 v[154:157], v252 offset:2048
	ds_read_b128 v[158:161], v252 offset:3072
	ds_read_b128 v[162:165], v253
	ds_read_b128 v[166:169], v253 offset:1024
	ds_read_b128 v[184:187], v253 offset:2048
	ds_read_b128 v[188:191], v253 offset:3072
	s_add_u32 s38, s38, 0x40000
	s_addc_u32 s39, s39, 0
	s_mov_b32 m0, s48
	ds_read_b128 v[192:195], v181 offset:32768
	ds_read_b128 v[196:199], v181 offset:33792
	ds_read_b128 v[200:203], v181 offset:34816
	ds_read_b128 v[204:207], v181 offset:35840
	ds_read_b128 v[208:211], v181 offset:36864
	ds_read_b128 v[212:215], v181 offset:37888
	ds_read_b128 v[216:219], v181 offset:38912
	ds_read_b128 v[220:223], v181 offset:39936
	global_load_lds_dwordx4 v128, s[38:39]
	s_mov_b32 m0, s49
	s_nop 0
	global_load_lds_dwordx4 v132, s[38:39]
	s_waitcnt vmcnt(8) lgkmcnt(0)
	s_barrier
; #define PG8_STAGE(bufoff, gbase, voff) do { _Pragma("unroll") for (int _i = 0; _i < 2; ++_i) \
;         __builtin_amdgcn_global_load_lds((const unsigned*)((const char*)(gbase) + (voff)[_i]), (PG8_LAS unsigned*)(lds + (bufoff) + ldsw + _i * 8192), 16, 0, 0); } while (0)
; #define PG8_LDA(dst, b, h) do { _Pragma("unroll") for (int m = 0; m < 4; ++m) _Pragma("unroll") for (int k = 0; k < 2; ++k) dst[m][k] = *(const PG8_LAS bf16x8*)(lds + PG8_SA(b, h) + aoff + m * 2048 + k * 1024); } while (0)
; #define PG8_MMA(ai, bj, At, Bt) do { __builtin_amdgcn_s_setprio(1); _Pragma("unroll") for (int m = 0; m < 4; ++m) _Pragma("unroll") for (int n = 0; n < 2; ++n) _Pragma("unroll") for (int k = 0; k < 2; ++k) \
;         acc[ai][bj][m][n] = __builtin_amdgcn_mfma_f32_16x16x32_bf16(Bt[n][k], At[m][k], acc[ai][bj][m][n], 0, 0, 0); __builtin_amdgcn_s_setprio(0); } while (0)
; #define PG8_WAIT_V(n) asm volatile("s_waitcnt vmcnt(" #n ")" ::: "memory")
; #define PG8_WAIT_L(n) asm volatile("s_waitcnt lgkmcnt(" #n ")" ::: "memory")
; #define PG8_BAR __builtin_amdgcn_s_barrier()
; #define PG8_SCHED __builtin_amdgcn_sched_barrier(0)
; template <class Epi, class Sched, bool ALIGN_EPI = false, bool SP2 = false>
; __device__ __forceinline__ void gemm_phase(PG8_LAS unsigned char* lds, const Gemm g, const Sched& S, const Epi& E, const int wid) {
;     ...
;             PG8_WAIT_V(8); PG8_WAIT_L(0); PG8_BAR; PG8_MMA(0, 0, At, B0); PG8_MMA(0, 1, At, B1); PG8_BAR; PG8_SCHED;
;             PG8_LDA(At, 1, 1); PG8_STAGE(PG8_SB(1, 0), b3, voffB); PG8_STAGE(PG8_SB(1, 1), b3 + hstepB, voffB); PG8_STAGE(PG8_SA(1, 0), a3, voffA);
;             PG8_WAIT_V(8); PG8_WAIT_L(0); PG8_BAR; PG8_MMA(1, 0, At, B0); PG8_MMA(1, 1, At, B1); PG8_BAR; PG8_SCHED;
;     ...
;         if constexpr (ALIGN_EPI) { if (wr == 0) PG8_BAR; }
	s_nop 0
	s_setprio 1
	v_mfma_f32_16x16x32_bf16 v[124:127], v[146:149], v[192:195], v[124:127]
	v_mfma_f32_16x16x32_bf16 v[120:123], v[154:157], v[192:195], v[120:123]
	v_mfma_f32_16x16x32_bf16 v[108:111], v[146:149], v[200:203], v[108:111]
	v_mfma_f32_16x16x32_bf16 v[104:107], v[154:157], v[200:203], v[104:107]
	v_mfma_f32_16x16x32_bf16 v[92:95], v[146:149], v[208:211], v[92:95]
	v_mfma_f32_16x16x32_bf16 v[88:91], v[154:157], v[208:211], v[88:91]
	v_mfma_f32_16x16x32_bf16 v[76:79], v[146:149], v[216:219], v[76:79]
	v_mfma_f32_16x16x32_bf16 v[72:75], v[154:157], v[216:219], v[72:75]
	v_mfma_f32_16x16x32_bf16 v[124:127], v[150:153], v[196:199], v[124:127]
	v_mfma_f32_16x16x32_bf16 v[120:123], v[158:161], v[196:199], v[120:123]
	v_mfma_f32_16x16x32_bf16 v[108:111], v[150:153], v[204:207], v[108:111]
	v_mfma_f32_16x16x32_bf16 v[104:107], v[158:161], v[204:207], v[104:107]
	v_mfma_f32_16x16x32_bf16 v[92:95], v[150:153], v[212:215], v[92:95]
	v_mfma_f32_16x16x32_bf16 v[88:91], v[158:161], v[212:215], v[88:91]
	v_mfma_f32_16x16x32_bf16 v[76:79], v[150:153], v[220:223], v[76:79]
	v_mfma_f32_16x16x32_bf16 v[72:75], v[158:161], v[220:223], v[72:75]
	s_setprio 0
	s_setprio 1
	v_mfma_f32_16x16x32_bf16 v[116:119], v[162:165], v[192:195], v[116:119]
	v_mfma_f32_16x16x32_bf16 v[112:115], v[184:187], v[192:195], v[112:115]
	v_mfma_f32_16x16x32_bf16 v[100:103], v[162:165], v[200:203], v[100:103]
	v_mfma_f32_16x16x32_bf16 v[96:99], v[184:187], v[200:203], v[96:99]
	v_mfma_f32_16x16x32_bf16 v[84:87], v[162:165], v[208:211], v[84:87]
	v_mfma_f32_16x16x32_bf16 v[80:83], v[184:187], v[208:211], v[80:83]
	v_mfma_f32_16x16x32_bf16 v[68:71], v[162:165], v[216:219], v[68:71]
	v_mfma_f32_16x16x32_bf16 v[64:67], v[184:187], v[216:219], v[64:67]
	v_mfma_f32_16x16x32_bf16 v[116:119], v[166:169], v[196:199], v[116:119]
	v_mfma_f32_16x16x32_bf16 v[112:115], v[188:191], v[196:199], v[112:115]
	v_mfma_f32_16x16x32_bf16 v[100:103], v[166:169], v[204:207], v[100:103]
	v_mfma_f32_16x16x32_bf16 v[96:99], v[188:191], v[204:207], v[96:99]
	v_mfma_f32_16x16x32_bf16 v[84:87], v[166:169], v[212:215], v[84:87]
	v_mfma_f32_16x16x32_bf16 v[80:83], v[188:191], v[212:215], v[80:83]
	v_mfma_f32_16x16x32_bf16 v[68:71], v[166:169], v[220:223], v[68:71]
	v_mfma_f32_16x16x32_bf16 v[64:67], v[188:191], v[220:223], v[64:67]
	s_setprio 0
	s_barrier
	s_add_i32 s38, s72, s45
	s_mov_b32 m0, s38
	ds_read_b128 v[192:195], v181 offset:49152
	ds_read_b128 v[196:199], v181 offset:50176
	ds_read_b128 v[200:203], v181 offset:51200
	ds_read_b128 v[204:207], v181 offset:52224
	ds_read_b128 v[208:211], v181 offset:53248
	ds_read_b128 v[212:215], v181 offset:54272
	ds_read_b128 v[216:219], v181 offset:55296
	ds_read_b128 v[220:223], v181 offset:56320
	global_load_lds_dwordx4 v130, s[98:99]
	s_add_i32 m0, s38, 0x2000
	s_add_u32 s12, s12, 0x40080
	s_addc_u32 s13, s13, 0
	s_add_i32 s38, s73, s45
	global_load_lds_dwordx4 v134, s[98:99]
	s_mov_b32 m0, s38
	s_nop 0
	global_load_lds_dwordx4 v130, s[12:13]
	s_add_i32 m0, s38, 0x2000
	s_nop 0
	global_load_lds_dwordx4 v134, s[12:13]
	s_mov_b32 m0, s65
	s_nop 0
	global_load_lds_dwordx4 v128, s[100:101]
	s_mov_b32 m0, s66
	s_nop 0
	global_load_lds_dwordx4 v132, s[100:101]
	s_waitcnt vmcnt(8) lgkmcnt(0)
	s_barrier
	s_setprio 1
	v_mfma_f32_16x16x32_bf16 v[60:63], v[146:149], v[192:195], v[60:63]
	v_mfma_f32_16x16x32_bf16 v[56:59], v[154:157], v[192:195], v[56:59]
	v_mfma_f32_16x16x32_bf16 v[44:47], v[146:149], v[200:203], v[44:47]
	v_mfma_f32_16x16x32_bf16 v[40:43], v[154:157], v[200:203], v[40:43]
	v_mfma_f32_16x16x32_bf16 v[28:31], v[146:149], v[208:211], v[28:31]
	v_mfma_f32_16x16x32_bf16 v[24:27], v[154:157], v[208:211], v[24:27]
	v_mfma_f32_16x16x32_bf16 v[12:15], v[146:149], v[216:219], v[12:15]
	v_mfma_f32_16x16x32_bf16 v[8:11], v[154:157], v[216:219], v[8:11]
	v_mfma_f32_16x16x32_bf16 v[60:63], v[150:153], v[196:199], v[60:63]
	v_mfma_f32_16x16x32_bf16 v[56:59], v[158:161], v[196:199], v[56:59]
	v_mfma_f32_16x16x32_bf16 v[44:47], v[150:153], v[204:207], v[44:47]
	v_mfma_f32_16x16x32_bf16 v[40:43], v[158:161], v[204:207], v[40:43]
	v_mfma_f32_16x16x32_bf16 v[28:31], v[150:153], v[212:215], v[28:31]
	v_mfma_f32_16x16x32_bf16 v[24:27], v[158:161], v[212:215], v[24:27]
	v_mfma_f32_16x16x32_bf16 v[12:15], v[150:153], v[220:223], v[12:15]
	v_mfma_f32_16x16x32_bf16 v[8:11], v[158:161], v[220:223], v[8:11]
	s_setprio 0
	s_setprio 1
	v_mfma_f32_16x16x32_bf16 v[52:55], v[162:165], v[192:195], v[52:55]
	v_mfma_f32_16x16x32_bf16 v[48:51], v[184:187], v[192:195], v[48:51]
	v_mfma_f32_16x16x32_bf16 v[36:39], v[162:165], v[200:203], v[36:39]
	v_mfma_f32_16x16x32_bf16 v[32:35], v[184:187], v[200:203], v[32:35]
	v_mfma_f32_16x16x32_bf16 v[20:23], v[162:165], v[208:211], v[20:23]
	v_mfma_f32_16x16x32_bf16 v[16:19], v[184:187], v[208:211], v[16:19]
	v_mfma_f32_16x16x32_bf16 v[4:7], v[162:165], v[216:219], v[4:7]
	v_mfma_f32_16x16x32_bf16 v[0:3], v[184:187], v[216:219], v[0:3]
	v_mfma_f32_16x16x32_bf16 v[52:55], v[166:169], v[196:199], v[52:55]
	v_mfma_f32_16x16x32_bf16 v[48:51], v[188:191], v[196:199], v[48:51]
	v_mfma_f32_16x16x32_bf16 v[36:39], v[166:169], v[204:207], v[36:39]
	v_mfma_f32_16x16x32_bf16 v[32:35], v[188:191], v[204:207], v[32:35]
	v_mfma_f32_16x16x32_bf16 v[20:23], v[166:169], v[212:215], v[20:23]
	v_mfma_f32_16x16x32_bf16 v[16:19], v[188:191], v[212:215], v[16:19]
	v_mfma_f32_16x16x32_bf16 v[4:7], v[166:169], v[220:223], v[4:7]
	v_mfma_f32_16x16x32_bf16 v[0:3], v[188:191], v[220:223], v[0:3]
	s_setprio 0
	s_barrier
	s_add_i32 s71, s71, 2
	s_add_u32 s8, s8, 0x100
	s_addc_u32 s9, s9, 0
	s_add_u32 s40, s40, 0x100
	s_addc_u32 s41, s41, 0
	s_cmp_gt_u32 s71, 13
	s_cbranch_scc0 .LBB0_2049
	s_and_b64 vcc, exec, s[20:21]
	s_cbranch_vccz .LBB0_2052
	s_barrier

; #define PG8_STAGE(bufoff, gbase, voff) do { _Pragma("unroll") for (int _i = 0; _i < 2; ++_i) \
;         __builtin_amdgcn_global_load_lds((const unsigned*)((const char*)(gbase) + (voff)[_i]), (PG8_LAS unsigned*)(lds + (bufoff) + ldsw + _i * 8192), 16, 0, 0); } while (0)
; #define PG8_LDA(dst, b, h) do { _Pragma("unroll") for (int m = 0; m < 4; ++m) _Pragma("unroll") for (int k = 0; k < 2; ++k) dst[m][k] = *(const PG8_LAS bf16x8*)(lds + PG8_SA(b, h) + aoff + m * 2048 + k * 1024); } while (0)
; #define PG8_LDB(dst, b, h) do { _Pragma("unroll") for (int n = 0; n < 2; ++n) _Pragma("unroll") for (int k = 0; k < 2; ++k) dst[n][k] = *(const PG8_LAS bf16x8*)(lds + PG8_SB(b, h) + boff + n * 2048 + k * 1024); } while (0)
; #define PG8_WAIT_V(n) asm volatile("s_waitcnt vmcnt(" #n ")" ::: "memory")
; #define PG8_WAIT_L(n) asm volatile("s_waitcnt lgkmcnt(" #n ")" ::: "memory")
; #define PG8_BAR __builtin_amdgcn_s_barrier()
; #define PG8_SCHED __builtin_amdgcn_sched_barrier(0)
; template <class Epi, class Sched, bool ALIGN_EPI = false, bool SP2 = false>
; __device__ __forceinline__ void gemm_phase(PG8_LAS unsigned char* lds, const Gemm g, const Sched& S, const Epi& E, const int wid) {
;     ...
;         const bool has_next = S.next(ui + 1, nxt);
;         const char* nA = has_next ? (const char*)g.A + (size_t)nxt.pm * tstepA : cA; const char* nB = has_next ? (const char*)g.Bt + (size_t)nxt.pn * tstepB : cB;
;         for (int t = 0; t < nt; t += 2) {
;             const bool last = (t == nt - 2);
;             const char* a1 = cA + (size_t)(t + 1) * kstep;
;             const char* a2 = last ? nA : cA + (size_t)(t + 2) * kstep; const char* b2 = last ? nB : cB + (size_t)(t + 2) * kstep;
;             const char* a3 = a2 + kstep; const char* b3 = b2 + kstep;
;             if (last && has_next) S.a_ready(nxt);
;             if constexpr (SP2) {
;             PG8_LDB(B0, 0, 0); PG8_LDB(B1, 0, 1); PG8_SCHED; PG8_LDA(At, 0, 0); PG8_STAGE(PG8_SA(1, 1), a1 + hstepA, voffA);
;             PG8_WAIT_V(8); PG8_WAIT_L(0); PG8_BAR; PG8_MMA(0, 0, At, B0); PG8_MMA(0, 1, At, B1); PG8_BAR; PG8_SCHED;
;             PG8_LDA(At, 0, 1); PG8_STAGE(PG8_SB(0, 0), b2, voffB); PG8_STAGE(PG8_SB(0, 1), b2 + hstepB, voffB); PG8_STAGE(PG8_SA(0, 0), a2, voffA);
;             PG8_WAIT_V(8); PG8_WAIT_L(0); PG8_BAR; PG8_MMA(1, 0, At, B0); PG8_MMA(1, 1, At, B1); PG8_BAR; PG8_SCHED;
.LBB0_2279:
	s_ashr_i32 s19, s18, 31
	s_lshl_b64 s[20:21], s[18:19], 20
	s_add_u32 s20, s65, s20
	s_addc_u32 s21, s66, s21
	s_and_b64 s[22:23], s[2:3], exec
	s_cselect_b32 s19, s21, s29
	s_cselect_b32 s81, s20, s28
	s_ashr_i32 s17, s16, 31
	s_lshl_b64 s[22:23], s[16:17], 17
	s_add_u32 s22, s67, s22
	s_addc_u32 s23, s68, s23
	s_and_b64 s[30:31], s[2:3], exec
	s_cselect_b32 s17, s23, s27
	s_cselect_b32 s82, s22, s26
	s_mov_b32 s36, 0
	s_mov_b64 s[30:31], -1
	s_mov_b64 s[34:35], 0
	v_add_u32_e32 v252, 0x18000, v156
	v_add_u32_e32 v253, 0x1c000, v156
	s_add_u32 s37, s28, s36
	s_addc_u32 s44, s29, 0
	s_add_u32 s40, s37, 0x100
	s_addc_u32 s41, s44, 0
	s_and_b64 s[38:39], s[34:35], exec
	s_cselect_b32 s39, s19, s41
	s_cselect_b32 s38, s81, s40
	s_add_u32 s36, s26, s36
	s_addc_u32 s40, s27, 0
	s_add_u32 s36, s36, 0x100
	s_addc_u32 s40, s40, 0
	s_and_b64 s[34:35], s[34:35], exec
	s_cselect_b32 s41, s17, s40
	s_cselect_b32 s40, s82, s36
	s_add_u32 s46, s37, 0x80080
	ds_read_b128 v[142:145], v157
	ds_read_b128 v[146:149], v157 offset:1024
	ds_read_b128 v[150:153], v157 offset:2048
	ds_read_b128 v[162:165], v157 offset:3072
	ds_read_b128 v[166:169], v158
	ds_read_b128 v[170:173], v158 offset:1024
	ds_read_b128 v[174:177], v158 offset:2048
	ds_read_b128 v[178:181], v158 offset:3072
	s_addc_u32 s47, s44, 0
	s_add_i32 s93, s77, s0
	s_add_i32 m0, s70, 0xc000
	s_add_i32 s94, s70, 0xe000
	s_add_i32 s89, s93, 0x2000
	s_add_u32 s44, s40, 0x10000
	s_addc_u32 s45, s41, 0
	s_add_i32 s92, s78, s0
	s_add_i32 s91, s92, 0x2000
	s_add_i32 s88, 0, 0x18000
	s_add_i32 s87, 0, 0x1c000
	s_add_u32 s36, s38, 0x80000
	s_addc_u32 s37, s39, 0
	s_add_i32 s86, s88, s0
	s_add_i32 s84, s86, 0x2000
	s_add_u32 s34, s40, 0x10080
	s_addc_u32 s35, s41, 0
	s_add_i32 s85, s87, s0
	s_add_i32 s83, s85, 0x2000
	ds_read_b128 v[182:185], v159
	ds_read_b128 v[186:189], v159 offset:1024
	ds_read_b128 v[190:193], v159 offset:2048
	ds_read_b128 v[194:197], v159 offset:3072
	ds_read_b128 v[198:201], v159 offset:4096
	ds_read_b128 v[202:205], v159 offset:5120
	ds_read_b128 v[206:209], v159 offset:6144
	ds_read_b128 v[210:213], v159 offset:7168
	global_load_lds_dwordx4 v134, s[46:47]
	s_mov_b32 m0, s94
	s_nop 0
	global_load_lds_dwordx4 v130, s[46:47]
	s_waitcnt vmcnt(8) lgkmcnt(0)
	s_barrier
	s_setprio 1
	v_mfma_f32_16x16x32_bf16 v[124:127], v[142:145], v[182:185], 0
	v_mfma_f32_16x16x32_bf16 v[120:123], v[150:153], v[182:185], 0
	v_mfma_f32_16x16x32_bf16 v[116:119], v[142:145], v[190:193], 0
	v_mfma_f32_16x16x32_bf16 v[112:115], v[150:153], v[190:193], 0
	v_mfma_f32_16x16x32_bf16 v[100:103], v[142:145], v[198:201], 0
	v_mfma_f32_16x16x32_bf16 v[96:99], v[150:153], v[198:201], 0
	v_mfma_f32_16x16x32_bf16 v[84:87], v[142:145], v[206:209], 0
	v_mfma_f32_16x16x32_bf16 v[80:83], v[150:153], v[206:209], 0
	v_mfma_f32_16x16x32_bf16 v[124:127], v[146:149], v[186:189], v[124:127]
	v_mfma_f32_16x16x32_bf16 v[120:123], v[162:165], v[186:189], v[120:123]
	v_mfma_f32_16x16x32_bf16 v[116:119], v[146:149], v[194:197], v[116:119]
	v_mfma_f32_16x16x32_bf16 v[112:115], v[162:165], v[194:197], v[112:115]
	v_mfma_f32_16x16x32_bf16 v[100:103], v[146:149], v[202:205], v[100:103]
	v_mfma_f32_16x16x32_bf16 v[96:99], v[162:165], v[202:205], v[96:99]
	v_mfma_f32_16x16x32_bf16 v[84:87], v[146:149], v[210:213], v[84:87]
	v_mfma_f32_16x16x32_bf16 v[80:83], v[162:165], v[210:213], v[80:83]
	s_setprio 0
	s_setprio 1
	v_mfma_f32_16x16x32_bf16 v[108:111], v[166:169], v[182:185], 0
	v_mfma_f32_16x16x32_bf16 v[104:107], v[174:177], v[182:185], 0
	v_mfma_f32_16x16x32_bf16 v[92:95], v[166:169], v[190:193], 0
	v_mfma_f32_16x16x32_bf16 v[88:91], v[174:177], v[190:193], 0
	v_mfma_f32_16x16x32_bf16 v[76:79], v[166:169], v[198:201], 0
	v_mfma_f32_16x16x32_bf16 v[72:75], v[174:177], v[198:201], 0
	v_mfma_f32_16x16x32_bf16 v[68:71], v[166:169], v[206:209], 0
	v_mfma_f32_16x16x32_bf16 v[64:67], v[174:177], v[206:209], 0
	v_mfma_f32_16x16x32_bf16 v[108:111], v[170:173], v[186:189], v[108:111]
	v_mfma_f32_16x16x32_bf16 v[104:107], v[178:181], v[186:189], v[104:107]
	v_mfma_f32_16x16x32_bf16 v[92:95], v[170:173], v[194:197], v[92:95]
	v_mfma_f32_16x16x32_bf16 v[88:91], v[178:181], v[194:197], v[88:91]
	v_mfma_f32_16x16x32_bf16 v[76:79], v[170:173], v[202:205], v[76:79]
	v_mfma_f32_16x16x32_bf16 v[72:75], v[178:181], v[202:205], v[72:75]
	v_mfma_f32_16x16x32_bf16 v[68:71], v[170:173], v[210:213], v[68:71]
	v_mfma_f32_16x16x32_bf16 v[64:67], v[178:181], v[210:213], v[64:67]
	s_setprio 0
	s_barrier
	s_mov_b32 m0, s93
	s_add_u32 s98, s40, 0x80
	s_addc_u32 s99, s41, 0
	ds_read_b128 v[182:185], v159 offset:16384
	ds_read_b128 v[186:189], v159 offset:17408
	ds_read_b128 v[190:193], v159 offset:18432
	ds_read_b128 v[194:197], v159 offset:19456
	ds_read_b128 v[198:201], v159 offset:20480
	ds_read_b128 v[202:205], v159 offset:21504
	ds_read_b128 v[206:209], v159 offset:22528
	ds_read_b128 v[210:213], v159 offset:23552
	global_load_lds_dwordx4 v132, s[40:41]
	s_mov_b32 m0, s89
	s_nop 0
	global_load_lds_dwordx4 v128, s[40:41]
	s_mov_b32 m0, s92
	s_add_u32 s100, s38, 0x80
	s_addc_u32 s101, s39, 0
	global_load_lds_dwordx4 v132, s[44:45]
	s_mov_b32 m0, s91
	s_nop 0
	global_load_lds_dwordx4 v128, s[44:45]
	s_mov_b32 m0, s70
	s_nop 0
	global_load_lds_dwordx4 v134, s[38:39]
	s_mov_b32 m0, s71
	s_nop 0
	global_load_lds_dwordx4 v130, s[38:39]
	s_waitcnt vmcnt(8) lgkmcnt(0)
	s_barrier
; #define PG8_STAGE(bufoff, gbase, voff) do { _Pragma("unroll") for (int _i = 0; _i < 2; ++_i) \
;         __builtin_amdgcn_global_load_lds((const unsigned*)((const char*)(gbase) + (voff)[_i]), (PG8_LAS unsigned*)(lds + (bufoff) + ldsw + _i * 8192), 16, 0, 0); } while (0)
; #define PG8_LDA(dst, b, h) do { _Pragma("unroll") for (int m = 0; m < 4; ++m) _Pragma("unroll") for (int k = 0; k < 2; ++k) dst[m][k] = *(const PG8_LAS bf16x8*)(lds + PG8_SA(b, h) + aoff + m * 2048 + k * 1024); } while (0)
; #define PG8_LDB(dst, b, h) do { _Pragma("unroll") for (int n = 0; n < 2; ++n) _Pragma("unroll") for (int k = 0; k < 2; ++k) dst[n][k] = *(const PG8_LAS bf16x8*)(lds + PG8_SB(b, h) + boff + n * 2048 + k * 1024); } while (0)
; #define PG8_MMA(ai, bj, At, Bt) do { __builtin_amdgcn_s_setprio(1); _Pragma("unroll") for (int m = 0; m < 4; ++m) _Pragma("unroll") for (int n = 0; n < 2; ++n) _Pragma("unroll") for (int k = 0; k < 2; ++k) \
;         acc[ai][bj][m][n] = __builtin_amdgcn_mfma_f32_16x16x32_bf16(Bt[n][k], At[m][k], acc[ai][bj][m][n], 0, 0, 0); __builtin_amdgcn_s_setprio(0); } while (0)
; #define PG8_WAIT_V(n) asm volatile("s_waitcnt vmcnt(" #n ")" ::: "memory")
; #define PG8_WAIT_L(n) asm volatile("s_waitcnt lgkmcnt(" #n ")" ::: "memory")
; #define PG8_BAR __builtin_amdgcn_s_barrier()
; #define PG8_SCHED __builtin_amdgcn_sched_barrier(0)
; template <class Epi, class Sched, bool ALIGN_EPI = false, bool SP2 = false>
; __device__ __forceinline__ void gemm_phase(PG8_LAS unsigned char* lds, const Gemm g, const Sched& S, const Epi& E, const int wid) {
;     ...
;             PG8_WAIT_V(8); PG8_WAIT_L(0); PG8_BAR; PG8_MMA(0, 0, At, B0); PG8_MMA(0, 1, At, B1); PG8_BAR; PG8_SCHED;
;             PG8_LDA(At, 0, 1); PG8_STAGE(PG8_SB(0, 0), b2, voffB); PG8_STAGE(PG8_SB(0, 1), b2 + hstepB, voffB); PG8_STAGE(PG8_SA(0, 0), a2, voffA);
;             PG8_WAIT_V(8); PG8_WAIT_L(0); PG8_BAR; PG8_MMA(1, 0, At, B0); PG8_MMA(1, 1, At, B1); PG8_BAR; PG8_SCHED;
;             PG8_LDB(B0, 1, 0); PG8_LDB(B1, 1, 1); PG8_SCHED; PG8_LDA(At, 1, 0); PG8_STAGE(PG8_SA(0, 1), a2 + hstepA, voffA);
;             PG8_WAIT_V(8); PG8_WAIT_L(0); PG8_BAR; PG8_MMA(0, 0, At, B0); PG8_MMA(0, 1, At, B1); PG8_BAR; PG8_SCHED;
	s_nop 0
	s_setprio 1
	v_mfma_f32_16x16x32_bf16 v[60:63], v[142:145], v[182:185], 0
	v_mfma_f32_16x16x32_bf16 v[56:59], v[150:153], v[182:185], 0
	v_mfma_f32_16x16x32_bf16 v[52:55], v[142:145], v[190:193], 0
	v_mfma_f32_16x16x32_bf16 v[48:51], v[150:153], v[190:193], 0
	v_mfma_f32_16x16x32_bf16 v[36:39], v[142:145], v[198:201], 0
	v_mfma_f32_16x16x32_bf16 v[32:35], v[150:153], v[198:201], 0
	v_mfma_f32_16x16x32_bf16 v[20:23], v[142:145], v[206:209], 0
	v_mfma_f32_16x16x32_bf16 v[16:19], v[150:153], v[206:209], 0
	v_mfma_f32_16x16x32_bf16 v[60:63], v[146:149], v[186:189], v[60:63]
	v_mfma_f32_16x16x32_bf16 v[56:59], v[162:165], v[186:189], v[56:59]
	v_mfma_f32_16x16x32_bf16 v[52:55], v[146:149], v[194:197], v[52:55]
	v_mfma_f32_16x16x32_bf16 v[48:51], v[162:165], v[194:197], v[48:51]
	v_mfma_f32_16x16x32_bf16 v[36:39], v[146:149], v[202:205], v[36:39]
	v_mfma_f32_16x16x32_bf16 v[32:35], v[162:165], v[202:205], v[32:35]
	v_mfma_f32_16x16x32_bf16 v[20:23], v[146:149], v[210:213], v[20:23]
	v_mfma_f32_16x16x32_bf16 v[16:19], v[162:165], v[210:213], v[16:19]
	s_setprio 0
	s_setprio 1
	v_mfma_f32_16x16x32_bf16 v[44:47], v[166:169], v[182:185], 0
	v_mfma_f32_16x16x32_bf16 v[40:43], v[174:177], v[182:185], 0
	v_mfma_f32_16x16x32_bf16 v[28:31], v[166:169], v[190:193], 0
	v_mfma_f32_16x16x32_bf16 v[24:27], v[174:177], v[190:193], 0
	v_mfma_f32_16x16x32_bf16 v[12:15], v[166:169], v[198:201], 0
	v_mfma_f32_16x16x32_bf16 v[8:11], v[174:177], v[198:201], 0
	v_mfma_f32_16x16x32_bf16 v[4:7], v[166:169], v[206:209], 0
	v_mfma_f32_16x16x32_bf16 v[0:3], v[174:177], v[206:209], 0
	v_mfma_f32_16x16x32_bf16 v[44:47], v[170:173], v[186:189], v[44:47]
	v_mfma_f32_16x16x32_bf16 v[40:43], v[178:181], v[186:189], v[40:43]
	v_mfma_f32_16x16x32_bf16 v[28:31], v[170:173], v[194:197], v[28:31]
	v_mfma_f32_16x16x32_bf16 v[24:27], v[178:181], v[194:197], v[24:27]
	v_mfma_f32_16x16x32_bf16 v[12:15], v[170:173], v[202:205], v[12:15]
	v_mfma_f32_16x16x32_bf16 v[8:11], v[178:181], v[202:205], v[8:11]
	v_mfma_f32_16x16x32_bf16 v[4:7], v[170:173], v[210:213], v[4:7]
	v_mfma_f32_16x16x32_bf16 v[0:3], v[178:181], v[210:213], v[0:3]
	s_setprio 0
	s_barrier
	ds_read_b128 v[142:145], v252
	ds_read_b128 v[146:149], v252 offset:1024
	ds_read_b128 v[150:153], v252 offset:2048
	ds_read_b128 v[162:165], v252 offset:3072
	ds_read_b128 v[166:169], v253
	ds_read_b128 v[170:173], v253 offset:1024
	ds_read_b128 v[174:177], v253 offset:2048
	ds_read_b128 v[178:181], v253 offset:3072
	s_mov_b32 m0, s72
	ds_read_b128 v[182:185], v159 offset:32768
	ds_read_b128 v[186:189], v159 offset:33792
	ds_read_b128 v[190:193], v159 offset:34816
	ds_read_b128 v[194:197], v159 offset:35840
	ds_read_b128 v[198:201], v159 offset:36864
	ds_read_b128 v[202:205], v159 offset:37888
	ds_read_b128 v[206:209], v159 offset:38912
	ds_read_b128 v[210:213], v159 offset:39936
	global_load_lds_dwordx4 v134, s[36:37]
	s_mov_b32 m0, s73
	s_nop 0
	global_load_lds_dwordx4 v130, s[36:37]
	s_waitcnt vmcnt(8) lgkmcnt(0)
	s_barrier
	s_setprio 1
	v_mfma_f32_16x16x32_bf16 v[124:127], v[142:145], v[182:185], v[124:127]
	v_mfma_f32_16x16x32_bf16 v[120:123], v[150:153], v[182:185], v[120:123]
	v_mfma_f32_16x16x32_bf16 v[116:119], v[142:145], v[190:193], v[116:119]
	v_mfma_f32_16x16x32_bf16 v[112:115], v[150:153], v[190:193], v[112:115]
	v_mfma_f32_16x16x32_bf16 v[100:103], v[142:145], v[198:201], v[100:103]
	v_mfma_f32_16x16x32_bf16 v[96:99], v[150:153], v[198:201], v[96:99]
	v_mfma_f32_16x16x32_bf16 v[84:87], v[142:145], v[206:209], v[84:87]
	v_mfma_f32_16x16x32_bf16 v[80:83], v[150:153], v[206:209], v[80:83]
	v_mfma_f32_16x16x32_bf16 v[124:127], v[146:149], v[186:189], v[124:127]
	v_mfma_f32_16x16x32_bf16 v[120:123], v[162:165], v[186:189], v[120:123]
	v_mfma_f32_16x16x32_bf16 v[116:119], v[146:149], v[194:197], v[116:119]
	v_mfma_f32_16x16x32_bf16 v[112:115], v[162:165], v[194:197], v[112:115]
	v_mfma_f32_16x16x32_bf16 v[100:103], v[146:149], v[202:205], v[100:103]
	v_mfma_f32_16x16x32_bf16 v[96:99], v[162:165], v[202:205], v[96:99]
	v_mfma_f32_16x16x32_bf16 v[84:87], v[146:149], v[210:213], v[84:87]
	v_mfma_f32_16x16x32_bf16 v[80:83], v[162:165], v[210:213], v[80:83]
	s_setprio 0
	s_setprio 1
	v_mfma_f32_16x16x32_bf16 v[108:111], v[166:169], v[182:185], v[108:111]
	v_mfma_f32_16x16x32_bf16 v[104:107], v[174:177], v[182:185], v[104:107]
	v_mfma_f32_16x16x32_bf16 v[92:95], v[166:169], v[190:193], v[92:95]
	v_mfma_f32_16x16x32_bf16 v[88:91], v[174:177], v[190:193], v[88:91]
	v_mfma_f32_16x16x32_bf16 v[76:79], v[166:169], v[198:201], v[76:79]
	v_mfma_f32_16x16x32_bf16 v[72:75], v[174:177], v[198:201], v[72:75]
	v_mfma_f32_16x16x32_bf16 v[68:71], v[166:169], v[206:209], v[68:71]
	v_mfma_f32_16x16x32_bf16 v[64:67], v[174:177], v[206:209], v[64:67]
	v_mfma_f32_16x16x32_bf16 v[108:111], v[170:173], v[186:189], v[108:111]
	v_mfma_f32_16x16x32_bf16 v[104:107], v[178:181], v[186:189], v[104:107]
	v_mfma_f32_16x16x32_bf16 v[92:95], v[170:173], v[194:197], v[92:95]
	v_mfma_f32_16x16x32_bf16 v[88:91], v[178:181], v[194:197], v[88:91]
	v_mfma_f32_16x16x32_bf16 v[76:79], v[170:173], v[202:205], v[76:79]
	v_mfma_f32_16x16x32_bf16 v[72:75], v[178:181], v[202:205], v[72:75]
	v_mfma_f32_16x16x32_bf16 v[68:71], v[170:173], v[210:213], v[68:71]
	v_mfma_f32_16x16x32_bf16 v[64:67], v[178:181], v[210:213], v[64:67]
	s_setprio 0
	s_barrier
; #define PG8_STAGE(bufoff, gbase, voff) do { _Pragma("unroll") for (int _i = 0; _i < 2; ++_i) \
;         __builtin_amdgcn_global_load_lds((const unsigned*)((const char*)(gbase) + (voff)[_i]), (PG8_LAS unsigned*)(lds + (bufoff) + ldsw + _i * 8192), 16, 0, 0); } while (0)
; #define PG8_LDA(dst, b, h) do { _Pragma("unroll") for (int m = 0; m < 4; ++m) _Pragma("unroll") for (int k = 0; k < 2; ++k) dst[m][k] = *(const PG8_LAS bf16x8*)(lds + PG8_SA(b, h) + aoff + m * 2048 + k * 1024); } while (0)
; #define PG8_LDB(dst, b, h) do { _Pragma("unroll") for (int n = 0; n < 2; ++n) _Pragma("unroll") for (int k = 0; k < 2; ++k) dst[n][k] = *(const PG8_LAS bf16x8*)(lds + PG8_SB(b, h) + boff + n * 2048 + k * 1024); } while (0)
; #define PG8_MMA(ai, bj, At, Bt) do { __builtin_amdgcn_s_setprio(1); _Pragma("unroll") for (int m = 0; m < 4; ++m) _Pragma("unroll") for (int n = 0; n < 2; ++n) _Pragma("unroll") for (int k = 0; k < 2; ++k) \
;         acc[ai][bj][m][n] = __builtin_amdgcn_mfma_f32_16x16x32_bf16(Bt[n][k], At[m][k], acc[ai][bj][m][n], 0, 0, 0); __builtin_amdgcn_s_setprio(0); } while (0)
; template <class Epi, class Sched, bool ALIGN_EPI = false, bool SP2 = false>
; __device__ __forceinline__ void gemm_phase(PG8_LAS unsigned char* lds, const Gemm g, const Sched& S, const Epi& E, const int wid) {
;     ...
;         const bool has_next = S.next(ui + 1, nxt);
;         const char* nA = has_next ? (const char*)g.A + (size_t)nxt.pm * tstepA : cA; const char* nB = has_next ? (const char*)g.Bt + (size_t)nxt.pn * tstepB : cB;
;         for (int t = 0; t < nt; t += 2) {
;             const bool last = (t == nt - 2);
;             const char* a1 = cA + (size_t)(t + 1) * kstep;
;             const char* a2 = last ? nA : cA + (size_t)(t + 2) * kstep; const char* b2 = last ? nB : cB + (size_t)(t + 2) * kstep;
;             const char* a3 = a2 + kstep; const char* b3 = b2 + kstep;
;             if (last && has_next) S.a_ready(nxt);
;             if constexpr (SP2) {
;             PG8_LDB(B0, 0, 0); PG8_LDB(B1, 0, 1); PG8_SCHED; PG8_LDA(At, 0, 0); PG8_STAGE(PG8_SA(1, 1), a1 + hstepA, voffA);
;     ...
;             PG8_LDA(At, 1, 1); PG8_STAGE(PG8_SB(1, 0), b3, voffB); PG8_STAGE(PG8_SB(1, 1), b3 + hstepB, voffB); PG8_STAGE(PG8_SA(1, 0), a3, voffA);
;             PG8_WAIT_V(8); PG8_WAIT_L(0); PG8_BAR; PG8_MMA(1, 0, At, B0); PG8_MMA(1, 1, At, B1); PG8_BAR; PG8_SCHED;
	s_mov_b32 m0, s86
	ds_read_b128 v[182:185], v159 offset:49152
	ds_read_b128 v[186:189], v159 offset:50176
	ds_read_b128 v[190:193], v159 offset:51200
	ds_read_b128 v[194:197], v159 offset:52224
	ds_read_b128 v[198:201], v159 offset:53248
	ds_read_b128 v[202:205], v159 offset:54272
	ds_read_b128 v[206:209], v159 offset:55296
	ds_read_b128 v[210:213], v159 offset:56320
	global_load_lds_dwordx4 v132, s[98:99]
	s_mov_b32 m0, s84
	s_nop 0
	global_load_lds_dwordx4 v128, s[98:99]
	s_mov_b32 m0, s85
	s_nop 0
	global_load_lds_dwordx4 v132, s[34:35]
	s_mov_b32 m0, s83
	s_nop 0
	global_load_lds_dwordx4 v128, s[34:35]
	s_mov_b32 m0, s74
	s_nop 0
	global_load_lds_dwordx4 v134, s[100:101]
	s_mov_b32 m0, s75
	s_nop 0
	global_load_lds_dwordx4 v130, s[100:101]
	s_waitcnt vmcnt(8) lgkmcnt(0)
	s_barrier
	s_setprio 1
	v_mfma_f32_16x16x32_bf16 v[60:63], v[142:145], v[182:185], v[60:63]
	v_mfma_f32_16x16x32_bf16 v[56:59], v[150:153], v[182:185], v[56:59]
	v_mfma_f32_16x16x32_bf16 v[52:55], v[142:145], v[190:193], v[52:55]
	v_mfma_f32_16x16x32_bf16 v[48:51], v[150:153], v[190:193], v[48:51]
	v_mfma_f32_16x16x32_bf16 v[36:39], v[142:145], v[198:201], v[36:39]
	v_mfma_f32_16x16x32_bf16 v[32:35], v[150:153], v[198:201], v[32:35]
	v_mfma_f32_16x16x32_bf16 v[20:23], v[142:145], v[206:209], v[20:23]
	v_mfma_f32_16x16x32_bf16 v[16:19], v[150:153], v[206:209], v[16:19]
	v_mfma_f32_16x16x32_bf16 v[60:63], v[146:149], v[186:189], v[60:63]
	v_mfma_f32_16x16x32_bf16 v[56:59], v[162:165], v[186:189], v[56:59]
	v_mfma_f32_16x16x32_bf16 v[52:55], v[146:149], v[194:197], v[52:55]
	v_mfma_f32_16x16x32_bf16 v[48:51], v[162:165], v[194:197], v[48:51]
	v_mfma_f32_16x16x32_bf16 v[36:39], v[146:149], v[202:205], v[36:39]
	v_mfma_f32_16x16x32_bf16 v[32:35], v[162:165], v[202:205], v[32:35]
	v_mfma_f32_16x16x32_bf16 v[20:23], v[146:149], v[210:213], v[20:23]
	v_mfma_f32_16x16x32_bf16 v[16:19], v[162:165], v[210:213], v[16:19]
	s_setprio 0
	s_setprio 1
	v_mfma_f32_16x16x32_bf16 v[44:47], v[166:169], v[182:185], v[44:47]
	v_mfma_f32_16x16x32_bf16 v[40:43], v[174:177], v[182:185], v[40:43]
	v_mfma_f32_16x16x32_bf16 v[28:31], v[166:169], v[190:193], v[28:31]
	v_mfma_f32_16x16x32_bf16 v[24:27], v[174:177], v[190:193], v[24:27]
	v_mfma_f32_16x16x32_bf16 v[12:15], v[166:169], v[198:201], v[12:15]
	v_mfma_f32_16x16x32_bf16 v[8:11], v[174:177], v[198:201], v[8:11]
	v_mfma_f32_16x16x32_bf16 v[4:7], v[166:169], v[206:209], v[4:7]
	v_mfma_f32_16x16x32_bf16 v[0:3], v[174:177], v[206:209], v[0:3]
	v_mfma_f32_16x16x32_bf16 v[44:47], v[170:173], v[186:189], v[44:47]
	v_mfma_f32_16x16x32_bf16 v[40:43], v[178:181], v[186:189], v[40:43]
	v_mfma_f32_16x16x32_bf16 v[28:31], v[170:173], v[194:197], v[28:31]
	v_mfma_f32_16x16x32_bf16 v[24:27], v[178:181], v[194:197], v[24:27]
	v_mfma_f32_16x16x32_bf16 v[12:15], v[170:173], v[202:205], v[12:15]
	v_mfma_f32_16x16x32_bf16 v[8:11], v[178:181], v[202:205], v[8:11]
	v_mfma_f32_16x16x32_bf16 v[4:7], v[170:173], v[210:213], v[4:7]
	v_mfma_f32_16x16x32_bf16 v[0:3], v[178:181], v[210:213], v[0:3]
	s_setprio 0
	s_barrier
	s_movk_i32 s36, 0x100
	s_andn2_b64 vcc, exec, s[30:31]
	s_mov_b64 s[34:35], -1
	s_mov_b64 s[30:31], 0
.LBB0_2280:
	s_add_u32 s37, s28, s36
	s_addc_u32 s44, s29, 0
	s_add_u32 s40, s37, 0x100
	s_addc_u32 s41, s44, 0
	s_and_b64 s[38:39], s[34:35], exec
	s_cselect_b32 s39, s19, s41
	s_cselect_b32 s38, s81, s40
	s_add_u32 s36, s26, s36
	s_addc_u32 s40, s27, 0
	s_add_u32 s36, s36, 0x100
	s_addc_u32 s40, s40, 0
	s_and_b64 s[34:35], s[34:35], exec
	s_cselect_b32 s41, s17, s40
	s_cselect_b32 s40, s82, s36
	s_add_u32 s46, s37, 0x80080
	ds_read_b128 v[142:145], v157
	ds_read_b128 v[146:149], v157 offset:1024
	ds_read_b128 v[150:153], v157 offset:2048
	ds_read_b128 v[162:165], v157 offset:3072
	ds_read_b128 v[166:169], v158
	ds_read_b128 v[170:173], v158 offset:1024
	ds_read_b128 v[174:177], v158 offset:2048
	ds_read_b128 v[178:181], v158 offset:3072
	s_addc_u32 s47, s44, 0
	s_add_i32 s93, s77, s0
	s_add_i32 m0, s70, 0xc000
	s_add_i32 s94, s70, 0xe000
	s_add_i32 s89, s93, 0x2000
	s_add_u32 s44, s40, 0x10000
	s_addc_u32 s45, s41, 0
	s_add_i32 s92, s78, s0
	s_add_i32 s91, s92, 0x2000
	s_add_i32 s88, 0, 0x18000
	s_add_i32 s87, 0, 0x1c000
	s_add_u32 s36, s38, 0x80000
	s_addc_u32 s37, s39, 0
	s_add_i32 s86, s88, s0
	s_add_i32 s84, s86, 0x2000
	s_add_u32 s34, s40, 0x10080
	s_addc_u32 s35, s41, 0
	s_add_i32 s85, s87, s0
	s_add_i32 s83, s85, 0x2000
	ds_read_b128 v[182:185], v159
	ds_read_b128 v[186:189], v159 offset:1024
	ds_read_b128 v[190:193], v159 offset:2048
	ds_read_b128 v[194:197], v159 offset:3072
	ds_read_b128 v[198:201], v159 offset:4096
	ds_read_b128 v[202:205], v159 offset:5120
	ds_read_b128 v[206:209], v159 offset:6144
	ds_read_b128 v[210:213], v159 offset:7168
	global_load_lds_dwordx4 v134, s[46:47]
	s_mov_b32 m0, s94
	s_nop 0
	global_load_lds_dwordx4 v130, s[46:47]
	s_waitcnt vmcnt(8) lgkmcnt(0)
	s_barrier
; #define PG8_STAGE(bufoff, gbase, voff) do { _Pragma("unroll") for (int _i = 0; _i < 2; ++_i) \
;         __builtin_amdgcn_global_load_lds((const unsigned*)((const char*)(gbase) + (voff)[_i]), (PG8_LAS unsigned*)(lds + (bufoff) + ldsw + _i * 8192), 16, 0, 0); } while (0)
; #define PG8_LDA(dst, b, h) do { _Pragma("unroll") for (int m = 0; m < 4; ++m) _Pragma("unroll") for (int k = 0; k < 2; ++k) dst[m][k] = *(const PG8_LAS bf16x8*)(lds + PG8_SA(b, h) + aoff + m * 2048 + k * 1024); } while (0)
; #define PG8_LDB(dst, b, h) do { _Pragma("unroll") for (int n = 0; n < 2; ++n) _Pragma("unroll") for (int k = 0; k < 2; ++k) dst[n][k] = *(const PG8_LAS bf16x8*)(lds + PG8_SB(b, h) + boff + n * 2048 + k * 1024); } while (0)
; #define PG8_MMA(ai, bj, At, Bt) do { __builtin_amdgcn_s_setprio(1); _Pragma("unroll") for (int m = 0; m < 4; ++m) _Pragma("unroll") for (int n = 0; n < 2; ++n) _Pragma("unroll") for (int k = 0; k < 2; ++k) \
;         acc[ai][bj][m][n] = __builtin_amdgcn_mfma_f32_16x16x32_bf16(Bt[n][k], At[m][k], acc[ai][bj][m][n], 0, 0, 0); __builtin_amdgcn_s_setprio(0); } while (0)
; #define PG8_WAIT_V(n) asm volatile("s_waitcnt vmcnt(" #n ")" ::: "memory")
; #define PG8_WAIT_L(n) asm volatile("s_waitcnt lgkmcnt(" #n ")" ::: "memory")
; #define PG8_BAR __builtin_amdgcn_s_barrier()
; #define PG8_SCHED __builtin_amdgcn_sched_barrier(0)
; template <class Epi, class Sched, bool ALIGN_EPI = false, bool SP2 = false>
; __device__ __forceinline__ void gemm_phase(PG8_LAS unsigned char* lds, const Gemm g, const Sched& S, const Epi& E, const int wid) {
;     ...
;             PG8_WAIT_V(8); PG8_WAIT_L(0); PG8_BAR; PG8_MMA(0, 0, At, B0); PG8_MMA(0, 1, At, B1); PG8_BAR; PG8_SCHED;
;             PG8_LDA(At, 0, 1); PG8_STAGE(PG8_SB(0, 0), b2, voffB); PG8_STAGE(PG8_SB(0, 1), b2 + hstepB, voffB); PG8_STAGE(PG8_SA(0, 0), a2, voffA);
;             PG8_WAIT_V(8); PG8_WAIT_L(0); PG8_BAR; PG8_MMA(1, 0, At, B0); PG8_MMA(1, 1, At, B1); PG8_BAR; PG8_SCHED;
;             PG8_LDB(B0, 1, 0); PG8_LDB(B1, 1, 1); PG8_SCHED; PG8_LDA(At, 1, 0); PG8_STAGE(PG8_SA(0, 1), a2 + hstepA, voffA);
	s_nop 0
	s_setprio 1
	v_mfma_f32_16x16x32_bf16 v[124:127], v[142:145], v[182:185], v[124:127]
	v_mfma_f32_16x16x32_bf16 v[120:123], v[150:153], v[182:185], v[120:123]
	v_mfma_f32_16x16x32_bf16 v[116:119], v[142:145], v[190:193], v[116:119]
	v_mfma_f32_16x16x32_bf16 v[112:115], v[150:153], v[190:193], v[112:115]
	v_mfma_f32_16x16x32_bf16 v[100:103], v[142:145], v[198:201], v[100:103]
	v_mfma_f32_16x16x32_bf16 v[96:99], v[150:153], v[198:201], v[96:99]
	v_mfma_f32_16x16x32_bf16 v[84:87], v[142:145], v[206:209], v[84:87]
	v_mfma_f32_16x16x32_bf16 v[80:83], v[150:153], v[206:209], v[80:83]
	v_mfma_f32_16x16x32_bf16 v[124:127], v[146:149], v[186:189], v[124:127]
	v_mfma_f32_16x16x32_bf16 v[120:123], v[162:165], v[186:189], v[120:123]
	v_mfma_f32_16x16x32_bf16 v[116:119], v[146:149], v[194:197], v[116:119]
	v_mfma_f32_16x16x32_bf16 v[112:115], v[162:165], v[194:197], v[112:115]
	v_mfma_f32_16x16x32_bf16 v[100:103], v[146:149], v[202:205], v[100:103]
	v_mfma_f32_16x16x32_bf16 v[96:99], v[162:165], v[202:205], v[96:99]
	v_mfma_f32_16x16x32_bf16 v[84:87], v[146:149], v[210:213], v[84:87]
	v_mfma_f32_16x16x32_bf16 v[80:83], v[162:165], v[210:213], v[80:83]
	s_setprio 0
	s_setprio 1
	v_mfma_f32_16x16x32_bf16 v[108:111], v[166:169], v[182:185], v[108:111]
	v_mfma_f32_16x16x32_bf16 v[104:107], v[174:177], v[182:185], v[104:107]
	v_mfma_f32_16x16x32_bf16 v[92:95], v[166:169], v[190:193], v[92:95]
	v_mfma_f32_16x16x32_bf16 v[88:91], v[174:177], v[190:193], v[88:91]
	v_mfma_f32_16x16x32_bf16 v[76:79], v[166:169], v[198:201], v[76:79]
	v_mfma_f32_16x16x32_bf16 v[72:75], v[174:177], v[198:201], v[72:75]
	v_mfma_f32_16x16x32_bf16 v[68:71], v[166:169], v[206:209], v[68:71]
	v_mfma_f32_16x16x32_bf16 v[64:67], v[174:177], v[206:209], v[64:67]
	v_mfma_f32_16x16x32_bf16 v[108:111], v[170:173], v[186:189], v[108:111]
	v_mfma_f32_16x16x32_bf16 v[104:107], v[178:181], v[186:189], v[104:107]
	v_mfma_f32_16x16x32_bf16 v[92:95], v[170:173], v[194:197], v[92:95]
	v_mfma_f32_16x16x32_bf16 v[88:91], v[178:181], v[194:197], v[88:91]
	v_mfma_f32_16x16x32_bf16 v[76:79], v[170:173], v[202:205], v[76:79]
	v_mfma_f32_16x16x32_bf16 v[72:75], v[178:181], v[202:205], v[72:75]
	v_mfma_f32_16x16x32_bf16 v[68:71], v[170:173], v[210:213], v[68:71]
	v_mfma_f32_16x16x32_bf16 v[64:67], v[178:181], v[210:213], v[64:67]
	s_setprio 0
	s_barrier
	s_mov_b32 m0, s93
	s_add_u32 s98, s40, 0x80
	s_addc_u32 s99, s41, 0
	ds_read_b128 v[182:185], v159 offset:16384
	ds_read_b128 v[186:189], v159 offset:17408
	ds_read_b128 v[190:193], v159 offset:18432
	ds_read_b128 v[194:197], v159 offset:19456
	ds_read_b128 v[198:201], v159 offset:20480
	ds_read_b128 v[202:205], v159 offset:21504
	ds_read_b128 v[206:209], v159 offset:22528
	ds_read_b128 v[210:213], v159 offset:23552
	global_load_lds_dwordx4 v132, s[40:41]
	s_mov_b32 m0, s89
	s_nop 0
	global_load_lds_dwordx4 v128, s[40:41]
	s_mov_b32 m0, s92
	s_add_u32 s100, s38, 0x80
	s_addc_u32 s101, s39, 0
	global_load_lds_dwordx4 v132, s[44:45]
	s_mov_b32 m0, s91
	s_nop 0
	global_load_lds_dwordx4 v128, s[44:45]
	s_mov_b32 m0, s70
	s_nop 0
	global_load_lds_dwordx4 v134, s[38:39]
	s_mov_b32 m0, s71
	s_nop 0
	global_load_lds_dwordx4 v130, s[38:39]
	s_waitcnt vmcnt(8) lgkmcnt(0)
	s_barrier
	s_nop 0
	s_setprio 1
	v_mfma_f32_16x16x32_bf16 v[60:63], v[142:145], v[182:185], v[60:63]
	v_mfma_f32_16x16x32_bf16 v[56:59], v[150:153], v[182:185], v[56:59]
	v_mfma_f32_16x16x32_bf16 v[52:55], v[142:145], v[190:193], v[52:55]
	v_mfma_f32_16x16x32_bf16 v[48:51], v[150:153], v[190:193], v[48:51]
	v_mfma_f32_16x16x32_bf16 v[36:39], v[142:145], v[198:201], v[36:39]
	v_mfma_f32_16x16x32_bf16 v[32:35], v[150:153], v[198:201], v[32:35]
	v_mfma_f32_16x16x32_bf16 v[20:23], v[142:145], v[206:209], v[20:23]
	v_mfma_f32_16x16x32_bf16 v[16:19], v[150:153], v[206:209], v[16:19]
	v_mfma_f32_16x16x32_bf16 v[60:63], v[146:149], v[186:189], v[60:63]
	v_mfma_f32_16x16x32_bf16 v[56:59], v[162:165], v[186:189], v[56:59]
	v_mfma_f32_16x16x32_bf16 v[52:55], v[146:149], v[194:197], v[52:55]
	v_mfma_f32_16x16x32_bf16 v[48:51], v[162:165], v[194:197], v[48:51]
	v_mfma_f32_16x16x32_bf16 v[36:39], v[146:149], v[202:205], v[36:39]
	v_mfma_f32_16x16x32_bf16 v[32:35], v[162:165], v[202:205], v[32:35]
	v_mfma_f32_16x16x32_bf16 v[20:23], v[146:149], v[210:213], v[20:23]
	v_mfma_f32_16x16x32_bf16 v[16:19], v[162:165], v[210:213], v[16:19]
	s_setprio 0
	s_setprio 1
	v_mfma_f32_16x16x32_bf16 v[44:47], v[166:169], v[182:185], v[44:47]
	v_mfma_f32_16x16x32_bf16 v[40:43], v[174:177], v[182:185], v[40:43]
	v_mfma_f32_16x16x32_bf16 v[28:31], v[166:169], v[190:193], v[28:31]
	v_mfma_f32_16x16x32_bf16 v[24:27], v[174:177], v[190:193], v[24:27]
	v_mfma_f32_16x16x32_bf16 v[12:15], v[166:169], v[198:201], v[12:15]
	v_mfma_f32_16x16x32_bf16 v[8:11], v[174:177], v[198:201], v[8:11]
	v_mfma_f32_16x16x32_bf16 v[4:7], v[166:169], v[206:209], v[4:7]
	v_mfma_f32_16x16x32_bf16 v[0:3], v[174:177], v[206:209], v[0:3]
	v_mfma_f32_16x16x32_bf16 v[44:47], v[170:173], v[186:189], v[44:47]
	v_mfma_f32_16x16x32_bf16 v[40:43], v[178:181], v[186:189], v[40:43]
	v_mfma_f32_16x16x32_bf16 v[28:31], v[170:173], v[194:197], v[28:31]
	v_mfma_f32_16x16x32_bf16 v[24:27], v[178:181], v[194:197], v[24:27]
	v_mfma_f32_16x16x32_bf16 v[12:15], v[170:173], v[202:205], v[12:15]
	v_mfma_f32_16x16x32_bf16 v[8:11], v[178:181], v[202:205], v[8:11]
	v_mfma_f32_16x16x32_bf16 v[4:7], v[170:173], v[210:213], v[4:7]
	v_mfma_f32_16x16x32_bf16 v[0:3], v[178:181], v[210:213], v[0:3]
	s_setprio 0
	s_barrier
; #define PG8_STAGE(bufoff, gbase, voff) do { _Pragma("unroll") for (int _i = 0; _i < 2; ++_i) \
;         __builtin_amdgcn_global_load_lds((const unsigned*)((const char*)(gbase) + (voff)[_i]), (PG8_LAS unsigned*)(lds + (bufoff) + ldsw + _i * 8192), 16, 0, 0); } while (0)
; #define PG8_LDA(dst, b, h) do { _Pragma("unroll") for (int m = 0; m < 4; ++m) _Pragma("unroll") for (int k = 0; k < 2; ++k) dst[m][k] = *(const PG8_LAS bf16x8*)(lds + PG8_SA(b, h) + aoff + m * 2048 + k * 1024); } while (0)
; #define PG8_LDB(dst, b, h) do { _Pragma("unroll") for (int n = 0; n < 2; ++n) _Pragma("unroll") for (int k = 0; k < 2; ++k) dst[n][k] = *(const PG8_LAS bf16x8*)(lds + PG8_SB(b, h) + boff + n * 2048 + k * 1024); } while (0)
; #define PG8_MMA(ai, bj, At, Bt) do { __builtin_amdgcn_s_setprio(1); _Pragma("unroll") for (int m = 0; m < 4; ++m) _Pragma("unroll") for (int n = 0; n < 2; ++n) _Pragma("unroll") for (int k = 0; k < 2; ++k) \
;         acc[ai][bj][m][n] = __builtin_amdgcn_mfma_f32_16x16x32_bf16(Bt[n][k], At[m][k], acc[ai][bj][m][n], 0, 0, 0); __builtin_amdgcn_s_setprio(0); } while (0)
; #define PG8_WAIT_V(n) asm volatile("s_waitcnt vmcnt(" #n ")" ::: "memory")
; #define PG8_WAIT_L(n) asm volatile("s_waitcnt lgkmcnt(" #n ")" ::: "memory")
; #define PG8_BAR __builtin_amdgcn_s_barrier()
; #define PG8_SCHED __builtin_amdgcn_sched_barrier(0)
; template <class Epi, class Sched, bool ALIGN_EPI = false, bool SP2 = false>
; __device__ __forceinline__ void gemm_phase(PG8_LAS unsigned char* lds, const Gemm g, const Sched& S, const Epi& E, const int wid) {
;     ...
;             PG8_LDB(B0, 1, 0); PG8_LDB(B1, 1, 1); PG8_SCHED; PG8_LDA(At, 1, 0); PG8_STAGE(PG8_SA(0, 1), a2 + hstepA, voffA);
;             PG8_WAIT_V(8); PG8_WAIT_L(0); PG8_BAR; PG8_MMA(0, 0, At, B0); PG8_MMA(0, 1, At, B1); PG8_BAR; PG8_SCHED;
;             PG8_LDA(At, 1, 1); PG8_STAGE(PG8_SB(1, 0), b3, voffB); PG8_STAGE(PG8_SB(1, 1), b3 + hstepB, voffB); PG8_STAGE(PG8_SA(1, 0), a3, voffA);
;             PG8_WAIT_V(8); PG8_WAIT_L(0); PG8_BAR; PG8_MMA(1, 0, At, B0); PG8_MMA(1, 1, At, B1); PG8_BAR; PG8_SCHED;
;     ...
;         if constexpr (ALIGN_EPI) { if (wr == 0) PG8_BAR; }
	ds_read_b128 v[142:145], v252
	ds_read_b128 v[146:149], v252 offset:1024
	ds_read_b128 v[150:153], v252 offset:2048
	ds_read_b128 v[162:165], v252 offset:3072
	ds_read_b128 v[166:169], v253
	ds_read_b128 v[170:173], v253 offset:1024
	ds_read_b128 v[174:177], v253 offset:2048
	ds_read_b128 v[178:181], v253 offset:3072
	s_mov_b32 m0, s72
	ds_read_b128 v[182:185], v159 offset:32768
	ds_read_b128 v[186:189], v159 offset:33792
	ds_read_b128 v[190:193], v159 offset:34816
	ds_read_b128 v[194:197], v159 offset:35840
	ds_read_b128 v[198:201], v159 offset:36864
	ds_read_b128 v[202:205], v159 offset:37888
	ds_read_b128 v[206:209], v159 offset:38912
	ds_read_b128 v[210:213], v159 offset:39936
	global_load_lds_dwordx4 v134, s[36:37]
	s_mov_b32 m0, s73
	s_nop 0
	global_load_lds_dwordx4 v130, s[36:37]
	s_waitcnt vmcnt(8) lgkmcnt(0)
	s_barrier
	s_setprio 1
	v_mfma_f32_16x16x32_bf16 v[124:127], v[142:145], v[182:185], v[124:127]
	v_mfma_f32_16x16x32_bf16 v[120:123], v[150:153], v[182:185], v[120:123]
	v_mfma_f32_16x16x32_bf16 v[116:119], v[142:145], v[190:193], v[116:119]
	v_mfma_f32_16x16x32_bf16 v[112:115], v[150:153], v[190:193], v[112:115]
	v_mfma_f32_16x16x32_bf16 v[100:103], v[142:145], v[198:201], v[100:103]
	v_mfma_f32_16x16x32_bf16 v[96:99], v[150:153], v[198:201], v[96:99]
	v_mfma_f32_16x16x32_bf16 v[84:87], v[142:145], v[206:209], v[84:87]
	v_mfma_f32_16x16x32_bf16 v[80:83], v[150:153], v[206:209], v[80:83]
	v_mfma_f32_16x16x32_bf16 v[124:127], v[146:149], v[186:189], v[124:127]
	v_mfma_f32_16x16x32_bf16 v[120:123], v[162:165], v[186:189], v[120:123]
	v_mfma_f32_16x16x32_bf16 v[116:119], v[146:149], v[194:197], v[116:119]
	v_mfma_f32_16x16x32_bf16 v[112:115], v[162:165], v[194:197], v[112:115]
	v_mfma_f32_16x16x32_bf16 v[100:103], v[146:149], v[202:205], v[100:103]
	v_mfma_f32_16x16x32_bf16 v[96:99], v[162:165], v[202:205], v[96:99]
	v_mfma_f32_16x16x32_bf16 v[84:87], v[146:149], v[210:213], v[84:87]
	v_mfma_f32_16x16x32_bf16 v[80:83], v[162:165], v[210:213], v[80:83]
	s_setprio 0
	s_setprio 1
	v_mfma_f32_16x16x32_bf16 v[108:111], v[166:169], v[182:185], v[108:111]
	v_mfma_f32_16x16x32_bf16 v[104:107], v[174:177], v[182:185], v[104:107]
	v_mfma_f32_16x16x32_bf16 v[92:95], v[166:169], v[190:193], v[92:95]
	v_mfma_f32_16x16x32_bf16 v[88:91], v[174:177], v[190:193], v[88:91]
	v_mfma_f32_16x16x32_bf16 v[76:79], v[166:169], v[198:201], v[76:79]
	v_mfma_f32_16x16x32_bf16 v[72:75], v[174:177], v[198:201], v[72:75]
	v_mfma_f32_16x16x32_bf16 v[68:71], v[166:169], v[206:209], v[68:71]
	v_mfma_f32_16x16x32_bf16 v[64:67], v[174:177], v[206:209], v[64:67]
	v_mfma_f32_16x16x32_bf16 v[108:111], v[170:173], v[186:189], v[108:111]
	v_mfma_f32_16x16x32_bf16 v[104:107], v[178:181], v[186:189], v[104:107]
	v_mfma_f32_16x16x32_bf16 v[92:95], v[170:173], v[194:197], v[92:95]
	v_mfma_f32_16x16x32_bf16 v[88:91], v[178:181], v[194:197], v[88:91]
	v_mfma_f32_16x16x32_bf16 v[76:79], v[170:173], v[202:205], v[76:79]
	v_mfma_f32_16x16x32_bf16 v[72:75], v[178:181], v[202:205], v[72:75]
	v_mfma_f32_16x16x32_bf16 v[68:71], v[170:173], v[210:213], v[68:71]
	v_mfma_f32_16x16x32_bf16 v[64:67], v[178:181], v[210:213], v[64:67]
	s_setprio 0
	s_barrier
	s_mov_b32 m0, s86
	ds_read_b128 v[182:185], v159 offset:49152
	ds_read_b128 v[186:189], v159 offset:50176
	ds_read_b128 v[190:193], v159 offset:51200
	ds_read_b128 v[194:197], v159 offset:52224
	ds_read_b128 v[198:201], v159 offset:53248
	ds_read_b128 v[202:205], v159 offset:54272
	ds_read_b128 v[206:209], v159 offset:55296
	ds_read_b128 v[210:213], v159 offset:56320
	global_load_lds_dwordx4 v132, s[98:99]
	s_mov_b32 m0, s84
	s_nop 0
	global_load_lds_dwordx4 v128, s[98:99]
	s_mov_b32 m0, s85
	s_nop 0
	global_load_lds_dwordx4 v132, s[34:35]
	s_mov_b32 m0, s83
	s_nop 0
	global_load_lds_dwordx4 v128, s[34:35]
	s_mov_b32 m0, s74
	s_nop 0
	global_load_lds_dwordx4 v134, s[100:101]
	s_mov_b32 m0, s75
	s_nop 0
	global_load_lds_dwordx4 v130, s[100:101]
	s_waitcnt vmcnt(8) lgkmcnt(0)
	s_barrier
	s_setprio 1
	v_mfma_f32_16x16x32_bf16 v[60:63], v[142:145], v[182:185], v[60:63]
	v_mfma_f32_16x16x32_bf16 v[56:59], v[150:153], v[182:185], v[56:59]
	v_mfma_f32_16x16x32_bf16 v[52:55], v[142:145], v[190:193], v[52:55]
	v_mfma_f32_16x16x32_bf16 v[48:51], v[150:153], v[190:193], v[48:51]
	v_mfma_f32_16x16x32_bf16 v[36:39], v[142:145], v[198:201], v[36:39]
	v_mfma_f32_16x16x32_bf16 v[32:35], v[150:153], v[198:201], v[32:35]
	v_mfma_f32_16x16x32_bf16 v[20:23], v[142:145], v[206:209], v[20:23]
	v_mfma_f32_16x16x32_bf16 v[16:19], v[150:153], v[206:209], v[16:19]
	v_mfma_f32_16x16x32_bf16 v[60:63], v[146:149], v[186:189], v[60:63]
	v_mfma_f32_16x16x32_bf16 v[56:59], v[162:165], v[186:189], v[56:59]
	v_mfma_f32_16x16x32_bf16 v[52:55], v[146:149], v[194:197], v[52:55]
	v_mfma_f32_16x16x32_bf16 v[48:51], v[162:165], v[194:197], v[48:51]
	v_mfma_f32_16x16x32_bf16 v[36:39], v[146:149], v[202:205], v[36:39]
	v_mfma_f32_16x16x32_bf16 v[32:35], v[162:165], v[202:205], v[32:35]
	v_mfma_f32_16x16x32_bf16 v[20:23], v[146:149], v[210:213], v[20:23]
	v_mfma_f32_16x16x32_bf16 v[16:19], v[162:165], v[210:213], v[16:19]
	s_setprio 0
	s_setprio 1
	v_mfma_f32_16x16x32_bf16 v[44:47], v[166:169], v[182:185], v[44:47]
	v_mfma_f32_16x16x32_bf16 v[40:43], v[174:177], v[182:185], v[40:43]
	v_mfma_f32_16x16x32_bf16 v[28:31], v[166:169], v[190:193], v[28:31]
	v_mfma_f32_16x16x32_bf16 v[24:27], v[174:177], v[190:193], v[24:27]
	v_mfma_f32_16x16x32_bf16 v[12:15], v[166:169], v[198:201], v[12:15]
	v_mfma_f32_16x16x32_bf16 v[8:11], v[174:177], v[198:201], v[8:11]
	v_mfma_f32_16x16x32_bf16 v[4:7], v[166:169], v[206:209], v[4:7]
	v_mfma_f32_16x16x32_bf16 v[0:3], v[174:177], v[206:209], v[0:3]
	v_mfma_f32_16x16x32_bf16 v[44:47], v[170:173], v[186:189], v[44:47]
	v_mfma_f32_16x16x32_bf16 v[40:43], v[178:181], v[186:189], v[40:43]
	v_mfma_f32_16x16x32_bf16 v[28:31], v[170:173], v[194:197], v[28:31]
	v_mfma_f32_16x16x32_bf16 v[24:27], v[178:181], v[194:197], v[24:27]
	v_mfma_f32_16x16x32_bf16 v[12:15], v[170:173], v[202:205], v[12:15]
	v_mfma_f32_16x16x32_bf16 v[8:11], v[178:181], v[202:205], v[8:11]
	v_mfma_f32_16x16x32_bf16 v[4:7], v[170:173], v[210:213], v[4:7]
	v_mfma_f32_16x16x32_bf16 v[0:3], v[178:181], v[210:213], v[0:3]
	s_setprio 0
	s_barrier
	s_movk_i32 s36, 0x100
	s_andn2_b64 vcc, exec, s[30:31]
	s_mov_b64 s[34:35], -1
	s_mov_b64 s[30:31], 0
	s_cbranch_vccz .LBB0_2280
	s_and_b64 vcc, exec, s[14:15]
	s_cbranch_vccz .LBB0_2283
	s_barrier

; #define PG8_STAGE(bufoff, gbase, voff) do { _Pragma("unroll") for (int _i = 0; _i < 2; ++_i) \
;         __builtin_amdgcn_global_load_lds((const unsigned*)((const char*)(gbase) + (voff)[_i]), (PG8_LAS unsigned*)(lds + (bufoff) + ldsw + _i * 8192), 16, 0, 0); } while (0)
; #define PG8_LDA(dst, b, h) do { _Pragma("unroll") for (int m = 0; m < 4; ++m) _Pragma("unroll") for (int k = 0; k < 2; ++k) dst[m][k] = *(const PG8_LAS bf16x8*)(lds + PG8_SA(b, h) + aoff + m * 2048 + k * 1024); } while (0)
; #define PG8_LDB(dst, b, h) do { _Pragma("unroll") for (int n = 0; n < 2; ++n) _Pragma("unroll") for (int k = 0; k < 2; ++k) dst[n][k] = *(const PG8_LAS bf16x8*)(lds + PG8_SB(b, h) + boff + n * 2048 + k * 1024); } while (0)
; #define PG8_WAIT_V(n) asm volatile("s_waitcnt vmcnt(" #n ")" ::: "memory")
; #define PG8_WAIT_L(n) asm volatile("s_waitcnt lgkmcnt(" #n ")" ::: "memory")
; #define PG8_BAR __builtin_amdgcn_s_barrier()
; #define PG8_SCHED __builtin_amdgcn_sched_barrier(0)
; template <class Epi, class Sched, bool ALIGN_EPI = false, bool SP2 = false>
; __device__ __forceinline__ void gemm_phase(PG8_LAS unsigned char* lds, const Gemm g, const Sched& S, const Epi& E, const int wid) {
;     ...
;         const bool has_next = S.next(ui + 1, nxt);
;         const char* nA = has_next ? (const char*)g.A + (size_t)nxt.pm * tstepA : cA; const char* nB = has_next ? (const char*)g.Bt + (size_t)nxt.pn * tstepB : cB;
;         for (int t = 0; t < nt; t += 2) {
;             const bool last = (t == nt - 2);
;             const char* a1 = cA + (size_t)(t + 1) * kstep;
;             const char* a2 = last ? nA : cA + (size_t)(t + 2) * kstep; const char* b2 = last ? nB : cB + (size_t)(t + 2) * kstep;
;             const char* a3 = a2 + kstep; const char* b3 = b2 + kstep;
;             if (last && has_next) S.a_ready(nxt);
;             if constexpr (SP2) {
;             PG8_LDB(B0, 0, 0); PG8_LDB(B1, 0, 1); PG8_SCHED; PG8_LDA(At, 0, 0); PG8_STAGE(PG8_SA(1, 1), a1 + hstepA, voffA);
;             PG8_WAIT_V(8); PG8_WAIT_L(0); PG8_BAR; PG8_MMA(0, 0, At, B0); PG8_MMA(0, 1, At, B1); PG8_BAR; PG8_SCHED;
;             PG8_LDA(At, 0, 1); PG8_STAGE(PG8_SB(0, 0), b2, voffB); PG8_STAGE(PG8_SB(0, 1), b2 + hstepB, voffB); PG8_STAGE(PG8_SA(0, 0), a2, voffA);
;             PG8_WAIT_V(8); PG8_WAIT_L(0); PG8_BAR; PG8_MMA(1, 0, At, B0); PG8_MMA(1, 1, At, B1); PG8_BAR; PG8_SCHED;
.LBB0_2724:
	s_ashr_i32 s21, s20, 31
	s_lshl_b64 s[22:23], s[20:21], 19
	s_add_u32 s22, s0, s22
	s_addc_u32 s23, s1, s23
	s_and_b64 s[24:25], s[4:5], exec
	s_cselect_b32 s21, s23, s31
	s_cselect_b32 s27, s22, s30
	s_ashr_i32 s19, s18, 31
	s_lshl_b64 s[24:25], s[18:19], 19
	s_add_u32 s24, s33, s24
	s_addc_u32 s25, s38, s25
	s_and_b64 s[36:37], s[4:5], exec
	s_cselect_b32 s19, s25, s35
	s_cselect_b32 s29, s24, s34
	s_add_u32 s30, s30, 0x40080
	s_addc_u32 s31, s31, 0
	s_add_u32 s58, s34, 0x100
	s_addc_u32 s59, s35, 0
	s_mov_b32 s60, -2
	s_waitcnt lgkmcnt(0)
	v_add_u32_e32 v252, 0x18000, v189
	v_add_u32_e32 v253, 0x1c000, v189
	ds_read_b128 v[128:131], v190
	ds_read_b128 v[132:135], v190 offset:1024
	ds_read_b128 v[136:139], v190 offset:2048
	ds_read_b128 v[140:143], v190 offset:3072
	ds_read_b128 v[144:147], v191
	ds_read_b128 v[148:151], v191 offset:1024
	ds_read_b128 v[172:175], v191 offset:2048
	ds_read_b128 v[176:179], v191 offset:3072
	s_add_u32 s34, s30, 0xfffc0080
	s_addc_u32 s35, s31, -1
	s_cmp_eq_u32 s60, 12
	s_cselect_b32 s37, s21, s35
	s_cselect_b32 s36, s27, s34
	s_cselect_b32 s35, s19, s59
	s_cselect_b32 s34, s29, s58
	s_add_i32 m0, s40, 0xc000
	ds_read_b128 v[180:183], v192
	ds_read_b128 v[184:187], v192 offset:1024
	ds_read_b128 v[194:197], v192 offset:2048
	ds_read_b128 v[198:201], v192 offset:3072
	ds_read_b128 v[202:205], v192 offset:4096
	ds_read_b128 v[206:209], v192 offset:5120
	ds_read_b128 v[210:213], v192 offset:6144
	ds_read_b128 v[214:217], v192 offset:7168
	global_load_lds_dwordx4 v164, s[30:31]
	s_add_i32 m0, s40, 0xe000
	s_nop 0
	global_load_lds_dwordx4 v166, s[30:31]
	s_waitcnt vmcnt(8) lgkmcnt(0)
	s_barrier
	s_nop 0
	s_setprio 1
	v_mfma_f32_16x16x32_bf16 v[124:127], v[128:131], v[180:183], 0
	v_mfma_f32_16x16x32_bf16 v[120:123], v[136:139], v[180:183], 0
	v_mfma_f32_16x16x32_bf16 v[108:111], v[128:131], v[194:197], 0
	v_mfma_f32_16x16x32_bf16 v[104:107], v[136:139], v[194:197], 0
	v_mfma_f32_16x16x32_bf16 v[92:95], v[128:131], v[202:205], 0
	v_mfma_f32_16x16x32_bf16 v[88:91], v[136:139], v[202:205], 0
	v_mfma_f32_16x16x32_bf16 v[76:79], v[128:131], v[210:213], 0
	v_mfma_f32_16x16x32_bf16 v[72:75], v[136:139], v[210:213], 0
	v_mfma_f32_16x16x32_bf16 v[124:127], v[132:135], v[184:187], v[124:127]
	v_mfma_f32_16x16x32_bf16 v[120:123], v[140:143], v[184:187], v[120:123]
	v_mfma_f32_16x16x32_bf16 v[108:111], v[132:135], v[198:201], v[108:111]
	v_mfma_f32_16x16x32_bf16 v[104:107], v[140:143], v[198:201], v[104:107]
	v_mfma_f32_16x16x32_bf16 v[92:95], v[132:135], v[206:209], v[92:95]
	v_mfma_f32_16x16x32_bf16 v[88:91], v[140:143], v[206:209], v[88:91]
	v_mfma_f32_16x16x32_bf16 v[76:79], v[132:135], v[214:217], v[76:79]
	v_mfma_f32_16x16x32_bf16 v[72:75], v[140:143], v[214:217], v[72:75]
	s_setprio 0
	s_setprio 1
	v_mfma_f32_16x16x32_bf16 v[116:119], v[144:147], v[180:183], 0
	v_mfma_f32_16x16x32_bf16 v[112:115], v[172:175], v[180:183], 0
	v_mfma_f32_16x16x32_bf16 v[100:103], v[144:147], v[194:197], 0
	v_mfma_f32_16x16x32_bf16 v[96:99], v[172:175], v[194:197], 0
	v_mfma_f32_16x16x32_bf16 v[84:87], v[144:147], v[202:205], 0
	v_mfma_f32_16x16x32_bf16 v[80:83], v[172:175], v[202:205], 0
	v_mfma_f32_16x16x32_bf16 v[68:71], v[144:147], v[210:213], 0
	v_mfma_f32_16x16x32_bf16 v[64:67], v[172:175], v[210:213], 0
	v_mfma_f32_16x16x32_bf16 v[116:119], v[148:151], v[184:187], v[116:119]
	v_mfma_f32_16x16x32_bf16 v[112:115], v[176:179], v[184:187], v[112:115]
	v_mfma_f32_16x16x32_bf16 v[100:103], v[148:151], v[198:201], v[100:103]
	v_mfma_f32_16x16x32_bf16 v[96:99], v[176:179], v[198:201], v[96:99]
	v_mfma_f32_16x16x32_bf16 v[84:87], v[148:151], v[206:209], v[84:87]
	v_mfma_f32_16x16x32_bf16 v[80:83], v[176:179], v[206:209], v[80:83]
	v_mfma_f32_16x16x32_bf16 v[68:71], v[148:151], v[214:217], v[68:71]
	v_mfma_f32_16x16x32_bf16 v[64:67], v[176:179], v[214:217], v[64:67]
	s_setprio 0
	s_barrier
	s_add_i32 s61, s49, s39
	s_add_u32 s98, s34, 0x80
	s_addc_u32 s99, s35, 0
	s_mov_b32 m0, s61
	ds_read_b128 v[180:183], v192 offset:16384
	ds_read_b128 v[184:187], v192 offset:17408
	ds_read_b128 v[194:197], v192 offset:18432
	ds_read_b128 v[198:201], v192 offset:19456
	ds_read_b128 v[202:205], v192 offset:20480
	ds_read_b128 v[206:209], v192 offset:21504
	ds_read_b128 v[210:213], v192 offset:22528
	ds_read_b128 v[214:217], v192 offset:23552
	global_load_lds_dwordx4 v154, s[34:35]
	s_add_i32 m0, s61, 0x2000
	s_add_u32 s62, s34, 0x40000
	s_addc_u32 s63, s35, 0
	s_add_i32 s61, s56, s39
	global_load_lds_dwordx4 v158, s[34:35]
	s_mov_b32 m0, s61
	s_add_u32 s100, s36, 0x80
	s_addc_u32 s101, s37, 0
	global_load_lds_dwordx4 v154, s[62:63]
	s_add_i32 m0, s61, 0x2000
	s_nop 0
	global_load_lds_dwordx4 v158, s[62:63]
	s_mov_b32 m0, s40
	s_nop 0
	global_load_lds_dwordx4 v152, s[36:37]
	s_mov_b32 m0, s41
	s_nop 0
	global_load_lds_dwordx4 v156, s[36:37]
	s_waitcnt vmcnt(8) lgkmcnt(0)
	s_barrier
; #define PG8_STAGE(bufoff, gbase, voff) do { _Pragma("unroll") for (int _i = 0; _i < 2; ++_i) \
;         __builtin_amdgcn_global_load_lds((const unsigned*)((const char*)(gbase) + (voff)[_i]), (PG8_LAS unsigned*)(lds + (bufoff) + ldsw + _i * 8192), 16, 0, 0); } while (0)
; #define PG8_LDA(dst, b, h) do { _Pragma("unroll") for (int m = 0; m < 4; ++m) _Pragma("unroll") for (int k = 0; k < 2; ++k) dst[m][k] = *(const PG8_LAS bf16x8*)(lds + PG8_SA(b, h) + aoff + m * 2048 + k * 1024); } while (0)
; #define PG8_LDB(dst, b, h) do { _Pragma("unroll") for (int n = 0; n < 2; ++n) _Pragma("unroll") for (int k = 0; k < 2; ++k) dst[n][k] = *(const PG8_LAS bf16x8*)(lds + PG8_SB(b, h) + boff + n * 2048 + k * 1024); } while (0)
; #define PG8_MMA(ai, bj, At, Bt) do { __builtin_amdgcn_s_setprio(1); _Pragma("unroll") for (int m = 0; m < 4; ++m) _Pragma("unroll") for (int n = 0; n < 2; ++n) _Pragma("unroll") for (int k = 0; k < 2; ++k) \
;         acc[ai][bj][m][n] = __builtin_amdgcn_mfma_f32_16x16x32_bf16(Bt[n][k], At[m][k], acc[ai][bj][m][n], 0, 0, 0); __builtin_amdgcn_s_setprio(0); } while (0)
; #define PG8_WAIT_V(n) asm volatile("s_waitcnt vmcnt(" #n ")" ::: "memory")
; #define PG8_WAIT_L(n) asm volatile("s_waitcnt lgkmcnt(" #n ")" ::: "memory")
; #define PG8_BAR __builtin_amdgcn_s_barrier()
; #define PG8_SCHED __builtin_amdgcn_sched_barrier(0)
; template <class Epi, class Sched, bool ALIGN_EPI = false, bool SP2 = false>
; __device__ __forceinline__ void gemm_phase(PG8_LAS unsigned char* lds, const Gemm g, const Sched& S, const Epi& E, const int wid) {
;     ...
;             PG8_WAIT_V(8); PG8_WAIT_L(0); PG8_BAR; PG8_MMA(0, 0, At, B0); PG8_MMA(0, 1, At, B1); PG8_BAR; PG8_SCHED;
;             PG8_LDA(At, 0, 1); PG8_STAGE(PG8_SB(0, 0), b2, voffB); PG8_STAGE(PG8_SB(0, 1), b2 + hstepB, voffB); PG8_STAGE(PG8_SA(0, 0), a2, voffA);
;             PG8_WAIT_V(8); PG8_WAIT_L(0); PG8_BAR; PG8_MMA(1, 0, At, B0); PG8_MMA(1, 1, At, B1); PG8_BAR; PG8_SCHED;
;             PG8_LDB(B0, 1, 0); PG8_LDB(B1, 1, 1); PG8_SCHED; PG8_LDA(At, 1, 0); PG8_STAGE(PG8_SA(0, 1), a2 + hstepA, voffA);
;             PG8_WAIT_V(8); PG8_WAIT_L(0); PG8_BAR; PG8_MMA(0, 0, At, B0); PG8_MMA(0, 1, At, B1); PG8_BAR; PG8_SCHED;
	s_nop 0
	s_setprio 1
	v_mfma_f32_16x16x32_bf16 v[60:63], v[128:131], v[180:183], 0
	v_mfma_f32_16x16x32_bf16 v[56:59], v[136:139], v[180:183], 0
	v_mfma_f32_16x16x32_bf16 v[44:47], v[128:131], v[194:197], 0
	v_mfma_f32_16x16x32_bf16 v[40:43], v[136:139], v[194:197], 0
	v_mfma_f32_16x16x32_bf16 v[28:31], v[128:131], v[202:205], 0
	v_mfma_f32_16x16x32_bf16 v[24:27], v[136:139], v[202:205], 0
	v_mfma_f32_16x16x32_bf16 v[12:15], v[128:131], v[210:213], 0
	v_mfma_f32_16x16x32_bf16 v[8:11], v[136:139], v[210:213], 0
	v_mfma_f32_16x16x32_bf16 v[60:63], v[132:135], v[184:187], v[60:63]
	v_mfma_f32_16x16x32_bf16 v[56:59], v[140:143], v[184:187], v[56:59]
	v_mfma_f32_16x16x32_bf16 v[44:47], v[132:135], v[198:201], v[44:47]
	v_mfma_f32_16x16x32_bf16 v[40:43], v[140:143], v[198:201], v[40:43]
	v_mfma_f32_16x16x32_bf16 v[28:31], v[132:135], v[206:209], v[28:31]
	v_mfma_f32_16x16x32_bf16 v[24:27], v[140:143], v[206:209], v[24:27]
	v_mfma_f32_16x16x32_bf16 v[12:15], v[132:135], v[214:217], v[12:15]
	v_mfma_f32_16x16x32_bf16 v[8:11], v[140:143], v[214:217], v[8:11]
	s_setprio 0
	s_setprio 1
	v_mfma_f32_16x16x32_bf16 v[52:55], v[144:147], v[180:183], 0
	v_mfma_f32_16x16x32_bf16 v[48:51], v[172:175], v[180:183], 0
	v_mfma_f32_16x16x32_bf16 v[36:39], v[144:147], v[194:197], 0
	v_mfma_f32_16x16x32_bf16 v[32:35], v[172:175], v[194:197], 0
	v_mfma_f32_16x16x32_bf16 v[20:23], v[144:147], v[202:205], 0
	v_mfma_f32_16x16x32_bf16 v[16:19], v[172:175], v[202:205], 0
	v_mfma_f32_16x16x32_bf16 v[4:7], v[144:147], v[210:213], 0
	v_mfma_f32_16x16x32_bf16 v[0:3], v[172:175], v[210:213], 0
	v_mfma_f32_16x16x32_bf16 v[52:55], v[148:151], v[184:187], v[52:55]
	v_mfma_f32_16x16x32_bf16 v[48:51], v[176:179], v[184:187], v[48:51]
	v_mfma_f32_16x16x32_bf16 v[36:39], v[148:151], v[198:201], v[36:39]
	v_mfma_f32_16x16x32_bf16 v[32:35], v[176:179], v[198:201], v[32:35]
	v_mfma_f32_16x16x32_bf16 v[20:23], v[148:151], v[206:209], v[20:23]
	v_mfma_f32_16x16x32_bf16 v[16:19], v[176:179], v[206:209], v[16:19]
	v_mfma_f32_16x16x32_bf16 v[4:7], v[148:151], v[214:217], v[4:7]
	v_mfma_f32_16x16x32_bf16 v[0:3], v[176:179], v[214:217], v[0:3]
	s_setprio 0
	s_barrier
	s_add_i32 s61, 0, 0x18000
	s_add_i32 s62, 0, 0x1c000
	ds_read_b128 v[128:131], v252
	ds_read_b128 v[132:135], v252 offset:1024
	ds_read_b128 v[136:139], v252 offset:2048
	ds_read_b128 v[140:143], v252 offset:3072
	ds_read_b128 v[144:147], v253
	ds_read_b128 v[148:151], v253 offset:1024
	ds_read_b128 v[172:175], v253 offset:2048
	ds_read_b128 v[176:179], v253 offset:3072
	s_add_u32 s36, s36, 0x40000
	s_addc_u32 s37, s37, 0
	s_mov_b32 m0, s42
	ds_read_b128 v[180:183], v192 offset:32768
	ds_read_b128 v[184:187], v192 offset:33792
	ds_read_b128 v[194:197], v192 offset:34816
	ds_read_b128 v[198:201], v192 offset:35840
	ds_read_b128 v[202:205], v192 offset:36864
	ds_read_b128 v[206:209], v192 offset:37888
	ds_read_b128 v[210:213], v192 offset:38912
	ds_read_b128 v[214:217], v192 offset:39936
	global_load_lds_dwordx4 v152, s[36:37]
	s_mov_b32 m0, s43
	s_nop 0
	global_load_lds_dwordx4 v156, s[36:37]
	s_waitcnt vmcnt(8) lgkmcnt(0)
	s_barrier
	s_nop 0
	s_setprio 1
	v_mfma_f32_16x16x32_bf16 v[124:127], v[128:131], v[180:183], v[124:127]
	v_mfma_f32_16x16x32_bf16 v[120:123], v[136:139], v[180:183], v[120:123]
	v_mfma_f32_16x16x32_bf16 v[108:111], v[128:131], v[194:197], v[108:111]
	v_mfma_f32_16x16x32_bf16 v[104:107], v[136:139], v[194:197], v[104:107]
	v_mfma_f32_16x16x32_bf16 v[92:95], v[128:131], v[202:205], v[92:95]
	v_mfma_f32_16x16x32_bf16 v[88:91], v[136:139], v[202:205], v[88:91]
	v_mfma_f32_16x16x32_bf16 v[76:79], v[128:131], v[210:213], v[76:79]
	v_mfma_f32_16x16x32_bf16 v[72:75], v[136:139], v[210:213], v[72:75]
	v_mfma_f32_16x16x32_bf16 v[124:127], v[132:135], v[184:187], v[124:127]
	v_mfma_f32_16x16x32_bf16 v[120:123], v[140:143], v[184:187], v[120:123]
	v_mfma_f32_16x16x32_bf16 v[108:111], v[132:135], v[198:201], v[108:111]
	v_mfma_f32_16x16x32_bf16 v[104:107], v[140:143], v[198:201], v[104:107]
	v_mfma_f32_16x16x32_bf16 v[92:95], v[132:135], v[206:209], v[92:95]
	v_mfma_f32_16x16x32_bf16 v[88:91], v[140:143], v[206:209], v[88:91]
	v_mfma_f32_16x16x32_bf16 v[76:79], v[132:135], v[214:217], v[76:79]
	v_mfma_f32_16x16x32_bf16 v[72:75], v[140:143], v[214:217], v[72:75]
	s_setprio 0
	s_setprio 1
	v_mfma_f32_16x16x32_bf16 v[116:119], v[144:147], v[180:183], v[116:119]
	v_mfma_f32_16x16x32_bf16 v[112:115], v[172:175], v[180:183], v[112:115]
	v_mfma_f32_16x16x32_bf16 v[100:103], v[144:147], v[194:197], v[100:103]
	v_mfma_f32_16x16x32_bf16 v[96:99], v[172:175], v[194:197], v[96:99]
	v_mfma_f32_16x16x32_bf16 v[84:87], v[144:147], v[202:205], v[84:87]
	v_mfma_f32_16x16x32_bf16 v[80:83], v[172:175], v[202:205], v[80:83]
	v_mfma_f32_16x16x32_bf16 v[68:71], v[144:147], v[210:213], v[68:71]
	v_mfma_f32_16x16x32_bf16 v[64:67], v[172:175], v[210:213], v[64:67]
	v_mfma_f32_16x16x32_bf16 v[116:119], v[148:151], v[184:187], v[116:119]
	v_mfma_f32_16x16x32_bf16 v[112:115], v[176:179], v[184:187], v[112:115]
	v_mfma_f32_16x16x32_bf16 v[100:103], v[148:151], v[198:201], v[100:103]
	v_mfma_f32_16x16x32_bf16 v[96:99], v[176:179], v[198:201], v[96:99]
	v_mfma_f32_16x16x32_bf16 v[84:87], v[148:151], v[206:209], v[84:87]
	v_mfma_f32_16x16x32_bf16 v[80:83], v[176:179], v[206:209], v[80:83]
	v_mfma_f32_16x16x32_bf16 v[68:71], v[148:151], v[214:217], v[68:71]
	v_mfma_f32_16x16x32_bf16 v[64:67], v[176:179], v[214:217], v[64:67]
	s_setprio 0
	s_barrier
; #define PG8_STAGE(bufoff, gbase, voff) do { _Pragma("unroll") for (int _i = 0; _i < 2; ++_i) \
;         __builtin_amdgcn_global_load_lds((const unsigned*)((const char*)(gbase) + (voff)[_i]), (PG8_LAS unsigned*)(lds + (bufoff) + ldsw + _i * 8192), 16, 0, 0); } while (0)
; #define PG8_LDA(dst, b, h) do { _Pragma("unroll") for (int m = 0; m < 4; ++m) _Pragma("unroll") for (int k = 0; k < 2; ++k) dst[m][k] = *(const PG8_LAS bf16x8*)(lds + PG8_SA(b, h) + aoff + m * 2048 + k * 1024); } while (0)
; #define PG8_LDB(dst, b, h) do { _Pragma("unroll") for (int n = 0; n < 2; ++n) _Pragma("unroll") for (int k = 0; k < 2; ++k) dst[n][k] = *(const PG8_LAS bf16x8*)(lds + PG8_SB(b, h) + boff + n * 2048 + k * 1024); } while (0)
; #define PG8_MMA(ai, bj, At, Bt) do { __builtin_amdgcn_s_setprio(1); _Pragma("unroll") for (int m = 0; m < 4; ++m) _Pragma("unroll") for (int n = 0; n < 2; ++n) _Pragma("unroll") for (int k = 0; k < 2; ++k) \
;         acc[ai][bj][m][n] = __builtin_amdgcn_mfma_f32_16x16x32_bf16(Bt[n][k], At[m][k], acc[ai][bj][m][n], 0, 0, 0); __builtin_amdgcn_s_setprio(0); } while (0)
; #define PG8_WAIT_V(n) asm volatile("s_waitcnt vmcnt(" #n ")" ::: "memory")
; #define PG8_WAIT_L(n) asm volatile("s_waitcnt lgkmcnt(" #n ")" ::: "memory")
; #define PG8_BAR __builtin_amdgcn_s_barrier()
; #define PG8_SCHED __builtin_amdgcn_sched_barrier(0)
; template <class Epi, class Sched, bool ALIGN_EPI = false, bool SP2 = false>
; __device__ __forceinline__ void gemm_phase(PG8_LAS unsigned char* lds, const Gemm g, const Sched& S, const Epi& E, const int wid) {
;     ...
;             if constexpr (SP2) {
;             PG8_LDB(B0, 0, 0); PG8_LDB(B1, 0, 1); PG8_SCHED; PG8_LDA(At, 0, 0); PG8_STAGE(PG8_SA(1, 1), a1 + hstepA, voffA);
;             PG8_WAIT_V(8); PG8_WAIT_L(0); PG8_BAR; PG8_MMA(0, 0, At, B0); PG8_MMA(0, 1, At, B1); PG8_BAR; PG8_SCHED;
;     ...
;             PG8_LDA(At, 1, 1); PG8_STAGE(PG8_SB(1, 0), b3, voffB); PG8_STAGE(PG8_SB(1, 1), b3 + hstepB, voffB); PG8_STAGE(PG8_SA(1, 0), a3, voffA);
;             PG8_WAIT_V(8); PG8_WAIT_L(0); PG8_BAR; PG8_MMA(1, 0, At, B0); PG8_MMA(1, 1, At, B1); PG8_BAR; PG8_SCHED;
	s_add_i32 s36, s61, s39
	s_mov_b32 m0, s36
	ds_read_b128 v[180:183], v192 offset:49152
	ds_read_b128 v[184:187], v192 offset:50176
	ds_read_b128 v[194:197], v192 offset:51200
	ds_read_b128 v[198:201], v192 offset:52224
	ds_read_b128 v[202:205], v192 offset:53248
	ds_read_b128 v[206:209], v192 offset:54272
	ds_read_b128 v[210:213], v192 offset:55296
	ds_read_b128 v[214:217], v192 offset:56320
	global_load_lds_dwordx4 v154, s[98:99]
	s_add_i32 m0, s36, 0x2000
	s_add_u32 s34, s34, 0x40080
	s_addc_u32 s35, s35, 0
	s_add_i32 s36, s62, s39
	global_load_lds_dwordx4 v158, s[98:99]
	s_mov_b32 m0, s36
	s_nop 0
	global_load_lds_dwordx4 v154, s[34:35]
	s_add_i32 m0, s36, 0x2000
	s_nop 0
	global_load_lds_dwordx4 v158, s[34:35]
	s_mov_b32 m0, s45
	s_nop 0
	global_load_lds_dwordx4 v152, s[100:101]
	s_mov_b32 m0, s46
	s_nop 0
	global_load_lds_dwordx4 v156, s[100:101]
	s_waitcnt vmcnt(8) lgkmcnt(0)
	s_barrier
	s_setprio 1
	v_mfma_f32_16x16x32_bf16 v[60:63], v[128:131], v[180:183], v[60:63]
	v_mfma_f32_16x16x32_bf16 v[56:59], v[136:139], v[180:183], v[56:59]
	v_mfma_f32_16x16x32_bf16 v[44:47], v[128:131], v[194:197], v[44:47]
	v_mfma_f32_16x16x32_bf16 v[40:43], v[136:139], v[194:197], v[40:43]
	v_mfma_f32_16x16x32_bf16 v[28:31], v[128:131], v[202:205], v[28:31]
	v_mfma_f32_16x16x32_bf16 v[24:27], v[136:139], v[202:205], v[24:27]
	v_mfma_f32_16x16x32_bf16 v[12:15], v[128:131], v[210:213], v[12:15]
	v_mfma_f32_16x16x32_bf16 v[8:11], v[136:139], v[210:213], v[8:11]
	v_mfma_f32_16x16x32_bf16 v[60:63], v[132:135], v[184:187], v[60:63]
	v_mfma_f32_16x16x32_bf16 v[56:59], v[140:143], v[184:187], v[56:59]
	v_mfma_f32_16x16x32_bf16 v[44:47], v[132:135], v[198:201], v[44:47]
	v_mfma_f32_16x16x32_bf16 v[40:43], v[140:143], v[198:201], v[40:43]
	v_mfma_f32_16x16x32_bf16 v[28:31], v[132:135], v[206:209], v[28:31]
	v_mfma_f32_16x16x32_bf16 v[24:27], v[140:143], v[206:209], v[24:27]
	v_mfma_f32_16x16x32_bf16 v[12:15], v[132:135], v[214:217], v[12:15]
	v_mfma_f32_16x16x32_bf16 v[8:11], v[140:143], v[214:217], v[8:11]
	s_setprio 0
	s_setprio 1
	v_mfma_f32_16x16x32_bf16 v[52:55], v[144:147], v[180:183], v[52:55]
	v_mfma_f32_16x16x32_bf16 v[48:51], v[172:175], v[180:183], v[48:51]
	v_mfma_f32_16x16x32_bf16 v[36:39], v[144:147], v[194:197], v[36:39]
	v_mfma_f32_16x16x32_bf16 v[32:35], v[172:175], v[194:197], v[32:35]
	v_mfma_f32_16x16x32_bf16 v[20:23], v[144:147], v[202:205], v[20:23]
	v_mfma_f32_16x16x32_bf16 v[16:19], v[172:175], v[202:205], v[16:19]
	v_mfma_f32_16x16x32_bf16 v[4:7], v[144:147], v[210:213], v[4:7]
	v_mfma_f32_16x16x32_bf16 v[0:3], v[172:175], v[210:213], v[0:3]
	v_mfma_f32_16x16x32_bf16 v[52:55], v[148:151], v[184:187], v[52:55]
	v_mfma_f32_16x16x32_bf16 v[48:51], v[176:179], v[184:187], v[48:51]
	v_mfma_f32_16x16x32_bf16 v[36:39], v[148:151], v[198:201], v[36:39]
	v_mfma_f32_16x16x32_bf16 v[32:35], v[176:179], v[198:201], v[32:35]
	v_mfma_f32_16x16x32_bf16 v[20:23], v[148:151], v[206:209], v[20:23]
	v_mfma_f32_16x16x32_bf16 v[16:19], v[176:179], v[206:209], v[16:19]
	v_mfma_f32_16x16x32_bf16 v[4:7], v[148:151], v[214:217], v[4:7]
	v_mfma_f32_16x16x32_bf16 v[0:3], v[176:179], v[214:217], v[0:3]
	s_setprio 0
	s_barrier
	s_add_i32 s60, s60, 2
	s_add_u32 s30, s30, 0x100
	s_addc_u32 s31, s31, 0
	s_add_u32 s58, s58, 0x100
	s_addc_u32 s59, s59, 0
	s_cmp_gt_u32 s60, 13
.LBB0_2725:
	ds_read_b128 v[128:131], v190
	ds_read_b128 v[132:135], v190 offset:1024
	ds_read_b128 v[136:139], v190 offset:2048
	ds_read_b128 v[140:143], v190 offset:3072
	ds_read_b128 v[144:147], v191
	ds_read_b128 v[148:151], v191 offset:1024
	ds_read_b128 v[172:175], v191 offset:2048
	ds_read_b128 v[176:179], v191 offset:3072
	s_add_u32 s34, s30, 0xfffc0080
	s_addc_u32 s35, s31, -1
	s_cmp_eq_u32 s60, 12
	s_cselect_b32 s37, s21, s35
	s_cselect_b32 s36, s27, s34
	s_cselect_b32 s35, s19, s59
	s_cselect_b32 s34, s29, s58
	s_add_i32 m0, s40, 0xc000
	ds_read_b128 v[180:183], v192
	ds_read_b128 v[184:187], v192 offset:1024
	ds_read_b128 v[194:197], v192 offset:2048
	ds_read_b128 v[198:201], v192 offset:3072
	ds_read_b128 v[202:205], v192 offset:4096
	ds_read_b128 v[206:209], v192 offset:5120
	ds_read_b128 v[210:213], v192 offset:6144
	ds_read_b128 v[214:217], v192 offset:7168
	global_load_lds_dwordx4 v164, s[30:31]
	s_add_i32 m0, s40, 0xe000
	s_nop 0
	global_load_lds_dwordx4 v166, s[30:31]
	s_waitcnt vmcnt(8) lgkmcnt(0)
	s_barrier
	s_setprio 1
	v_mfma_f32_16x16x32_bf16 v[124:127], v[128:131], v[180:183], v[124:127]
	v_mfma_f32_16x16x32_bf16 v[120:123], v[136:139], v[180:183], v[120:123]
	v_mfma_f32_16x16x32_bf16 v[108:111], v[128:131], v[194:197], v[108:111]
	v_mfma_f32_16x16x32_bf16 v[104:107], v[136:139], v[194:197], v[104:107]
	v_mfma_f32_16x16x32_bf16 v[92:95], v[128:131], v[202:205], v[92:95]
	v_mfma_f32_16x16x32_bf16 v[88:91], v[136:139], v[202:205], v[88:91]
	v_mfma_f32_16x16x32_bf16 v[76:79], v[128:131], v[210:213], v[76:79]
	v_mfma_f32_16x16x32_bf16 v[72:75], v[136:139], v[210:213], v[72:75]
	v_mfma_f32_16x16x32_bf16 v[124:127], v[132:135], v[184:187], v[124:127]
	v_mfma_f32_16x16x32_bf16 v[120:123], v[140:143], v[184:187], v[120:123]
	v_mfma_f32_16x16x32_bf16 v[108:111], v[132:135], v[198:201], v[108:111]
	v_mfma_f32_16x16x32_bf16 v[104:107], v[140:143], v[198:201], v[104:107]
	v_mfma_f32_16x16x32_bf16 v[92:95], v[132:135], v[206:209], v[92:95]
	v_mfma_f32_16x16x32_bf16 v[88:91], v[140:143], v[206:209], v[88:91]
	v_mfma_f32_16x16x32_bf16 v[76:79], v[132:135], v[214:217], v[76:79]
	v_mfma_f32_16x16x32_bf16 v[72:75], v[140:143], v[214:217], v[72:75]
	s_setprio 0
	s_setprio 1
	v_mfma_f32_16x16x32_bf16 v[116:119], v[144:147], v[180:183], v[116:119]
	v_mfma_f32_16x16x32_bf16 v[112:115], v[172:175], v[180:183], v[112:115]
	v_mfma_f32_16x16x32_bf16 v[100:103], v[144:147], v[194:197], v[100:103]
	v_mfma_f32_16x16x32_bf16 v[96:99], v[172:175], v[194:197], v[96:99]
	v_mfma_f32_16x16x32_bf16 v[84:87], v[144:147], v[202:205], v[84:87]
	v_mfma_f32_16x16x32_bf16 v[80:83], v[172:175], v[202:205], v[80:83]
	v_mfma_f32_16x16x32_bf16 v[68:71], v[144:147], v[210:213], v[68:71]
	v_mfma_f32_16x16x32_bf16 v[64:67], v[172:175], v[210:213], v[64:67]
	v_mfma_f32_16x16x32_bf16 v[116:119], v[148:151], v[184:187], v[116:119]
	v_mfma_f32_16x16x32_bf16 v[112:115], v[176:179], v[184:187], v[112:115]
	v_mfma_f32_16x16x32_bf16 v[100:103], v[148:151], v[198:201], v[100:103]
	v_mfma_f32_16x16x32_bf16 v[96:99], v[176:179], v[198:201], v[96:99]
	v_mfma_f32_16x16x32_bf16 v[84:87], v[148:151], v[206:209], v[84:87]
	v_mfma_f32_16x16x32_bf16 v[80:83], v[176:179], v[206:209], v[80:83]
	v_mfma_f32_16x16x32_bf16 v[68:71], v[148:151], v[214:217], v[68:71]
	v_mfma_f32_16x16x32_bf16 v[64:67], v[176:179], v[214:217], v[64:67]
	s_setprio 0
	s_barrier
; #define PG8_STAGE(bufoff, gbase, voff) do { _Pragma("unroll") for (int _i = 0; _i < 2; ++_i) \
;         __builtin_amdgcn_global_load_lds((const unsigned*)((const char*)(gbase) + (voff)[_i]), (PG8_LAS unsigned*)(lds + (bufoff) + ldsw + _i * 8192), 16, 0, 0); } while (0)
; #define PG8_LDA(dst, b, h) do { _Pragma("unroll") for (int m = 0; m < 4; ++m) _Pragma("unroll") for (int k = 0; k < 2; ++k) dst[m][k] = *(const PG8_LAS bf16x8*)(lds + PG8_SA(b, h) + aoff + m * 2048 + k * 1024); } while (0)
; #define PG8_LDB(dst, b, h) do { _Pragma("unroll") for (int n = 0; n < 2; ++n) _Pragma("unroll") for (int k = 0; k < 2; ++k) dst[n][k] = *(const PG8_LAS bf16x8*)(lds + PG8_SB(b, h) + boff + n * 2048 + k * 1024); } while (0)
; #define PG8_MMA(ai, bj, At, Bt) do { __builtin_amdgcn_s_setprio(1); _Pragma("unroll") for (int m = 0; m < 4; ++m) _Pragma("unroll") for (int n = 0; n < 2; ++n) _Pragma("unroll") for (int k = 0; k < 2; ++k) \
;         acc[ai][bj][m][n] = __builtin_amdgcn_mfma_f32_16x16x32_bf16(Bt[n][k], At[m][k], acc[ai][bj][m][n], 0, 0, 0); __builtin_amdgcn_s_setprio(0); } while (0)
; #define PG8_WAIT_V(n) asm volatile("s_waitcnt vmcnt(" #n ")" ::: "memory")
; #define PG8_WAIT_L(n) asm volatile("s_waitcnt lgkmcnt(" #n ")" ::: "memory")
; #define PG8_BAR __builtin_amdgcn_s_barrier()
; #define PG8_SCHED __builtin_amdgcn_sched_barrier(0)
; template <class Epi, class Sched, bool ALIGN_EPI = false, bool SP2 = false>
; __device__ __forceinline__ void gemm_phase(PG8_LAS unsigned char* lds, const Gemm g, const Sched& S, const Epi& E, const int wid) {
;     ...
;             PG8_LDA(At, 0, 1); PG8_STAGE(PG8_SB(0, 0), b2, voffB); PG8_STAGE(PG8_SB(0, 1), b2 + hstepB, voffB); PG8_STAGE(PG8_SA(0, 0), a2, voffA);
;             PG8_WAIT_V(8); PG8_WAIT_L(0); PG8_BAR; PG8_MMA(1, 0, At, B0); PG8_MMA(1, 1, At, B1); PG8_BAR; PG8_SCHED;
;             PG8_LDB(B0, 1, 0); PG8_LDB(B1, 1, 1); PG8_SCHED; PG8_LDA(At, 1, 0); PG8_STAGE(PG8_SA(0, 1), a2 + hstepA, voffA);
	s_add_i32 s61, s49, s39
	s_add_u32 s98, s34, 0x80
	s_addc_u32 s99, s35, 0
	s_mov_b32 m0, s61
	ds_read_b128 v[180:183], v192 offset:16384
	ds_read_b128 v[184:187], v192 offset:17408
	ds_read_b128 v[194:197], v192 offset:18432
	ds_read_b128 v[198:201], v192 offset:19456
	ds_read_b128 v[202:205], v192 offset:20480
	ds_read_b128 v[206:209], v192 offset:21504
	ds_read_b128 v[210:213], v192 offset:22528
	ds_read_b128 v[214:217], v192 offset:23552
	global_load_lds_dwordx4 v154, s[34:35]
	s_add_i32 m0, s61, 0x2000
	s_add_u32 s62, s34, 0x40000
	s_addc_u32 s63, s35, 0
	s_add_i32 s61, s56, s39
	global_load_lds_dwordx4 v158, s[34:35]
	s_mov_b32 m0, s61
	s_add_u32 s100, s36, 0x80
	s_addc_u32 s101, s37, 0
	global_load_lds_dwordx4 v154, s[62:63]
	s_add_i32 m0, s61, 0x2000
	s_nop 0
	global_load_lds_dwordx4 v158, s[62:63]
	s_mov_b32 m0, s40
	s_nop 0
	global_load_lds_dwordx4 v152, s[36:37]
	s_mov_b32 m0, s41
	s_nop 0
	global_load_lds_dwordx4 v156, s[36:37]
	s_waitcnt vmcnt(8) lgkmcnt(0)
	s_barrier
	s_nop 0
	s_setprio 1
	v_mfma_f32_16x16x32_bf16 v[60:63], v[128:131], v[180:183], v[60:63]
	v_mfma_f32_16x16x32_bf16 v[56:59], v[136:139], v[180:183], v[56:59]
	v_mfma_f32_16x16x32_bf16 v[44:47], v[128:131], v[194:197], v[44:47]
	v_mfma_f32_16x16x32_bf16 v[40:43], v[136:139], v[194:197], v[40:43]
	v_mfma_f32_16x16x32_bf16 v[28:31], v[128:131], v[202:205], v[28:31]
	v_mfma_f32_16x16x32_bf16 v[24:27], v[136:139], v[202:205], v[24:27]
	v_mfma_f32_16x16x32_bf16 v[12:15], v[128:131], v[210:213], v[12:15]
	v_mfma_f32_16x16x32_bf16 v[8:11], v[136:139], v[210:213], v[8:11]
	v_mfma_f32_16x16x32_bf16 v[60:63], v[132:135], v[184:187], v[60:63]
	v_mfma_f32_16x16x32_bf16 v[56:59], v[140:143], v[184:187], v[56:59]
	v_mfma_f32_16x16x32_bf16 v[44:47], v[132:135], v[198:201], v[44:47]
	v_mfma_f32_16x16x32_bf16 v[40:43], v[140:143], v[198:201], v[40:43]
	v_mfma_f32_16x16x32_bf16 v[28:31], v[132:135], v[206:209], v[28:31]
	v_mfma_f32_16x16x32_bf16 v[24:27], v[140:143], v[206:209], v[24:27]
	v_mfma_f32_16x16x32_bf16 v[12:15], v[132:135], v[214:217], v[12:15]
	v_mfma_f32_16x16x32_bf16 v[8:11], v[140:143], v[214:217], v[8:11]
	s_setprio 0
	s_setprio 1
	v_mfma_f32_16x16x32_bf16 v[52:55], v[144:147], v[180:183], v[52:55]
	v_mfma_f32_16x16x32_bf16 v[48:51], v[172:175], v[180:183], v[48:51]
	v_mfma_f32_16x16x32_bf16 v[36:39], v[144:147], v[194:197], v[36:39]
	v_mfma_f32_16x16x32_bf16 v[32:35], v[172:175], v[194:197], v[32:35]
	v_mfma_f32_16x16x32_bf16 v[20:23], v[144:147], v[202:205], v[20:23]
	v_mfma_f32_16x16x32_bf16 v[16:19], v[172:175], v[202:205], v[16:19]
	v_mfma_f32_16x16x32_bf16 v[4:7], v[144:147], v[210:213], v[4:7]
	v_mfma_f32_16x16x32_bf16 v[0:3], v[172:175], v[210:213], v[0:3]
	v_mfma_f32_16x16x32_bf16 v[52:55], v[148:151], v[184:187], v[52:55]
	v_mfma_f32_16x16x32_bf16 v[48:51], v[176:179], v[184:187], v[48:51]
	v_mfma_f32_16x16x32_bf16 v[36:39], v[148:151], v[198:201], v[36:39]
	v_mfma_f32_16x16x32_bf16 v[32:35], v[176:179], v[198:201], v[32:35]
	v_mfma_f32_16x16x32_bf16 v[20:23], v[148:151], v[206:209], v[20:23]
	v_mfma_f32_16x16x32_bf16 v[16:19], v[176:179], v[206:209], v[16:19]
	v_mfma_f32_16x16x32_bf16 v[4:7], v[148:151], v[214:217], v[4:7]
	v_mfma_f32_16x16x32_bf16 v[0:3], v[176:179], v[214:217], v[0:3]
	s_setprio 0
	s_barrier
	s_add_i32 s61, 0, 0x18000
	s_add_i32 s62, 0, 0x1c000
	ds_read_b128 v[128:131], v252
	ds_read_b128 v[132:135], v252 offset:1024
	ds_read_b128 v[136:139], v252 offset:2048
	ds_read_b128 v[140:143], v252 offset:3072
	ds_read_b128 v[144:147], v253
	ds_read_b128 v[148:151], v253 offset:1024
	ds_read_b128 v[172:175], v253 offset:2048
	ds_read_b128 v[176:179], v253 offset:3072
	s_add_u32 s36, s36, 0x40000
	s_addc_u32 s37, s37, 0
	s_mov_b32 m0, s42
	ds_read_b128 v[180:183], v192 offset:32768
	ds_read_b128 v[184:187], v192 offset:33792
	ds_read_b128 v[194:197], v192 offset:34816
	ds_read_b128 v[198:201], v192 offset:35840
	ds_read_b128 v[202:205], v192 offset:36864
	ds_read_b128 v[206:209], v192 offset:37888
	ds_read_b128 v[210:213], v192 offset:38912
	ds_read_b128 v[214:217], v192 offset:39936
	global_load_lds_dwordx4 v152, s[36:37]
	s_mov_b32 m0, s43
	s_nop 0
	global_load_lds_dwordx4 v156, s[36:37]
	s_waitcnt vmcnt(8) lgkmcnt(0)
	s_barrier
; #define PG8_STAGE(bufoff, gbase, voff) do { _Pragma("unroll") for (int _i = 0; _i < 2; ++_i) \
;         __builtin_amdgcn_global_load_lds((const unsigned*)((const char*)(gbase) + (voff)[_i]), (PG8_LAS unsigned*)(lds + (bufoff) + ldsw + _i * 8192), 16, 0, 0); } while (0)
; #define PG8_LDA(dst, b, h) do { _Pragma("unroll") for (int m = 0; m < 4; ++m) _Pragma("unroll") for (int k = 0; k < 2; ++k) dst[m][k] = *(const PG8_LAS bf16x8*)(lds + PG8_SA(b, h) + aoff + m * 2048 + k * 1024); } while (0)
; #define PG8_MMA(ai, bj, At, Bt) do { __builtin_amdgcn_s_setprio(1); _Pragma("unroll") for (int m = 0; m < 4; ++m) _Pragma("unroll") for (int n = 0; n < 2; ++n) _Pragma("unroll") for (int k = 0; k < 2; ++k) \
;         acc[ai][bj][m][n] = __builtin_amdgcn_mfma_f32_16x16x32_bf16(Bt[n][k], At[m][k], acc[ai][bj][m][n], 0, 0, 0); __builtin_amdgcn_s_setprio(0); } while (0)
; #define PG8_WAIT_V(n) asm volatile("s_waitcnt vmcnt(" #n ")" ::: "memory")
; #define PG8_WAIT_L(n) asm volatile("s_waitcnt lgkmcnt(" #n ")" ::: "memory")
; #define PG8_BAR __builtin_amdgcn_s_barrier()
; #define PG8_SCHED __builtin_amdgcn_sched_barrier(0)
; template <class Epi, class Sched, bool ALIGN_EPI = false, bool SP2 = false>
; __device__ __forceinline__ void gemm_phase(PG8_LAS unsigned char* lds, const Gemm g, const Sched& S, const Epi& E, const int wid) {
;     ...
;             PG8_WAIT_V(8); PG8_WAIT_L(0); PG8_BAR; PG8_MMA(0, 0, At, B0); PG8_MMA(0, 1, At, B1); PG8_BAR; PG8_SCHED;
;             PG8_LDA(At, 1, 1); PG8_STAGE(PG8_SB(1, 0), b3, voffB); PG8_STAGE(PG8_SB(1, 1), b3 + hstepB, voffB); PG8_STAGE(PG8_SA(1, 0), a3, voffA);
;             PG8_WAIT_V(8); PG8_WAIT_L(0); PG8_BAR; PG8_MMA(1, 0, At, B0); PG8_MMA(1, 1, At, B1); PG8_BAR; PG8_SCHED;
;     ...
;         if constexpr (ALIGN_EPI) { if (wr == 0) PG8_BAR; }
	s_nop 0
	s_setprio 1
	v_mfma_f32_16x16x32_bf16 v[124:127], v[128:131], v[180:183], v[124:127]
	v_mfma_f32_16x16x32_bf16 v[120:123], v[136:139], v[180:183], v[120:123]
	v_mfma_f32_16x16x32_bf16 v[108:111], v[128:131], v[194:197], v[108:111]
	v_mfma_f32_16x16x32_bf16 v[104:107], v[136:139], v[194:197], v[104:107]
	v_mfma_f32_16x16x32_bf16 v[92:95], v[128:131], v[202:205], v[92:95]
	v_mfma_f32_16x16x32_bf16 v[88:91], v[136:139], v[202:205], v[88:91]
	v_mfma_f32_16x16x32_bf16 v[76:79], v[128:131], v[210:213], v[76:79]
	v_mfma_f32_16x16x32_bf16 v[72:75], v[136:139], v[210:213], v[72:75]
	v_mfma_f32_16x16x32_bf16 v[124:127], v[132:135], v[184:187], v[124:127]
	v_mfma_f32_16x16x32_bf16 v[120:123], v[140:143], v[184:187], v[120:123]
	v_mfma_f32_16x16x32_bf16 v[108:111], v[132:135], v[198:201], v[108:111]
	v_mfma_f32_16x16x32_bf16 v[104:107], v[140:143], v[198:201], v[104:107]
	v_mfma_f32_16x16x32_bf16 v[92:95], v[132:135], v[206:209], v[92:95]
	v_mfma_f32_16x16x32_bf16 v[88:91], v[140:143], v[206:209], v[88:91]
	v_mfma_f32_16x16x32_bf16 v[76:79], v[132:135], v[214:217], v[76:79]
	v_mfma_f32_16x16x32_bf16 v[72:75], v[140:143], v[214:217], v[72:75]
	s_setprio 0
	s_setprio 1
	v_mfma_f32_16x16x32_bf16 v[116:119], v[144:147], v[180:183], v[116:119]
	v_mfma_f32_16x16x32_bf16 v[112:115], v[172:175], v[180:183], v[112:115]
	v_mfma_f32_16x16x32_bf16 v[100:103], v[144:147], v[194:197], v[100:103]
	v_mfma_f32_16x16x32_bf16 v[96:99], v[172:175], v[194:197], v[96:99]
	v_mfma_f32_16x16x32_bf16 v[84:87], v[144:147], v[202:205], v[84:87]
	v_mfma_f32_16x16x32_bf16 v[80:83], v[172:175], v[202:205], v[80:83]
	v_mfma_f32_16x16x32_bf16 v[68:71], v[144:147], v[210:213], v[68:71]
	v_mfma_f32_16x16x32_bf16 v[64:67], v[172:175], v[210:213], v[64:67]
	v_mfma_f32_16x16x32_bf16 v[116:119], v[148:151], v[184:187], v[116:119]
	v_mfma_f32_16x16x32_bf16 v[112:115], v[176:179], v[184:187], v[112:115]
	v_mfma_f32_16x16x32_bf16 v[100:103], v[148:151], v[198:201], v[100:103]
	v_mfma_f32_16x16x32_bf16 v[96:99], v[176:179], v[198:201], v[96:99]
	v_mfma_f32_16x16x32_bf16 v[84:87], v[148:151], v[206:209], v[84:87]
	v_mfma_f32_16x16x32_bf16 v[80:83], v[176:179], v[206:209], v[80:83]
	v_mfma_f32_16x16x32_bf16 v[68:71], v[148:151], v[214:217], v[68:71]
	v_mfma_f32_16x16x32_bf16 v[64:67], v[176:179], v[214:217], v[64:67]
	s_setprio 0
	s_barrier
	s_add_i32 s36, s61, s39
	s_mov_b32 m0, s36
	ds_read_b128 v[180:183], v192 offset:49152
	ds_read_b128 v[184:187], v192 offset:50176
	ds_read_b128 v[194:197], v192 offset:51200
	ds_read_b128 v[198:201], v192 offset:52224
	ds_read_b128 v[202:205], v192 offset:53248
	ds_read_b128 v[206:209], v192 offset:54272
	ds_read_b128 v[210:213], v192 offset:55296
	ds_read_b128 v[214:217], v192 offset:56320
	global_load_lds_dwordx4 v154, s[98:99]
	s_add_i32 m0, s36, 0x2000
	s_add_u32 s34, s34, 0x40080
	s_addc_u32 s35, s35, 0
	s_add_i32 s36, s62, s39
	global_load_lds_dwordx4 v158, s[98:99]
	s_mov_b32 m0, s36
	s_nop 0
	global_load_lds_dwordx4 v154, s[34:35]
	s_add_i32 m0, s36, 0x2000
	s_nop 0
	global_load_lds_dwordx4 v158, s[34:35]
	s_mov_b32 m0, s45
	s_nop 0
	global_load_lds_dwordx4 v152, s[100:101]
	s_mov_b32 m0, s46
	s_nop 0
	global_load_lds_dwordx4 v156, s[100:101]
	s_waitcnt vmcnt(8) lgkmcnt(0)
	s_barrier
	s_setprio 1
	v_mfma_f32_16x16x32_bf16 v[60:63], v[128:131], v[180:183], v[60:63]
	v_mfma_f32_16x16x32_bf16 v[56:59], v[136:139], v[180:183], v[56:59]
	v_mfma_f32_16x16x32_bf16 v[44:47], v[128:131], v[194:197], v[44:47]
	v_mfma_f32_16x16x32_bf16 v[40:43], v[136:139], v[194:197], v[40:43]
	v_mfma_f32_16x16x32_bf16 v[28:31], v[128:131], v[202:205], v[28:31]
	v_mfma_f32_16x16x32_bf16 v[24:27], v[136:139], v[202:205], v[24:27]
	v_mfma_f32_16x16x32_bf16 v[12:15], v[128:131], v[210:213], v[12:15]
	v_mfma_f32_16x16x32_bf16 v[8:11], v[136:139], v[210:213], v[8:11]
	v_mfma_f32_16x16x32_bf16 v[60:63], v[132:135], v[184:187], v[60:63]
	v_mfma_f32_16x16x32_bf16 v[56:59], v[140:143], v[184:187], v[56:59]
	v_mfma_f32_16x16x32_bf16 v[44:47], v[132:135], v[198:201], v[44:47]
	v_mfma_f32_16x16x32_bf16 v[40:43], v[140:143], v[198:201], v[40:43]
	v_mfma_f32_16x16x32_bf16 v[28:31], v[132:135], v[206:209], v[28:31]
	v_mfma_f32_16x16x32_bf16 v[24:27], v[140:143], v[206:209], v[24:27]
	v_mfma_f32_16x16x32_bf16 v[12:15], v[132:135], v[214:217], v[12:15]
	v_mfma_f32_16x16x32_bf16 v[8:11], v[140:143], v[214:217], v[8:11]
	s_setprio 0
	s_setprio 1
	v_mfma_f32_16x16x32_bf16 v[52:55], v[144:147], v[180:183], v[52:55]
	v_mfma_f32_16x16x32_bf16 v[48:51], v[172:175], v[180:183], v[48:51]
	v_mfma_f32_16x16x32_bf16 v[36:39], v[144:147], v[194:197], v[36:39]
	v_mfma_f32_16x16x32_bf16 v[32:35], v[172:175], v[194:197], v[32:35]
	v_mfma_f32_16x16x32_bf16 v[20:23], v[144:147], v[202:205], v[20:23]
	v_mfma_f32_16x16x32_bf16 v[16:19], v[172:175], v[202:205], v[16:19]
	v_mfma_f32_16x16x32_bf16 v[4:7], v[144:147], v[210:213], v[4:7]
	v_mfma_f32_16x16x32_bf16 v[0:3], v[172:175], v[210:213], v[0:3]
	v_mfma_f32_16x16x32_bf16 v[52:55], v[148:151], v[184:187], v[52:55]
	v_mfma_f32_16x16x32_bf16 v[48:51], v[176:179], v[184:187], v[48:51]
	v_mfma_f32_16x16x32_bf16 v[36:39], v[148:151], v[198:201], v[36:39]
	v_mfma_f32_16x16x32_bf16 v[32:35], v[176:179], v[198:201], v[32:35]
	v_mfma_f32_16x16x32_bf16 v[20:23], v[148:151], v[206:209], v[20:23]
	v_mfma_f32_16x16x32_bf16 v[16:19], v[176:179], v[206:209], v[16:19]
	v_mfma_f32_16x16x32_bf16 v[4:7], v[148:151], v[214:217], v[4:7]
	v_mfma_f32_16x16x32_bf16 v[0:3], v[176:179], v[214:217], v[0:3]
	s_setprio 0
	s_barrier
	s_add_i32 s60, s60, 2
	s_add_u32 s30, s30, 0x100
	s_addc_u32 s31, s31, 0
	s_add_u32 s58, s58, 0x100
	s_addc_u32 s59, s59, 0
	s_cmp_gt_u32 s60, 13
	s_cbranch_scc0 .LBB0_2725
	s_and_b64 vcc, exec, s[16:17]
	s_cbranch_vccz .LBB0_2728
	s_barrier

; #define PG8_STAGE(bufoff, gbase, voff) do { _Pragma("unroll") for (int _i = 0; _i < 2; ++_i) \
;         __builtin_amdgcn_global_load_lds((const unsigned*)((const char*)(gbase) + (voff)[_i]), (PG8_LAS unsigned*)(lds + (bufoff) + ldsw + _i * 8192), 16, 0, 0); } while (0)
; #define PG8_LDA(dst, b, h) do { _Pragma("unroll") for (int m = 0; m < 4; ++m) _Pragma("unroll") for (int k = 0; k < 2; ++k) dst[m][k] = *(const PG8_LAS bf16x8*)(lds + PG8_SA(b, h) + aoff + m * 2048 + k * 1024); } while (0)
;     __device__ __forceinline__ void operator()(const f32x4 (&acc)[2][2][4][2], const Unit& u, int wr, int wc, int fr, int fq) const {
;     ...
;             for (int ai = 0; ai < 2; ++ai)
; #pragma unroll
;                 for (int m = 0; m < 4; ++m) qd[ai][m] = row_quad(ssq, u.pm * BM + ai * HALF + wr * 64 + m * 16 + fr, fq);
; #pragma unroll
;             for (int ai = 0; ai < 2; ++ai)
; #pragma unroll
;                 for (int m = 0; m < 4; ++m) asm volatile("" : "+v"(qd[ai][m]));
; template <class Epi, class Sched, bool ALIGN_EPI = false, bool SP2 = false>
; __device__ __forceinline__ void gemm_phase(PG8_LAS unsigned char* lds, const Gemm g, const Sched& S, const Epi& E, const int wid) {
;     ...
;         const bool has_next = S.next(ui + 1, nxt);
;         const char* nA = has_next ? (const char*)g.A + (size_t)nxt.pm * tstepA : cA; const char* nB = has_next ? (const char*)g.Bt + (size_t)nxt.pn * tstepB : cB;
;         for (int t = 0; t < nt; t += 2) {
;             const bool last = (t == nt - 2);
;             const char* a1 = cA + (size_t)(t + 1) * kstep;
;             const char* a2 = last ? nA : cA + (size_t)(t + 2) * kstep; const char* b2 = last ? nB : cB + (size_t)(t + 2) * kstep;
;             const char* a3 = a2 + kstep; const char* b3 = b2 + kstep;
;             if (last && has_next) S.a_ready(nxt);
;             if constexpr (SP2) {
;             PG8_LDB(B0, 0, 0); PG8_LDB(B1, 0, 1); PG8_SCHED; PG8_LDA(At, 0, 0); PG8_STAGE(PG8_SA(1, 1), a1 + hstepA, voffA);
;             PG8_WAIT_V(8); PG8_WAIT_L(0); PG8_BAR; PG8_MMA(0, 0, At, B0); PG8_MMA(0, 1, At, B1); PG8_BAR; PG8_SCHED;
;             PG8_LDA(At, 0, 1); PG8_STAGE(PG8_SB(0, 0), b2, voffB); PG8_STAGE(PG8_SB(0, 1), b2 + hstepB, voffB); PG8_STAGE(PG8_SA(0, 0), a2, voffA);
;             PG8_WAIT_V(8); PG8_WAIT_L(0); PG8_BAR; PG8_MMA(1, 0, At, B0); PG8_MMA(1, 1, At, B1); PG8_BAR; PG8_SCHED;
.LBB0_2811:
	s_ashr_i32 s17, s16, 31
	s_lshl_b64 s[18:19], s[16:17], 19
	s_add_u32 s18, s0, s18
	s_addc_u32 s19, s1, s19
	s_and_b64 s[20:21], s[2:3], exec
	s_cselect_b32 s17, s19, s25
	s_cselect_b32 s47, s18, s24
	s_ashr_i32 s15, s14, 31
	s_lshl_b64 s[20:21], s[14:15], 19
	s_add_u32 s20, s30, s20
	s_addc_u32 s21, s31, s21
	s_and_b64 s[28:29], s[2:3], exec
	s_cselect_b32 s15, s21, s27
	s_cselect_b32 s48, s20, s26
	s_add_u32 s24, s24, 0x40080
	s_addc_u32 s25, s25, 0
	s_add_u32 s49, s26, 0x100
	s_addc_u32 s56, s27, 0
	s_mov_b32 s57, -2
	v_add_u32_e32 v252, 0x18000, v165
	v_add_u32_e32 v253, 0x1c000, v165
	ds_read_b128 v[148:151], v166
	ds_read_b128 v[152:155], v166 offset:1024
	ds_read_b128 v[156:159], v166 offset:2048
	ds_read_b128 v[160:163], v166 offset:3072
	ds_read_b128 v[172:175], v167
	ds_read_b128 v[176:179], v167 offset:1024
	ds_read_b128 v[180:183], v167 offset:2048
	ds_read_b128 v[184:187], v167 offset:3072
	s_add_u32 s26, s24, 0xfffc0080
	s_addc_u32 s27, s25, -1
	s_cmp_eq_u32 s57, 12
	s_cselect_b32 s29, s17, s27
	s_cselect_b32 s28, s47, s26
	s_cselect_b32 s27, s15, s56
	s_cselect_b32 s26, s48, s49
	s_add_i32 m0, s36, 0xc000
	ds_read_b128 v[188:191], v168
	ds_read_b128 v[192:195], v168 offset:1024
	ds_read_b128 v[196:199], v168 offset:2048
	ds_read_b128 v[200:203], v168 offset:3072
	ds_read_b128 v[204:207], v168 offset:4096
	ds_read_b128 v[208:211], v168 offset:5120
	ds_read_b128 v[212:215], v168 offset:6144
	ds_read_b128 v[216:219], v168 offset:7168
	global_load_lds_dwordx4 v140, s[24:25]
	s_add_i32 m0, s36, 0xe000
	s_nop 0
	global_load_lds_dwordx4 v142, s[24:25]
	s_waitcnt vmcnt(8) lgkmcnt(0)
	v_lshl_add_u32 v220, s22, 8, v164
	v_add_u32_e32 v236, 0x80, v220
	v_ashrrev_i32_e32 v221, 31, v220
	v_ashrrev_i32_e32 v237, 31, v236
	v_lshlrev_b64 v[220:221], 6, v[220:221]
	v_lshlrev_b64 v[236:237], 6, v[236:237]
	v_lshl_add_u64 v[220:221], v[138:139], 0, v[220:221]
	v_lshl_add_u64 v[236:237], v[138:139], 0, v[236:237]
	global_load_dwordx4 v[224:227], v[220:221], off offset:1024
	global_load_dwordx4 v[228:231], v[220:221], off offset:2048
	global_load_dwordx4 v[232:235], v[220:221], off offset:3072
	global_load_dwordx4 v[240:243], v[236:237], off offset:1024
	global_load_dwordx4 v[244:247], v[236:237], off offset:2048
	global_load_dwordx4 v[248:251], v[236:237], off offset:3072
	s_nop 0
	global_load_dwordx4 v[220:223], v[220:221], off
	s_nop 0
	global_load_dwordx4 v[236:239], v[236:237], off
	s_barrier
	s_nop 0
	s_setprio 1
	v_mfma_f32_16x16x32_bf16 v[124:127], v[148:151], v[188:191], 0
	v_mfma_f32_16x16x32_bf16 v[116:119], v[156:159], v[188:191], 0
	v_mfma_f32_16x16x32_bf16 v[108:111], v[148:151], v[196:199], 0
	v_mfma_f32_16x16x32_bf16 v[100:103], v[156:159], v[196:199], 0
	v_mfma_f32_16x16x32_bf16 v[92:95], v[148:151], v[204:207], 0
	v_mfma_f32_16x16x32_bf16 v[84:87], v[156:159], v[204:207], 0
	v_mfma_f32_16x16x32_bf16 v[76:79], v[148:151], v[212:215], 0
	v_mfma_f32_16x16x32_bf16 v[68:71], v[156:159], v[212:215], 0
	v_mfma_f32_16x16x32_bf16 v[124:127], v[152:155], v[192:195], v[124:127]
	v_mfma_f32_16x16x32_bf16 v[116:119], v[160:163], v[192:195], v[116:119]
	v_mfma_f32_16x16x32_bf16 v[108:111], v[152:155], v[200:203], v[108:111]
	v_mfma_f32_16x16x32_bf16 v[100:103], v[160:163], v[200:203], v[100:103]
	v_mfma_f32_16x16x32_bf16 v[92:95], v[152:155], v[208:211], v[92:95]
	v_mfma_f32_16x16x32_bf16 v[84:87], v[160:163], v[208:211], v[84:87]
	v_mfma_f32_16x16x32_bf16 v[76:79], v[152:155], v[216:219], v[76:79]
	v_mfma_f32_16x16x32_bf16 v[68:71], v[160:163], v[216:219], v[68:71]
	s_setprio 0
	s_setprio 1
	v_mfma_f32_16x16x32_bf16 v[120:123], v[172:175], v[188:191], 0
	v_mfma_f32_16x16x32_bf16 v[112:115], v[180:183], v[188:191], 0
	v_mfma_f32_16x16x32_bf16 v[104:107], v[172:175], v[196:199], 0
	v_mfma_f32_16x16x32_bf16 v[96:99], v[180:183], v[196:199], 0
	v_mfma_f32_16x16x32_bf16 v[88:91], v[172:175], v[204:207], 0
	v_mfma_f32_16x16x32_bf16 v[80:83], v[180:183], v[204:207], 0
	v_mfma_f32_16x16x32_bf16 v[72:75], v[172:175], v[212:215], 0
	v_mfma_f32_16x16x32_bf16 v[64:67], v[180:183], v[212:215], 0
	v_mfma_f32_16x16x32_bf16 v[120:123], v[176:179], v[192:195], v[120:123]
	v_mfma_f32_16x16x32_bf16 v[112:115], v[184:187], v[192:195], v[112:115]
	v_mfma_f32_16x16x32_bf16 v[104:107], v[176:179], v[200:203], v[104:107]
	v_mfma_f32_16x16x32_bf16 v[96:99], v[184:187], v[200:203], v[96:99]
	v_mfma_f32_16x16x32_bf16 v[88:91], v[176:179], v[208:211], v[88:91]
	v_mfma_f32_16x16x32_bf16 v[80:83], v[184:187], v[208:211], v[80:83]
	v_mfma_f32_16x16x32_bf16 v[72:75], v[176:179], v[216:219], v[72:75]
	v_mfma_f32_16x16x32_bf16 v[64:67], v[184:187], v[216:219], v[64:67]
	s_setprio 0
	s_barrier
	s_add_i32 s58, s43, s33
	s_add_u32 s98, s26, 0x80
	s_addc_u32 s99, s27, 0
	s_mov_b32 m0, s58
	ds_read_b128 v[188:191], v168 offset:16384
	ds_read_b128 v[192:195], v168 offset:17408
	ds_read_b128 v[196:199], v168 offset:18432
	ds_read_b128 v[200:203], v168 offset:19456
	ds_read_b128 v[204:207], v168 offset:20480
	ds_read_b128 v[208:211], v168 offset:21504
	ds_read_b128 v[212:215], v168 offset:22528
	ds_read_b128 v[216:219], v168 offset:23552
	global_load_lds_dwordx4 v132, s[26:27]
	s_add_i32 m0, s58, 0x2000
	s_add_u32 s58, s26, 0x40000
	s_addc_u32 s59, s27, 0
	s_add_i32 s60, s44, s33
	global_load_lds_dwordx4 v128, s[26:27]
	s_mov_b32 m0, s60
	s_add_u32 s100, s28, 0x80
	s_addc_u32 s101, s29, 0
	global_load_lds_dwordx4 v132, s[58:59]
	s_add_i32 m0, s60, 0x2000
	s_nop 0
	global_load_lds_dwordx4 v128, s[58:59]
	s_mov_b32 m0, s36
	s_nop 0
	global_load_lds_dwordx4 v134, s[28:29]
	s_mov_b32 m0, s37
	s_nop 0
	global_load_lds_dwordx4 v130, s[28:29]
	s_waitcnt vmcnt(8) lgkmcnt(0)
	s_barrier
; #define PG8_STAGE(bufoff, gbase, voff) do { _Pragma("unroll") for (int _i = 0; _i < 2; ++_i) \
;         __builtin_amdgcn_global_load_lds((const unsigned*)((const char*)(gbase) + (voff)[_i]), (PG8_LAS unsigned*)(lds + (bufoff) + ldsw + _i * 8192), 16, 0, 0); } while (0)
; #define PG8_LDA(dst, b, h) do { _Pragma("unroll") for (int m = 0; m < 4; ++m) _Pragma("unroll") for (int k = 0; k < 2; ++k) dst[m][k] = *(const PG8_LAS bf16x8*)(lds + PG8_SA(b, h) + aoff + m * 2048 + k * 1024); } while (0)
; #define PG8_LDB(dst, b, h) do { _Pragma("unroll") for (int n = 0; n < 2; ++n) _Pragma("unroll") for (int k = 0; k < 2; ++k) dst[n][k] = *(const PG8_LAS bf16x8*)(lds + PG8_SB(b, h) + boff + n * 2048 + k * 1024); } while (0)
; #define PG8_MMA(ai, bj, At, Bt) do { __builtin_amdgcn_s_setprio(1); _Pragma("unroll") for (int m = 0; m < 4; ++m) _Pragma("unroll") for (int n = 0; n < 2; ++n) _Pragma("unroll") for (int k = 0; k < 2; ++k) \
;         acc[ai][bj][m][n] = __builtin_amdgcn_mfma_f32_16x16x32_bf16(Bt[n][k], At[m][k], acc[ai][bj][m][n], 0, 0, 0); __builtin_amdgcn_s_setprio(0); } while (0)
; #define PG8_WAIT_V(n) asm volatile("s_waitcnt vmcnt(" #n ")" ::: "memory")
; #define PG8_WAIT_L(n) asm volatile("s_waitcnt lgkmcnt(" #n ")" ::: "memory")
; #define PG8_BAR __builtin_amdgcn_s_barrier()
; #define PG8_SCHED __builtin_amdgcn_sched_barrier(0)
; template <class Epi, class Sched, bool ALIGN_EPI = false, bool SP2 = false>
; __device__ __forceinline__ void gemm_phase(PG8_LAS unsigned char* lds, const Gemm g, const Sched& S, const Epi& E, const int wid) {
;     ...
;             PG8_WAIT_V(8); PG8_WAIT_L(0); PG8_BAR; PG8_MMA(0, 0, At, B0); PG8_MMA(0, 1, At, B1); PG8_BAR; PG8_SCHED;
;             PG8_LDA(At, 0, 1); PG8_STAGE(PG8_SB(0, 0), b2, voffB); PG8_STAGE(PG8_SB(0, 1), b2 + hstepB, voffB); PG8_STAGE(PG8_SA(0, 0), a2, voffA);
;             PG8_WAIT_V(8); PG8_WAIT_L(0); PG8_BAR; PG8_MMA(1, 0, At, B0); PG8_MMA(1, 1, At, B1); PG8_BAR; PG8_SCHED;
;             PG8_LDB(B0, 1, 0); PG8_LDB(B1, 1, 1); PG8_SCHED; PG8_LDA(At, 1, 0); PG8_STAGE(PG8_SA(0, 1), a2 + hstepA, voffA);
;             PG8_WAIT_V(8); PG8_WAIT_L(0); PG8_BAR; PG8_MMA(0, 0, At, B0); PG8_MMA(0, 1, At, B1); PG8_BAR; PG8_SCHED;
	s_nop 0
	s_setprio 1
	v_mfma_f32_16x16x32_bf16 v[60:63], v[148:151], v[188:191], 0
	v_mfma_f32_16x16x32_bf16 v[52:55], v[156:159], v[188:191], 0
	v_mfma_f32_16x16x32_bf16 v[44:47], v[148:151], v[196:199], 0
	v_mfma_f32_16x16x32_bf16 v[36:39], v[156:159], v[196:199], 0
	v_mfma_f32_16x16x32_bf16 v[28:31], v[148:151], v[204:207], 0
	v_mfma_f32_16x16x32_bf16 v[20:23], v[156:159], v[204:207], 0
	v_mfma_f32_16x16x32_bf16 v[12:15], v[148:151], v[212:215], 0
	v_mfma_f32_16x16x32_bf16 v[4:7], v[156:159], v[212:215], 0
	v_mfma_f32_16x16x32_bf16 v[60:63], v[152:155], v[192:195], v[60:63]
	v_mfma_f32_16x16x32_bf16 v[52:55], v[160:163], v[192:195], v[52:55]
	v_mfma_f32_16x16x32_bf16 v[44:47], v[152:155], v[200:203], v[44:47]
	v_mfma_f32_16x16x32_bf16 v[36:39], v[160:163], v[200:203], v[36:39]
	v_mfma_f32_16x16x32_bf16 v[28:31], v[152:155], v[208:211], v[28:31]
	v_mfma_f32_16x16x32_bf16 v[20:23], v[160:163], v[208:211], v[20:23]
	v_mfma_f32_16x16x32_bf16 v[12:15], v[152:155], v[216:219], v[12:15]
	v_mfma_f32_16x16x32_bf16 v[4:7], v[160:163], v[216:219], v[4:7]
	s_setprio 0
	s_setprio 1
	v_mfma_f32_16x16x32_bf16 v[56:59], v[172:175], v[188:191], 0
	v_mfma_f32_16x16x32_bf16 v[48:51], v[180:183], v[188:191], 0
	v_mfma_f32_16x16x32_bf16 v[40:43], v[172:175], v[196:199], 0
	v_mfma_f32_16x16x32_bf16 v[32:35], v[180:183], v[196:199], 0
	v_mfma_f32_16x16x32_bf16 v[24:27], v[172:175], v[204:207], 0
	v_mfma_f32_16x16x32_bf16 v[16:19], v[180:183], v[204:207], 0
	v_mfma_f32_16x16x32_bf16 v[8:11], v[172:175], v[212:215], 0
	v_mfma_f32_16x16x32_bf16 v[0:3], v[180:183], v[212:215], 0
	v_mfma_f32_16x16x32_bf16 v[56:59], v[176:179], v[192:195], v[56:59]
	v_mfma_f32_16x16x32_bf16 v[48:51], v[184:187], v[192:195], v[48:51]
	v_mfma_f32_16x16x32_bf16 v[40:43], v[176:179], v[200:203], v[40:43]
	v_mfma_f32_16x16x32_bf16 v[32:35], v[184:187], v[200:203], v[32:35]
	v_mfma_f32_16x16x32_bf16 v[24:27], v[176:179], v[208:211], v[24:27]
	v_mfma_f32_16x16x32_bf16 v[16:19], v[184:187], v[208:211], v[16:19]
	v_mfma_f32_16x16x32_bf16 v[8:11], v[176:179], v[216:219], v[8:11]
	v_mfma_f32_16x16x32_bf16 v[0:3], v[184:187], v[216:219], v[0:3]
	s_setprio 0
	s_barrier
	s_add_i32 s58, 0, 0x18000
	s_add_i32 s59, 0, 0x1c000
	ds_read_b128 v[148:151], v252
	ds_read_b128 v[152:155], v252 offset:1024
	ds_read_b128 v[156:159], v252 offset:2048
	ds_read_b128 v[160:163], v252 offset:3072
	ds_read_b128 v[172:175], v253
	ds_read_b128 v[176:179], v253 offset:1024
	ds_read_b128 v[180:183], v253 offset:2048
	ds_read_b128 v[184:187], v253 offset:3072
	s_add_u32 s28, s28, 0x40000
	s_addc_u32 s29, s29, 0
	s_mov_b32 m0, s38
	ds_read_b128 v[188:191], v168 offset:32768
	ds_read_b128 v[192:195], v168 offset:33792
	ds_read_b128 v[196:199], v168 offset:34816
	ds_read_b128 v[200:203], v168 offset:35840
	ds_read_b128 v[204:207], v168 offset:36864
	ds_read_b128 v[208:211], v168 offset:37888
	ds_read_b128 v[212:215], v168 offset:38912
	ds_read_b128 v[216:219], v168 offset:39936
	global_load_lds_dwordx4 v134, s[28:29]
	s_mov_b32 m0, s39
	s_nop 0
	global_load_lds_dwordx4 v130, s[28:29]
	s_waitcnt vmcnt(8) lgkmcnt(0)
	s_barrier
	s_nop 0
	s_setprio 1
	v_mfma_f32_16x16x32_bf16 v[124:127], v[148:151], v[188:191], v[124:127]
	v_mfma_f32_16x16x32_bf16 v[116:119], v[156:159], v[188:191], v[116:119]
	v_mfma_f32_16x16x32_bf16 v[108:111], v[148:151], v[196:199], v[108:111]
	v_mfma_f32_16x16x32_bf16 v[100:103], v[156:159], v[196:199], v[100:103]
	v_mfma_f32_16x16x32_bf16 v[92:95], v[148:151], v[204:207], v[92:95]
	v_mfma_f32_16x16x32_bf16 v[84:87], v[156:159], v[204:207], v[84:87]
	v_mfma_f32_16x16x32_bf16 v[76:79], v[148:151], v[212:215], v[76:79]
	v_mfma_f32_16x16x32_bf16 v[68:71], v[156:159], v[212:215], v[68:71]
	v_mfma_f32_16x16x32_bf16 v[124:127], v[152:155], v[192:195], v[124:127]
	v_mfma_f32_16x16x32_bf16 v[116:119], v[160:163], v[192:195], v[116:119]
	v_mfma_f32_16x16x32_bf16 v[108:111], v[152:155], v[200:203], v[108:111]
	v_mfma_f32_16x16x32_bf16 v[100:103], v[160:163], v[200:203], v[100:103]
	v_mfma_f32_16x16x32_bf16 v[92:95], v[152:155], v[208:211], v[92:95]
	v_mfma_f32_16x16x32_bf16 v[84:87], v[160:163], v[208:211], v[84:87]
	v_mfma_f32_16x16x32_bf16 v[76:79], v[152:155], v[216:219], v[76:79]
	v_mfma_f32_16x16x32_bf16 v[68:71], v[160:163], v[216:219], v[68:71]
	s_setprio 0
	s_setprio 1
	v_mfma_f32_16x16x32_bf16 v[120:123], v[172:175], v[188:191], v[120:123]
	v_mfma_f32_16x16x32_bf16 v[112:115], v[180:183], v[188:191], v[112:115]
	v_mfma_f32_16x16x32_bf16 v[104:107], v[172:175], v[196:199], v[104:107]
	v_mfma_f32_16x16x32_bf16 v[96:99], v[180:183], v[196:199], v[96:99]
	v_mfma_f32_16x16x32_bf16 v[88:91], v[172:175], v[204:207], v[88:91]
	v_mfma_f32_16x16x32_bf16 v[80:83], v[180:183], v[204:207], v[80:83]
	v_mfma_f32_16x16x32_bf16 v[72:75], v[172:175], v[212:215], v[72:75]
	v_mfma_f32_16x16x32_bf16 v[64:67], v[180:183], v[212:215], v[64:67]
	v_mfma_f32_16x16x32_bf16 v[120:123], v[176:179], v[192:195], v[120:123]
	v_mfma_f32_16x16x32_bf16 v[112:115], v[184:187], v[192:195], v[112:115]
	v_mfma_f32_16x16x32_bf16 v[104:107], v[176:179], v[200:203], v[104:107]
	v_mfma_f32_16x16x32_bf16 v[96:99], v[184:187], v[200:203], v[96:99]
	v_mfma_f32_16x16x32_bf16 v[88:91], v[176:179], v[208:211], v[88:91]
	v_mfma_f32_16x16x32_bf16 v[80:83], v[184:187], v[208:211], v[80:83]
	v_mfma_f32_16x16x32_bf16 v[72:75], v[176:179], v[216:219], v[72:75]
	v_mfma_f32_16x16x32_bf16 v[64:67], v[184:187], v[216:219], v[64:67]
	s_setprio 0
	s_barrier
; #define PG8_STAGE(bufoff, gbase, voff) do { _Pragma("unroll") for (int _i = 0; _i < 2; ++_i) \
;         __builtin_amdgcn_global_load_lds((const unsigned*)((const char*)(gbase) + (voff)[_i]), (PG8_LAS unsigned*)(lds + (bufoff) + ldsw + _i * 8192), 16, 0, 0); } while (0)
; #define PG8_LDA(dst, b, h) do { _Pragma("unroll") for (int m = 0; m < 4; ++m) _Pragma("unroll") for (int k = 0; k < 2; ++k) dst[m][k] = *(const PG8_LAS bf16x8*)(lds + PG8_SA(b, h) + aoff + m * 2048 + k * 1024); } while (0)
; #define PG8_LDB(dst, b, h) do { _Pragma("unroll") for (int n = 0; n < 2; ++n) _Pragma("unroll") for (int k = 0; k < 2; ++k) dst[n][k] = *(const PG8_LAS bf16x8*)(lds + PG8_SB(b, h) + boff + n * 2048 + k * 1024); } while (0)
; #define PG8_MMA(ai, bj, At, Bt) do { __builtin_amdgcn_s_setprio(1); _Pragma("unroll") for (int m = 0; m < 4; ++m) _Pragma("unroll") for (int n = 0; n < 2; ++n) _Pragma("unroll") for (int k = 0; k < 2; ++k) \
;         acc[ai][bj][m][n] = __builtin_amdgcn_mfma_f32_16x16x32_bf16(Bt[n][k], At[m][k], acc[ai][bj][m][n], 0, 0, 0); __builtin_amdgcn_s_setprio(0); } while (0)
; #define PG8_WAIT_V(n) asm volatile("s_waitcnt vmcnt(" #n ")" ::: "memory")
; #define PG8_WAIT_L(n) asm volatile("s_waitcnt lgkmcnt(" #n ")" ::: "memory")
; #define PG8_BAR __builtin_amdgcn_s_barrier()
; #define PG8_SCHED __builtin_amdgcn_sched_barrier(0)
; template <class Epi, class Sched, bool ALIGN_EPI = false, bool SP2 = false>
; __device__ __forceinline__ void gemm_phase(PG8_LAS unsigned char* lds, const Gemm g, const Sched& S, const Epi& E, const int wid) {
;     ...
;             if constexpr (SP2) {
;             PG8_LDB(B0, 0, 0); PG8_LDB(B1, 0, 1); PG8_SCHED; PG8_LDA(At, 0, 0); PG8_STAGE(PG8_SA(1, 1), a1 + hstepA, voffA);
;             PG8_WAIT_V(8); PG8_WAIT_L(0); PG8_BAR; PG8_MMA(0, 0, At, B0); PG8_MMA(0, 1, At, B1); PG8_BAR; PG8_SCHED;
;     ...
;             PG8_LDA(At, 1, 1); PG8_STAGE(PG8_SB(1, 0), b3, voffB); PG8_STAGE(PG8_SB(1, 1), b3 + hstepB, voffB); PG8_STAGE(PG8_SA(1, 0), a3, voffA);
;             PG8_WAIT_V(8); PG8_WAIT_L(0); PG8_BAR; PG8_MMA(1, 0, At, B0); PG8_MMA(1, 1, At, B1); PG8_BAR; PG8_SCHED;
	s_add_i32 s28, s58, s33
	s_mov_b32 m0, s28
	ds_read_b128 v[188:191], v168 offset:49152
	ds_read_b128 v[192:195], v168 offset:50176
	ds_read_b128 v[196:199], v168 offset:51200
	ds_read_b128 v[200:203], v168 offset:52224
	ds_read_b128 v[204:207], v168 offset:53248
	ds_read_b128 v[208:211], v168 offset:54272
	ds_read_b128 v[212:215], v168 offset:55296
	ds_read_b128 v[216:219], v168 offset:56320
	global_load_lds_dwordx4 v132, s[98:99]
	s_add_i32 m0, s28, 0x2000
	s_add_u32 s26, s26, 0x40080
	s_addc_u32 s27, s27, 0
	s_add_i32 s28, s59, s33
	global_load_lds_dwordx4 v128, s[98:99]
	s_mov_b32 m0, s28
	s_nop 0
	global_load_lds_dwordx4 v132, s[26:27]
	s_add_i32 m0, s28, 0x2000
	s_nop 0
	global_load_lds_dwordx4 v128, s[26:27]
	s_mov_b32 m0, s40
	s_nop 0
	global_load_lds_dwordx4 v134, s[100:101]
	s_mov_b32 m0, s41
	s_nop 0
	global_load_lds_dwordx4 v130, s[100:101]
	s_waitcnt vmcnt(8) lgkmcnt(0)
	s_barrier
	s_setprio 1
	v_mfma_f32_16x16x32_bf16 v[60:63], v[148:151], v[188:191], v[60:63]
	v_mfma_f32_16x16x32_bf16 v[52:55], v[156:159], v[188:191], v[52:55]
	v_mfma_f32_16x16x32_bf16 v[44:47], v[148:151], v[196:199], v[44:47]
	v_mfma_f32_16x16x32_bf16 v[36:39], v[156:159], v[196:199], v[36:39]
	v_mfma_f32_16x16x32_bf16 v[28:31], v[148:151], v[204:207], v[28:31]
	v_mfma_f32_16x16x32_bf16 v[20:23], v[156:159], v[204:207], v[20:23]
	v_mfma_f32_16x16x32_bf16 v[12:15], v[148:151], v[212:215], v[12:15]
	v_mfma_f32_16x16x32_bf16 v[4:7], v[156:159], v[212:215], v[4:7]
	v_mfma_f32_16x16x32_bf16 v[60:63], v[152:155], v[192:195], v[60:63]
	v_mfma_f32_16x16x32_bf16 v[52:55], v[160:163], v[192:195], v[52:55]
	v_mfma_f32_16x16x32_bf16 v[44:47], v[152:155], v[200:203], v[44:47]
	v_mfma_f32_16x16x32_bf16 v[36:39], v[160:163], v[200:203], v[36:39]
	v_mfma_f32_16x16x32_bf16 v[28:31], v[152:155], v[208:211], v[28:31]
	v_mfma_f32_16x16x32_bf16 v[20:23], v[160:163], v[208:211], v[20:23]
	v_mfma_f32_16x16x32_bf16 v[12:15], v[152:155], v[216:219], v[12:15]
	v_mfma_f32_16x16x32_bf16 v[4:7], v[160:163], v[216:219], v[4:7]
	s_setprio 0
	s_setprio 1
	v_mfma_f32_16x16x32_bf16 v[56:59], v[172:175], v[188:191], v[56:59]
	v_mfma_f32_16x16x32_bf16 v[48:51], v[180:183], v[188:191], v[48:51]
	v_mfma_f32_16x16x32_bf16 v[40:43], v[172:175], v[196:199], v[40:43]
	v_mfma_f32_16x16x32_bf16 v[32:35], v[180:183], v[196:199], v[32:35]
	v_mfma_f32_16x16x32_bf16 v[24:27], v[172:175], v[204:207], v[24:27]
	v_mfma_f32_16x16x32_bf16 v[16:19], v[180:183], v[204:207], v[16:19]
	v_mfma_f32_16x16x32_bf16 v[8:11], v[172:175], v[212:215], v[8:11]
	v_mfma_f32_16x16x32_bf16 v[0:3], v[180:183], v[212:215], v[0:3]
	v_mfma_f32_16x16x32_bf16 v[56:59], v[176:179], v[192:195], v[56:59]
	v_mfma_f32_16x16x32_bf16 v[48:51], v[184:187], v[192:195], v[48:51]
	v_mfma_f32_16x16x32_bf16 v[40:43], v[176:179], v[200:203], v[40:43]
	v_mfma_f32_16x16x32_bf16 v[32:35], v[184:187], v[200:203], v[32:35]
	v_mfma_f32_16x16x32_bf16 v[24:27], v[176:179], v[208:211], v[24:27]
	v_mfma_f32_16x16x32_bf16 v[16:19], v[184:187], v[208:211], v[16:19]
	v_mfma_f32_16x16x32_bf16 v[8:11], v[176:179], v[216:219], v[8:11]
	v_mfma_f32_16x16x32_bf16 v[0:3], v[184:187], v[216:219], v[0:3]
	s_setprio 0
	s_barrier
	s_add_i32 s57, s57, 2
	s_add_u32 s24, s24, 0x100
	s_addc_u32 s25, s25, 0
	s_add_u32 s49, s49, 0x100
	s_addc_u32 s56, s56, 0
	s_cmp_gt_u32 s57, 13
.LBB0_2812:
	ds_read_b128 v[148:151], v166
	ds_read_b128 v[152:155], v166 offset:1024
	ds_read_b128 v[156:159], v166 offset:2048
	ds_read_b128 v[160:163], v166 offset:3072
	ds_read_b128 v[172:175], v167
	ds_read_b128 v[176:179], v167 offset:1024
	ds_read_b128 v[180:183], v167 offset:2048
	ds_read_b128 v[184:187], v167 offset:3072
	s_add_u32 s26, s24, 0xfffc0080
	s_addc_u32 s27, s25, -1
	s_cmp_eq_u32 s57, 12
	s_cselect_b32 s29, s17, s27
	s_cselect_b32 s28, s47, s26
	s_cselect_b32 s27, s15, s56
	s_cselect_b32 s26, s48, s49
	s_add_i32 m0, s36, 0xc000
	ds_read_b128 v[188:191], v168
	ds_read_b128 v[192:195], v168 offset:1024
	ds_read_b128 v[196:199], v168 offset:2048
	ds_read_b128 v[200:203], v168 offset:3072
	ds_read_b128 v[204:207], v168 offset:4096
	ds_read_b128 v[208:211], v168 offset:5120
	ds_read_b128 v[212:215], v168 offset:6144
	ds_read_b128 v[216:219], v168 offset:7168
	global_load_lds_dwordx4 v140, s[24:25]
	s_add_i32 m0, s36, 0xe000
	s_nop 0
	global_load_lds_dwordx4 v142, s[24:25]
	s_waitcnt vmcnt(8) lgkmcnt(0)
	s_barrier
	s_setprio 1
	v_mfma_f32_16x16x32_bf16 v[124:127], v[148:151], v[188:191], v[124:127]
	v_mfma_f32_16x16x32_bf16 v[116:119], v[156:159], v[188:191], v[116:119]
	v_mfma_f32_16x16x32_bf16 v[108:111], v[148:151], v[196:199], v[108:111]
	v_mfma_f32_16x16x32_bf16 v[100:103], v[156:159], v[196:199], v[100:103]
	v_mfma_f32_16x16x32_bf16 v[92:95], v[148:151], v[204:207], v[92:95]
	v_mfma_f32_16x16x32_bf16 v[84:87], v[156:159], v[204:207], v[84:87]
	v_mfma_f32_16x16x32_bf16 v[76:79], v[148:151], v[212:215], v[76:79]
	v_mfma_f32_16x16x32_bf16 v[68:71], v[156:159], v[212:215], v[68:71]
	v_mfma_f32_16x16x32_bf16 v[124:127], v[152:155], v[192:195], v[124:127]
	v_mfma_f32_16x16x32_bf16 v[116:119], v[160:163], v[192:195], v[116:119]
	v_mfma_f32_16x16x32_bf16 v[108:111], v[152:155], v[200:203], v[108:111]
	v_mfma_f32_16x16x32_bf16 v[100:103], v[160:163], v[200:203], v[100:103]
	v_mfma_f32_16x16x32_bf16 v[92:95], v[152:155], v[208:211], v[92:95]
	v_mfma_f32_16x16x32_bf16 v[84:87], v[160:163], v[208:211], v[84:87]
	v_mfma_f32_16x16x32_bf16 v[76:79], v[152:155], v[216:219], v[76:79]
	v_mfma_f32_16x16x32_bf16 v[68:71], v[160:163], v[216:219], v[68:71]
	s_setprio 0
	s_setprio 1
	v_mfma_f32_16x16x32_bf16 v[120:123], v[172:175], v[188:191], v[120:123]
	v_mfma_f32_16x16x32_bf16 v[112:115], v[180:183], v[188:191], v[112:115]
	v_mfma_f32_16x16x32_bf16 v[104:107], v[172:175], v[196:199], v[104:107]
	v_mfma_f32_16x16x32_bf16 v[96:99], v[180:183], v[196:199], v[96:99]
	v_mfma_f32_16x16x32_bf16 v[88:91], v[172:175], v[204:207], v[88:91]
	v_mfma_f32_16x16x32_bf16 v[80:83], v[180:183], v[204:207], v[80:83]
	v_mfma_f32_16x16x32_bf16 v[72:75], v[172:175], v[212:215], v[72:75]
	v_mfma_f32_16x16x32_bf16 v[64:67], v[180:183], v[212:215], v[64:67]
	v_mfma_f32_16x16x32_bf16 v[120:123], v[176:179], v[192:195], v[120:123]
	v_mfma_f32_16x16x32_bf16 v[112:115], v[184:187], v[192:195], v[112:115]
	v_mfma_f32_16x16x32_bf16 v[104:107], v[176:179], v[200:203], v[104:107]
	v_mfma_f32_16x16x32_bf16 v[96:99], v[184:187], v[200:203], v[96:99]
	v_mfma_f32_16x16x32_bf16 v[88:91], v[176:179], v[208:211], v[88:91]
	v_mfma_f32_16x16x32_bf16 v[80:83], v[184:187], v[208:211], v[80:83]
	v_mfma_f32_16x16x32_bf16 v[72:75], v[176:179], v[216:219], v[72:75]
	v_mfma_f32_16x16x32_bf16 v[64:67], v[184:187], v[216:219], v[64:67]
	s_setprio 0
	s_barrier
; #define PG8_STAGE(bufoff, gbase, voff) do { _Pragma("unroll") for (int _i = 0; _i < 2; ++_i) \
;         __builtin_amdgcn_global_load_lds((const unsigned*)((const char*)(gbase) + (voff)[_i]), (PG8_LAS unsigned*)(lds + (bufoff) + ldsw + _i * 8192), 16, 0, 0); } while (0)
; #define PG8_LDA(dst, b, h) do { _Pragma("unroll") for (int m = 0; m < 4; ++m) _Pragma("unroll") for (int k = 0; k < 2; ++k) dst[m][k] = *(const PG8_LAS bf16x8*)(lds + PG8_SA(b, h) + aoff + m * 2048 + k * 1024); } while (0)
; #define PG8_LDB(dst, b, h) do { _Pragma("unroll") for (int n = 0; n < 2; ++n) _Pragma("unroll") for (int k = 0; k < 2; ++k) dst[n][k] = *(const PG8_LAS bf16x8*)(lds + PG8_SB(b, h) + boff + n * 2048 + k * 1024); } while (0)
; #define PG8_MMA(ai, bj, At, Bt) do { __builtin_amdgcn_s_setprio(1); _Pragma("unroll") for (int m = 0; m < 4; ++m) _Pragma("unroll") for (int n = 0; n < 2; ++n) _Pragma("unroll") for (int k = 0; k < 2; ++k) \
;         acc[ai][bj][m][n] = __builtin_amdgcn_mfma_f32_16x16x32_bf16(Bt[n][k], At[m][k], acc[ai][bj][m][n], 0, 0, 0); __builtin_amdgcn_s_setprio(0); } while (0)
; #define PG8_WAIT_V(n) asm volatile("s_waitcnt vmcnt(" #n ")" ::: "memory")
; #define PG8_WAIT_L(n) asm volatile("s_waitcnt lgkmcnt(" #n ")" ::: "memory")
; #define PG8_BAR __builtin_amdgcn_s_barrier()
; #define PG8_SCHED __builtin_amdgcn_sched_barrier(0)
; template <class Epi, class Sched, bool ALIGN_EPI = false, bool SP2 = false>
; __device__ __forceinline__ void gemm_phase(PG8_LAS unsigned char* lds, const Gemm g, const Sched& S, const Epi& E, const int wid) {
;     ...
;             PG8_LDA(At, 0, 1); PG8_STAGE(PG8_SB(0, 0), b2, voffB); PG8_STAGE(PG8_SB(0, 1), b2 + hstepB, voffB); PG8_STAGE(PG8_SA(0, 0), a2, voffA);
;             PG8_WAIT_V(8); PG8_WAIT_L(0); PG8_BAR; PG8_MMA(1, 0, At, B0); PG8_MMA(1, 1, At, B1); PG8_BAR; PG8_SCHED;
;             PG8_LDB(B0, 1, 0); PG8_LDB(B1, 1, 1); PG8_SCHED; PG8_LDA(At, 1, 0); PG8_STAGE(PG8_SA(0, 1), a2 + hstepA, voffA);
	s_add_i32 s58, s43, s33
	s_add_u32 s98, s26, 0x80
	s_addc_u32 s99, s27, 0
	s_mov_b32 m0, s58
	ds_read_b128 v[188:191], v168 offset:16384
	ds_read_b128 v[192:195], v168 offset:17408
	ds_read_b128 v[196:199], v168 offset:18432
	ds_read_b128 v[200:203], v168 offset:19456
	ds_read_b128 v[204:207], v168 offset:20480
	ds_read_b128 v[208:211], v168 offset:21504
	ds_read_b128 v[212:215], v168 offset:22528
	ds_read_b128 v[216:219], v168 offset:23552
	global_load_lds_dwordx4 v132, s[26:27]
	s_add_i32 m0, s58, 0x2000
	s_add_u32 s58, s26, 0x40000
	s_addc_u32 s59, s27, 0
	s_add_i32 s60, s44, s33
	global_load_lds_dwordx4 v128, s[26:27]
	s_mov_b32 m0, s60
	s_add_u32 s100, s28, 0x80
	s_addc_u32 s101, s29, 0
	global_load_lds_dwordx4 v132, s[58:59]
	s_add_i32 m0, s60, 0x2000
	s_nop 0
	global_load_lds_dwordx4 v128, s[58:59]
	s_mov_b32 m0, s36
	s_nop 0
	global_load_lds_dwordx4 v134, s[28:29]
	s_mov_b32 m0, s37
	s_nop 0
	global_load_lds_dwordx4 v130, s[28:29]
	s_waitcnt vmcnt(8) lgkmcnt(0)
	s_barrier
	s_nop 0
	s_setprio 1
	v_mfma_f32_16x16x32_bf16 v[60:63], v[148:151], v[188:191], v[60:63]
	v_mfma_f32_16x16x32_bf16 v[52:55], v[156:159], v[188:191], v[52:55]
	v_mfma_f32_16x16x32_bf16 v[44:47], v[148:151], v[196:199], v[44:47]
	v_mfma_f32_16x16x32_bf16 v[36:39], v[156:159], v[196:199], v[36:39]
	v_mfma_f32_16x16x32_bf16 v[28:31], v[148:151], v[204:207], v[28:31]
	v_mfma_f32_16x16x32_bf16 v[20:23], v[156:159], v[204:207], v[20:23]
	v_mfma_f32_16x16x32_bf16 v[12:15], v[148:151], v[212:215], v[12:15]
	v_mfma_f32_16x16x32_bf16 v[4:7], v[156:159], v[212:215], v[4:7]
	v_mfma_f32_16x16x32_bf16 v[60:63], v[152:155], v[192:195], v[60:63]
	v_mfma_f32_16x16x32_bf16 v[52:55], v[160:163], v[192:195], v[52:55]
	v_mfma_f32_16x16x32_bf16 v[44:47], v[152:155], v[200:203], v[44:47]
	v_mfma_f32_16x16x32_bf16 v[36:39], v[160:163], v[200:203], v[36:39]
	v_mfma_f32_16x16x32_bf16 v[28:31], v[152:155], v[208:211], v[28:31]
	v_mfma_f32_16x16x32_bf16 v[20:23], v[160:163], v[208:211], v[20:23]
	v_mfma_f32_16x16x32_bf16 v[12:15], v[152:155], v[216:219], v[12:15]
	v_mfma_f32_16x16x32_bf16 v[4:7], v[160:163], v[216:219], v[4:7]
	s_setprio 0
	s_setprio 1
	v_mfma_f32_16x16x32_bf16 v[56:59], v[172:175], v[188:191], v[56:59]
	v_mfma_f32_16x16x32_bf16 v[48:51], v[180:183], v[188:191], v[48:51]
	v_mfma_f32_16x16x32_bf16 v[40:43], v[172:175], v[196:199], v[40:43]
	v_mfma_f32_16x16x32_bf16 v[32:35], v[180:183], v[196:199], v[32:35]
	v_mfma_f32_16x16x32_bf16 v[24:27], v[172:175], v[204:207], v[24:27]
	v_mfma_f32_16x16x32_bf16 v[16:19], v[180:183], v[204:207], v[16:19]
	v_mfma_f32_16x16x32_bf16 v[8:11], v[172:175], v[212:215], v[8:11]
	v_mfma_f32_16x16x32_bf16 v[0:3], v[180:183], v[212:215], v[0:3]
	v_mfma_f32_16x16x32_bf16 v[56:59], v[176:179], v[192:195], v[56:59]
	v_mfma_f32_16x16x32_bf16 v[48:51], v[184:187], v[192:195], v[48:51]
	v_mfma_f32_16x16x32_bf16 v[40:43], v[176:179], v[200:203], v[40:43]
	v_mfma_f32_16x16x32_bf16 v[32:35], v[184:187], v[200:203], v[32:35]
	v_mfma_f32_16x16x32_bf16 v[24:27], v[176:179], v[208:211], v[24:27]
	v_mfma_f32_16x16x32_bf16 v[16:19], v[184:187], v[208:211], v[16:19]
	v_mfma_f32_16x16x32_bf16 v[8:11], v[176:179], v[216:219], v[8:11]
	v_mfma_f32_16x16x32_bf16 v[0:3], v[184:187], v[216:219], v[0:3]
	s_setprio 0
	s_barrier
	s_add_i32 s58, 0, 0x18000
	s_add_i32 s59, 0, 0x1c000
	ds_read_b128 v[148:151], v252
	ds_read_b128 v[152:155], v252 offset:1024
	ds_read_b128 v[156:159], v252 offset:2048
	ds_read_b128 v[160:163], v252 offset:3072
	ds_read_b128 v[172:175], v253
	ds_read_b128 v[176:179], v253 offset:1024
	ds_read_b128 v[180:183], v253 offset:2048
	ds_read_b128 v[184:187], v253 offset:3072
	s_add_u32 s28, s28, 0x40000
	s_addc_u32 s29, s29, 0
	s_mov_b32 m0, s38
	ds_read_b128 v[188:191], v168 offset:32768
	ds_read_b128 v[192:195], v168 offset:33792
	ds_read_b128 v[196:199], v168 offset:34816
	ds_read_b128 v[200:203], v168 offset:35840
	ds_read_b128 v[204:207], v168 offset:36864
	ds_read_b128 v[208:211], v168 offset:37888
	ds_read_b128 v[212:215], v168 offset:38912
	ds_read_b128 v[216:219], v168 offset:39936
	global_load_lds_dwordx4 v134, s[28:29]
	s_mov_b32 m0, s39
	s_nop 0
	global_load_lds_dwordx4 v130, s[28:29]
	s_waitcnt vmcnt(8) lgkmcnt(0)
	s_barrier
; #define PG8_STAGE(bufoff, gbase, voff) do { _Pragma("unroll") for (int _i = 0; _i < 2; ++_i) \
;         __builtin_amdgcn_global_load_lds((const unsigned*)((const char*)(gbase) + (voff)[_i]), (PG8_LAS unsigned*)(lds + (bufoff) + ldsw + _i * 8192), 16, 0, 0); } while (0)
; #define PG8_LDA(dst, b, h) do { _Pragma("unroll") for (int m = 0; m < 4; ++m) _Pragma("unroll") for (int k = 0; k < 2; ++k) dst[m][k] = *(const PG8_LAS bf16x8*)(lds + PG8_SA(b, h) + aoff + m * 2048 + k * 1024); } while (0)
; #define PG8_MMA(ai, bj, At, Bt) do { __builtin_amdgcn_s_setprio(1); _Pragma("unroll") for (int m = 0; m < 4; ++m) _Pragma("unroll") for (int n = 0; n < 2; ++n) _Pragma("unroll") for (int k = 0; k < 2; ++k) \
;         acc[ai][bj][m][n] = __builtin_amdgcn_mfma_f32_16x16x32_bf16(Bt[n][k], At[m][k], acc[ai][bj][m][n], 0, 0, 0); __builtin_amdgcn_s_setprio(0); } while (0)
; #define PG8_WAIT_V(n) asm volatile("s_waitcnt vmcnt(" #n ")" ::: "memory")
; #define PG8_WAIT_L(n) asm volatile("s_waitcnt lgkmcnt(" #n ")" ::: "memory")
; #define PG8_BAR __builtin_amdgcn_s_barrier()
; #define PG8_SCHED __builtin_amdgcn_sched_barrier(0)
; template <class Epi, class Sched, bool ALIGN_EPI = false, bool SP2 = false>
; __device__ __forceinline__ void gemm_phase(PG8_LAS unsigned char* lds, const Gemm g, const Sched& S, const Epi& E, const int wid) {
;     ...
;             PG8_WAIT_V(8); PG8_WAIT_L(0); PG8_BAR; PG8_MMA(0, 0, At, B0); PG8_MMA(0, 1, At, B1); PG8_BAR; PG8_SCHED;
;             PG8_LDA(At, 1, 1); PG8_STAGE(PG8_SB(1, 0), b3, voffB); PG8_STAGE(PG8_SB(1, 1), b3 + hstepB, voffB); PG8_STAGE(PG8_SA(1, 0), a3, voffA);
;             PG8_WAIT_V(8); PG8_WAIT_L(0); PG8_BAR; PG8_MMA(1, 0, At, B0); PG8_MMA(1, 1, At, B1); PG8_BAR; PG8_SCHED;
;     ...
;         if constexpr (ALIGN_EPI) { if (wr == 0) PG8_BAR; }
	s_nop 0
	s_setprio 1
	v_mfma_f32_16x16x32_bf16 v[124:127], v[148:151], v[188:191], v[124:127]
	v_mfma_f32_16x16x32_bf16 v[116:119], v[156:159], v[188:191], v[116:119]
	v_mfma_f32_16x16x32_bf16 v[108:111], v[148:151], v[196:199], v[108:111]
	v_mfma_f32_16x16x32_bf16 v[100:103], v[156:159], v[196:199], v[100:103]
	v_mfma_f32_16x16x32_bf16 v[92:95], v[148:151], v[204:207], v[92:95]
	v_mfma_f32_16x16x32_bf16 v[84:87], v[156:159], v[204:207], v[84:87]
	v_mfma_f32_16x16x32_bf16 v[76:79], v[148:151], v[212:215], v[76:79]
	v_mfma_f32_16x16x32_bf16 v[68:71], v[156:159], v[212:215], v[68:71]
	v_mfma_f32_16x16x32_bf16 v[124:127], v[152:155], v[192:195], v[124:127]
	v_mfma_f32_16x16x32_bf16 v[116:119], v[160:163], v[192:195], v[116:119]
	v_mfma_f32_16x16x32_bf16 v[108:111], v[152:155], v[200:203], v[108:111]
	v_mfma_f32_16x16x32_bf16 v[100:103], v[160:163], v[200:203], v[100:103]
	v_mfma_f32_16x16x32_bf16 v[92:95], v[152:155], v[208:211], v[92:95]
	v_mfma_f32_16x16x32_bf16 v[84:87], v[160:163], v[208:211], v[84:87]
	v_mfma_f32_16x16x32_bf16 v[76:79], v[152:155], v[216:219], v[76:79]
	v_mfma_f32_16x16x32_bf16 v[68:71], v[160:163], v[216:219], v[68:71]
	s_setprio 0
	s_setprio 1
	v_mfma_f32_16x16x32_bf16 v[120:123], v[172:175], v[188:191], v[120:123]
	v_mfma_f32_16x16x32_bf16 v[112:115], v[180:183], v[188:191], v[112:115]
	v_mfma_f32_16x16x32_bf16 v[104:107], v[172:175], v[196:199], v[104:107]
	v_mfma_f32_16x16x32_bf16 v[96:99], v[180:183], v[196:199], v[96:99]
	v_mfma_f32_16x16x32_bf16 v[88:91], v[172:175], v[204:207], v[88:91]
	v_mfma_f32_16x16x32_bf16 v[80:83], v[180:183], v[204:207], v[80:83]
	v_mfma_f32_16x16x32_bf16 v[72:75], v[172:175], v[212:215], v[72:75]
	v_mfma_f32_16x16x32_bf16 v[64:67], v[180:183], v[212:215], v[64:67]
	v_mfma_f32_16x16x32_bf16 v[120:123], v[176:179], v[192:195], v[120:123]
	v_mfma_f32_16x16x32_bf16 v[112:115], v[184:187], v[192:195], v[112:115]
	v_mfma_f32_16x16x32_bf16 v[104:107], v[176:179], v[200:203], v[104:107]
	v_mfma_f32_16x16x32_bf16 v[96:99], v[184:187], v[200:203], v[96:99]
	v_mfma_f32_16x16x32_bf16 v[88:91], v[176:179], v[208:211], v[88:91]
	v_mfma_f32_16x16x32_bf16 v[80:83], v[184:187], v[208:211], v[80:83]
	v_mfma_f32_16x16x32_bf16 v[72:75], v[176:179], v[216:219], v[72:75]
	v_mfma_f32_16x16x32_bf16 v[64:67], v[184:187], v[216:219], v[64:67]
	s_setprio 0
	s_barrier
	s_add_i32 s28, s58, s33
	s_mov_b32 m0, s28
	ds_read_b128 v[188:191], v168 offset:49152
	ds_read_b128 v[192:195], v168 offset:50176
	ds_read_b128 v[196:199], v168 offset:51200
	ds_read_b128 v[200:203], v168 offset:52224
	ds_read_b128 v[204:207], v168 offset:53248
	ds_read_b128 v[208:211], v168 offset:54272
	ds_read_b128 v[212:215], v168 offset:55296
	ds_read_b128 v[216:219], v168 offset:56320
	global_load_lds_dwordx4 v132, s[98:99]
	s_add_i32 m0, s28, 0x2000
	s_add_u32 s26, s26, 0x40080
	s_addc_u32 s27, s27, 0
	s_add_i32 s28, s59, s33
	global_load_lds_dwordx4 v128, s[98:99]
	s_mov_b32 m0, s28
	s_nop 0
	global_load_lds_dwordx4 v132, s[26:27]
	s_add_i32 m0, s28, 0x2000
	s_nop 0
	global_load_lds_dwordx4 v128, s[26:27]
	s_mov_b32 m0, s40
	s_nop 0
	global_load_lds_dwordx4 v134, s[100:101]
	s_mov_b32 m0, s41
	s_nop 0
	global_load_lds_dwordx4 v130, s[100:101]
	s_waitcnt vmcnt(8) lgkmcnt(0)
	s_barrier
	s_setprio 1
	v_mfma_f32_16x16x32_bf16 v[60:63], v[148:151], v[188:191], v[60:63]
	v_mfma_f32_16x16x32_bf16 v[52:55], v[156:159], v[188:191], v[52:55]
	v_mfma_f32_16x16x32_bf16 v[44:47], v[148:151], v[196:199], v[44:47]
	v_mfma_f32_16x16x32_bf16 v[36:39], v[156:159], v[196:199], v[36:39]
	v_mfma_f32_16x16x32_bf16 v[28:31], v[148:151], v[204:207], v[28:31]
	v_mfma_f32_16x16x32_bf16 v[20:23], v[156:159], v[204:207], v[20:23]
	v_mfma_f32_16x16x32_bf16 v[12:15], v[148:151], v[212:215], v[12:15]
	v_mfma_f32_16x16x32_bf16 v[4:7], v[156:159], v[212:215], v[4:7]
	v_mfma_f32_16x16x32_bf16 v[60:63], v[152:155], v[192:195], v[60:63]
	v_mfma_f32_16x16x32_bf16 v[52:55], v[160:163], v[192:195], v[52:55]
	v_mfma_f32_16x16x32_bf16 v[44:47], v[152:155], v[200:203], v[44:47]
	v_mfma_f32_16x16x32_bf16 v[36:39], v[160:163], v[200:203], v[36:39]
	v_mfma_f32_16x16x32_bf16 v[28:31], v[152:155], v[208:211], v[28:31]
	v_mfma_f32_16x16x32_bf16 v[20:23], v[160:163], v[208:211], v[20:23]
	v_mfma_f32_16x16x32_bf16 v[12:15], v[152:155], v[216:219], v[12:15]
	v_mfma_f32_16x16x32_bf16 v[4:7], v[160:163], v[216:219], v[4:7]
	s_setprio 0
	s_setprio 1
	v_mfma_f32_16x16x32_bf16 v[56:59], v[172:175], v[188:191], v[56:59]
	v_mfma_f32_16x16x32_bf16 v[48:51], v[180:183], v[188:191], v[48:51]
	v_mfma_f32_16x16x32_bf16 v[40:43], v[172:175], v[196:199], v[40:43]
	v_mfma_f32_16x16x32_bf16 v[32:35], v[180:183], v[196:199], v[32:35]
	v_mfma_f32_16x16x32_bf16 v[24:27], v[172:175], v[204:207], v[24:27]
	v_mfma_f32_16x16x32_bf16 v[16:19], v[180:183], v[204:207], v[16:19]
	v_mfma_f32_16x16x32_bf16 v[8:11], v[172:175], v[212:215], v[8:11]
	v_mfma_f32_16x16x32_bf16 v[0:3], v[180:183], v[212:215], v[0:3]
	v_mfma_f32_16x16x32_bf16 v[56:59], v[176:179], v[192:195], v[56:59]
	v_mfma_f32_16x16x32_bf16 v[48:51], v[184:187], v[192:195], v[48:51]
	v_mfma_f32_16x16x32_bf16 v[40:43], v[176:179], v[200:203], v[40:43]
	v_mfma_f32_16x16x32_bf16 v[32:35], v[184:187], v[200:203], v[32:35]
	v_mfma_f32_16x16x32_bf16 v[24:27], v[176:179], v[208:211], v[24:27]
	v_mfma_f32_16x16x32_bf16 v[16:19], v[184:187], v[208:211], v[16:19]
	v_mfma_f32_16x16x32_bf16 v[8:11], v[176:179], v[216:219], v[8:11]
	v_mfma_f32_16x16x32_bf16 v[0:3], v[184:187], v[216:219], v[0:3]
	s_setprio 0
	s_barrier
	s_add_i32 s57, s57, 2
	s_add_u32 s24, s24, 0x100
	s_addc_u32 s25, s25, 0
	s_add_u32 s49, s49, 0x100
	s_addc_u32 s56, s56, 0
	s_cmp_gt_u32 s57, 13
	s_cbranch_scc0 .LBB0_2812
	s_and_b64 vcc, exec, s[12:13]
	s_cbranch_vccz .LBB0_2815
	s_barrier

; #define PG8_STAGE(bufoff, gbase, voff) do { _Pragma("unroll") for (int _i = 0; _i < 2; ++_i) \
;         __builtin_amdgcn_global_load_lds((const unsigned*)((const char*)(gbase) + (voff)[_i]), (PG8_LAS unsigned*)(lds + (bufoff) + ldsw + _i * 8192), 16, 0, 0); } while (0)
; #define PG8_LDA(dst, b, h) do { _Pragma("unroll") for (int m = 0; m < 4; ++m) _Pragma("unroll") for (int k = 0; k < 2; ++k) dst[m][k] = *(const PG8_LAS bf16x8*)(lds + PG8_SA(b, h) + aoff + m * 2048 + k * 1024); } while (0)
; #define PG8_LDB(dst, b, h) do { _Pragma("unroll") for (int n = 0; n < 2; ++n) _Pragma("unroll") for (int k = 0; k < 2; ++k) dst[n][k] = *(const PG8_LAS bf16x8*)(lds + PG8_SB(b, h) + boff + n * 2048 + k * 1024); } while (0)
; #define PG8_WAIT_V(n) asm volatile("s_waitcnt vmcnt(" #n ")" ::: "memory")
; #define PG8_WAIT_L(n) asm volatile("s_waitcnt lgkmcnt(" #n ")" ::: "memory")
; #define PG8_BAR __builtin_amdgcn_s_barrier()
; #define PG8_SCHED __builtin_amdgcn_sched_barrier(0)
; template <class Epi, class Sched, bool ALIGN_EPI = false, bool SP2 = false>
; __device__ __forceinline__ void gemm_phase(PG8_LAS unsigned char* lds, const Gemm g, const Sched& S, const Epi& E, const int wid) {
;     ...
;         const bool has_next = S.next(ui + 1, nxt);
;         const char* nA = has_next ? (const char*)g.A + (size_t)nxt.pm * tstepA : cA; const char* nB = has_next ? (const char*)g.Bt + (size_t)nxt.pn * tstepB : cB;
;         for (int t = 0; t < nt; t += 2) {
;             const bool last = (t == nt - 2);
;             const char* a1 = cA + (size_t)(t + 1) * kstep;
;             const char* a2 = last ? nA : cA + (size_t)(t + 2) * kstep; const char* b2 = last ? nB : cB + (size_t)(t + 2) * kstep;
;             const char* a3 = a2 + kstep; const char* b3 = b2 + kstep;
;             if (last && has_next) S.a_ready(nxt);
;             if constexpr (SP2) {
;             PG8_LDB(B0, 0, 0); PG8_LDB(B1, 0, 1); PG8_SCHED; PG8_LDA(At, 0, 0); PG8_STAGE(PG8_SA(1, 1), a1 + hstepA, voffA);
;             PG8_WAIT_V(8); PG8_WAIT_L(0); PG8_BAR; PG8_MMA(0, 0, At, B0); PG8_MMA(0, 1, At, B1); PG8_BAR; PG8_SCHED;
;             PG8_LDA(At, 0, 1); PG8_STAGE(PG8_SB(0, 0), b2, voffB); PG8_STAGE(PG8_SB(0, 1), b2 + hstepB, voffB); PG8_STAGE(PG8_SA(0, 0), a2, voffA);
;             PG8_WAIT_V(8); PG8_WAIT_L(0); PG8_BAR; PG8_MMA(1, 0, At, B0); PG8_MMA(1, 1, At, B1); PG8_BAR; PG8_SCHED;
.LBB0_2896:
	s_add_u32 s56, s24, 0x100
	s_addc_u32 s57, s25, 0
	s_mov_b32 s58, -2
	s_waitcnt lgkmcnt(0)
	v_add_u32_e32 v252, 0x18000, v189
	v_add_u32_e32 v253, 0x1c000, v189
	ds_read_b128 v[128:131], v190
	ds_read_b128 v[132:135], v190 offset:1024
	ds_read_b128 v[136:139], v190 offset:2048
	ds_read_b128 v[140:143], v190 offset:3072
	ds_read_b128 v[144:147], v191
	ds_read_b128 v[148:151], v191 offset:1024
	ds_read_b128 v[172:175], v191 offset:2048
	ds_read_b128 v[176:179], v191 offset:3072
	s_add_u32 s24, s22, 0x100
	s_addc_u32 s25, s23, 0
	s_cmp_eq_u32 s58, 40
	s_cselect_b32 s29, s7, s25
	s_cselect_b32 s28, s6, s24
	s_cselect_b32 s27, s21, s57
	s_cselect_b32 s26, s20, s56
	s_add_i32 m0, s34, 0xc000
	ds_read_b128 v[180:183], v192
	ds_read_b128 v[184:187], v192 offset:1024
	ds_read_b128 v[194:197], v192 offset:2048
	ds_read_b128 v[198:201], v192 offset:3072
	ds_read_b128 v[202:205], v192 offset:4096
	ds_read_b128 v[206:209], v192 offset:5120
	ds_read_b128 v[210:213], v192 offset:6144
	ds_read_b128 v[214:217], v192 offset:7168
	global_load_lds_dwordx4 v164, s[22:23]
	s_add_i32 m0, s34, 0xe000
	s_nop 0
	global_load_lds_dwordx4 v166, s[22:23]
	s_waitcnt vmcnt(8) lgkmcnt(0)
	s_barrier
	s_setprio 1
	v_mfma_f32_16x16x32_bf16 v[124:127], v[128:131], v[180:183], 0
	v_mfma_f32_16x16x32_bf16 v[120:123], v[136:139], v[180:183], 0
	v_mfma_f32_16x16x32_bf16 v[108:111], v[128:131], v[194:197], 0
	v_mfma_f32_16x16x32_bf16 v[104:107], v[136:139], v[194:197], 0
	v_mfma_f32_16x16x32_bf16 v[92:95], v[128:131], v[202:205], 0
	v_mfma_f32_16x16x32_bf16 v[88:91], v[136:139], v[202:205], 0
	v_mfma_f32_16x16x32_bf16 v[76:79], v[128:131], v[210:213], 0
	v_mfma_f32_16x16x32_bf16 v[72:75], v[136:139], v[210:213], 0
	v_mfma_f32_16x16x32_bf16 v[124:127], v[132:135], v[184:187], v[124:127]
	v_mfma_f32_16x16x32_bf16 v[120:123], v[140:143], v[184:187], v[120:123]
	v_mfma_f32_16x16x32_bf16 v[108:111], v[132:135], v[198:201], v[108:111]
	v_mfma_f32_16x16x32_bf16 v[104:107], v[140:143], v[198:201], v[104:107]
	v_mfma_f32_16x16x32_bf16 v[92:95], v[132:135], v[206:209], v[92:95]
	v_mfma_f32_16x16x32_bf16 v[88:91], v[140:143], v[206:209], v[88:91]
	v_mfma_f32_16x16x32_bf16 v[76:79], v[132:135], v[214:217], v[76:79]
	v_mfma_f32_16x16x32_bf16 v[72:75], v[140:143], v[214:217], v[72:75]
	s_setprio 0
	s_setprio 1
	v_mfma_f32_16x16x32_bf16 v[116:119], v[144:147], v[180:183], 0
	v_mfma_f32_16x16x32_bf16 v[112:115], v[172:175], v[180:183], 0
	v_mfma_f32_16x16x32_bf16 v[100:103], v[144:147], v[194:197], 0
	v_mfma_f32_16x16x32_bf16 v[96:99], v[172:175], v[194:197], 0
	v_mfma_f32_16x16x32_bf16 v[84:87], v[144:147], v[202:205], 0
	v_mfma_f32_16x16x32_bf16 v[80:83], v[172:175], v[202:205], 0
	v_mfma_f32_16x16x32_bf16 v[68:71], v[144:147], v[210:213], 0
	v_mfma_f32_16x16x32_bf16 v[64:67], v[172:175], v[210:213], 0
	v_mfma_f32_16x16x32_bf16 v[116:119], v[148:151], v[184:187], v[116:119]
	v_mfma_f32_16x16x32_bf16 v[112:115], v[176:179], v[184:187], v[112:115]
	v_mfma_f32_16x16x32_bf16 v[100:103], v[148:151], v[198:201], v[100:103]
	v_mfma_f32_16x16x32_bf16 v[96:99], v[176:179], v[198:201], v[96:99]
	v_mfma_f32_16x16x32_bf16 v[84:87], v[148:151], v[206:209], v[84:87]
	v_mfma_f32_16x16x32_bf16 v[80:83], v[176:179], v[206:209], v[80:83]
	v_mfma_f32_16x16x32_bf16 v[68:71], v[148:151], v[214:217], v[68:71]
	v_mfma_f32_16x16x32_bf16 v[64:67], v[176:179], v[214:217], v[64:67]
	s_setprio 0
	s_barrier
	s_add_i32 s22, s43, s33
	s_add_u32 s98, s26, 0x80
	s_addc_u32 s99, s27, 0
	s_mov_b32 m0, s22
	ds_read_b128 v[180:183], v192 offset:16384
	ds_read_b128 v[184:187], v192 offset:17408
	ds_read_b128 v[194:197], v192 offset:18432
	ds_read_b128 v[198:201], v192 offset:19456
	ds_read_b128 v[202:205], v192 offset:20480
	ds_read_b128 v[206:209], v192 offset:21504
	ds_read_b128 v[210:213], v192 offset:22528
	ds_read_b128 v[214:217], v192 offset:23552
	global_load_lds_dwordx4 v154, s[26:27]
	s_add_i32 m0, s22, 0x2000
	s_add_u32 s22, s26, 0xb0000
	s_addc_u32 s23, s27, 0
	s_add_i32 s59, s44, s33
	global_load_lds_dwordx4 v158, s[26:27]
	s_mov_b32 m0, s59
	s_add_u32 s100, s28, 0x80
	s_addc_u32 s101, s29, 0
	global_load_lds_dwordx4 v154, s[22:23]
	s_add_i32 m0, s59, 0x2000
	s_nop 0
	global_load_lds_dwordx4 v158, s[22:23]
	s_mov_b32 m0, s34
	s_nop 0
	global_load_lds_dwordx4 v152, s[28:29]
	s_mov_b32 m0, s35
	s_nop 0
	global_load_lds_dwordx4 v156, s[28:29]
	s_waitcnt vmcnt(8) lgkmcnt(0)
	s_barrier
	s_nop 0
	s_setprio 1
	v_mfma_f32_16x16x32_bf16 v[60:63], v[128:131], v[180:183], 0
	v_mfma_f32_16x16x32_bf16 v[56:59], v[136:139], v[180:183], 0
	v_mfma_f32_16x16x32_bf16 v[44:47], v[128:131], v[194:197], 0
	v_mfma_f32_16x16x32_bf16 v[40:43], v[136:139], v[194:197], 0
	v_mfma_f32_16x16x32_bf16 v[28:31], v[128:131], v[202:205], 0
	v_mfma_f32_16x16x32_bf16 v[24:27], v[136:139], v[202:205], 0
	v_mfma_f32_16x16x32_bf16 v[12:15], v[128:131], v[210:213], 0
	v_mfma_f32_16x16x32_bf16 v[8:11], v[136:139], v[210:213], 0
	v_mfma_f32_16x16x32_bf16 v[60:63], v[132:135], v[184:187], v[60:63]
	v_mfma_f32_16x16x32_bf16 v[56:59], v[140:143], v[184:187], v[56:59]
	v_mfma_f32_16x16x32_bf16 v[44:47], v[132:135], v[198:201], v[44:47]
	v_mfma_f32_16x16x32_bf16 v[40:43], v[140:143], v[198:201], v[40:43]
	v_mfma_f32_16x16x32_bf16 v[28:31], v[132:135], v[206:209], v[28:31]
	v_mfma_f32_16x16x32_bf16 v[24:27], v[140:143], v[206:209], v[24:27]
	v_mfma_f32_16x16x32_bf16 v[12:15], v[132:135], v[214:217], v[12:15]
	v_mfma_f32_16x16x32_bf16 v[8:11], v[140:143], v[214:217], v[8:11]
	s_setprio 0
	s_setprio 1
	v_mfma_f32_16x16x32_bf16 v[52:55], v[144:147], v[180:183], 0
	v_mfma_f32_16x16x32_bf16 v[48:51], v[172:175], v[180:183], 0
	v_mfma_f32_16x16x32_bf16 v[36:39], v[144:147], v[194:197], 0
	v_mfma_f32_16x16x32_bf16 v[32:35], v[172:175], v[194:197], 0
	v_mfma_f32_16x16x32_bf16 v[20:23], v[144:147], v[202:205], 0
	v_mfma_f32_16x16x32_bf16 v[16:19], v[172:175], v[202:205], 0
	v_mfma_f32_16x16x32_bf16 v[4:7], v[144:147], v[210:213], 0
	v_mfma_f32_16x16x32_bf16 v[0:3], v[172:175], v[210:213], 0
	v_mfma_f32_16x16x32_bf16 v[52:55], v[148:151], v[184:187], v[52:55]
	v_mfma_f32_16x16x32_bf16 v[48:51], v[176:179], v[184:187], v[48:51]
	v_mfma_f32_16x16x32_bf16 v[36:39], v[148:151], v[198:201], v[36:39]
	v_mfma_f32_16x16x32_bf16 v[32:35], v[176:179], v[198:201], v[32:35]
	v_mfma_f32_16x16x32_bf16 v[20:23], v[148:151], v[206:209], v[20:23]
	v_mfma_f32_16x16x32_bf16 v[16:19], v[176:179], v[206:209], v[16:19]
	v_mfma_f32_16x16x32_bf16 v[4:7], v[148:151], v[214:217], v[4:7]
	v_mfma_f32_16x16x32_bf16 v[0:3], v[176:179], v[214:217], v[0:3]
	s_setprio 0
	s_barrier
; #define PG8_STAGE(bufoff, gbase, voff) do { _Pragma("unroll") for (int _i = 0; _i < 2; ++_i) \
;         __builtin_amdgcn_global_load_lds((const unsigned*)((const char*)(gbase) + (voff)[_i]), (PG8_LAS unsigned*)(lds + (bufoff) + ldsw + _i * 8192), 16, 0, 0); } while (0)
; #define PG8_LDA(dst, b, h) do { _Pragma("unroll") for (int m = 0; m < 4; ++m) _Pragma("unroll") for (int k = 0; k < 2; ++k) dst[m][k] = *(const PG8_LAS bf16x8*)(lds + PG8_SA(b, h) + aoff + m * 2048 + k * 1024); } while (0)
; #define PG8_WAIT_V(n) asm volatile("s_waitcnt vmcnt(" #n ")" ::: "memory")
; #define PG8_WAIT_L(n) asm volatile("s_waitcnt lgkmcnt(" #n ")" ::: "memory")
; #define PG8_BAR __builtin_amdgcn_s_barrier()
; template <class Epi, class Sched, bool ALIGN_EPI = false, bool SP2 = false>
; __device__ __forceinline__ void gemm_phase(PG8_LAS unsigned char* lds, const Gemm g, const Sched& S, const Epi& E, const int wid) {
;     ...
;         for (int t = 0; t < nt; t += 2) {
;             const bool last = (t == nt - 2);
;             const char* a1 = cA + (size_t)(t + 1) * kstep;
;             const char* a2 = last ? nA : cA + (size_t)(t + 2) * kstep; const char* b2 = last ? nB : cB + (size_t)(t + 2) * kstep;
;             const char* a3 = a2 + kstep; const char* b3 = b2 + kstep;
;             if (last && has_next) S.a_ready(nxt);
;             if constexpr (SP2) {
;             PG8_LDB(B0, 0, 0); PG8_LDB(B1, 0, 1); PG8_SCHED; PG8_LDA(At, 0, 0); PG8_STAGE(PG8_SA(1, 1), a1 + hstepA, voffA);
;             PG8_WAIT_V(8); PG8_WAIT_L(0); PG8_BAR; PG8_MMA(0, 0, At, B0); PG8_MMA(0, 1, At, B1); PG8_BAR; PG8_SCHED;
;             PG8_LDA(At, 0, 1); PG8_STAGE(PG8_SB(0, 0), b2, voffB); PG8_STAGE(PG8_SB(0, 1), b2 + hstepB, voffB); PG8_STAGE(PG8_SA(0, 0), a2, voffA);
;             PG8_WAIT_V(8); PG8_WAIT_L(0); PG8_BAR; PG8_MMA(1, 0, At, B0); PG8_MMA(1, 1, At, B1); PG8_BAR; PG8_SCHED;
;             PG8_LDB(B0, 1, 0); PG8_LDB(B1, 1, 1); PG8_SCHED; PG8_LDA(At, 1, 0); PG8_STAGE(PG8_SA(0, 1), a2 + hstepA, voffA);
;             PG8_WAIT_V(8); PG8_WAIT_L(0); PG8_BAR; PG8_MMA(0, 0, At, B0); PG8_MMA(0, 1, At, B1); PG8_BAR; PG8_SCHED;
;             PG8_LDA(At, 1, 1); PG8_STAGE(PG8_SB(1, 0), b3, voffB); PG8_STAGE(PG8_SB(1, 1), b3 + hstepB, voffB); PG8_STAGE(PG8_SA(1, 0), a3, voffA);
;             PG8_WAIT_V(8); PG8_WAIT_L(0); PG8_BAR; PG8_MMA(1, 0, At, B0); PG8_MMA(1, 1, At, B1); PG8_BAR; PG8_SCHED;
	s_add_i32 s59, 0, 0x18000
	s_add_i32 s60, 0, 0x1c000
	ds_read_b128 v[128:131], v252
	ds_read_b128 v[132:135], v252 offset:1024
	ds_read_b128 v[136:139], v252 offset:2048
	ds_read_b128 v[140:143], v252 offset:3072
	ds_read_b128 v[144:147], v253
	ds_read_b128 v[148:151], v253 offset:1024
	ds_read_b128 v[172:175], v253 offset:2048
	ds_read_b128 v[176:179], v253 offset:3072
	s_add_u32 s22, s28, 0xb0000
	s_addc_u32 s23, s29, 0
	s_mov_b32 m0, s36
	ds_read_b128 v[180:183], v192 offset:32768
	ds_read_b128 v[184:187], v192 offset:33792
	ds_read_b128 v[194:197], v192 offset:34816
	ds_read_b128 v[198:201], v192 offset:35840
	ds_read_b128 v[202:205], v192 offset:36864
	ds_read_b128 v[206:209], v192 offset:37888
	ds_read_b128 v[210:213], v192 offset:38912
	ds_read_b128 v[214:217], v192 offset:39936
	global_load_lds_dwordx4 v152, s[22:23]
	s_mov_b32 m0, s37
	s_nop 0
	global_load_lds_dwordx4 v156, s[22:23]
	s_waitcnt vmcnt(8) lgkmcnt(0)
	s_barrier
	s_nop 0
	s_setprio 1
	v_mfma_f32_16x16x32_bf16 v[124:127], v[128:131], v[180:183], v[124:127]
	v_mfma_f32_16x16x32_bf16 v[120:123], v[136:139], v[180:183], v[120:123]
	v_mfma_f32_16x16x32_bf16 v[108:111], v[128:131], v[194:197], v[108:111]
	v_mfma_f32_16x16x32_bf16 v[104:107], v[136:139], v[194:197], v[104:107]
	v_mfma_f32_16x16x32_bf16 v[92:95], v[128:131], v[202:205], v[92:95]
	v_mfma_f32_16x16x32_bf16 v[88:91], v[136:139], v[202:205], v[88:91]
	v_mfma_f32_16x16x32_bf16 v[76:79], v[128:131], v[210:213], v[76:79]
	v_mfma_f32_16x16x32_bf16 v[72:75], v[136:139], v[210:213], v[72:75]
	v_mfma_f32_16x16x32_bf16 v[124:127], v[132:135], v[184:187], v[124:127]
	v_mfma_f32_16x16x32_bf16 v[120:123], v[140:143], v[184:187], v[120:123]
	v_mfma_f32_16x16x32_bf16 v[108:111], v[132:135], v[198:201], v[108:111]
	v_mfma_f32_16x16x32_bf16 v[104:107], v[140:143], v[198:201], v[104:107]
	v_mfma_f32_16x16x32_bf16 v[92:95], v[132:135], v[206:209], v[92:95]
	v_mfma_f32_16x16x32_bf16 v[88:91], v[140:143], v[206:209], v[88:91]
	v_mfma_f32_16x16x32_bf16 v[76:79], v[132:135], v[214:217], v[76:79]
	v_mfma_f32_16x16x32_bf16 v[72:75], v[140:143], v[214:217], v[72:75]
	s_setprio 0
	s_setprio 1
	v_mfma_f32_16x16x32_bf16 v[116:119], v[144:147], v[180:183], v[116:119]
	v_mfma_f32_16x16x32_bf16 v[112:115], v[172:175], v[180:183], v[112:115]
	v_mfma_f32_16x16x32_bf16 v[100:103], v[144:147], v[194:197], v[100:103]
	v_mfma_f32_16x16x32_bf16 v[96:99], v[172:175], v[194:197], v[96:99]
	v_mfma_f32_16x16x32_bf16 v[84:87], v[144:147], v[202:205], v[84:87]
	v_mfma_f32_16x16x32_bf16 v[80:83], v[172:175], v[202:205], v[80:83]
	v_mfma_f32_16x16x32_bf16 v[68:71], v[144:147], v[210:213], v[68:71]
	v_mfma_f32_16x16x32_bf16 v[64:67], v[172:175], v[210:213], v[64:67]
	v_mfma_f32_16x16x32_bf16 v[116:119], v[148:151], v[184:187], v[116:119]
	v_mfma_f32_16x16x32_bf16 v[112:115], v[176:179], v[184:187], v[112:115]
	v_mfma_f32_16x16x32_bf16 v[100:103], v[148:151], v[198:201], v[100:103]
	v_mfma_f32_16x16x32_bf16 v[96:99], v[176:179], v[198:201], v[96:99]
	v_mfma_f32_16x16x32_bf16 v[84:87], v[148:151], v[206:209], v[84:87]
	v_mfma_f32_16x16x32_bf16 v[80:83], v[176:179], v[206:209], v[80:83]
	v_mfma_f32_16x16x32_bf16 v[68:71], v[148:151], v[214:217], v[68:71]
	v_mfma_f32_16x16x32_bf16 v[64:67], v[176:179], v[214:217], v[64:67]
	s_setprio 0
	s_barrier
	s_add_i32 s22, s59, s33
	s_mov_b32 m0, s22
	ds_read_b128 v[180:183], v192 offset:49152
	ds_read_b128 v[184:187], v192 offset:50176
	ds_read_b128 v[194:197], v192 offset:51200
	ds_read_b128 v[198:201], v192 offset:52224
	ds_read_b128 v[202:205], v192 offset:53248
	ds_read_b128 v[206:209], v192 offset:54272
	ds_read_b128 v[210:213], v192 offset:55296
	ds_read_b128 v[214:217], v192 offset:56320
	global_load_lds_dwordx4 v154, s[98:99]
	s_add_i32 m0, s22, 0x2000
	s_add_u32 s22, s26, 0xb0080
	s_addc_u32 s23, s27, 0
	s_add_i32 s26, s60, s33
	global_load_lds_dwordx4 v158, s[98:99]
	s_mov_b32 m0, s26
	s_nop 0
	global_load_lds_dwordx4 v154, s[22:23]
	s_add_i32 m0, s26, 0x2000
	s_nop 0
	global_load_lds_dwordx4 v158, s[22:23]
	s_mov_b32 m0, s39
	s_nop 0
	global_load_lds_dwordx4 v152, s[100:101]
	s_mov_b32 m0, s40
	s_nop 0
	global_load_lds_dwordx4 v156, s[100:101]
	s_waitcnt vmcnt(8) lgkmcnt(0)
	s_barrier
	s_setprio 1
	v_mfma_f32_16x16x32_bf16 v[60:63], v[128:131], v[180:183], v[60:63]
	v_mfma_f32_16x16x32_bf16 v[56:59], v[136:139], v[180:183], v[56:59]
	v_mfma_f32_16x16x32_bf16 v[44:47], v[128:131], v[194:197], v[44:47]
	v_mfma_f32_16x16x32_bf16 v[40:43], v[136:139], v[194:197], v[40:43]
	v_mfma_f32_16x16x32_bf16 v[28:31], v[128:131], v[202:205], v[28:31]
	v_mfma_f32_16x16x32_bf16 v[24:27], v[136:139], v[202:205], v[24:27]
	v_mfma_f32_16x16x32_bf16 v[12:15], v[128:131], v[210:213], v[12:15]
	v_mfma_f32_16x16x32_bf16 v[8:11], v[136:139], v[210:213], v[8:11]
	v_mfma_f32_16x16x32_bf16 v[60:63], v[132:135], v[184:187], v[60:63]
	v_mfma_f32_16x16x32_bf16 v[56:59], v[140:143], v[184:187], v[56:59]
	v_mfma_f32_16x16x32_bf16 v[44:47], v[132:135], v[198:201], v[44:47]
	v_mfma_f32_16x16x32_bf16 v[40:43], v[140:143], v[198:201], v[40:43]
	v_mfma_f32_16x16x32_bf16 v[28:31], v[132:135], v[206:209], v[28:31]
	v_mfma_f32_16x16x32_bf16 v[24:27], v[140:143], v[206:209], v[24:27]
	v_mfma_f32_16x16x32_bf16 v[12:15], v[132:135], v[214:217], v[12:15]
	v_mfma_f32_16x16x32_bf16 v[8:11], v[140:143], v[214:217], v[8:11]
	s_setprio 0
	s_setprio 1
	v_mfma_f32_16x16x32_bf16 v[52:55], v[144:147], v[180:183], v[52:55]
	v_mfma_f32_16x16x32_bf16 v[48:51], v[172:175], v[180:183], v[48:51]
	v_mfma_f32_16x16x32_bf16 v[36:39], v[144:147], v[194:197], v[36:39]
	v_mfma_f32_16x16x32_bf16 v[32:35], v[172:175], v[194:197], v[32:35]
	v_mfma_f32_16x16x32_bf16 v[20:23], v[144:147], v[202:205], v[20:23]
	v_mfma_f32_16x16x32_bf16 v[16:19], v[172:175], v[202:205], v[16:19]
	v_mfma_f32_16x16x32_bf16 v[4:7], v[144:147], v[210:213], v[4:7]
	v_mfma_f32_16x16x32_bf16 v[0:3], v[172:175], v[210:213], v[0:3]
	v_mfma_f32_16x16x32_bf16 v[52:55], v[148:151], v[184:187], v[52:55]
	v_mfma_f32_16x16x32_bf16 v[48:51], v[176:179], v[184:187], v[48:51]
	v_mfma_f32_16x16x32_bf16 v[36:39], v[148:151], v[198:201], v[36:39]
	v_mfma_f32_16x16x32_bf16 v[32:35], v[176:179], v[198:201], v[32:35]
	v_mfma_f32_16x16x32_bf16 v[20:23], v[148:151], v[206:209], v[20:23]
	v_mfma_f32_16x16x32_bf16 v[16:19], v[176:179], v[206:209], v[16:19]
	v_mfma_f32_16x16x32_bf16 v[4:7], v[148:151], v[214:217], v[4:7]
	v_mfma_f32_16x16x32_bf16 v[0:3], v[176:179], v[214:217], v[0:3]
	s_setprio 0
	s_barrier
	s_add_i32 s58, s58, 2
	s_add_u32 s56, s56, 0x100
	s_addc_u32 s57, s57, 0
	s_cmp_gt_u32 s58, 41
	s_mov_b64 s[22:23], s[24:25]
; #define PG8_STAGE(bufoff, gbase, voff) do { _Pragma("unroll") for (int _i = 0; _i < 2; ++_i) \
;         __builtin_amdgcn_global_load_lds((const unsigned*)((const char*)(gbase) + (voff)[_i]), (PG8_LAS unsigned*)(lds + (bufoff) + ldsw + _i * 8192), 16, 0, 0); } while (0)
; #define PG8_LDA(dst, b, h) do { _Pragma("unroll") for (int m = 0; m < 4; ++m) _Pragma("unroll") for (int k = 0; k < 2; ++k) dst[m][k] = *(const PG8_LAS bf16x8*)(lds + PG8_SA(b, h) + aoff + m * 2048 + k * 1024); } while (0)
; #define PG8_LDB(dst, b, h) do { _Pragma("unroll") for (int n = 0; n < 2; ++n) _Pragma("unroll") for (int k = 0; k < 2; ++k) dst[n][k] = *(const PG8_LAS bf16x8*)(lds + PG8_SB(b, h) + boff + n * 2048 + k * 1024); } while (0)
; #define PG8_MMA(ai, bj, At, Bt) do { __builtin_amdgcn_s_setprio(1); _Pragma("unroll") for (int m = 0; m < 4; ++m) _Pragma("unroll") for (int n = 0; n < 2; ++n) _Pragma("unroll") for (int k = 0; k < 2; ++k) \
;         acc[ai][bj][m][n] = __builtin_amdgcn_mfma_f32_16x16x32_bf16(Bt[n][k], At[m][k], acc[ai][bj][m][n], 0, 0, 0); __builtin_amdgcn_s_setprio(0); } while (0)
; #define PG8_WAIT_V(n) asm volatile("s_waitcnt vmcnt(" #n ")" ::: "memory")
; #define PG8_BAR __builtin_amdgcn_s_barrier()
; template <class Epi, class Sched, bool ALIGN_EPI = false, bool SP2 = false>
; __device__ __forceinline__ void gemm_phase(PG8_LAS unsigned char* lds, const Gemm g, const Sched& S, const Epi& E, const int wid) {
;     ...
;         for (int t = 0; t < nt; t += 2) {
;             const bool last = (t == nt - 2);
;             const char* a1 = cA + (size_t)(t + 1) * kstep;
;             const char* a2 = last ? nA : cA + (size_t)(t + 2) * kstep; const char* b2 = last ? nB : cB + (size_t)(t + 2) * kstep;
;             const char* a3 = a2 + kstep; const char* b3 = b2 + kstep;
;             if (last && has_next) S.a_ready(nxt);
;             if constexpr (SP2) {
;             PG8_LDB(B0, 0, 0); PG8_LDB(B1, 0, 1); PG8_SCHED; PG8_LDA(At, 0, 0); PG8_STAGE(PG8_SA(1, 1), a1 + hstepA, voffA);
;             PG8_WAIT_V(8); PG8_WAIT_L(0); PG8_BAR; PG8_MMA(0, 0, At, B0); PG8_MMA(0, 1, At, B1); PG8_BAR; PG8_SCHED;
;             PG8_LDA(At, 0, 1); PG8_STAGE(PG8_SB(0, 0), b2, voffB); PG8_STAGE(PG8_SB(0, 1), b2 + hstepB, voffB); PG8_STAGE(PG8_SA(0, 0), a2, voffA);
;             PG8_WAIT_V(8); PG8_WAIT_L(0); PG8_BAR; PG8_MMA(1, 0, At, B0); PG8_MMA(1, 1, At, B1); PG8_BAR; PG8_SCHED;
.LBB0_2897:
	ds_read_b128 v[128:131], v190
	ds_read_b128 v[132:135], v190 offset:1024
	ds_read_b128 v[136:139], v190 offset:2048
	ds_read_b128 v[140:143], v190 offset:3072
	ds_read_b128 v[144:147], v191
	ds_read_b128 v[148:151], v191 offset:1024
	ds_read_b128 v[172:175], v191 offset:2048
	ds_read_b128 v[176:179], v191 offset:3072
	s_add_u32 s24, s22, 0x100
	s_addc_u32 s25, s23, 0
	s_cmp_eq_u32 s58, 40
	s_cselect_b32 s29, s7, s25
	s_cselect_b32 s28, s6, s24
	s_cselect_b32 s27, s21, s57
	s_cselect_b32 s26, s20, s56
	s_add_i32 m0, s34, 0xc000
	ds_read_b128 v[180:183], v192
	ds_read_b128 v[184:187], v192 offset:1024
	ds_read_b128 v[194:197], v192 offset:2048
	ds_read_b128 v[198:201], v192 offset:3072
	ds_read_b128 v[202:205], v192 offset:4096
	ds_read_b128 v[206:209], v192 offset:5120
	ds_read_b128 v[210:213], v192 offset:6144
	ds_read_b128 v[214:217], v192 offset:7168
	global_load_lds_dwordx4 v164, s[22:23]
	s_add_i32 m0, s34, 0xe000
	s_nop 0
	global_load_lds_dwordx4 v166, s[22:23]
	s_waitcnt vmcnt(8) lgkmcnt(0)
	s_barrier
	s_setprio 1
	v_mfma_f32_16x16x32_bf16 v[124:127], v[128:131], v[180:183], v[124:127]
	v_mfma_f32_16x16x32_bf16 v[120:123], v[136:139], v[180:183], v[120:123]
	v_mfma_f32_16x16x32_bf16 v[108:111], v[128:131], v[194:197], v[108:111]
	v_mfma_f32_16x16x32_bf16 v[104:107], v[136:139], v[194:197], v[104:107]
	v_mfma_f32_16x16x32_bf16 v[92:95], v[128:131], v[202:205], v[92:95]
	v_mfma_f32_16x16x32_bf16 v[88:91], v[136:139], v[202:205], v[88:91]
	v_mfma_f32_16x16x32_bf16 v[76:79], v[128:131], v[210:213], v[76:79]
	v_mfma_f32_16x16x32_bf16 v[72:75], v[136:139], v[210:213], v[72:75]
	v_mfma_f32_16x16x32_bf16 v[124:127], v[132:135], v[184:187], v[124:127]
	v_mfma_f32_16x16x32_bf16 v[120:123], v[140:143], v[184:187], v[120:123]
	v_mfma_f32_16x16x32_bf16 v[108:111], v[132:135], v[198:201], v[108:111]
	v_mfma_f32_16x16x32_bf16 v[104:107], v[140:143], v[198:201], v[104:107]
	v_mfma_f32_16x16x32_bf16 v[92:95], v[132:135], v[206:209], v[92:95]
	v_mfma_f32_16x16x32_bf16 v[88:91], v[140:143], v[206:209], v[88:91]
	v_mfma_f32_16x16x32_bf16 v[76:79], v[132:135], v[214:217], v[76:79]
	v_mfma_f32_16x16x32_bf16 v[72:75], v[140:143], v[214:217], v[72:75]
	s_setprio 0
	s_setprio 1
	v_mfma_f32_16x16x32_bf16 v[116:119], v[144:147], v[180:183], v[116:119]
	v_mfma_f32_16x16x32_bf16 v[112:115], v[172:175], v[180:183], v[112:115]
	v_mfma_f32_16x16x32_bf16 v[100:103], v[144:147], v[194:197], v[100:103]
	v_mfma_f32_16x16x32_bf16 v[96:99], v[172:175], v[194:197], v[96:99]
	v_mfma_f32_16x16x32_bf16 v[84:87], v[144:147], v[202:205], v[84:87]
	v_mfma_f32_16x16x32_bf16 v[80:83], v[172:175], v[202:205], v[80:83]
	v_mfma_f32_16x16x32_bf16 v[68:71], v[144:147], v[210:213], v[68:71]
	v_mfma_f32_16x16x32_bf16 v[64:67], v[172:175], v[210:213], v[64:67]
	v_mfma_f32_16x16x32_bf16 v[116:119], v[148:151], v[184:187], v[116:119]
	v_mfma_f32_16x16x32_bf16 v[112:115], v[176:179], v[184:187], v[112:115]
	v_mfma_f32_16x16x32_bf16 v[100:103], v[148:151], v[198:201], v[100:103]
	v_mfma_f32_16x16x32_bf16 v[96:99], v[176:179], v[198:201], v[96:99]
	v_mfma_f32_16x16x32_bf16 v[84:87], v[148:151], v[206:209], v[84:87]
	v_mfma_f32_16x16x32_bf16 v[80:83], v[176:179], v[206:209], v[80:83]
	v_mfma_f32_16x16x32_bf16 v[68:71], v[148:151], v[214:217], v[68:71]
	v_mfma_f32_16x16x32_bf16 v[64:67], v[176:179], v[214:217], v[64:67]
	s_setprio 0
	s_barrier
	s_add_i32 s22, s43, s33
	s_add_u32 s98, s26, 0x80
	s_addc_u32 s99, s27, 0
	s_mov_b32 m0, s22
	ds_read_b128 v[180:183], v192 offset:16384
	ds_read_b128 v[184:187], v192 offset:17408
	ds_read_b128 v[194:197], v192 offset:18432
	ds_read_b128 v[198:201], v192 offset:19456
	ds_read_b128 v[202:205], v192 offset:20480
	ds_read_b128 v[206:209], v192 offset:21504
	ds_read_b128 v[210:213], v192 offset:22528
	ds_read_b128 v[214:217], v192 offset:23552
	global_load_lds_dwordx4 v154, s[26:27]
	s_add_i32 m0, s22, 0x2000
	s_add_u32 s22, s26, 0xb0000
	s_addc_u32 s23, s27, 0
	s_add_i32 s59, s44, s33
	global_load_lds_dwordx4 v158, s[26:27]
	s_mov_b32 m0, s59
	s_add_u32 s100, s28, 0x80
	s_addc_u32 s101, s29, 0
	global_load_lds_dwordx4 v154, s[22:23]
	s_add_i32 m0, s59, 0x2000
	s_nop 0
	global_load_lds_dwordx4 v158, s[22:23]
	s_mov_b32 m0, s34
	s_nop 0
	global_load_lds_dwordx4 v152, s[28:29]
	s_mov_b32 m0, s35
	s_nop 0
	global_load_lds_dwordx4 v156, s[28:29]
	s_waitcnt vmcnt(8) lgkmcnt(0)
	s_barrier
	s_nop 0
	s_setprio 1
	v_mfma_f32_16x16x32_bf16 v[60:63], v[128:131], v[180:183], v[60:63]
	v_mfma_f32_16x16x32_bf16 v[56:59], v[136:139], v[180:183], v[56:59]
	v_mfma_f32_16x16x32_bf16 v[44:47], v[128:131], v[194:197], v[44:47]
	v_mfma_f32_16x16x32_bf16 v[40:43], v[136:139], v[194:197], v[40:43]
	v_mfma_f32_16x16x32_bf16 v[28:31], v[128:131], v[202:205], v[28:31]
	v_mfma_f32_16x16x32_bf16 v[24:27], v[136:139], v[202:205], v[24:27]
	v_mfma_f32_16x16x32_bf16 v[12:15], v[128:131], v[210:213], v[12:15]
	v_mfma_f32_16x16x32_bf16 v[8:11], v[136:139], v[210:213], v[8:11]
	v_mfma_f32_16x16x32_bf16 v[60:63], v[132:135], v[184:187], v[60:63]
	v_mfma_f32_16x16x32_bf16 v[56:59], v[140:143], v[184:187], v[56:59]
	v_mfma_f32_16x16x32_bf16 v[44:47], v[132:135], v[198:201], v[44:47]
	v_mfma_f32_16x16x32_bf16 v[40:43], v[140:143], v[198:201], v[40:43]
	v_mfma_f32_16x16x32_bf16 v[28:31], v[132:135], v[206:209], v[28:31]
	v_mfma_f32_16x16x32_bf16 v[24:27], v[140:143], v[206:209], v[24:27]
	v_mfma_f32_16x16x32_bf16 v[12:15], v[132:135], v[214:217], v[12:15]
	v_mfma_f32_16x16x32_bf16 v[8:11], v[140:143], v[214:217], v[8:11]
	s_setprio 0
	s_setprio 1
	v_mfma_f32_16x16x32_bf16 v[52:55], v[144:147], v[180:183], v[52:55]
	v_mfma_f32_16x16x32_bf16 v[48:51], v[172:175], v[180:183], v[48:51]
	v_mfma_f32_16x16x32_bf16 v[36:39], v[144:147], v[194:197], v[36:39]
	v_mfma_f32_16x16x32_bf16 v[32:35], v[172:175], v[194:197], v[32:35]
	v_mfma_f32_16x16x32_bf16 v[20:23], v[144:147], v[202:205], v[20:23]
	v_mfma_f32_16x16x32_bf16 v[16:19], v[172:175], v[202:205], v[16:19]
	v_mfma_f32_16x16x32_bf16 v[4:7], v[144:147], v[210:213], v[4:7]
	v_mfma_f32_16x16x32_bf16 v[0:3], v[172:175], v[210:213], v[0:3]
	v_mfma_f32_16x16x32_bf16 v[52:55], v[148:151], v[184:187], v[52:55]
	v_mfma_f32_16x16x32_bf16 v[48:51], v[176:179], v[184:187], v[48:51]
	v_mfma_f32_16x16x32_bf16 v[36:39], v[148:151], v[198:201], v[36:39]
	v_mfma_f32_16x16x32_bf16 v[32:35], v[176:179], v[198:201], v[32:35]
	v_mfma_f32_16x16x32_bf16 v[20:23], v[148:151], v[206:209], v[20:23]
	v_mfma_f32_16x16x32_bf16 v[16:19], v[176:179], v[206:209], v[16:19]
	v_mfma_f32_16x16x32_bf16 v[4:7], v[148:151], v[214:217], v[4:7]
	v_mfma_f32_16x16x32_bf16 v[0:3], v[176:179], v[214:217], v[0:3]
	s_setprio 0
	s_barrier
; #define PG8_STAGE(bufoff, gbase, voff) do { _Pragma("unroll") for (int _i = 0; _i < 2; ++_i) \
;         __builtin_amdgcn_global_load_lds((const unsigned*)((const char*)(gbase) + (voff)[_i]), (PG8_LAS unsigned*)(lds + (bufoff) + ldsw + _i * 8192), 16, 0, 0); } while (0)
; #define PG8_LDA(dst, b, h) do { _Pragma("unroll") for (int m = 0; m < 4; ++m) _Pragma("unroll") for (int k = 0; k < 2; ++k) dst[m][k] = *(const PG8_LAS bf16x8*)(lds + PG8_SA(b, h) + aoff + m * 2048 + k * 1024); } while (0)
; #define PG8_WAIT_V(n) asm volatile("s_waitcnt vmcnt(" #n ")" ::: "memory")
; #define PG8_WAIT_L(n) asm volatile("s_waitcnt lgkmcnt(" #n ")" ::: "memory")
; #define PG8_BAR __builtin_amdgcn_s_barrier()
; template <class Epi, class Sched, bool ALIGN_EPI = false, bool SP2 = false>
; __device__ __forceinline__ void gemm_phase(PG8_LAS unsigned char* lds, const Gemm g, const Sched& S, const Epi& E, const int wid) {
;     ...
;         for (int t = 0; t < nt; t += 2) {
;             const bool last = (t == nt - 2);
;             const char* a1 = cA + (size_t)(t + 1) * kstep;
;             const char* a2 = last ? nA : cA + (size_t)(t + 2) * kstep; const char* b2 = last ? nB : cB + (size_t)(t + 2) * kstep;
;             const char* a3 = a2 + kstep; const char* b3 = b2 + kstep;
;             if (last && has_next) S.a_ready(nxt);
;             if constexpr (SP2) {
;             PG8_LDB(B0, 0, 0); PG8_LDB(B1, 0, 1); PG8_SCHED; PG8_LDA(At, 0, 0); PG8_STAGE(PG8_SA(1, 1), a1 + hstepA, voffA);
;             PG8_WAIT_V(8); PG8_WAIT_L(0); PG8_BAR; PG8_MMA(0, 0, At, B0); PG8_MMA(0, 1, At, B1); PG8_BAR; PG8_SCHED;
;             PG8_LDA(At, 0, 1); PG8_STAGE(PG8_SB(0, 0), b2, voffB); PG8_STAGE(PG8_SB(0, 1), b2 + hstepB, voffB); PG8_STAGE(PG8_SA(0, 0), a2, voffA);
;             PG8_WAIT_V(8); PG8_WAIT_L(0); PG8_BAR; PG8_MMA(1, 0, At, B0); PG8_MMA(1, 1, At, B1); PG8_BAR; PG8_SCHED;
;             PG8_LDB(B0, 1, 0); PG8_LDB(B1, 1, 1); PG8_SCHED; PG8_LDA(At, 1, 0); PG8_STAGE(PG8_SA(0, 1), a2 + hstepA, voffA);
;             PG8_WAIT_V(8); PG8_WAIT_L(0); PG8_BAR; PG8_MMA(0, 0, At, B0); PG8_MMA(0, 1, At, B1); PG8_BAR; PG8_SCHED;
;             PG8_LDA(At, 1, 1); PG8_STAGE(PG8_SB(1, 0), b3, voffB); PG8_STAGE(PG8_SB(1, 1), b3 + hstepB, voffB); PG8_STAGE(PG8_SA(1, 0), a3, voffA);
;             PG8_WAIT_V(8); PG8_WAIT_L(0); PG8_BAR; PG8_MMA(1, 0, At, B0); PG8_MMA(1, 1, At, B1); PG8_BAR; PG8_SCHED;
	s_add_i32 s59, 0, 0x18000
	s_add_i32 s60, 0, 0x1c000
	ds_read_b128 v[128:131], v252
	ds_read_b128 v[132:135], v252 offset:1024
	ds_read_b128 v[136:139], v252 offset:2048
	ds_read_b128 v[140:143], v252 offset:3072
	ds_read_b128 v[144:147], v253
	ds_read_b128 v[148:151], v253 offset:1024
	ds_read_b128 v[172:175], v253 offset:2048
	ds_read_b128 v[176:179], v253 offset:3072
	s_add_u32 s22, s28, 0xb0000
	s_addc_u32 s23, s29, 0
	s_mov_b32 m0, s36
	ds_read_b128 v[180:183], v192 offset:32768
	ds_read_b128 v[184:187], v192 offset:33792
	ds_read_b128 v[194:197], v192 offset:34816
	ds_read_b128 v[198:201], v192 offset:35840
	ds_read_b128 v[202:205], v192 offset:36864
	ds_read_b128 v[206:209], v192 offset:37888
	ds_read_b128 v[210:213], v192 offset:38912
	ds_read_b128 v[214:217], v192 offset:39936
	global_load_lds_dwordx4 v152, s[22:23]
	s_mov_b32 m0, s37
	s_nop 0
	global_load_lds_dwordx4 v156, s[22:23]
	s_waitcnt vmcnt(8) lgkmcnt(0)
	s_barrier
	s_nop 0
	s_setprio 1
	v_mfma_f32_16x16x32_bf16 v[124:127], v[128:131], v[180:183], v[124:127]
	v_mfma_f32_16x16x32_bf16 v[120:123], v[136:139], v[180:183], v[120:123]
	v_mfma_f32_16x16x32_bf16 v[108:111], v[128:131], v[194:197], v[108:111]
	v_mfma_f32_16x16x32_bf16 v[104:107], v[136:139], v[194:197], v[104:107]
	v_mfma_f32_16x16x32_bf16 v[92:95], v[128:131], v[202:205], v[92:95]
	v_mfma_f32_16x16x32_bf16 v[88:91], v[136:139], v[202:205], v[88:91]
	v_mfma_f32_16x16x32_bf16 v[76:79], v[128:131], v[210:213], v[76:79]
	v_mfma_f32_16x16x32_bf16 v[72:75], v[136:139], v[210:213], v[72:75]
	v_mfma_f32_16x16x32_bf16 v[124:127], v[132:135], v[184:187], v[124:127]
	v_mfma_f32_16x16x32_bf16 v[120:123], v[140:143], v[184:187], v[120:123]
	v_mfma_f32_16x16x32_bf16 v[108:111], v[132:135], v[198:201], v[108:111]
	v_mfma_f32_16x16x32_bf16 v[104:107], v[140:143], v[198:201], v[104:107]
	v_mfma_f32_16x16x32_bf16 v[92:95], v[132:135], v[206:209], v[92:95]
	v_mfma_f32_16x16x32_bf16 v[88:91], v[140:143], v[206:209], v[88:91]
	v_mfma_f32_16x16x32_bf16 v[76:79], v[132:135], v[214:217], v[76:79]
	v_mfma_f32_16x16x32_bf16 v[72:75], v[140:143], v[214:217], v[72:75]
	s_setprio 0
	s_setprio 1
	v_mfma_f32_16x16x32_bf16 v[116:119], v[144:147], v[180:183], v[116:119]
	v_mfma_f32_16x16x32_bf16 v[112:115], v[172:175], v[180:183], v[112:115]
	v_mfma_f32_16x16x32_bf16 v[100:103], v[144:147], v[194:197], v[100:103]
	v_mfma_f32_16x16x32_bf16 v[96:99], v[172:175], v[194:197], v[96:99]
	v_mfma_f32_16x16x32_bf16 v[84:87], v[144:147], v[202:205], v[84:87]
	v_mfma_f32_16x16x32_bf16 v[80:83], v[172:175], v[202:205], v[80:83]
	v_mfma_f32_16x16x32_bf16 v[68:71], v[144:147], v[210:213], v[68:71]
	v_mfma_f32_16x16x32_bf16 v[64:67], v[172:175], v[210:213], v[64:67]
	v_mfma_f32_16x16x32_bf16 v[116:119], v[148:151], v[184:187], v[116:119]
	v_mfma_f32_16x16x32_bf16 v[112:115], v[176:179], v[184:187], v[112:115]
	v_mfma_f32_16x16x32_bf16 v[100:103], v[148:151], v[198:201], v[100:103]
	v_mfma_f32_16x16x32_bf16 v[96:99], v[176:179], v[198:201], v[96:99]
	v_mfma_f32_16x16x32_bf16 v[84:87], v[148:151], v[206:209], v[84:87]
	v_mfma_f32_16x16x32_bf16 v[80:83], v[176:179], v[206:209], v[80:83]
	v_mfma_f32_16x16x32_bf16 v[68:71], v[148:151], v[214:217], v[68:71]
	v_mfma_f32_16x16x32_bf16 v[64:67], v[176:179], v[214:217], v[64:67]
	s_setprio 0
	s_barrier
	s_add_i32 s22, s59, s33
	s_mov_b32 m0, s22
	ds_read_b128 v[180:183], v192 offset:49152
	ds_read_b128 v[184:187], v192 offset:50176
	ds_read_b128 v[194:197], v192 offset:51200
	ds_read_b128 v[198:201], v192 offset:52224
	ds_read_b128 v[202:205], v192 offset:53248
	ds_read_b128 v[206:209], v192 offset:54272
	ds_read_b128 v[210:213], v192 offset:55296
	ds_read_b128 v[214:217], v192 offset:56320
	global_load_lds_dwordx4 v154, s[98:99]
	s_add_i32 m0, s22, 0x2000
	s_add_u32 s22, s26, 0xb0080
	s_addc_u32 s23, s27, 0
	s_add_i32 s26, s60, s33
	global_load_lds_dwordx4 v158, s[98:99]
	s_mov_b32 m0, s26
	s_nop 0
	global_load_lds_dwordx4 v154, s[22:23]
	s_add_i32 m0, s26, 0x2000
	s_nop 0
	global_load_lds_dwordx4 v158, s[22:23]
	s_mov_b32 m0, s39
	s_nop 0
	global_load_lds_dwordx4 v152, s[100:101]
	s_mov_b32 m0, s40
	s_nop 0
	global_load_lds_dwordx4 v156, s[100:101]
	s_waitcnt vmcnt(8) lgkmcnt(0)
	s_barrier
	s_setprio 1
	v_mfma_f32_16x16x32_bf16 v[60:63], v[128:131], v[180:183], v[60:63]
	v_mfma_f32_16x16x32_bf16 v[56:59], v[136:139], v[180:183], v[56:59]
	v_mfma_f32_16x16x32_bf16 v[44:47], v[128:131], v[194:197], v[44:47]
	v_mfma_f32_16x16x32_bf16 v[40:43], v[136:139], v[194:197], v[40:43]
	v_mfma_f32_16x16x32_bf16 v[28:31], v[128:131], v[202:205], v[28:31]
	v_mfma_f32_16x16x32_bf16 v[24:27], v[136:139], v[202:205], v[24:27]
	v_mfma_f32_16x16x32_bf16 v[12:15], v[128:131], v[210:213], v[12:15]
	v_mfma_f32_16x16x32_bf16 v[8:11], v[136:139], v[210:213], v[8:11]
	v_mfma_f32_16x16x32_bf16 v[60:63], v[132:135], v[184:187], v[60:63]
	v_mfma_f32_16x16x32_bf16 v[56:59], v[140:143], v[184:187], v[56:59]
	v_mfma_f32_16x16x32_bf16 v[44:47], v[132:135], v[198:201], v[44:47]
	v_mfma_f32_16x16x32_bf16 v[40:43], v[140:143], v[198:201], v[40:43]
	v_mfma_f32_16x16x32_bf16 v[28:31], v[132:135], v[206:209], v[28:31]
	v_mfma_f32_16x16x32_bf16 v[24:27], v[140:143], v[206:209], v[24:27]
	v_mfma_f32_16x16x32_bf16 v[12:15], v[132:135], v[214:217], v[12:15]
	v_mfma_f32_16x16x32_bf16 v[8:11], v[140:143], v[214:217], v[8:11]
	s_setprio 0
	s_setprio 1
	v_mfma_f32_16x16x32_bf16 v[52:55], v[144:147], v[180:183], v[52:55]
	v_mfma_f32_16x16x32_bf16 v[48:51], v[172:175], v[180:183], v[48:51]
	v_mfma_f32_16x16x32_bf16 v[36:39], v[144:147], v[194:197], v[36:39]
	v_mfma_f32_16x16x32_bf16 v[32:35], v[172:175], v[194:197], v[32:35]
	v_mfma_f32_16x16x32_bf16 v[20:23], v[144:147], v[202:205], v[20:23]
	v_mfma_f32_16x16x32_bf16 v[16:19], v[172:175], v[202:205], v[16:19]
	v_mfma_f32_16x16x32_bf16 v[4:7], v[144:147], v[210:213], v[4:7]
	v_mfma_f32_16x16x32_bf16 v[0:3], v[172:175], v[210:213], v[0:3]
	v_mfma_f32_16x16x32_bf16 v[52:55], v[148:151], v[184:187], v[52:55]
	v_mfma_f32_16x16x32_bf16 v[48:51], v[176:179], v[184:187], v[48:51]
	v_mfma_f32_16x16x32_bf16 v[36:39], v[148:151], v[198:201], v[36:39]
	v_mfma_f32_16x16x32_bf16 v[32:35], v[176:179], v[198:201], v[32:35]
	v_mfma_f32_16x16x32_bf16 v[20:23], v[148:151], v[206:209], v[20:23]
	v_mfma_f32_16x16x32_bf16 v[16:19], v[176:179], v[206:209], v[16:19]
	v_mfma_f32_16x16x32_bf16 v[4:7], v[148:151], v[214:217], v[4:7]
	v_mfma_f32_16x16x32_bf16 v[0:3], v[176:179], v[214:217], v[0:3]
	s_setprio 0
	s_barrier
	s_add_i32 s58, s58, 2
	s_add_u32 s56, s56, 0x100
	s_addc_u32 s57, s57, 0
	s_cmp_gt_u32 s58, 41
	s_mov_b64 s[22:23], s[24:25]
	s_cbranch_scc0 .LBB0_2897
	s_and_b64 vcc, exec, s[18:19]
	s_cbranch_vccz .LBB0_2900
	s_barrier
